# remaining f32->bf16 bit-trick roundings consumed through the high half -> v_cvt_pk_bf16_f32 (118 sites in the layer loop), hazard nops re-derived
# speedup vs baseline: 1.0223x; 1.0040x over previous
; __device__ __forceinline__ f32x4 bf4(u32x2 v) { return (f32x4){lo_bf(v.x), hi_bf(v.x), lo_bf(v.y), hi_bf(v.y)}; }
; __device__ __forceinline__ void ph_prep_conv(CArgs& a, int l, LAS unsigned char* lds, int bid, int nblk) {
;     ...
;     for (int it = bid + (l == DEPTH - 1 ? 64 : 0); it < 576; it += nblk) {
;         const Chunk c = chunk_of(it);
;         const int tb = c.t0 + tg * 8;
;         const bf16* pb = P + (size_t)(c.row0 + tg * 8) * D_INP;
;         f32x4 x1[10], vv[10], mm[10];
; #pragma unroll
;         for (int r = 0; r < 10; ++r) { const int t = tb + r - 1, tc = min(max(t, c.lo), c.hi - 1); const float ok = (t == tc) ? 1.f : 0.f; const bf16* p = pb + (ptrdiff_t)(tc - tb) * D_INP;
;             x1[r] = ok * bf4(*(const u32x2*)(p + HY0 + 256 + c4)); vv[r] = ok * bf4(*(const u32x2*)(p + HY0 + 512 + c4));
;             mm[r] = ok * bf4(*(const u32x2*)(p + SC0 + 256 + c4)) * bf4(*(const u32x2*)(p + SC0 + 512 + c4)); }
.LBB0_266:
	v_add_u32_e32 v59, s28, v1
	v_add_u32_e32 v56, s11, v1
	v_mov_b64_e32 v[52:53], s[14:15]
	v_mad_i64_i32 v[78:79], s[16:17], v56, s65, v[52:53]
	v_max_i32_e32 v52, s10, v59
	v_min_u32_e32 v60, s9, v52
	v_sub_u32_e32 v52, v60, v59
	v_add_u32_e32 v58, -1, v59
	v_mad_i64_i32 v[52:53], s[16:17], v52, s65, v[78:79]
	v_lshl_add_u64 v[54:55], v[52:53], 0, v[34:35]
	v_max_i32_e32 v52, s10, v58
	v_min_u32_e32 v64, s9, v52
	v_sub_u32_e32 v52, v64, v59
	v_mad_i64_i32 v[52:53], s[16:17], v52, s65, v[78:79]
	v_or_b32_e32 v65, 1, v59
	v_lshl_add_u64 v[62:63], v[52:53], 0, v[34:35]
	v_max_i32_e32 v52, s10, v65
	v_min_u32_e32 v66, s9, v52
	v_sub_u32_e32 v52, v66, v59
	global_load_dwordx2 v[68:69], v[54:55], off offset:2048
	global_load_dwordx2 v[70:71], v[54:55], off offset:2560
	v_mad_i64_i32 v[52:53], s[16:17], v52, s65, v[78:79]
	v_lshl_add_u64 v[86:87], v[52:53], 0, v[34:35]
	global_load_dwordx2 v[82:83], v[62:63], off offset:2048
	global_load_dwordx2 v[84:85], v[62:63], off offset:2560
	global_load_dwordx2 v[88:89], v[86:87], off offset:2048
	global_load_dwordx2 v[90:91], v[86:87], off offset:2560
	v_lshl_add_u64 v[52:53], v[78:79], 0, v[34:35]
	global_load_dwordx2 v[92:93], v[52:53], off offset:1536
	v_or_b32_e32 v61, 2, v59
	v_max_i32_e32 v67, s10, v61
	v_cmp_eq_u32_e32 vcc, v60, v59
	v_min_u32_e32 v73, s9, v67
	v_or_b32_e32 v137, 3, v59
	v_cndmask_b32_e64 v60, 0, 1.0, vcc
	v_cmp_eq_u32_e32 vcc, v58, v64
	v_sub_u32_e32 v64, v73, v59
	v_or_b32_e32 v212, 4, v59
	v_cndmask_b32_e64 v72, 0, 1.0, vcc
	v_cmp_eq_u32_e32 vcc, v65, v66
	v_mad_i64_i32 v[64:65], s[16:17], v64, s65, v[78:79]
	global_load_dwordx2 v[74:75], v[54:55], off offset:512
	global_load_dwordx2 v[66:67], v[54:55], off offset:1024
	v_cndmask_b32_e64 v58, 0, 1.0, vcc
	v_lshl_add_u64 v[98:99], v[64:65], 0, v[34:35]
	global_load_dwordx2 v[80:81], v[62:63], off offset:512
	global_load_dwordx2 v[76:77], v[62:63], off offset:1024
	global_load_dwordx2 v[64:65], v[86:87], off offset:512
	s_nop 0
	global_load_dwordx2 v[62:63], v[86:87], off offset:1024
	v_or_b32_e32 v214, 5, v59
	v_or_b32_e32 v216, 6, v59
	v_or_b32_e32 v211, 7, v59
	v_add_u32_e32 v209, 8, v59
	v_ashrrev_i32_e32 v57, 31, v56
	v_lshlrev_b64 v[56:57], 11, v[56:57]
	v_lshl_add_u64 v[56:57], s[2:3], 0, v[56:57]
	v_lshl_add_u64 v[56:57], v[56:57], 0, v[34:35]
	s_lshl_b32 s78, s30, 1
	s_mov_b32 s29, s79
	s_add_i32 s0, s0, s68
	s_waitcnt vmcnt(0)
	v_lshlrev_b32_e32 v54, 16, v68
	v_and_b32_e32 v55, 0xffff0000, v68
	v_lshlrev_b32_e32 v68, 16, v69
	v_and_b32_e32 v69, 0xffff0000, v69
	v_lshlrev_b32_e32 v86, 16, v70
	v_and_b32_e32 v87, 0xffff0000, v70
	v_lshlrev_b32_e32 v70, 16, v71
	v_and_b32_e32 v71, 0xffff0000, v71
	v_lshlrev_b32_e32 v94, 16, v82
	v_and_b32_e32 v95, 0xffff0000, v82
	v_lshlrev_b32_e32 v82, 16, v83
	v_and_b32_e32 v83, 0xffff0000, v83
	v_pk_mul_f32 v[54:55], v[60:61], v[54:55] op_sel_hi:[0,1]
	v_pk_mul_f32 v[68:69], v[60:61], v[68:69] op_sel_hi:[0,1]
	v_lshlrev_b32_e32 v102, 16, v88
	v_and_b32_e32 v103, 0xffff0000, v88
	v_lshlrev_b32_e32 v88, 16, v89
	v_and_b32_e32 v89, 0xffff0000, v89
	v_lshlrev_b32_e32 v96, 16, v84
	v_and_b32_e32 v97, 0xffff0000, v84
	v_lshlrev_b32_e32 v100, 16, v85
	v_and_b32_e32 v101, 0xffff0000, v85
	v_lshlrev_b32_e32 v104, 16, v90
	v_and_b32_e32 v105, 0xffff0000, v90
	v_lshlrev_b32_e32 v90, 16, v91
	v_and_b32_e32 v91, 0xffff0000, v91
	v_pk_mul_f32 v[82:83], v[72:73], v[82:83] op_sel_hi:[0,1]
	v_pk_mul_f32 v[94:95], v[72:73], v[94:95] op_sel_hi:[0,1]
	v_pk_mul_f32 v[84:85], v[68:69], v[70:71]
	v_pk_mul_f32 v[86:87], v[54:55], v[86:87]
	v_pk_mul_f32 v[54:55], v[58:59], v[102:103] op_sel_hi:[0,1]
	v_pk_mul_f32 v[68:69], v[58:59], v[88:89] op_sel_hi:[0,1]
	v_pk_mul_f32 v[94:95], v[94:95], v[96:97]
	v_pk_mul_f32 v[96:97], v[82:83], v[100:101]
	v_pk_mul_f32 v[68:69], v[68:69], v[90:91]
	v_pk_mul_f32 v[70:71], v[54:55], v[104:105]
	global_load_dwordx2 v[82:83], v[98:99], off offset:512
	global_load_dwordx2 v[54:55], v[98:99], off offset:1024
	global_load_dwordx2 v[90:91], v[98:99], off offset:2048
	global_load_dwordx2 v[88:89], v[98:99], off offset:2560
	v_max_i32_e32 v98, s10, v137
	v_min_u32_e32 v142, s9, v98
	v_sub_u32_e32 v98, v142, v59
	v_mad_i64_i32 v[98:99], s[16:17], v98, s65, v[78:79]
	v_lshl_add_u64 v[98:99], v[98:99], 0, v[34:35]
	global_load_dwordx2 v[120:121], v[98:99], off offset:512
	global_load_dwordx2 v[118:119], v[98:99], off offset:1024
	global_load_dwordx2 v[124:125], v[98:99], off offset:2048
	global_load_dwordx2 v[122:123], v[98:99], off offset:2560
	v_max_i32_e32 v98, s10, v212
	v_min_u32_e32 v213, s9, v98
	v_sub_u32_e32 v98, v213, v59
	v_mad_i64_i32 v[98:99], s[16:17], v98, s65, v[78:79]
	v_lshl_add_u64 v[98:99], v[98:99], 0, v[34:35]
	global_load_dwordx2 v[174:175], v[98:99], off offset:512
	global_load_dwordx2 v[172:173], v[98:99], off offset:1024
	global_load_dwordx2 v[170:171], v[98:99], off offset:2048
	global_load_dwordx2 v[162:163], v[98:99], off offset:2560
	v_max_i32_e32 v98, s10, v214
	v_min_u32_e32 v215, s9, v98
	v_sub_u32_e32 v98, v215, v59
	v_mad_i64_i32 v[98:99], s[16:17], v98, s65, v[78:79]
	v_lshl_add_u64 v[98:99], v[98:99], 0, v[34:35]
	global_load_dwordx2 v[160:161], v[98:99], off offset:512
	global_load_dwordx2 v[158:159], v[98:99], off offset:1024
	global_load_dwordx2 v[128:129], v[98:99], off offset:2048
	global_load_dwordx2 v[126:127], v[98:99], off offset:2560
	v_max_i32_e32 v98, s10, v216
	v_min_u32_e32 v217, s9, v98
	v_sub_u32_e32 v98, v217, v59
	v_mad_i64_i32 v[98:99], s[16:17], v98, s65, v[78:79]
	v_lshl_add_u64 v[98:99], v[98:99], 0, v[34:35]
	global_load_dwordx2 v[156:157], v[98:99], off offset:512
	global_load_dwordx2 v[116:117], v[98:99], off offset:1024
; #define LAS __attribute__((address_space(3)))
; __device__ __forceinline__ unsigned pk2(float lo, float hi) { return f2bf(lo) | (f2bf(hi) << 16); }
; __device__ __forceinline__ f32x4 bf4(u32x2 v) { return (f32x4){lo_bf(v.x), hi_bf(v.x), lo_bf(v.y), hi_bf(v.y)}; }
; __device__ __forceinline__ void ph_prep_conv(CArgs& a, int l, LAS unsigned char* lds, int bid, int nblk) {
;     ...
;         for (int r = 0; r < 10; ++r) { const int t = tb + r - 1, tc = min(max(t, c.lo), c.hi - 1); const float ok = (t == tc) ? 1.f : 0.f; const bf16* p = pb + (ptrdiff_t)(tc - tb) * D_INP;
;             x1[r] = ok * bf4(*(const u32x2*)(p + HY0 + 256 + c4)); vv[r] = ok * bf4(*(const u32x2*)(p + HY0 + 512 + c4));
;             mm[r] = ok * bf4(*(const u32x2*)(p + SC0 + 256 + c4)) * bf4(*(const u32x2*)(p + SC0 + 512 + c4)); }
; #pragma unroll
;         for (int tt = 0; tt < 8; ++tt) {
;             const f32x4 xx = wx[0] * x1[tt] + wx[1] * x1[tt + 1] + wx[2] * x1[tt + 2] + bx, v2 = wv[0] * vv[tt] + wv[1] * vv[tt + 1] + wv[2] * vv[tt + 2] + bv, z = xx * v2;
;             u32x2 zo; zo.x = pk2(z[0], z[1]); zo.y = pk2(z[2], z[3]); *(LAS u32x2*)(zt + (tg * 8 + tt) * 264 + c4) = zo;
;             const f32x4 bg = bf4(*(const u32x2*)(pb + (size_t)tt * D_INP + SC0 + c4));
;             const f32x4 y = bg * (ws3[0] * mm[tt] + ws3[1] * mm[tt + 1] + ws3[2] * mm[tt + 2]);
;             u32x2 yo; yo.x = pk2(y[0], y[1]); yo.y = pk2(y[2], y[3]); *(u32x2*)(YMIX + (size_t)(c.row0 + tg * 8 + tt) * D + 256 + c4) = yo;
	global_load_dwordx2 v[114:115], v[98:99], off offset:2048
	global_load_dwordx2 v[112:113], v[98:99], off offset:2560
	v_max_i32_e32 v98, s10, v211
	v_min_u32_e32 v218, s9, v98
	v_sub_u32_e32 v98, v218, v59
	v_mad_i64_i32 v[98:99], s[16:17], v98, s65, v[78:79]
	v_lshl_add_u64 v[98:99], v[98:99], 0, v[34:35]
	v_pk_mul_f32 v[132:133], v[14:15], v[86:87]
	global_load_dwordx2 v[110:111], v[98:99], off offset:512
	global_load_dwordx2 v[108:109], v[98:99], off offset:1024
	global_load_dwordx2 v[106:107], v[98:99], off offset:2048
	global_load_dwordx2 v[104:105], v[98:99], off offset:2560
	v_max_i32_e32 v98, s10, v209
	v_pk_fma_f32 v[94:95], v[10:11], v[94:95], v[132:133]
	v_min_u32_e32 v210, s9, v98
	v_lshlrev_b32_e32 v130, 16, v92
	v_and_b32_e32 v131, 0xffff0000, v92
	v_pk_fma_f32 v[94:95], v[36:37], v[70:71], v[94:95]
	v_sub_u32_e32 v59, v210, v59
	v_pk_mul_f32 v[134:135], v[16:17], v[84:85]
	v_pk_mul_f32 v[94:95], v[94:95], v[130:131]
	v_mad_i64_i32 v[78:79], s[10:11], v59, s65, v[78:79]
	v_pk_fma_f32 v[96:97], v[12:13], v[96:97], v[134:135]
	v_lshlrev_b32_e32 v92, 16, v93
	v_and_b32_e32 v93, 0xffff0000, v93
	v_pk_fma_f32 v[96:97], v[38:39], v[68:69], v[96:97]
	v_pk_mul_f32 v[92:93], v[96:97], v[92:93]
	v_cvt_pk_bf16_f32 v94, v94, v95
	s_mov_b32 s9, 0x2dc00000
	v_add_co_u32_e32 v96, vcc, s9, v56
	s_nop 1
	v_addc_co_u32_e32 v97, vcc, 0, v57, vcc
	s_movk_i32 s9, 0x2000
	v_lshl_add_u64 v[78:79], v[78:79], 0, v[34:35]
	v_cvt_pk_bf16_f32 v95, v92, v93
	v_add_co_u32_e32 v92, vcc, s9, v52
	global_load_dwordx2 v[102:103], v[78:79], off offset:512
	global_load_dwordx2 v[100:101], v[78:79], off offset:1024
	global_load_dwordx2 v[98:99], v[78:79], off offset:2048
	s_nop 0
	global_load_dwordx2 v[78:79], v[78:79], off offset:2560
	v_addc_co_u32_e32 v93, vcc, 0, v53, vcc
	global_store_dwordx2 v[96:97], v[94:95], off offset:512
	global_load_dwordx2 v[130:131], v[92:93], off offset:512
	v_add_co_u32_e32 v232, vcc, 0x3000, v52
	s_nop 1
	v_addc_co_u32_e32 v233, vcc, 0, v53, vcc
	global_load_dwordx2 v[220:221], v[232:233], off offset:3584
	v_add_co_u32_e32 v232, vcc, 0x5000, v52
	s_nop 1
	v_addc_co_u32_e32 v233, vcc, 0, v53, vcc
	global_load_dwordx2 v[222:223], v[232:233], off offset:2560
	v_add_co_u32_e32 v232, vcc, 0x7000, v52
	s_nop 1
	v_addc_co_u32_e32 v233, vcc, 0, v53, vcc
	global_load_dwordx2 v[224:225], v[232:233], off offset:1536
	v_add_co_u32_e32 v232, vcc, 0x9000, v52
	s_nop 1
	v_addc_co_u32_e32 v233, vcc, 0, v53, vcc
	global_load_dwordx2 v[226:227], v[232:233], off offset:512
	v_add_co_u32_e32 v232, vcc, 0xa000, v52
	s_nop 1
	v_addc_co_u32_e32 v233, vcc, 0, v53, vcc
	global_load_dwordx2 v[228:229], v[232:233], off offset:3584
	v_add_co_u32_e32 v232, vcc, 0xc000, v52
	s_nop 1
	v_addc_co_u32_e32 v233, vcc, 0, v53, vcc
	global_load_dwordx2 v[230:231], v[232:233], off offset:2560
	v_cmp_eq_u32_e32 vcc, v61, v73
	s_waitcnt vmcnt(27)
	v_lshlrev_b32_e32 v92, 16, v90
	v_and_b32_e32 v93, 0xffff0000, v90
	v_cndmask_b32_e64 v136, 0, 1.0, vcc
	v_lshlrev_b32_e32 v90, 16, v91
	v_and_b32_e32 v91, 0xffff0000, v91
	v_pk_mul_f32 v[90:91], v[136:137], v[90:91] op_sel_hi:[0,1]
	s_waitcnt vmcnt(26)
	v_lshlrev_b32_e32 v132, 16, v88
	v_and_b32_e32 v133, 0xffff0000, v88
	v_lshlrev_b32_e32 v88, 16, v89
	v_and_b32_e32 v89, 0xffff0000, v89
	v_pk_mul_f32 v[94:95], v[136:137], v[92:93] op_sel_hi:[0,1]
	v_pk_mul_f32 v[92:93], v[90:91], v[88:89]
	v_pk_mul_f32 v[94:95], v[94:95], v[132:133]
	v_pk_mul_f32 v[132:133], v[16:17], v[68:69]
	s_movk_i32 s9, 0x3000
	v_pk_fma_f32 v[84:85], v[12:13], v[84:85], v[132:133]
	s_waitcnt vmcnt(0)
	v_lshlrev_b32_e32 v88, 16, v130
	v_and_b32_e32 v89, 0xffff0000, v130
	v_lshlrev_b32_e32 v90, 16, v131
	v_and_b32_e32 v91, 0xffff0000, v131
	v_pk_mul_f32 v[130:131], v[14:15], v[70:71]
	v_pk_fma_f32 v[84:85], v[38:39], v[92:93], v[84:85]
	v_pk_fma_f32 v[86:87], v[10:11], v[86:87], v[130:131]
	v_pk_mul_f32 v[84:85], v[84:85], v[90:91]
	v_pk_fma_f32 v[86:87], v[36:37], v[94:95], v[86:87]
	s_nop 0
	v_pk_mul_f32 v[86:87], v[86:87], v[88:89]
	s_nop 0
	v_cvt_pk_bf16_f32 v86, v86, v87
	v_cvt_pk_bf16_f32 v59, v84, v84
	v_bfe_u32 v61, v85, 16, 1
	v_lshrrev_b32_e32 v59, 16, v59
	v_add3_u32 v61, v85, v61, s81
	v_and_or_b32 v87, v61, s80, v59
	global_store_dwordx2 v[96:97], v[86:87], off offset:2560
	s_nop 0
	v_lshlrev_b32_e32 v86, 16, v80
	v_and_b32_e32 v87, 0xffff0000, v80
	v_lshlrev_b32_e32 v80, 16, v81
	v_and_b32_e32 v81, 0xffff0000, v81
	v_pk_mul_f32 v[176:177], v[72:73], v[80:81] op_sel_hi:[0,1]
	v_lshlrev_b32_e32 v80, 16, v76
	v_and_b32_e32 v81, 0xffff0000, v76
	v_lshlrev_b32_e32 v76, 16, v77
	v_and_b32_e32 v77, 0xffff0000, v77
	v_pk_mul_f32 v[178:179], v[72:73], v[86:87] op_sel_hi:[0,1]
	v_pk_mul_f32 v[152:153], v[72:73], v[76:77] op_sel_hi:[0,1]
	v_pk_mul_f32 v[154:155], v[72:73], v[80:81] op_sel_hi:[0,1]
	v_lshlrev_b32_e32 v72, 16, v74
	v_and_b32_e32 v73, 0xffff0000, v74
	v_lshlrev_b32_e32 v74, 16, v75
	v_and_b32_e32 v75, 0xffff0000, v75
	v_pk_mul_f32 v[148:149], v[60:61], v[72:73] op_sel_hi:[0,1]
	v_lshlrev_b32_e32 v72, 16, v66
	v_and_b32_e32 v73, 0xffff0000, v66
	v_lshlrev_b32_e32 v66, 16, v67
	v_and_b32_e32 v67, 0xffff0000, v67
	v_pk_mul_f32 v[150:151], v[60:61], v[74:75] op_sel_hi:[0,1]
	v_pk_mul_f32 v[144:145], v[60:61], v[72:73] op_sel_hi:[0,1]
	v_pk_mul_f32 v[146:147], v[60:61], v[66:67] op_sel_hi:[0,1]
	v_lshlrev_b32_e32 v60, 16, v64
	v_and_b32_e32 v61, 0xffff0000, v64
	v_lshlrev_b32_e32 v64, 16, v65
	v_and_b32_e32 v65, 0xffff0000, v65
	v_pk_mul_f32 v[138:139], v[58:59], v[60:61] op_sel_hi:[0,1]
	v_lshlrev_b32_e32 v60, 16, v62
	v_and_b32_e32 v61, 0xffff0000, v62
	v_lshlrev_b32_e32 v62, 16, v63
	v_and_b32_e32 v63, 0xffff0000, v63
; #define LAS __attribute__((address_space(3)))
; __device__ __forceinline__ unsigned pk2(float lo, float hi) { return f2bf(lo) | (f2bf(hi) << 16); }
; __device__ __forceinline__ f32x4 bf4(u32x2 v) { return (f32x4){lo_bf(v.x), hi_bf(v.x), lo_bf(v.y), hi_bf(v.y)}; }
; __device__ __forceinline__ void ph_prep_conv(CArgs& a, int l, LAS unsigned char* lds, int bid, int nblk) {
;     ...
; #pragma unroll
;         for (int tt = 0; tt < 8; ++tt) {
;             const f32x4 xx = wx[0] * x1[tt] + wx[1] * x1[tt + 1] + wx[2] * x1[tt + 2] + bx, v2 = wv[0] * vv[tt] + wv[1] * vv[tt + 1] + wv[2] * vv[tt + 2] + bv, z = xx * v2;
;             u32x2 zo; zo.x = pk2(z[0], z[1]); zo.y = pk2(z[2], z[3]); *(LAS u32x2*)(zt + (tg * 8 + tt) * 264 + c4) = zo;
;             const f32x4 bg = bf4(*(const u32x2*)(pb + (size_t)tt * D_INP + SC0 + c4));
;             const f32x4 y = bg * (ws3[0] * mm[tt] + ws3[1] * mm[tt + 1] + ws3[2] * mm[tt + 2]);
;             u32x2 yo; yo.x = pk2(y[0], y[1]); yo.y = pk2(y[2], y[3]); *(u32x2*)(YMIX + (size_t)(c.row0 + tg * 8 + tt) * D + 256 + c4) = yo;
	v_pk_mul_f32 v[140:141], v[58:59], v[64:65] op_sel_hi:[0,1]
	v_pk_mul_f32 v[130:131], v[58:59], v[60:61] op_sel_hi:[0,1]
	v_pk_mul_f32 v[132:133], v[58:59], v[62:63] op_sel_hi:[0,1]
	v_lshlrev_b32_e32 v58, 16, v82
	v_and_b32_e32 v59, 0xffff0000, v82
	v_cmp_eq_u32_e32 vcc, v137, v142
	v_pk_mul_f32 v[72:73], v[136:137], v[58:59] op_sel_hi:[0,1]
	v_lshlrev_b32_e32 v62, 16, v124
	v_cndmask_b32_e64 v58, 0, 1.0, vcc
	v_and_b32_e32 v63, 0xffff0000, v124
	v_pk_mul_f32 v[62:63], v[58:59], v[62:63] op_sel_hi:[0,1]
	v_lshlrev_b32_e32 v66, 16, v122
	v_and_b32_e32 v67, 0xffff0000, v122
	v_pk_mul_f32 v[182:183], v[62:63], v[66:67]
	v_pk_mul_f32 v[66:67], v[14:15], v[94:95]
	v_lshlrev_b32_e32 v64, 16, v125
	v_and_b32_e32 v65, 0xffff0000, v125
	v_pk_fma_f32 v[66:67], v[10:11], v[70:71], v[66:67]
	v_pk_mul_f32 v[64:65], v[58:59], v[64:65] op_sel_hi:[0,1]
	v_lshlrev_b32_e32 v74, 16, v123
	v_and_b32_e32 v75, 0xffff0000, v123
	v_pk_fma_f32 v[66:67], v[36:37], v[182:183], v[66:67]
	v_pk_mul_f32 v[180:181], v[64:65], v[74:75]
	v_pk_mul_f32 v[74:75], v[16:17], v[92:93]
	s_mov_b32 s9, 0x2dc01000
	v_pk_fma_f32 v[68:69], v[12:13], v[68:69], v[74:75]
	v_lshlrev_b32_e32 v60, 16, v83
	v_pk_fma_f32 v[68:69], v[38:39], v[180:181], v[68:69]
	v_and_b32_e32 v61, 0xffff0000, v83
	v_pk_mul_f32 v[142:143], v[136:137], v[60:61] op_sel_hi:[0,1]
	v_lshlrev_b32_e32 v60, 16, v54
	v_and_b32_e32 v61, 0xffff0000, v54
	v_lshlrev_b32_e32 v54, 16, v55
	v_and_b32_e32 v55, 0xffff0000, v55
	v_pk_mul_f32 v[134:135], v[136:137], v[60:61] op_sel_hi:[0,1]
	v_pk_mul_f32 v[136:137], v[136:137], v[54:55] op_sel_hi:[0,1]
	v_lshlrev_b32_e32 v54, 16, v120
	v_and_b32_e32 v55, 0xffff0000, v120
	v_lshlrev_b32_e32 v60, 16, v121
	v_and_b32_e32 v61, 0xffff0000, v121
	v_lshlrev_b32_e32 v74, 16, v129
	v_and_b32_e32 v75, 0xffff0000, v129
	v_lshlrev_b32_e32 v76, 16, v127
	v_and_b32_e32 v77, 0xffff0000, v127
	v_pk_mul_f32 v[82:83], v[16:17], v[180:181]
	v_lshlrev_b32_e32 v96, 16, v109
	v_lshlrev_b32_e32 v62, 16, v220
	v_and_b32_e32 v63, 0xffff0000, v220
	v_pk_mul_f32 v[62:63], v[66:67], v[62:63]
	v_lshlrev_b32_e32 v64, 16, v221
	v_and_b32_e32 v65, 0xffff0000, v221
	v_pk_mul_f32 v[64:65], v[68:69], v[64:65]
	v_cvt_pk_bf16_f32 v62, v62, v63
	v_cvt_pk_bf16_f32 v59, v64, v64
	v_lshrrev_b32_e32 v59, 16, v59
	v_cvt_pk_bf16_f32 v63, v65, v65
	v_add_co_u32_e32 v68, vcc, s9, v56
	v_and_or_b32 v63, v63, s80, v59
	s_nop 0
	v_addc_co_u32_e32 v69, vcc, 0, v57, vcc
	s_movk_i32 s9, 0x5000
	global_store_dwordx2 v[68:69], v[62:63], off offset:512
	v_pk_mul_f32 v[122:123], v[58:59], v[54:55] op_sel_hi:[0,1]
	s_nop 0
	v_pk_mul_f32 v[124:125], v[58:59], v[60:61] op_sel_hi:[0,1]
	v_lshlrev_b32_e32 v54, 16, v118
	v_and_b32_e32 v55, 0xffff0000, v118
	v_lshlrev_b32_e32 v60, 16, v119
	v_and_b32_e32 v61, 0xffff0000, v119
	v_cmp_eq_u32_e32 vcc, v212, v213
	v_pk_mul_f32 v[118:119], v[58:59], v[54:55] op_sel_hi:[0,1]
	v_pk_mul_f32 v[120:121], v[58:59], v[60:61] op_sel_hi:[0,1]
	v_cndmask_b32_e64 v54, 0, 1.0, vcc
	v_lshlrev_b32_e32 v58, 16, v174
	v_and_b32_e32 v59, 0xffff0000, v174
	v_lshlrev_b32_e32 v60, 16, v175
	v_and_b32_e32 v61, 0xffff0000, v175
	v_pk_mul_f32 v[88:89], v[54:55], v[58:59] op_sel_hi:[0,1]
	v_pk_mul_f32 v[90:91], v[54:55], v[60:61] op_sel_hi:[0,1]
	v_lshlrev_b32_e32 v58, 16, v172
	v_and_b32_e32 v59, 0xffff0000, v172
	v_lshlrev_b32_e32 v60, 16, v173
	v_and_b32_e32 v61, 0xffff0000, v173
	v_pk_mul_f32 v[84:85], v[54:55], v[58:59] op_sel_hi:[0,1]
	v_pk_mul_f32 v[86:87], v[54:55], v[60:61] op_sel_hi:[0,1]
	v_lshlrev_b32_e32 v58, 16, v170
	v_and_b32_e32 v59, 0xffff0000, v170
	v_lshlrev_b32_e32 v60, 16, v171
	v_and_b32_e32 v61, 0xffff0000, v171
	v_pk_mul_f32 v[58:59], v[54:55], v[58:59] op_sel_hi:[0,1]
	v_pk_mul_f32 v[54:55], v[54:55], v[60:61] op_sel_hi:[0,1]
	v_lshlrev_b32_e32 v60, 16, v162
	v_and_b32_e32 v61, 0xffff0000, v162
	v_lshlrev_b32_e32 v62, 16, v163
	v_and_b32_e32 v63, 0xffff0000, v163
	v_cmp_eq_u32_e32 vcc, v214, v215
	v_pk_mul_f32 v[162:163], v[54:55], v[62:63]
	v_pk_mul_f32 v[170:171], v[58:59], v[60:61]
	v_cndmask_b32_e64 v54, 0, 1.0, vcc
	v_lshlrev_b32_e32 v58, 16, v160
	v_and_b32_e32 v59, 0xffff0000, v160
	v_lshlrev_b32_e32 v60, 16, v161
	v_and_b32_e32 v61, 0xffff0000, v161
	v_pk_mul_f32 v[64:65], v[54:55], v[58:59] op_sel_hi:[0,1]
	v_lshlrev_b32_e32 v58, 16, v158
	v_and_b32_e32 v59, 0xffff0000, v158
	v_pk_mul_f32 v[66:67], v[54:55], v[60:61] op_sel_hi:[0,1]
	v_lshlrev_b32_e32 v62, 16, v159
	v_and_b32_e32 v63, 0xffff0000, v159
	v_pk_mul_f32 v[60:61], v[54:55], v[58:59] op_sel_hi:[0,1]
	v_lshlrev_b32_e32 v58, 16, v128
	v_and_b32_e32 v59, 0xffff0000, v128
	v_pk_mul_f32 v[62:63], v[54:55], v[62:63] op_sel_hi:[0,1]
	v_pk_mul_f32 v[58:59], v[54:55], v[58:59] op_sel_hi:[0,1]
	v_pk_mul_f32 v[54:55], v[54:55], v[74:75] op_sel_hi:[0,1]
	v_lshlrev_b32_e32 v74, 16, v126
	v_and_b32_e32 v75, 0xffff0000, v126
	v_pk_mul_f32 v[126:127], v[54:55], v[76:77]
	v_pk_mul_f32 v[76:77], v[14:15], v[182:183]
	v_pk_mul_f32 v[128:129], v[58:59], v[74:75]
	v_pk_fma_f32 v[76:77], v[10:11], v[94:95], v[76:77]
	v_pk_fma_f32 v[82:83], v[12:13], v[92:93], v[82:83]
	v_pk_fma_f32 v[76:77], v[36:37], v[170:171], v[76:77]
	v_pk_fma_f32 v[82:83], v[38:39], v[162:163], v[82:83]
	v_cmp_eq_u32_e32 vcc, v216, v217
	s_movk_i32 s9, 0x7000
	v_lshlrev_b32_e32 v54, 16, v156
	v_cndmask_b32_e64 v80, 0, 1.0, vcc
	v_and_b32_e32 v55, 0xffff0000, v156
	v_lshlrev_b32_e32 v58, 16, v157
	v_and_b32_e32 v59, 0xffff0000, v157
	v_pk_mul_f32 v[158:159], v[14:15], v[170:171]
	v_pk_mul_f32 v[160:161], v[16:17], v[162:163]
	v_pk_fma_f32 v[158:159], v[10:11], v[182:183], v[158:159]
	v_pk_fma_f32 v[160:161], v[12:13], v[180:181], v[160:161]
; #define LAS __attribute__((address_space(3)))
; __device__ __forceinline__ unsigned pk2(float lo, float hi) { return f2bf(lo) | (f2bf(hi) << 16); }
; __device__ __forceinline__ f32x4 bf4(u32x2 v) { return (f32x4){lo_bf(v.x), hi_bf(v.x), lo_bf(v.y), hi_bf(v.y)}; }
; __device__ __forceinline__ void ph_prep_conv(CArgs& a, int l, LAS unsigned char* lds, int bid, int nblk) {
;     ...
; #pragma unroll
;         for (int tt = 0; tt < 8; ++tt) {
;             const f32x4 xx = wx[0] * x1[tt] + wx[1] * x1[tt + 1] + wx[2] * x1[tt + 2] + bx, v2 = wv[0] * vv[tt] + wv[1] * vv[tt + 1] + wv[2] * vv[tt + 2] + bv, z = xx * v2;
;             u32x2 zo; zo.x = pk2(z[0], z[1]); zo.y = pk2(z[2], z[3]); *(LAS u32x2*)(zt + (tg * 8 + tt) * 264 + c4) = zo;
;             const f32x4 bg = bf4(*(const u32x2*)(pb + (size_t)tt * D_INP + SC0 + c4));
;             const f32x4 y = bg * (ws3[0] * mm[tt] + ws3[1] * mm[tt + 1] + ws3[2] * mm[tt + 2]);
;             u32x2 yo; yo.x = pk2(y[0], y[1]); yo.y = pk2(y[2], y[3]); *(u32x2*)(YMIX + (size_t)(c.row0 + tg * 8 + tt) * D + 256 + c4) = yo;
	v_pk_fma_f32 v[158:159], v[36:37], v[128:129], v[158:159]
	v_pk_fma_f32 v[160:161], v[38:39], v[126:127], v[160:161]
	v_pk_mul_f32 v[54:55], v[80:81], v[54:55] op_sel_hi:[0,1]
	v_pk_mul_f32 v[58:59], v[80:81], v[58:59] op_sel_hi:[0,1]
	v_lshlrev_b32_e32 v92, 16, v111
	v_and_b32_e32 v93, 0xffff0000, v111
	v_and_b32_e32 v97, 0xffff0000, v109
	v_lshlrev_b32_e32 v74, 16, v222
	v_and_b32_e32 v75, 0xffff0000, v222
	v_pk_mul_f32 v[74:75], v[76:77], v[74:75]
	v_lshlrev_b32_e32 v70, 16, v223
	v_and_b32_e32 v71, 0xffff0000, v223
	v_pk_mul_f32 v[70:71], v[82:83], v[70:71]
	v_cvt_pk_bf16_f32 v74, v74, v75
	v_cvt_pk_bf16_f32 v75, v70, v71
	global_store_dwordx2 v[68:69], v[74:75], off offset:2560
	v_lshlrev_b32_e32 v70, 16, v117
	s_nop 0
	v_lshlrev_b32_e32 v68, 16, v116
	v_and_b32_e32 v69, 0xffff0000, v116
	v_and_b32_e32 v71, 0xffff0000, v117
	v_pk_mul_f32 v[74:75], v[80:81], v[68:69] op_sel_hi:[0,1]
	v_pk_mul_f32 v[76:77], v[80:81], v[70:71] op_sel_hi:[0,1]
	v_lshlrev_b32_e32 v68, 16, v114
	v_and_b32_e32 v69, 0xffff0000, v114
	v_lshlrev_b32_e32 v70, 16, v115
	v_and_b32_e32 v71, 0xffff0000, v115
	v_pk_mul_f32 v[82:83], v[80:81], v[68:69] op_sel_hi:[0,1]
	v_pk_mul_f32 v[68:69], v[80:81], v[70:71] op_sel_hi:[0,1]
	v_lshlrev_b32_e32 v70, 16, v112
	v_and_b32_e32 v71, 0xffff0000, v112
	v_lshlrev_b32_e32 v80, 16, v113
	v_and_b32_e32 v81, 0xffff0000, v113
	v_cmp_eq_u32_e32 vcc, v211, v218
	v_pk_mul_f32 v[68:69], v[68:69], v[80:81]
	v_pk_mul_f32 v[70:71], v[82:83], v[70:71]
	v_cndmask_b32_e64 v80, 0, 1.0, vcc
	v_lshlrev_b32_e32 v82, 16, v110
	v_and_b32_e32 v83, 0xffff0000, v110
	v_cmp_eq_u32_e32 vcc, v209, v210
	s_mov_b32 s9, 0x2dc02000
	v_pk_mul_f32 v[94:95], v[80:81], v[82:83] op_sel_hi:[0,1]
	v_lshlrev_b32_e32 v82, 16, v108
	v_and_b32_e32 v83, 0xffff0000, v108
	v_cndmask_b32_e64 v108, 0, 1.0, vcc
	v_pk_mul_f32 v[110:111], v[80:81], v[92:93] op_sel_hi:[0,1]
	v_pk_mul_f32 v[92:93], v[80:81], v[82:83] op_sel_hi:[0,1]
	v_lshlrev_b32_e32 v82, 16, v106
	v_and_b32_e32 v83, 0xffff0000, v106
	v_lshlrev_b32_e32 v106, 16, v107
	v_and_b32_e32 v107, 0xffff0000, v107
	v_pk_mul_f32 v[96:97], v[80:81], v[96:97] op_sel_hi:[0,1]
	v_pk_mul_f32 v[82:83], v[80:81], v[82:83] op_sel_hi:[0,1]
	v_pk_mul_f32 v[80:81], v[80:81], v[106:107] op_sel_hi:[0,1]
	v_lshlrev_b32_e32 v106, 16, v104
	v_and_b32_e32 v107, 0xffff0000, v104
	v_lshlrev_b32_e32 v104, 16, v105
	v_and_b32_e32 v105, 0xffff0000, v105
	v_pk_mul_f32 v[80:81], v[80:81], v[104:105]
	v_lshlrev_b32_e32 v104, 16, v102
	v_and_b32_e32 v105, 0xffff0000, v102
	v_pk_mul_f32 v[82:83], v[82:83], v[106:107]
	v_lshlrev_b32_e32 v106, 16, v103
	v_and_b32_e32 v107, 0xffff0000, v103
	v_pk_mul_f32 v[102:103], v[108:109], v[104:105] op_sel_hi:[0,1]
	v_lshlrev_b32_e32 v104, 16, v100
	v_and_b32_e32 v105, 0xffff0000, v100
	v_lshlrev_b32_e32 v112, 16, v101
	v_and_b32_e32 v113, 0xffff0000, v101
	v_pk_mul_f32 v[100:101], v[108:109], v[104:105] op_sel_hi:[0,1]
	v_pk_mul_f32 v[104:105], v[108:109], v[112:113] op_sel_hi:[0,1]
	v_lshlrev_b32_e32 v112, 16, v98
	v_and_b32_e32 v113, 0xffff0000, v98
	v_lshlrev_b32_e32 v98, 16, v99
	v_and_b32_e32 v99, 0xffff0000, v99
	v_pk_mul_f32 v[106:107], v[108:109], v[106:107] op_sel_hi:[0,1]
	v_pk_mul_f32 v[112:113], v[108:109], v[112:113] op_sel_hi:[0,1]
	v_pk_mul_f32 v[98:99], v[108:109], v[98:99] op_sel_hi:[0,1]
	v_lshlrev_b32_e32 v108, 16, v78
	v_and_b32_e32 v109, 0xffff0000, v78
	v_lshlrev_b32_e32 v78, 16, v79
	v_and_b32_e32 v79, 0xffff0000, v79
	v_pk_mul_f32 v[78:79], v[98:99], v[78:79]
	v_pk_mul_f32 v[98:99], v[112:113], v[108:109]
	v_pk_mul_f32 v[112:113], v[26:27], v[148:149]
	v_pk_mul_f32 v[108:109], v[28:29], v[150:151]
	v_pk_fma_f32 v[112:113], v[2:3], v[178:179], v[112:113]
	v_pk_mul_f32 v[114:115], v[20:21], v[146:147]
	v_pk_fma_f32 v[108:109], v[4:5], v[176:177], v[108:109]
	v_pk_fma_f32 v[112:113], v[22:23], v[138:139], v[112:113]
	v_pk_fma_f32 v[114:115], v[8:9], v[152:153], v[114:115]
	v_pk_fma_f32 v[108:109], v[24:25], v[140:141], v[108:109]
	v_pk_add_f32 v[112:113], v[40:41], v[112:113]
	v_pk_fma_f32 v[114:115], v[32:33], v[132:133], v[114:115]
	v_pk_add_f32 v[108:109], v[42:43], v[108:109]
	v_pk_add_f32 v[114:115], v[46:47], v[114:115]
	v_lshlrev_b32_e32 v116, 16, v224
	v_and_b32_e32 v117, 0xffff0000, v224
	v_pk_mul_f32 v[116:117], v[158:159], v[116:117]
	v_lshlrev_b32_e32 v156, 16, v225
	v_and_b32_e32 v157, 0xffff0000, v225
	v_pk_mul_f32 v[156:157], v[160:161], v[156:157]
	v_cvt_pk_bf16_f32 v116, v116, v117
	v_cvt_pk_bf16_f32 v117, v156, v157
	v_add_co_u32_e32 v156, vcc, s9, v56
	s_mov_b32 s9, 0x9000
	s_nop 0
	v_addc_co_u32_e32 v157, vcc, 0, v57, vcc
	global_store_dwordx2 v[156:157], v[116:117], off offset:512
	v_pk_mul_f32 v[158:159], v[18:19], v[144:145]
	s_nop 0
	v_pk_fma_f32 v[154:155], v[6:7], v[154:155], v[158:159]
	v_pk_mul_f32 v[108:109], v[108:109], v[114:115]
	v_pk_fma_f32 v[152:153], v[30:31], v[130:131], v[154:155]
	s_mov_b32 s9, 0xa000
	v_pk_add_f32 v[152:153], v[44:45], v[152:153]
	s_nop 0
	v_pk_mul_f32 v[112:113], v[112:113], v[152:153]
	s_nop 0
	v_cvt_pk_bf16_f32 v112, v112, v113
	v_cvt_pk_bf16_f32 v113, v108, v109
	v_pk_mul_f32 v[108:109], v[28:29], v[140:141]
	v_pk_mul_f32 v[114:115], v[26:27], v[138:139]
	v_pk_fma_f32 v[108:109], v[4:5], v[150:151], v[108:109]
	v_pk_mul_f32 v[150:151], v[18:19], v[130:131]
	v_pk_fma_f32 v[114:115], v[2:3], v[148:149], v[114:115]
	v_pk_fma_f32 v[144:145], v[6:7], v[144:145], v[150:151]
	v_pk_fma_f32 v[114:115], v[22:23], v[72:73], v[114:115]
	v_pk_fma_f32 v[144:145], v[30:31], v[134:135], v[144:145]
	v_pk_add_f32 v[114:115], v[40:41], v[114:115]
	v_pk_mul_f32 v[148:149], v[20:21], v[132:133]
	v_pk_add_f32 v[144:145], v[44:45], v[144:145]
; #define LAS __attribute__((address_space(3)))
; __device__ __forceinline__ unsigned pk2(float lo, float hi) { return f2bf(lo) | (f2bf(hi) << 16); }
; __device__ __forceinline__ f32x4 bf4(u32x2 v) { return (f32x4){lo_bf(v.x), hi_bf(v.x), lo_bf(v.y), hi_bf(v.y)}; }
; __device__ __forceinline__ void ph_prep_conv(CArgs& a, int l, LAS unsigned char* lds, int bid, int nblk) {
;     ...
; #pragma unroll
;         for (int tt = 0; tt < 8; ++tt) {
;             const f32x4 xx = wx[0] * x1[tt] + wx[1] * x1[tt + 1] + wx[2] * x1[tt + 2] + bx, v2 = wv[0] * vv[tt] + wv[1] * vv[tt + 1] + wv[2] * vv[tt + 2] + bv, z = xx * v2;
;             u32x2 zo; zo.x = pk2(z[0], z[1]); zo.y = pk2(z[2], z[3]); *(LAS u32x2*)(zt + (tg * 8 + tt) * 264 + c4) = zo;
;             const f32x4 bg = bf4(*(const u32x2*)(pb + (size_t)tt * D_INP + SC0 + c4));
;             const f32x4 y = bg * (ws3[0] * mm[tt] + ws3[1] * mm[tt + 1] + ws3[2] * mm[tt + 2]);
;             u32x2 yo; yo.x = pk2(y[0], y[1]); yo.y = pk2(y[2], y[3]); *(u32x2*)(YMIX + (size_t)(c.row0 + tg * 8 + tt) * D + 256 + c4) = yo;
	v_pk_fma_f32 v[146:147], v[8:9], v[146:147], v[148:149]
	v_pk_mul_f32 v[114:115], v[114:115], v[144:145]
	v_pk_fma_f32 v[108:109], v[24:25], v[142:143], v[108:109]
	v_pk_fma_f32 v[146:147], v[32:33], v[136:137], v[146:147]
	v_pk_add_f32 v[108:109], v[42:43], v[108:109]
	v_pk_add_f32 v[146:147], v[46:47], v[146:147]
	v_cvt_pk_bf16_f32 v114, v114, v114
	v_pk_mul_f32 v[108:109], v[108:109], v[146:147]
	v_lshrrev_b32_e32 v114, 16, v114
	v_cvt_pk_bf16_f32 v115, v115, v115
	v_and_or_b32 v114, v115, s80, v114
	v_cvt_pk_bf16_f32 v115, v108, v109
	ds_write2_b64 v185, v[112:113], v[114:115] offset1:66
	v_pk_mul_f32 v[112:113], v[26:27], v[72:73]
	v_pk_mul_f32 v[108:109], v[28:29], v[142:143]
	v_pk_fma_f32 v[112:113], v[2:3], v[138:139], v[112:113]
	v_pk_mul_f32 v[138:139], v[18:19], v[134:135]
	v_pk_mul_f32 v[114:115], v[20:21], v[136:137]
	v_pk_fma_f32 v[130:131], v[6:7], v[130:131], v[138:139]
	v_pk_fma_f32 v[108:109], v[4:5], v[140:141], v[108:109]
	v_pk_fma_f32 v[112:113], v[22:23], v[122:123], v[112:113]
	v_pk_fma_f32 v[114:115], v[8:9], v[132:133], v[114:115]
	v_pk_fma_f32 v[130:131], v[30:31], v[118:119], v[130:131]
	v_pk_fma_f32 v[108:109], v[24:25], v[124:125], v[108:109]
	v_pk_add_f32 v[112:113], v[40:41], v[112:113]
	v_pk_fma_f32 v[114:115], v[32:33], v[120:121], v[114:115]
	v_pk_add_f32 v[130:131], v[44:45], v[130:131]
	v_pk_add_f32 v[108:109], v[42:43], v[108:109]
	v_pk_add_f32 v[114:115], v[46:47], v[114:115]
	v_pk_mul_f32 v[112:113], v[112:113], v[130:131]
	v_pk_mul_f32 v[108:109], v[108:109], v[114:115]
	v_pk_mul_f32 v[130:131], v[14:15], v[128:129]
	v_pk_fma_f32 v[130:131], v[10:11], v[170:171], v[130:131]
	v_pk_fma_f32 v[130:131], v[36:37], v[70:71], v[130:131]
	v_cvt_pk_bf16_f32 v112, v112, v113
	v_lshlrev_b32_e32 v114, 16, v226
	v_and_b32_e32 v115, 0xffff0000, v226
	v_pk_mul_f32 v[132:133], v[16:17], v[126:127]
	v_pk_mul_f32 v[114:115], v[130:131], v[114:115]
	v_pk_fma_f32 v[132:133], v[12:13], v[162:163], v[132:133]
	v_lshlrev_b32_e32 v116, 16, v227
	v_and_b32_e32 v117, 0xffff0000, v227
	v_pk_fma_f32 v[132:133], v[38:39], v[68:69], v[132:133]
	v_pk_mul_f32 v[116:117], v[132:133], v[116:117]
	v_cvt_pk_bf16_f32 v114, v114, v115
	v_cvt_pk_bf16_f32 v115, v116, v117
	global_store_dwordx2 v[156:157], v[114:115], off offset:2560
	s_nop 0
	v_pk_mul_f32 v[116:117], v[26:27], v[122:123]
	v_pk_mul_f32 v[130:131], v[18:19], v[118:119]
	v_cvt_pk_bf16_f32 v113, v108, v109
	v_pk_mul_f32 v[108:109], v[28:29], v[124:125]
	v_pk_fma_f32 v[72:73], v[2:3], v[72:73], v[116:117]
	v_pk_mul_f32 v[116:117], v[20:21], v[120:121]
	v_pk_fma_f32 v[130:131], v[6:7], v[134:135], v[130:131]
	v_pk_fma_f32 v[108:109], v[4:5], v[142:143], v[108:109]
	v_pk_fma_f32 v[72:73], v[22:23], v[88:89], v[72:73]
	v_pk_fma_f32 v[116:117], v[8:9], v[136:137], v[116:117]
	v_pk_fma_f32 v[130:131], v[30:31], v[84:85], v[130:131]
	v_pk_fma_f32 v[108:109], v[24:25], v[90:91], v[108:109]
	v_pk_add_f32 v[72:73], v[40:41], v[72:73]
	v_pk_fma_f32 v[116:117], v[32:33], v[86:87], v[116:117]
	v_pk_add_f32 v[130:131], v[44:45], v[130:131]
	v_pk_add_f32 v[108:109], v[42:43], v[108:109]
	v_pk_add_f32 v[116:117], v[46:47], v[116:117]
	v_pk_mul_f32 v[72:73], v[72:73], v[130:131]
	v_pk_mul_f32 v[108:109], v[108:109], v[116:117]
	v_cvt_pk_bf16_f32 v72, v72, v73
	v_cvt_pk_bf16_f32 v73, v108, v109
	v_pk_mul_f32 v[108:109], v[26:27], v[88:89]
	v_pk_mul_f32 v[116:117], v[18:19], v[84:85]
	ds_write2_b64 v185, v[112:113], v[72:73] offset0:132 offset1:198
	v_pk_mul_f32 v[72:73], v[28:29], v[90:91]
	v_pk_fma_f32 v[108:109], v[2:3], v[122:123], v[108:109]
	v_pk_mul_f32 v[112:113], v[20:21], v[86:87]
	v_pk_fma_f32 v[116:117], v[6:7], v[118:119], v[116:117]
	v_pk_fma_f32 v[72:73], v[4:5], v[124:125], v[72:73]
	v_pk_fma_f32 v[108:109], v[22:23], v[64:65], v[108:109]
	v_pk_fma_f32 v[112:113], v[8:9], v[120:121], v[112:113]
	v_pk_fma_f32 v[116:117], v[30:31], v[60:61], v[116:117]
	v_pk_fma_f32 v[72:73], v[24:25], v[66:67], v[72:73]
	v_pk_add_f32 v[108:109], v[40:41], v[108:109]
	v_pk_fma_f32 v[112:113], v[32:33], v[62:63], v[112:113]
	v_pk_add_f32 v[116:117], v[44:45], v[116:117]
	v_pk_add_f32 v[72:73], v[42:43], v[72:73]
	v_pk_add_f32 v[112:113], v[46:47], v[112:113]
	v_pk_mul_f32 v[108:109], v[108:109], v[116:117]
	v_pk_mul_f32 v[72:73], v[72:73], v[112:113]
	v_cvt_pk_bf16_f32 v108, v108, v109
	v_cvt_pk_bf16_f32 v109, v72, v73
	v_pk_mul_f32 v[72:73], v[28:29], v[66:67]
	v_pk_mul_f32 v[112:113], v[26:27], v[64:65]
	v_pk_fma_f32 v[72:73], v[4:5], v[90:91], v[72:73]
	v_pk_fma_f32 v[88:89], v[2:3], v[88:89], v[112:113]
	v_pk_mul_f32 v[90:91], v[20:21], v[62:63]
	v_pk_mul_f32 v[112:113], v[18:19], v[60:61]
	v_pk_fma_f32 v[86:87], v[8:9], v[86:87], v[90:91]
	v_pk_fma_f32 v[84:85], v[6:7], v[84:85], v[112:113]
	v_pk_mul_f32 v[116:117], v[16:17], v[68:69]
	s_mov_b32 s9, 0x2dc03000
	v_pk_fma_f32 v[116:117], v[12:13], v[126:127], v[116:117]
	v_add_co_u32_e32 v56, vcc, s9, v56
	v_pk_fma_f32 v[116:117], v[38:39], v[80:81], v[116:117]
	s_nop 0
	v_addc_co_u32_e32 v57, vcc, 0, v57, vcc
	v_lshlrev_b32_e32 v90, 16, v228
	v_and_b32_e32 v91, 0xffff0000, v228
	v_lshlrev_b32_e32 v112, 16, v229
	v_and_b32_e32 v113, 0xffff0000, v229
	v_pk_mul_f32 v[114:115], v[14:15], v[70:71]
	v_pk_mul_f32 v[112:113], v[116:117], v[112:113]
	v_pk_fma_f32 v[114:115], v[10:11], v[128:129], v[114:115]
	s_mov_b32 s9, 0xc000
	v_pk_fma_f32 v[114:115], v[36:37], v[82:83], v[114:115]
	v_pk_mul_f32 v[90:91], v[114:115], v[90:91]
	s_nop 0
	v_cvt_pk_bf16_f32 v90, v90, v90
	v_lshrrev_b32_e32 v90, 16, v90
	v_cvt_pk_bf16_f32 v91, v91, v91
	v_and_or_b32 v90, v91, s80, v90
	v_cvt_pk_bf16_f32 v91, v112, v112
	v_bfe_u32 v112, v113, 16, 1
	v_lshrrev_b32_e32 v91, 16, v91
; #define LAS __attribute__((address_space(3)))
; __device__ __forceinline__ unsigned pk2(float lo, float hi) { return f2bf(lo) | (f2bf(hi) << 16); }
; __device__ __forceinline__ f32x4 bf4(u32x2 v) { return (f32x4){lo_bf(v.x), hi_bf(v.x), lo_bf(v.y), hi_bf(v.y)}; }
; __device__ __forceinline__ void ph_prep_conv(CArgs& a, int l, LAS unsigned char* lds, int bid, int nblk) {
;     ...
; #pragma unroll
;         for (int tt = 0; tt < 8; ++tt) {
;             const f32x4 xx = wx[0] * x1[tt] + wx[1] * x1[tt + 1] + wx[2] * x1[tt + 2] + bx, v2 = wv[0] * vv[tt] + wv[1] * vv[tt + 1] + wv[2] * vv[tt + 2] + bv, z = xx * v2;
;             u32x2 zo; zo.x = pk2(z[0], z[1]); zo.y = pk2(z[2], z[3]); *(LAS u32x2*)(zt + (tg * 8 + tt) * 264 + c4) = zo;
;             const f32x4 bg = bf4(*(const u32x2*)(pb + (size_t)tt * D_INP + SC0 + c4));
;             const f32x4 y = bg * (ws3[0] * mm[tt] + ws3[1] * mm[tt + 1] + ws3[2] * mm[tt + 2]);
;             u32x2 yo; yo.x = pk2(y[0], y[1]); yo.y = pk2(y[2], y[3]); *(u32x2*)(YMIX + (size_t)(c.row0 + tg * 8 + tt) * D + 256 + c4) = yo;
;         }
;         __syncthreads();
;         { const int ch = tid & 255, g0 = (tid >> 8) * 4;
;           const int soff = c.L == CTXL ? 0 : CTXL;
; #pragma unroll
;           for (int g = 0; g < 4; ++g) { const int t8 = (g0 + g) * 8; unsigned short e[8];
; #pragma unroll
;               for (int j = 0; j < 8; ++j) e[j] = zt[(t8 + j) * 264 + ch];
;               u32x4 o; o.x = e[0] | ((unsigned)e[1] << 16); o.y = e[2] | ((unsigned)e[3] << 16); o.z = e[4] | ((unsigned)e[5] << 16); o.w = e[6] | ((unsigned)e[7] << 16);
;               *(u32x4*)(ZT + ((size_t)(ch * 16 + c.b)) * 2304 + soff + c.t0 + t8) = o; } }
;         __syncthreads();
	v_add3_u32 v112, v113, v112, s81
	v_and_or_b32 v91, v112, s80, v91
	global_store_dwordx2 v[56:57], v[90:91], off offset:512
	v_pk_fma_f32 v[88:89], v[22:23], v[54:55], v[88:89]
	v_pk_fma_f32 v[84:85], v[30:31], v[74:75], v[84:85]
	v_pk_fma_f32 v[72:73], v[24:25], v[58:59], v[72:73]
	v_pk_add_f32 v[88:89], v[40:41], v[88:89]
	v_pk_fma_f32 v[86:87], v[32:33], v[76:77], v[86:87]
	v_pk_add_f32 v[84:85], v[44:45], v[84:85]
	v_pk_add_f32 v[72:73], v[42:43], v[72:73]
	v_pk_add_f32 v[86:87], v[46:47], v[86:87]
	v_pk_mul_f32 v[84:85], v[88:89], v[84:85]
	v_pk_mul_f32 v[72:73], v[72:73], v[86:87]
	v_cvt_pk_bf16_f32 v84, v84, v84
	v_lshrrev_b32_e32 v84, 16, v84
	v_cvt_pk_bf16_f32 v85, v85, v85
	v_and_or_b32 v84, v85, s80, v84
	v_cvt_pk_bf16_f32 v85, v72, v73
	v_add_u32_e32 v72, 0x800, v185
	ds_write2_b64 v72, v[108:109], v[84:85] offset0:8 offset1:74
	v_pk_mul_f32 v[84:85], v[26:27], v[54:55]
	v_pk_mul_f32 v[72:73], v[28:29], v[58:59]
	v_pk_fma_f32 v[64:65], v[2:3], v[64:65], v[84:85]
	v_pk_mul_f32 v[84:85], v[18:19], v[74:75]
	v_pk_fma_f32 v[64:65], v[22:23], v[94:95], v[64:65]
	v_pk_fma_f32 v[60:61], v[6:7], v[60:61], v[84:85]
	v_pk_fma_f32 v[66:67], v[4:5], v[66:67], v[72:73]
	v_pk_fma_f32 v[60:61], v[30:31], v[92:93], v[60:61]
	v_pk_add_f32 v[64:65], v[40:41], v[64:65]
	v_pk_mul_f32 v[72:73], v[20:21], v[76:77]
	v_pk_add_f32 v[60:61], v[44:45], v[60:61]
	v_pk_fma_f32 v[62:63], v[8:9], v[62:63], v[72:73]
	v_pk_mul_f32 v[60:61], v[64:65], v[60:61]
	v_pk_fma_f32 v[66:67], v[24:25], v[110:111], v[66:67]
	v_pk_fma_f32 v[62:63], v[32:33], v[96:97], v[62:63]
	v_pk_add_f32 v[66:67], v[42:43], v[66:67]
	v_pk_add_f32 v[62:63], v[46:47], v[62:63]
	v_pk_mul_f32 v[62:63], v[66:67], v[62:63]
	v_cvt_pk_bf16_f32 v60, v60, v61
	v_cvt_pk_bf16_f32 v61, v62, v63
	v_pk_mul_f32 v[62:63], v[26:27], v[94:95]
	ds_write_b64 v185, v[60:61] offset:3168
	v_pk_mul_f32 v[60:61], v[28:29], v[110:111]
	v_pk_fma_f32 v[54:55], v[2:3], v[54:55], v[62:63]
	v_pk_mul_f32 v[62:63], v[18:19], v[92:93]
	v_pk_fma_f32 v[58:59], v[4:5], v[58:59], v[60:61]
	v_pk_mul_f32 v[60:61], v[20:21], v[96:97]
	v_pk_fma_f32 v[62:63], v[6:7], v[74:75], v[62:63]
	v_pk_fma_f32 v[54:55], v[22:23], v[102:103], v[54:55]
	v_pk_fma_f32 v[60:61], v[8:9], v[76:77], v[60:61]
	v_pk_fma_f32 v[62:63], v[30:31], v[100:101], v[62:63]
	v_pk_fma_f32 v[58:59], v[24:25], v[106:107], v[58:59]
	v_pk_add_f32 v[54:55], v[40:41], v[54:55]
	v_pk_fma_f32 v[60:61], v[32:33], v[104:105], v[60:61]
	v_pk_add_f32 v[62:63], v[44:45], v[62:63]
	v_pk_add_f32 v[58:59], v[42:43], v[58:59]
	v_pk_add_f32 v[60:61], v[46:47], v[60:61]
	v_pk_mul_f32 v[54:55], v[54:55], v[62:63]
	v_pk_mul_f32 v[58:59], v[58:59], v[60:61]
	v_cvt_pk_bf16_f32 v54, v54, v55
	v_cvt_pk_bf16_f32 v55, v58, v59
	v_pk_mul_f32 v[58:59], v[14:15], v[82:83]
	ds_write_b64 v186, v[54:55]
	v_pk_fma_f32 v[58:59], v[10:11], v[70:71], v[58:59]
	v_lshlrev_b32_e32 v54, 16, v230
	v_and_b32_e32 v55, 0xffff0000, v230
	v_pk_fma_f32 v[58:59], v[36:37], v[98:99], v[58:59]
	v_pk_mul_f32 v[60:61], v[16:17], v[80:81]
	v_pk_mul_f32 v[54:55], v[58:59], v[54:55]
	v_pk_fma_f32 v[60:61], v[12:13], v[68:69], v[60:61]
	v_lshlrev_b32_e32 v52, 16, v231
	v_and_b32_e32 v53, 0xffff0000, v231
	v_pk_fma_f32 v[60:61], v[38:39], v[78:79], v[60:61]
	v_pk_mul_f32 v[52:53], v[60:61], v[52:53]
	v_cvt_pk_bf16_f32 v54, v54, v55
	v_cvt_pk_bf16_f32 v55, v52, v53
	global_store_dwordx2 v[56:57], v[54:55], off offset:2560
	v_add_u32_e32 v54, s8, v184
	v_mov_b64_e32 v[52:53], s[26:27]
	s_movk_i32 s8, 0x1200
	s_waitcnt lgkmcnt(0)
	s_barrier
	v_mad_i64_i32 v[52:53], s[8:9], v54, s8, v[52:53]
	ds_read_u16 v58, v187
	ds_read_u16 v59, v187 offset:528
	ds_read_u16 v60, v187 offset:1056
	ds_read_u16 v61, v187 offset:1584
	ds_read_u16 v54, v187 offset:2112
	ds_read_u16 v62, v187 offset:2640
	ds_read_u16 v55, v187 offset:3168
	ds_read_u16 v63, v187 offset:3696
	v_lshl_add_u64 v[52:53], v[52:53], 0, s[78:79]
	v_lshl_add_u64 v[56:57], s[28:29], 1, v[52:53]
	s_mov_b32 s8, 0x5040100
	s_waitcnt lgkmcnt(2)
	v_perm_b32 v54, v62, v54, s8
	s_waitcnt lgkmcnt(0)
	v_perm_b32 v55, v63, v55, s8
	v_perm_b32 v53, v61, v60, s8
	v_perm_b32 v52, v59, v58, s8
	v_lshl_add_u64 v[58:59], v[50:51], 1, v[56:57]
	global_store_dwordx4 v[58:59], v[52:55], off
	ds_read_u16 v52, v187 offset:4752
	ds_read_u16 v53, v187 offset:5280
	ds_read_u16 v54, v187 offset:7392
	ds_read_u16 v55, v187 offset:7920
	ds_read_u16 v60, v187 offset:5808
	ds_read_u16 v61, v187 offset:6336
	ds_read_u16 v62, v187 offset:8976
	ds_read_u16 v63, v187 offset:6864
	ds_read_u16 v64, v188
	ds_read_u16 v65, v188 offset:4224
	ds_read_u16 v66, v187 offset:9504
	ds_read_u16 v67, v187 offset:10032
	ds_read_u16 v68, v187 offset:10560
	ds_read_u16 v69, v187 offset:11088
	ds_read_u16 v70, v187 offset:11616
	ds_read_u16 v71, v187 offset:12144
	s_waitcnt lgkmcnt(12)
	v_perm_b32 v55, v55, v54, s8
	s_waitcnt lgkmcnt(11)
	v_perm_b32 v53, v60, v53, s8
	s_waitcnt lgkmcnt(7)
	v_perm_b32 v52, v52, v64, s8
	v_perm_b32 v54, v63, v61, s8
	global_store_dwordx4 v[58:59], v[52:55], off offset:16
	v_lshl_add_u64 v[56:57], v[48:49], 1, v[56:57]
	s_waitcnt lgkmcnt(0)
	v_perm_b32 v55, v71, v70, s8
	ds_read_u16 v60, v189
	ds_read_u16 v61, v202
	ds_read_u16 v63, v203
	ds_read_u16 v64, v204
	ds_read_u16 v70, v205
	ds_read_u16 v71, v206
	ds_read_u16 v72, v207
	ds_read_u16 v73, v208
	v_perm_b32 v54, v69, v68, s8
	v_perm_b32 v53, v67, v66, s8
	v_perm_b32 v52, v62, v65, s8
	global_store_dwordx4 v[58:59], v[52:55], off offset:32
	s_waitcnt lgkmcnt(0)
	s_nop 0
	v_perm_b32 v55, v73, v72, s8
	v_perm_b32 v54, v71, v70, s8
	v_perm_b32 v53, v64, v63, s8
	v_perm_b32 v52, v61, v60, s8
	v_readlane_b32 s8, v252, 57
	s_add_i32 s1, s1, s8
	s_cmpk_lt_i32 s0, 0x240
	global_store_dwordx4 v[56:57], v[52:55], off
	s_barrier
	s_cbranch_scc0 .LBB0_271

; #define LAS __attribute__((address_space(3)))
; __device__ __forceinline__ float bf2f(unsigned v) { return __uint_as_float(v << 16); }
; __device__ __forceinline__ float rdlane_f(float v, int l) { return __builtin_bit_cast(float, __builtin_amdgcn_readlane(__builtin_bit_cast(int, v), l)); }
; __device__ __forceinline__ void ph_prep_tok(CArgs& a, int l, LAS unsigned char* lds, int gw, int ngw) {
;     ...
;     for (int row0 = gw * 4; row0 < NTOK; row0 += ngw * 4) {
;         int z = 0; asm volatile("" : "+v"(z));
;         const LAS float* wa = swa + z; const LAS float* cw = scw + z;
;         const bf16* pr0 = P + (size_t)row0 * D_INP;
;         int tpos, lo, hi;
;         if (row0 < NTOK_C) { tpos = row0 & 255; lo = 0; hi = CTXL; } else { tpos = (row0 - NTOK_C) & 2047; lo = tpos & ~63; hi = lo + 64; }
;         bf16 avb[4]; u32x2 xr[3][6]; bf16 gb4[4];
; #pragma unroll
;         for (int r = 0; r < 4; ++r) avb[r] = pr0[(size_t)r * D_INP + GLA0 + 768 + (lane & 31)];
; #pragma unroll
;         for (int g = 0; g < 3; ++g)
; #pragma unroll
;             for (int r = 0; r < 6; ++r) { const int tc = min(max(tpos + r - 1, lo), hi - 1); xr[g][r] = *(const u32x2*)(pr0 + (ptrdiff_t)(tc - tpos) * D_INP + GDN0 + g * 256 + 4 * lane); }
; #pragma unroll
;         for (int i = 0; i < 4; ++i) gb4[i] = pr0[(size_t)gr * D_INP + GDN0 + 1024 + 4 * i + gh];
;         float av[4], s[4][4];
; #pragma unroll
;         for (int r = 0; r < 4; ++r) { av[r] = bf2f(avb[r]); s[r][0] = sba[lane]; s[r][1] = sba[64 + lane]; s[r][2] = sba[128 + lane]; s[r][3] = sba[192 + lane]; }
; #pragma unroll
;         for (int i = 0; i < 16; ++i) { const float w0 = wa[i * 128 + lane], w1 = wa[i * 128 + 64 + lane], w2 = wa[2048 + i * 128 + lane], w3 = wa[2048 + i * 128 + 64 + lane];
; #pragma unroll
;             for (int r = 0; r < 4; ++r) { const float af = rdlane_f(av[r], i), ab = rdlane_f(av[r], 16 + i); s[r][0] += af * w0; s[r][1] += af * w1; s[r][2] += ab * w2; s[r][3] += ab * w3; } }
.LBB0_302:
	s_and_b32 s4, s0, 0x7c0
	s_add_i32 s1, s4, 64
	s_cmpk_lt_i32 s0, 0x1000
	s_movk_i32 s5, 0x7fc
	s_cselect_b32 s5, 0xfc, s5
	s_cselect_b32 s1, 0x100, s1
	s_cselect_b32 s8, 0, s4
	s_and_b32 s9, s5, s0
	s_add_i32 s4, s9, -1
	s_add_i32 s6, s1, -1
	s_max_i32 s4, s4, s8
	s_min_u32 s4, s4, s6
	s_sub_i32 s4, s4, s9
	s_mul_hi_i32 s5, s4, 0x1c00
	s_mulk_i32 s4, 0x1c00
	v_mov_b32_e32 v2, v35
	s_add_u32 s4, s2, s4
	s_addc_u32 s5, s3, s5
	v_lshl_add_u32 v52, v2, 2, 0
	v_lshl_add_u64 v[2:3], s[4:5], 0, v[26:27]
	s_max_u32 s4, s9, s8
	s_min_u32 s4, s4, s6
	s_sub_i32 s4, s4, s9
	s_mulk_i32 s4, 0x1c00
	s_ashr_i32 s5, s4, 31
	s_add_u32 s4, s2, s4
	s_addc_u32 s5, s3, s5
	v_lshl_add_u64 v[4:5], s[4:5], 0, v[26:27]
	s_or_b32 s4, s9, 1
	s_max_u32 s4, s4, s8
	s_min_u32 s4, s4, s6
	s_sub_i32 s4, s4, s9
	s_mulk_i32 s4, 0x1c00
	s_ashr_i32 s5, s4, 31
	s_add_u32 s4, s2, s4
	s_addc_u32 s5, s3, s5
	v_lshl_add_u64 v[6:7], s[4:5], 0, v[26:27]
	s_or_b32 s4, s9, 2
	s_max_u32 s4, s4, s8
	s_min_u32 s4, s4, s6
	s_sub_i32 s4, s4, s9
	s_mulk_i32 s4, 0x1c00
	s_ashr_i32 s5, s4, 31
	s_add_u32 s4, s2, s4
	s_mov_b32 s7, 0x1e001000
	s_addc_u32 s5, s3, s5
	s_or_b32 s10, s9, 3
	v_add_co_u32_e32 v2, vcc, s7, v2
	v_lshl_add_u64 v[8:9], s[4:5], 0, v[26:27]
	s_max_u32 s4, s10, s8
	v_addc_co_u32_e32 v3, vcc, 0, v3, vcc
	s_min_u32 s4, s4, s6
	v_add_co_u32_e32 v4, vcc, s7, v4
	s_sub_i32 s4, s4, s9
	s_nop 0
	v_addc_co_u32_e32 v5, vcc, 0, v5, vcc
	s_mulk_i32 s4, 0x1c00
	v_add_co_u32_e32 v6, vcc, s7, v6
	s_ashr_i32 s5, s4, 31
	s_nop 0
	v_addc_co_u32_e32 v7, vcc, 0, v7, vcc
	s_add_u32 s4, s2, s4
	v_add_co_u32_e32 v44, vcc, s7, v8
	s_addc_u32 s5, s3, s5
	s_nop 0
	v_addc_co_u32_e32 v45, vcc, 0, v9, vcc
	v_lshl_add_u64 v[8:9], s[4:5], 0, v[26:27]
	s_add_i32 s4, s9, 4
	s_max_u32 s4, s4, s8
	s_min_u32 s4, s4, s6
	s_sub_i32 s4, s4, s9
	s_mulk_i32 s4, 0x1c00
	s_ashr_i32 s5, s4, 31
	s_add_u32 s4, s2, s4
	v_add_co_u32_e32 v46, vcc, s7, v8
	s_addc_u32 s5, s3, s5
	s_nop 0
	v_addc_co_u32_e32 v47, vcc, 0, v9, vcc
	v_lshl_add_u64 v[8:9], s[4:5], 0, v[26:27]
	v_add_co_u32_e32 v50, vcc, s7, v8
	global_load_dwordx2 v[40:41], v[2:3], off offset:576
	global_load_dwordx2 v[38:39], v[4:5], off offset:576
	global_load_dwordx2 v[42:43], v[6:7], off offset:576
	global_load_dwordx2 v[32:33], v[44:45], off offset:576
	v_addc_co_u32_e32 v51, vcc, 0, v9, vcc
	global_load_dwordx2 v[36:37], v[46:47], off offset:576
	global_load_dwordx2 v[30:31], v[50:51], off offset:576
	global_load_dwordx2 v[66:67], v[2:3], off offset:1088
	global_load_dwordx2 v[64:65], v[4:5], off offset:1088
	global_load_dwordx2 v[62:63], v[6:7], off offset:1088
	global_load_dwordx2 v[60:61], v[44:45], off offset:1088
	global_load_dwordx2 v[58:59], v[46:47], off offset:1088
	global_load_dwordx2 v[56:57], v[50:51], off offset:1088
	global_load_dwordx2 v[12:13], v[2:3], off offset:1600
	global_load_dwordx2 v[10:11], v[4:5], off offset:1600
	global_load_dwordx2 v[8:9], v[6:7], off offset:1600
	s_nop 0
	global_load_dwordx2 v[6:7], v[44:45], off offset:1600
	global_load_dwordx2 v[4:5], v[46:47], off offset:1600
	global_load_dwordx2 v[2:3], v[50:51], off offset:1600
	v_lshl_add_u64 v[44:45], s[2:3], 0, v[24:25]
	s_mov_b32 s4, 0x1e000000
	v_add_co_u32_e32 v44, vcc, s4, v44
	v_lshl_add_u64 v[48:49], s[2:3], 0, v[28:29]
	s_nop 0
	v_addc_co_u32_e32 v45, vcc, 0, v45, vcc
	v_add_co_u32_e32 v50, vcc, s7, v48
	global_load_ushort v34, v[44:45], off
	global_load_ushort v113, v[44:45], off offset:8
	global_load_ushort v114, v[44:45], off offset:16
	global_load_ushort v115, v[44:45], off offset:24
	v_addc_co_u32_e32 v51, vcc, 0, v49, vcc
	ds_read2st64_b32 v[46:47], v110 offset0:224 offset1:225
	ds_read2st64_b32 v[44:45], v110 offset0:226 offset1:227
	global_load_ushort v50, v[50:51], off offset:512
	s_mov_b32 s4, 0x1e002000
	v_lshl_add_u32 v79, v108, 2, v52
	s_mov_b32 s6, 0x7f800000
	s_mov_b32 s7, 0x52800000
	s_mov_b32 s11, 0x53c00000
	s_cmp_le_u32 s9, s8
	v_lshl_add_u32 v117, v109, 2, v52
	v_add_u32_e32 v116, 0xfc00, v52
	s_waitcnt vmcnt(0)
	v_lshlrev_b32_e32 v71, 16, v50
	v_add_co_u32_e32 v50, vcc, s4, v48
	s_mov_b32 s4, 0x1e004000
	s_nop 0
	v_addc_co_u32_e32 v51, vcc, 0, v49, vcc
	global_load_ushort v50, v[50:51], off offset:3584
	v_readlane_b32 s5, v71, 16
	s_waitcnt vmcnt(0)
	v_lshlrev_b32_e32 v72, 16, v50
	v_add_co_u32_e32 v50, vcc, s4, v48
	s_mov_b32 s4, 0x1e006000
	s_nop 0
	v_addc_co_u32_e32 v51, vcc, 0, v49, vcc
	v_add_co_u32_e32 v48, vcc, s4, v48
	global_load_ushort v50, v[50:51], off offset:2560
	s_nop 0
	v_addc_co_u32_e32 v49, vcc, 0, v49, vcc
	global_load_ushort v48, v[48:49], off offset:1536
	v_readlane_b32 s4, v71, 0
	s_waitcnt vmcnt(1)
	v_lshlrev_b32_e32 v73, 16, v50
	s_waitcnt vmcnt(0)
	v_lshlrev_b32_e32 v76, 16, v48
	ds_read2st64_b32 v[48:49], v79 offset0:160 offset1:161
	ds_read2st64_b32 v[80:81], v79 offset0:192 offset1:193
	s_waitcnt lgkmcnt(1)
	v_fma_f32 v78, s4, v48, v46
	v_fma_f32 v77, s4, v49, v47
	s_waitcnt lgkmcnt(0)
	v_fma_f32 v75, s5, v80, v44
	v_fma_f32 v74, s5, v81, v45
	v_readlane_b32 s4, v72, 0
	v_readlane_b32 s5, v72, 16
	s_nop 0
	v_fma_f32 v70, s4, v48, v46
	v_fma_f32 v51, s4, v49, v47
	v_fma_f32 v50, s5, v80, v44
	v_fma_f32 v69, s5, v81, v45
	v_readlane_b32 s4, v73, 0
	v_readlane_b32 s5, v73, 16
	s_nop 0
	v_fma_f32 v68, s4, v48, v46
	v_fma_f32 v55, s4, v49, v47
	v_fma_f32 v54, s5, v80, v44
	v_fma_f32 v53, s5, v81, v45
	v_readlane_b32 s4, v76, 0
	v_readlane_b32 s5, v76, 16
	s_nop 0
	v_fma_f32 v46, s4, v48, v46
	v_fmac_f32_e32 v47, s4, v49
	v_fma_f32 v44, s5, v80, v44
	v_fmac_f32_e32 v45, s5, v81
	ds_read2st64_b32 v[48:49], v79 offset0:162 offset1:163
	ds_read2st64_b32 v[80:81], v79 offset0:194 offset1:195
	v_readlane_b32 s4, v71, 1
	v_readlane_b32 s5, v71, 17
	s_waitcnt lgkmcnt(1)
; __device__ __forceinline__ float rdlane_f(float v, int l) { return __builtin_bit_cast(float, __builtin_amdgcn_readlane(__builtin_bit_cast(int, v), l)); }
; __device__ __forceinline__ void ph_prep_tok(CArgs& a, int l, LAS unsigned char* lds, int gw, int ngw) {
;     ...
;         for (int i = 0; i < 16; ++i) { const float w0 = wa[i * 128 + lane], w1 = wa[i * 128 + 64 + lane], w2 = wa[2048 + i * 128 + lane], w3 = wa[2048 + i * 128 + 64 + lane];
; #pragma unroll
;             for (int r = 0; r < 4; ++r) { const float af = rdlane_f(av[r], i), ab = rdlane_f(av[r], 16 + i); s[r][0] += af * w0; s[r][1] += af * w1; s[r][2] += ab * w2; s[r][3] += ab * w3; } }
	v_fmac_f32_e32 v78, s4, v48
	v_fmac_f32_e32 v77, s4, v49
	s_waitcnt lgkmcnt(0)
	v_fmac_f32_e32 v75, s5, v80
	v_fmac_f32_e32 v74, s5, v81
	v_readlane_b32 s4, v72, 1
	v_readlane_b32 s5, v72, 17
	s_nop 0
	v_fmac_f32_e32 v70, s4, v48
	v_fmac_f32_e32 v51, s4, v49
	v_fmac_f32_e32 v50, s5, v80
	v_fmac_f32_e32 v69, s5, v81
	v_readlane_b32 s4, v73, 1
	v_readlane_b32 s5, v73, 17
	s_nop 0
	v_fmac_f32_e32 v68, s4, v48
	v_fmac_f32_e32 v55, s4, v49
	v_fmac_f32_e32 v54, s5, v80
	v_fmac_f32_e32 v53, s5, v81
	v_readlane_b32 s4, v76, 1
	v_readlane_b32 s5, v76, 17
	s_nop 0
	v_fmac_f32_e32 v46, s4, v48
	v_fmac_f32_e32 v47, s4, v49
	v_fmac_f32_e32 v44, s5, v80
	v_fmac_f32_e32 v45, s5, v81
	ds_read2st64_b32 v[48:49], v79 offset0:164 offset1:165
	ds_read2st64_b32 v[80:81], v79 offset0:196 offset1:197
	v_readlane_b32 s4, v71, 2
	v_readlane_b32 s5, v71, 18
	s_waitcnt lgkmcnt(1)
	v_fmac_f32_e32 v78, s4, v48
	v_fmac_f32_e32 v77, s4, v49
	s_waitcnt lgkmcnt(0)
	v_fmac_f32_e32 v75, s5, v80
	v_fmac_f32_e32 v74, s5, v81
	v_readlane_b32 s4, v72, 2
	v_readlane_b32 s5, v72, 18
	s_nop 0
	v_fmac_f32_e32 v70, s4, v48
	v_fmac_f32_e32 v51, s4, v49
	v_fmac_f32_e32 v50, s5, v80
	v_fmac_f32_e32 v69, s5, v81
	v_readlane_b32 s4, v73, 2
	v_readlane_b32 s5, v73, 18
	s_nop 0
	v_fmac_f32_e32 v68, s4, v48
	v_fmac_f32_e32 v55, s4, v49
	v_fmac_f32_e32 v54, s5, v80
	v_fmac_f32_e32 v53, s5, v81
	v_readlane_b32 s4, v76, 2
	v_readlane_b32 s5, v76, 18
	s_nop 0
	v_fmac_f32_e32 v46, s4, v48
	v_fmac_f32_e32 v47, s4, v49
	v_fmac_f32_e32 v44, s5, v80
	v_fmac_f32_e32 v45, s5, v81
	ds_read2st64_b32 v[48:49], v79 offset0:166 offset1:167
	ds_read2st64_b32 v[80:81], v79 offset0:198 offset1:199
	v_readlane_b32 s4, v71, 3
	v_readlane_b32 s5, v71, 19
	s_waitcnt lgkmcnt(1)
	v_fmac_f32_e32 v78, s4, v48
	v_fmac_f32_e32 v77, s4, v49
	s_waitcnt lgkmcnt(0)
	v_fmac_f32_e32 v75, s5, v80
	v_fmac_f32_e32 v74, s5, v81
	v_readlane_b32 s4, v72, 3
	v_readlane_b32 s5, v72, 19
	s_nop 0
	v_fmac_f32_e32 v70, s4, v48
	v_fmac_f32_e32 v51, s4, v49
	v_fmac_f32_e32 v50, s5, v80
	v_fmac_f32_e32 v69, s5, v81
	v_readlane_b32 s4, v73, 3
	v_readlane_b32 s5, v73, 19
	s_nop 0
	v_fmac_f32_e32 v68, s4, v48
	v_fmac_f32_e32 v55, s4, v49
	v_fmac_f32_e32 v54, s5, v80
	v_fmac_f32_e32 v53, s5, v81
	v_readlane_b32 s4, v76, 3
	v_readlane_b32 s5, v76, 19
	s_nop 0
	v_fmac_f32_e32 v46, s4, v48
	v_fmac_f32_e32 v47, s4, v49
	v_fmac_f32_e32 v44, s5, v80
	v_fmac_f32_e32 v45, s5, v81
	ds_read2st64_b32 v[48:49], v79 offset0:168 offset1:169
	ds_read2st64_b32 v[80:81], v79 offset0:200 offset1:201
	v_readlane_b32 s4, v71, 4
	v_readlane_b32 s5, v71, 20
	s_waitcnt lgkmcnt(1)
	v_fmac_f32_e32 v78, s4, v48
	v_fmac_f32_e32 v77, s4, v49
	s_waitcnt lgkmcnt(0)
	v_fmac_f32_e32 v75, s5, v80
	v_fmac_f32_e32 v74, s5, v81
	v_readlane_b32 s4, v72, 4
	v_readlane_b32 s5, v72, 20
	s_nop 0
	v_fmac_f32_e32 v70, s4, v48
	v_fmac_f32_e32 v51, s4, v49
	v_fmac_f32_e32 v50, s5, v80
	v_fmac_f32_e32 v69, s5, v81
	v_readlane_b32 s4, v73, 4
	v_readlane_b32 s5, v73, 20
	s_nop 0
	v_fmac_f32_e32 v68, s4, v48
	v_fmac_f32_e32 v55, s4, v49
	v_fmac_f32_e32 v54, s5, v80
	v_fmac_f32_e32 v53, s5, v81
	v_readlane_b32 s4, v76, 4
	v_readlane_b32 s5, v76, 20
	s_nop 0
	v_fmac_f32_e32 v46, s4, v48
	v_fmac_f32_e32 v47, s4, v49
	v_fmac_f32_e32 v44, s5, v80
	v_fmac_f32_e32 v45, s5, v81
	ds_read2st64_b32 v[48:49], v79 offset0:170 offset1:171
	ds_read2st64_b32 v[80:81], v79 offset0:202 offset1:203
	v_readlane_b32 s4, v71, 5
	v_readlane_b32 s5, v71, 21
	s_waitcnt lgkmcnt(1)
	v_fmac_f32_e32 v78, s4, v48
	v_fmac_f32_e32 v77, s4, v49
	s_waitcnt lgkmcnt(0)
	v_fmac_f32_e32 v75, s5, v80
	v_fmac_f32_e32 v74, s5, v81
	v_readlane_b32 s4, v72, 5
	v_readlane_b32 s5, v72, 21
	s_nop 0
	v_fmac_f32_e32 v70, s4, v48
	v_fmac_f32_e32 v51, s4, v49
	v_fmac_f32_e32 v50, s5, v80
	v_fmac_f32_e32 v69, s5, v81
	v_readlane_b32 s4, v73, 5
	v_readlane_b32 s5, v73, 21
	s_nop 0
	v_fmac_f32_e32 v68, s4, v48
	v_fmac_f32_e32 v55, s4, v49
	v_fmac_f32_e32 v54, s5, v80
	v_fmac_f32_e32 v53, s5, v81
	v_readlane_b32 s4, v76, 5
	v_readlane_b32 s5, v76, 21
	s_nop 0
	v_fmac_f32_e32 v46, s4, v48
	v_fmac_f32_e32 v47, s4, v49
	v_fmac_f32_e32 v44, s5, v80
	v_fmac_f32_e32 v45, s5, v81
	ds_read2st64_b32 v[48:49], v79 offset0:172 offset1:173
	ds_read2st64_b32 v[80:81], v79 offset0:204 offset1:205
	v_readlane_b32 s4, v71, 6
	v_readlane_b32 s5, v71, 22
	s_waitcnt lgkmcnt(1)
	v_fmac_f32_e32 v78, s4, v48
	v_fmac_f32_e32 v77, s4, v49
	s_waitcnt lgkmcnt(0)
	v_fmac_f32_e32 v75, s5, v80
	v_fmac_f32_e32 v74, s5, v81
	v_readlane_b32 s4, v72, 6
	v_readlane_b32 s5, v72, 22
	s_nop 0
	v_fmac_f32_e32 v70, s4, v48
	v_fmac_f32_e32 v51, s4, v49
	v_fmac_f32_e32 v50, s5, v80
	v_fmac_f32_e32 v69, s5, v81
	v_readlane_b32 s4, v73, 6
	v_readlane_b32 s5, v73, 22
	s_nop 0
	v_fmac_f32_e32 v68, s4, v48
	v_fmac_f32_e32 v55, s4, v49
	v_fmac_f32_e32 v54, s5, v80
	v_fmac_f32_e32 v53, s5, v81
	v_readlane_b32 s4, v76, 6
	v_readlane_b32 s5, v76, 22
	s_nop 0
	v_fmac_f32_e32 v46, s4, v48
	v_fmac_f32_e32 v47, s4, v49
	v_fmac_f32_e32 v44, s5, v80
	v_fmac_f32_e32 v45, s5, v81
	ds_read2st64_b32 v[48:49], v79 offset0:174 offset1:175
	ds_read2st64_b32 v[80:81], v79 offset0:206 offset1:207
	v_readlane_b32 s4, v71, 7
	v_readlane_b32 s5, v71, 23
	s_waitcnt lgkmcnt(1)
	v_fmac_f32_e32 v78, s4, v48
	v_fmac_f32_e32 v77, s4, v49
	s_waitcnt lgkmcnt(0)
; __device__ __forceinline__ float rdlane_f(float v, int l) { return __builtin_bit_cast(float, __builtin_amdgcn_readlane(__builtin_bit_cast(int, v), l)); }
; __device__ __forceinline__ void ph_prep_tok(CArgs& a, int l, LAS unsigned char* lds, int gw, int ngw) {
;     ...
;         for (int i = 0; i < 16; ++i) { const float w0 = wa[i * 128 + lane], w1 = wa[i * 128 + 64 + lane], w2 = wa[2048 + i * 128 + lane], w3 = wa[2048 + i * 128 + 64 + lane];
; #pragma unroll
;             for (int r = 0; r < 4; ++r) { const float af = rdlane_f(av[r], i), ab = rdlane_f(av[r], 16 + i); s[r][0] += af * w0; s[r][1] += af * w1; s[r][2] += ab * w2; s[r][3] += ab * w3; } }
	v_fmac_f32_e32 v75, s5, v80
	v_fmac_f32_e32 v74, s5, v81
	v_readlane_b32 s4, v72, 7
	v_readlane_b32 s5, v72, 23
	s_nop 0
	v_fmac_f32_e32 v70, s4, v48
	v_fmac_f32_e32 v51, s4, v49
	v_fmac_f32_e32 v50, s5, v80
	v_fmac_f32_e32 v69, s5, v81
	v_readlane_b32 s4, v73, 7
	v_readlane_b32 s5, v73, 23
	s_nop 0
	v_fmac_f32_e32 v68, s4, v48
	v_fmac_f32_e32 v55, s4, v49
	v_fmac_f32_e32 v54, s5, v80
	v_fmac_f32_e32 v53, s5, v81
	v_readlane_b32 s4, v76, 7
	v_readlane_b32 s5, v76, 23
	s_nop 0
	v_fmac_f32_e32 v46, s4, v48
	v_fmac_f32_e32 v47, s4, v49
	v_fmac_f32_e32 v44, s5, v80
	v_fmac_f32_e32 v45, s5, v81
	ds_read2st64_b32 v[48:49], v79 offset0:176 offset1:177
	ds_read2st64_b32 v[80:81], v79 offset0:208 offset1:209
	v_readlane_b32 s4, v71, 8
	v_readlane_b32 s5, v71, 24
	s_waitcnt lgkmcnt(1)
	v_fmac_f32_e32 v78, s4, v48
	v_fmac_f32_e32 v77, s4, v49
	s_waitcnt lgkmcnt(0)
	v_fmac_f32_e32 v75, s5, v80
	v_fmac_f32_e32 v74, s5, v81
	v_readlane_b32 s4, v72, 8
	v_readlane_b32 s5, v72, 24
	s_nop 0
	v_fmac_f32_e32 v70, s4, v48
	v_fmac_f32_e32 v51, s4, v49
	v_fmac_f32_e32 v50, s5, v80
	v_fmac_f32_e32 v69, s5, v81
	v_readlane_b32 s4, v73, 8
	v_readlane_b32 s5, v73, 24
	s_nop 0
	v_fmac_f32_e32 v68, s4, v48
	v_fmac_f32_e32 v55, s4, v49
	v_fmac_f32_e32 v54, s5, v80
	v_fmac_f32_e32 v53, s5, v81
	v_readlane_b32 s4, v76, 8
	v_readlane_b32 s5, v76, 24
	s_nop 0
	v_fmac_f32_e32 v46, s4, v48
	v_fmac_f32_e32 v47, s4, v49
	v_fmac_f32_e32 v44, s5, v80
	v_fmac_f32_e32 v45, s5, v81
	ds_read2st64_b32 v[48:49], v79 offset0:178 offset1:179
	ds_read2st64_b32 v[80:81], v79 offset0:210 offset1:211
	v_readlane_b32 s4, v71, 9
	v_readlane_b32 s5, v71, 25
	s_waitcnt lgkmcnt(1)
	v_fmac_f32_e32 v78, s4, v48
	v_fmac_f32_e32 v77, s4, v49
	s_waitcnt lgkmcnt(0)
	v_fmac_f32_e32 v75, s5, v80
	v_fmac_f32_e32 v74, s5, v81
	v_readlane_b32 s4, v72, 9
	v_readlane_b32 s5, v72, 25
	s_nop 0
	v_fmac_f32_e32 v70, s4, v48
	v_fmac_f32_e32 v51, s4, v49
	v_fmac_f32_e32 v50, s5, v80
	v_fmac_f32_e32 v69, s5, v81
	v_readlane_b32 s4, v73, 9
	v_readlane_b32 s5, v73, 25
	s_nop 0
	v_fmac_f32_e32 v68, s4, v48
	v_fmac_f32_e32 v55, s4, v49
	v_fmac_f32_e32 v54, s5, v80
	v_fmac_f32_e32 v53, s5, v81
	v_readlane_b32 s4, v76, 9
	v_readlane_b32 s5, v76, 25
	s_nop 0
	v_fmac_f32_e32 v46, s4, v48
	v_fmac_f32_e32 v47, s4, v49
	v_fmac_f32_e32 v44, s5, v80
	v_fmac_f32_e32 v45, s5, v81
	ds_read2st64_b32 v[48:49], v79 offset0:180 offset1:181
	ds_read2st64_b32 v[80:81], v79 offset0:212 offset1:213
	v_readlane_b32 s4, v71, 10
	v_readlane_b32 s5, v71, 26
	s_waitcnt lgkmcnt(1)
	v_fmac_f32_e32 v78, s4, v48
	v_fmac_f32_e32 v77, s4, v49
	s_waitcnt lgkmcnt(0)
	v_fmac_f32_e32 v75, s5, v80
	v_fmac_f32_e32 v74, s5, v81
	v_readlane_b32 s4, v72, 10
	v_readlane_b32 s5, v72, 26
	s_nop 0
	v_fmac_f32_e32 v70, s4, v48
	v_fmac_f32_e32 v51, s4, v49
	v_fmac_f32_e32 v50, s5, v80
	v_fmac_f32_e32 v69, s5, v81
	v_readlane_b32 s4, v73, 10
	v_readlane_b32 s5, v73, 26
	s_nop 0
	v_fmac_f32_e32 v68, s4, v48
	v_fmac_f32_e32 v55, s4, v49
	v_fmac_f32_e32 v54, s5, v80
	v_fmac_f32_e32 v53, s5, v81
	v_readlane_b32 s4, v76, 10
	v_readlane_b32 s5, v76, 26
	s_nop 0
	v_fmac_f32_e32 v46, s4, v48
	v_fmac_f32_e32 v47, s4, v49
	v_fmac_f32_e32 v44, s5, v80
	v_fmac_f32_e32 v45, s5, v81
	ds_read2st64_b32 v[48:49], v79 offset0:182 offset1:183
	ds_read2st64_b32 v[80:81], v79 offset0:214 offset1:215
	v_readlane_b32 s4, v71, 11
	v_readlane_b32 s5, v71, 27
	s_waitcnt lgkmcnt(1)
	v_fmac_f32_e32 v78, s4, v48
	v_fmac_f32_e32 v77, s4, v49
	s_waitcnt lgkmcnt(0)
	v_fmac_f32_e32 v75, s5, v80
	v_fmac_f32_e32 v74, s5, v81
	v_readlane_b32 s4, v72, 11
	v_readlane_b32 s5, v72, 27
	s_nop 0
	v_fmac_f32_e32 v70, s4, v48
	v_fmac_f32_e32 v51, s4, v49
	v_fmac_f32_e32 v50, s5, v80
	v_fmac_f32_e32 v69, s5, v81
	v_readlane_b32 s4, v73, 11
	v_readlane_b32 s5, v73, 27
	s_nop 0
	v_fmac_f32_e32 v68, s4, v48
	v_fmac_f32_e32 v55, s4, v49
	v_fmac_f32_e32 v54, s5, v80
	v_fmac_f32_e32 v53, s5, v81
	v_readlane_b32 s4, v76, 11
	v_readlane_b32 s5, v76, 27
	s_nop 0
	v_fmac_f32_e32 v46, s4, v48
	v_fmac_f32_e32 v47, s4, v49
	v_fmac_f32_e32 v44, s5, v80
	v_fmac_f32_e32 v45, s5, v81
	ds_read2st64_b32 v[48:49], v79 offset0:184 offset1:185
	ds_read2st64_b32 v[80:81], v79 offset0:216 offset1:217
	v_readlane_b32 s4, v71, 12
	v_readlane_b32 s5, v71, 28
	s_waitcnt lgkmcnt(1)
	v_fmac_f32_e32 v78, s4, v48
	v_fmac_f32_e32 v77, s4, v49
	s_waitcnt lgkmcnt(0)
	v_fmac_f32_e32 v75, s5, v80
	v_fmac_f32_e32 v74, s5, v81
	v_readlane_b32 s4, v72, 12
	v_readlane_b32 s5, v72, 28
	s_nop 0
	v_fmac_f32_e32 v70, s4, v48
	v_fmac_f32_e32 v51, s4, v49
	v_fmac_f32_e32 v50, s5, v80
	v_fmac_f32_e32 v69, s5, v81
	v_readlane_b32 s4, v73, 12
	v_readlane_b32 s5, v73, 28
	s_nop 0
	v_fmac_f32_e32 v68, s4, v48
	v_fmac_f32_e32 v55, s4, v49
	v_fmac_f32_e32 v54, s5, v80
	v_fmac_f32_e32 v53, s5, v81
	v_readlane_b32 s4, v76, 12
	v_readlane_b32 s5, v76, 28
	s_nop 0
	v_fmac_f32_e32 v46, s4, v48
	v_fmac_f32_e32 v47, s4, v49
	v_fmac_f32_e32 v44, s5, v80
	v_fmac_f32_e32 v45, s5, v81
	ds_read2st64_b32 v[48:49], v79 offset0:186 offset1:187
	ds_read2st64_b32 v[80:81], v79 offset0:218 offset1:219
	v_readlane_b32 s4, v71, 13
	v_readlane_b32 s5, v71, 29
	s_waitcnt lgkmcnt(1)
	v_fmac_f32_e32 v78, s4, v48
	v_fmac_f32_e32 v77, s4, v49
	s_waitcnt lgkmcnt(0)
	v_fmac_f32_e32 v75, s5, v80
	v_fmac_f32_e32 v74, s5, v81
	v_readlane_b32 s4, v72, 13
	v_readlane_b32 s5, v72, 29
	s_nop 0
	v_fmac_f32_e32 v70, s4, v48
	v_fmac_f32_e32 v51, s4, v49
	v_fmac_f32_e32 v50, s5, v80
	v_fmac_f32_e32 v69, s5, v81
	v_readlane_b32 s4, v73, 13
	v_readlane_b32 s5, v73, 29
	s_nop 0
	v_fmac_f32_e32 v68, s4, v48
	v_fmac_f32_e32 v55, s4, v49
	v_fmac_f32_e32 v54, s5, v80
	v_fmac_f32_e32 v53, s5, v81
	v_readlane_b32 s4, v76, 13
	v_readlane_b32 s5, v76, 29
	s_nop 0
	v_fmac_f32_e32 v46, s4, v48
	v_fmac_f32_e32 v47, s4, v49
	v_fmac_f32_e32 v44, s5, v80
	v_fmac_f32_e32 v45, s5, v81
	ds_read2st64_b32 v[48:49], v79 offset0:188 offset1:189
	ds_read2st64_b32 v[80:81], v79 offset0:220 offset1:221
	v_readlane_b32 s4, v71, 14
	v_readlane_b32 s5, v71, 30
	s_waitcnt lgkmcnt(1)
; __device__ __forceinline__ unsigned f2bf(float f) { unsigned u = __float_as_uint(f); return (u + 0x7fffu + ((u >> 16) & 1u)) >> 16; }
; __device__ __forceinline__ float logsigmoidf_(float x) { return fminf(x, 0.f) - __logf(1.f + __expf(-fabsf(x))); }
; __device__ __forceinline__ float rdlane_f(float v, int l) { return __builtin_bit_cast(float, __builtin_amdgcn_readlane(__builtin_bit_cast(int, v), l)); }
; __device__ __forceinline__ void ph_prep_tok(CArgs& a, int l, LAS unsigned char* lds, int gw, int ngw) {
;     ...
;         for (int i = 0; i < 16; ++i) { const float w0 = wa[i * 128 + lane], w1 = wa[i * 128 + 64 + lane], w2 = wa[2048 + i * 128 + lane], w3 = wa[2048 + i * 128 + 64 + lane];
; #pragma unroll
;             for (int r = 0; r < 4; ++r) { const float af = rdlane_f(av[r], i), ab = rdlane_f(av[r], 16 + i); s[r][0] += af * w0; s[r][1] += af * w1; s[r][2] += ab * w2; s[r][3] += ab * w3; } }
; #pragma unroll
;         for (int r = 0; r < 4; ++r) { const size_t o = (size_t)(row0 + r) * 128;
;             ((bf16*)GDF)[o + lane] = (bf16)f2bf(logsigmoidf_(s[r][0]) * 0.0625f); ((bf16*)GDF)[o + 64 + lane] = (bf16)f2bf(logsigmoidf_(s[r][1]) * 0.0625f);
;             ((bf16*)GDB)[o + lane] = (bf16)f2bf(logsigmoidf_(s[r][2]) * 0.0625f); ((bf16*)GDB)[o + 64 + lane] = (bf16)f2bf(logsigmoidf_(s[r][3]) * 0.0625f); }
	v_fmac_f32_e32 v78, s4, v48
	v_fmac_f32_e32 v77, s4, v49
	s_waitcnt lgkmcnt(0)
	v_fmac_f32_e32 v75, s5, v80
	v_fmac_f32_e32 v74, s5, v81
	v_readlane_b32 s4, v72, 14
	v_readlane_b32 s5, v72, 30
	s_nop 0
	v_fmac_f32_e32 v70, s4, v48
	v_fmac_f32_e32 v51, s4, v49
	v_fmac_f32_e32 v50, s5, v80
	v_fmac_f32_e32 v69, s5, v81
	v_readlane_b32 s4, v73, 14
	v_readlane_b32 s5, v73, 30
	s_nop 0
	v_fmac_f32_e32 v68, s4, v48
	v_fmac_f32_e32 v55, s4, v49
	v_fmac_f32_e32 v54, s5, v80
	v_fmac_f32_e32 v53, s5, v81
	v_readlane_b32 s4, v76, 14
	v_readlane_b32 s5, v76, 30
	s_nop 0
	v_fmac_f32_e32 v46, s4, v48
	v_fmac_f32_e32 v47, s4, v49
	v_fmac_f32_e32 v44, s5, v80
	v_fmac_f32_e32 v45, s5, v81
	ds_read2st64_b32 v[48:49], v79 offset0:190 offset1:191
	ds_read2st64_b32 v[80:81], v79 offset0:222 offset1:223
	v_readlane_b32 s4, v71, 15
	v_readlane_b32 s5, v71, 31
	s_waitcnt lgkmcnt(1)
	v_fmac_f32_e32 v78, s4, v48
	v_fmac_f32_e32 v77, s4, v49
	v_readlane_b32 s4, v72, 15
	s_waitcnt lgkmcnt(0)
	v_fmac_f32_e32 v75, s5, v80
	v_fmac_f32_e32 v74, s5, v81
	v_fmac_f32_e32 v70, s4, v48
	v_fmac_f32_e32 v51, s4, v49
	v_readlane_b32 s4, v73, 15
	v_readlane_b32 s5, v72, 31
	s_nop 0
	v_fmac_f32_e32 v68, s4, v48
	v_fmac_f32_e32 v55, s4, v49
	v_readlane_b32 s4, v76, 15
	v_fmac_f32_e32 v50, s5, v80
	v_fmac_f32_e32 v69, s5, v81
	v_fmac_f32_e32 v46, s4, v48
	v_fmac_f32_e32 v47, s4, v49
	s_mov_b32 s4, 0xbfb8aa3b
	v_mul_f32_e64 v49, |v78|, s4
	v_exp_f32_e32 v49, v49
	v_readlane_b32 s5, v73, 31
	v_min_f32_e32 v48, 0, v78
	v_add_f32_e32 v49, 1.0, v49
	v_cmp_gt_f32_e32 vcc, s21, v49
	v_fmac_f32_e32 v54, s5, v80
	v_fmac_f32_e32 v53, s5, v81
	v_cndmask_b32_e64 v71, 0, 32, vcc
	v_ldexp_f32 v49, v49, v71
	v_log_f32_e32 v49, v49
	v_readlane_b32 s5, v76, 31
	v_mul_f32_e64 v76, |v77|, s4
	v_exp_f32_e32 v76, v76
	v_fmac_f32_e32 v44, s5, v80
	v_fmac_f32_e32 v45, s5, v81
	v_mul_f32_e32 v71, 0x3f317217, v49
	s_mov_b32 s5, 0x3f317217
	v_fma_f32 v71, v49, s5, -v71
	v_fmac_f32_e32 v71, 0x3377d1cf, v49
	v_fmac_f32_e32 v71, 0x3f317217, v49
	v_cmp_lt_f32_e64 s[40:41], |v49|, s6
	v_add_f32_e32 v76, 1.0, v76
	s_nop 0
	v_cndmask_b32_e64 v49, v49, v71, s[40:41]
	v_cndmask_b32_e32 v71, 0, v193, vcc
	v_sub_f32_e32 v49, v49, v71
	v_sub_f32_e32 v48, v48, v49
	v_mul_f32_e32 v48, 0x3d800000, v48
	v_cvt_pk_bf16_f32 v71, v48, v48
	v_lshl_add_u64 v[48:49], s[2:3], 0, v[22:23]
	v_add_co_u32_e32 v72, vcc, s7, v48
	s_nop 1
	v_addc_co_u32_e32 v73, vcc, 0, v49, vcc
	v_cmp_gt_f32_e32 vcc, s21, v76
	global_store_short v[72:73], v71, off
	v_min_f32_e32 v71, 0, v77
	v_cndmask_b32_e64 v77, 0, 32, vcc
	v_ldexp_f32 v76, v76, v77
	v_log_f32_e32 v76, v76
	s_nop 0
	v_mul_f32_e32 v77, 0x3f317217, v76
	v_fma_f32 v77, v76, s5, -v77
	v_fmac_f32_e32 v77, 0x3377d1cf, v76
	v_fmac_f32_e32 v77, 0x3f317217, v76
	v_cmp_lt_f32_e64 s[40:41], |v76|, s6
	s_nop 1
	v_cndmask_b32_e64 v76, v76, v77, s[40:41]
	v_cndmask_b32_e32 v77, 0, v193, vcc
	v_sub_f32_e32 v76, v76, v77
	v_sub_f32_e32 v71, v71, v76
	v_mul_f32_e32 v71, 0x3d800000, v71
	v_cvt_pk_bf16_f32 v71, v71, v71
	global_store_short v[72:73], v71, off offset:128
	v_mul_f32_e64 v72, |v75|, s4
	v_exp_f32_e32 v72, v72
	v_min_f32_e32 v71, 0, v75
	v_add_f32_e32 v72, 1.0, v72
	v_cmp_gt_f32_e32 vcc, s21, v72
	s_nop 1
	v_cndmask_b32_e64 v73, 0, 32, vcc
	v_ldexp_f32 v72, v72, v73
	v_log_f32_e32 v72, v72
	s_nop 0
	v_mul_f32_e32 v73, 0x3f317217, v72
	v_fma_f32 v73, v72, s5, -v73
	v_fmac_f32_e32 v73, 0x3377d1cf, v72
	v_fmac_f32_e32 v73, 0x3f317217, v72
	v_cmp_lt_f32_e64 s[40:41], |v72|, s6
	s_nop 1
	v_cndmask_b32_e64 v72, v72, v73, s[40:41]
	v_cndmask_b32_e32 v73, 0, v193, vcc
	v_sub_f32_e32 v72, v72, v73
	v_sub_f32_e32 v71, v71, v72
	v_mul_f32_e32 v71, 0x3d800000, v71
	v_cvt_pk_bf16_f32 v71, v71, v71
	v_mul_f32_e64 v72, |v74|, s4
	v_exp_f32_e32 v72, v72
	v_add_co_u32_e32 v48, vcc, s11, v48
	v_add_f32_e32 v72, 1.0, v72
	s_nop 0
	v_addc_co_u32_e32 v49, vcc, 0, v49, vcc
	v_cmp_gt_f32_e32 vcc, s21, v72
	global_store_short v[48:49], v71, off
	v_min_f32_e32 v71, 0, v74
	v_cndmask_b32_e64 v73, 0, 32, vcc
	v_ldexp_f32 v72, v72, v73
	v_log_f32_e32 v72, v72
	s_nop 0
	v_mul_f32_e32 v73, 0x3f317217, v72
	v_fma_f32 v73, v72, s5, -v73
	v_fmac_f32_e32 v73, 0x3377d1cf, v72
	v_fmac_f32_e32 v73, 0x3f317217, v72
	v_cmp_lt_f32_e64 s[40:41], |v72|, s6
	s_nop 1
	v_cndmask_b32_e64 v72, v72, v73, s[40:41]
	v_cndmask_b32_e32 v73, 0, v193, vcc
	v_sub_f32_e32 v72, v72, v73
	v_sub_f32_e32 v71, v71, v72
	v_mul_f32_e32 v71, 0x3d800000, v71
	v_cvt_pk_bf16_f32 v71, v71, v71
	global_store_short v[48:49], v71, off offset:128
	v_mul_f32_e64 v49, |v70|, s4
	v_exp_f32_e32 v49, v49
	v_min_f32_e32 v48, 0, v70
	v_add_f32_e32 v49, 1.0, v49
	v_cmp_gt_f32_e32 vcc, s21, v49
	s_nop 1
	v_cndmask_b32_e64 v70, 0, 32, vcc
	v_ldexp_f32 v49, v49, v70
	v_log_f32_e32 v49, v49
	s_nop 0
	v_mul_f32_e32 v70, 0x3f317217, v49
	v_fma_f32 v70, v49, s5, -v70
	v_fmac_f32_e32 v70, 0x3377d1cf, v49
	v_fmac_f32_e32 v70, 0x3f317217, v49
	v_cmp_lt_f32_e64 s[40:41], |v49|, s6
	s_nop 1
	v_cndmask_b32_e64 v49, v49, v70, s[40:41]
	v_cndmask_b32_e32 v70, 0, v193, vcc
	v_sub_f32_e32 v49, v49, v70
	v_sub_f32_e32 v48, v48, v49
	v_mul_f32_e32 v48, 0x3d800000, v48
	v_lshl_add_u64 v[70:71], s[2:3], 0, v[18:19]
	v_cvt_pk_bf16_f32 v72, v48, v48
	v_add_co_u32_e32 v48, vcc, s7, v70
	s_nop 1
	v_addc_co_u32_e32 v49, vcc, 0, v71, vcc
	global_store_short v[48:49], v72, off offset:256
	v_min_f32_e32 v72, 0, v51
	v_mul_f32_e64 v51, |v51|, s4
	v_exp_f32_e32 v51, v51
	s_nop 0
	v_add_f32_e32 v51, 1.0, v51
	v_cmp_gt_f32_e32 vcc, s21, v51
	s_nop 1
	v_cndmask_b32_e64 v73, 0, 32, vcc
	v_ldexp_f32 v51, v51, v73
	v_log_f32_e32 v51, v51
	s_nop 0
	v_mul_f32_e32 v73, 0x3f317217, v51
	v_fma_f32 v73, v51, s5, -v73
; __device__ __forceinline__ unsigned f2bf(float f) { unsigned u = __float_as_uint(f); return (u + 0x7fffu + ((u >> 16) & 1u)) >> 16; }
; __device__ __forceinline__ float logsigmoidf_(float x) { return fminf(x, 0.f) - __logf(1.f + __expf(-fabsf(x))); }
; __device__ __forceinline__ void ph_prep_tok(CArgs& a, int l, LAS unsigned char* lds, int gw, int ngw) {
;     ...
;         for (int r = 0; r < 4; ++r) { const size_t o = (size_t)(row0 + r) * 128;
;             ((bf16*)GDF)[o + lane] = (bf16)f2bf(logsigmoidf_(s[r][0]) * 0.0625f); ((bf16*)GDF)[o + 64 + lane] = (bf16)f2bf(logsigmoidf_(s[r][1]) * 0.0625f);
;             ((bf16*)GDB)[o + lane] = (bf16)f2bf(logsigmoidf_(s[r][2]) * 0.0625f); ((bf16*)GDB)[o + 64 + lane] = (bf16)f2bf(logsigmoidf_(s[r][3]) * 0.0625f); }
	v_fmac_f32_e32 v73, 0x3377d1cf, v51
	v_fmac_f32_e32 v73, 0x3f317217, v51
	v_cmp_lt_f32_e64 s[40:41], |v51|, s6
	s_nop 1
	v_cndmask_b32_e64 v51, v51, v73, s[40:41]
	v_cndmask_b32_e32 v73, 0, v193, vcc
	v_sub_f32_e32 v51, v51, v73
	v_sub_f32_e32 v51, v72, v51
	v_mul_f32_e32 v51, 0x3d800000, v51
	v_cvt_pk_bf16_f32 v51, v51, v51
	global_store_short v[48:49], v51, off offset:384
	v_min_f32_e32 v51, 0, v50
	v_mul_f32_e64 v50, |v50|, s4
	v_exp_f32_e32 v50, v50
	s_nop 0
	v_add_f32_e32 v50, 1.0, v50
	v_cmp_gt_f32_e32 vcc, s21, v50
	s_nop 1
	v_cndmask_b32_e64 v72, 0, 32, vcc
	v_ldexp_f32 v50, v50, v72
	v_log_f32_e32 v50, v50
	s_nop 0
	v_mul_f32_e32 v72, 0x3f317217, v50
	v_fma_f32 v72, v50, s5, -v72
	v_fmac_f32_e32 v72, 0x3377d1cf, v50
	v_fmac_f32_e32 v72, 0x3f317217, v50
	v_cmp_lt_f32_e64 s[40:41], |v50|, s6
	s_nop 1
	v_cndmask_b32_e64 v50, v50, v72, s[40:41]
	v_cndmask_b32_e32 v72, 0, v193, vcc
	v_sub_f32_e32 v50, v50, v72
	v_sub_f32_e32 v50, v51, v50
	v_mul_f32_e32 v50, 0x3d800000, v50
	v_cvt_pk_bf16_f32 v72, v50, v50
	v_add_co_u32_e32 v50, vcc, s11, v70
	v_min_f32_e32 v70, 0, v69
	v_mul_f32_e64 v69, |v69|, s4
	v_exp_f32_e32 v69, v69
	v_addc_co_u32_e32 v51, vcc, 0, v71, vcc
	global_store_short v[50:51], v72, off offset:256
	v_add_f32_e32 v69, 1.0, v69
	v_cmp_gt_f32_e32 vcc, s21, v69
	s_nop 1
	v_cndmask_b32_e64 v71, 0, 32, vcc
	v_ldexp_f32 v69, v69, v71
	v_log_f32_e32 v69, v69
	s_nop 0
	v_mul_f32_e32 v71, 0x3f317217, v69
	v_fma_f32 v71, v69, s5, -v71
	v_fmac_f32_e32 v71, 0x3377d1cf, v69
	v_fmac_f32_e32 v71, 0x3f317217, v69
	v_cmp_lt_f32_e64 s[40:41], |v69|, s6
	s_nop 1
	v_cndmask_b32_e64 v69, v69, v71, s[40:41]
	v_cndmask_b32_e32 v71, 0, v193, vcc
	v_sub_f32_e32 v69, v69, v71
	v_sub_f32_e32 v69, v70, v69
	v_mul_f32_e32 v69, 0x3d800000, v69
	v_cvt_pk_bf16_f32 v69, v69, v69
	global_store_short v[50:51], v69, off offset:384
	v_min_f32_e32 v69, 0, v68
	v_mul_f32_e64 v68, |v68|, s4
	v_exp_f32_e32 v68, v68
	s_nop 0
	v_add_f32_e32 v68, 1.0, v68
	v_cmp_gt_f32_e32 vcc, s21, v68
	s_nop 1
	v_cndmask_b32_e64 v70, 0, 32, vcc
	v_ldexp_f32 v68, v68, v70
	v_log_f32_e32 v68, v68
	s_nop 0
	v_mul_f32_e32 v70, 0x3f317217, v68
	v_fma_f32 v70, v68, s5, -v70
	v_fmac_f32_e32 v70, 0x3377d1cf, v68
	v_fmac_f32_e32 v70, 0x3f317217, v68
	v_cmp_lt_f32_e64 s[40:41], |v68|, s6
	s_nop 1
	v_cndmask_b32_e64 v68, v68, v70, s[40:41]
	v_cndmask_b32_e32 v70, 0, v193, vcc
	v_sub_f32_e32 v68, v68, v70
	v_sub_f32_e32 v68, v69, v68
	v_mul_f32_e32 v68, 0x3d800000, v68
	v_cvt_pk_bf16_f32 v68, v68, v68
	global_store_short v[48:49], v68, off offset:512
	v_min_f32_e32 v68, 0, v55
	v_mul_f32_e64 v55, |v55|, s4
	v_exp_f32_e32 v55, v55
	s_nop 0
	v_add_f32_e32 v55, 1.0, v55
	v_cmp_gt_f32_e32 vcc, s21, v55
	s_nop 1
	v_cndmask_b32_e64 v69, 0, 32, vcc
	v_ldexp_f32 v55, v55, v69
	v_log_f32_e32 v55, v55
	s_nop 0
	v_mul_f32_e32 v69, 0x3f317217, v55
	v_fma_f32 v69, v55, s5, -v69
	v_fmac_f32_e32 v69, 0x3377d1cf, v55
	v_fmac_f32_e32 v69, 0x3f317217, v55
	v_cmp_lt_f32_e64 s[40:41], |v55|, s6
	s_nop 1
	v_cndmask_b32_e64 v55, v55, v69, s[40:41]
	v_cndmask_b32_e32 v69, 0, v193, vcc
	v_sub_f32_e32 v55, v55, v69
	v_sub_f32_e32 v55, v68, v55
	v_mul_f32_e32 v55, 0x3d800000, v55
	v_cvt_pk_bf16_f32 v55, v55, v55
	global_store_short v[48:49], v55, off offset:640
	v_min_f32_e32 v55, 0, v54
	v_mul_f32_e64 v54, |v54|, s4
	v_exp_f32_e32 v54, v54
	s_nop 0
	v_add_f32_e32 v54, 1.0, v54
	v_cmp_gt_f32_e32 vcc, s21, v54
	s_nop 1
	v_cndmask_b32_e64 v68, 0, 32, vcc
	v_ldexp_f32 v54, v54, v68
	v_log_f32_e32 v54, v54
	s_nop 0
	v_mul_f32_e32 v68, 0x3f317217, v54
	v_fma_f32 v68, v54, s5, -v68
	v_fmac_f32_e32 v68, 0x3377d1cf, v54
	v_fmac_f32_e32 v68, 0x3f317217, v54
	v_cmp_lt_f32_e64 s[40:41], |v54|, s6
	s_nop 1
	v_cndmask_b32_e64 v54, v54, v68, s[40:41]
	v_cndmask_b32_e32 v68, 0, v193, vcc
	v_sub_f32_e32 v54, v54, v68
	v_sub_f32_e32 v54, v55, v54
	v_mul_f32_e32 v54, 0x3d800000, v54
	v_cvt_pk_bf16_f32 v54, v54, v54
	global_store_short v[50:51], v54, off offset:512
	v_min_f32_e32 v54, 0, v53
	v_mul_f32_e64 v53, |v53|, s4
	v_exp_f32_e32 v53, v53
	s_nop 0
	v_add_f32_e32 v53, 1.0, v53
	v_cmp_gt_f32_e32 vcc, s21, v53
	s_nop 1
	v_cndmask_b32_e64 v55, 0, 32, vcc
	v_ldexp_f32 v53, v53, v55
	v_log_f32_e32 v53, v53
	s_nop 0
	v_mul_f32_e32 v55, 0x3f317217, v53
	v_fma_f32 v55, v53, s5, -v55
	v_fmac_f32_e32 v55, 0x3377d1cf, v53
	v_fmac_f32_e32 v55, 0x3f317217, v53
	v_cmp_lt_f32_e64 s[40:41], |v53|, s6
	s_nop 1
	v_cndmask_b32_e64 v53, v53, v55, s[40:41]
	v_cndmask_b32_e32 v55, 0, v193, vcc
	v_sub_f32_e32 v53, v53, v55
	v_sub_f32_e32 v53, v54, v53
	v_mul_f32_e32 v53, 0x3d800000, v53
	v_cvt_pk_bf16_f32 v53, v53, v53
	global_store_short v[50:51], v53, off offset:640
	v_min_f32_e32 v53, 0, v46
	v_mul_f32_e64 v46, |v46|, s4
	v_exp_f32_e32 v46, v46
	s_nop 0
	v_add_f32_e32 v46, 1.0, v46
	v_cmp_gt_f32_e32 vcc, s21, v46
	s_nop 1
	v_cndmask_b32_e64 v54, 0, 32, vcc
	v_ldexp_f32 v46, v46, v54
	v_log_f32_e32 v46, v46
	s_nop 0
	v_mul_f32_e32 v54, 0x3f317217, v46
	v_fma_f32 v54, v46, s5, -v54
	v_fmac_f32_e32 v54, 0x3377d1cf, v46
	v_fmac_f32_e32 v54, 0x3f317217, v46
	v_cmp_lt_f32_e64 s[40:41], |v46|, s6
	s_nop 1
	v_cndmask_b32_e64 v46, v46, v54, s[40:41]
	v_cndmask_b32_e32 v54, 0, v193, vcc
	v_sub_f32_e32 v46, v46, v54
	v_sub_f32_e32 v46, v53, v46
	v_mul_f32_e32 v46, 0x3d800000, v46
	v_cvt_pk_bf16_f32 v46, v46, v46
	global_store_short v[48:49], v46, off offset:768
	v_min_f32_e32 v46, 0, v47
	v_mul_f32_e64 v47, |v47|, s4
	v_exp_f32_e32 v47, v47
	s_nop 0
	v_add_f32_e32 v47, 1.0, v47
	v_cmp_gt_f32_e32 vcc, s21, v47
	s_nop 1
	v_cndmask_b32_e64 v53, 0, 32, vcc
	v_ldexp_f32 v47, v47, v53
	v_log_f32_e32 v47, v47
	s_nop 0
	v_mul_f32_e32 v53, 0x3f317217, v47
; #define LAS __attribute__((address_space(3)))
; __device__ __forceinline__ unsigned f2bf(float f) { unsigned u = __float_as_uint(f); return (u + 0x7fffu + ((u >> 16) & 1u)) >> 16; }
; __device__ __forceinline__ float logsigmoidf_(float x) { return fminf(x, 0.f) - __logf(1.f + __expf(-fabsf(x))); }
; __device__ __forceinline__ f32x4 bf4(u32x2 v) { return (f32x4){lo_bf(v.x), hi_bf(v.x), lo_bf(v.y), hi_bf(v.y)}; }
; __device__ __forceinline__ void ph_prep_tok(CArgs& a, int l, LAS unsigned char* lds, int gw, int ngw) {
;     ...
;         for (int r = 0; r < 4; ++r) { const size_t o = (size_t)(row0 + r) * 128;
;             ((bf16*)GDF)[o + lane] = (bf16)f2bf(logsigmoidf_(s[r][0]) * 0.0625f); ((bf16*)GDF)[o + 64 + lane] = (bf16)f2bf(logsigmoidf_(s[r][1]) * 0.0625f);
;             ((bf16*)GDB)[o + lane] = (bf16)f2bf(logsigmoidf_(s[r][2]) * 0.0625f); ((bf16*)GDB)[o + 64 + lane] = (bf16)f2bf(logsigmoidf_(s[r][3]) * 0.0625f); }
;         float sq[4] = {0.f, 0.f, 0.f, 0.f}, sk[4] = {0.f, 0.f, 0.f, 0.f}; f32x4 qv[4], kv[4];
; #pragma unroll
;         for (int g = 0; g < 3; ++g) { const int col = g * 256 + 4 * lane;
;             f32x4 x[6];
; #pragma unroll
;             for (int r = 0; r < 6; ++r) { const int t = tpos + r - 1; x[r] = (t >= lo && t < hi) ? bf4(xr[g][r]) : (f32x4){0.f, 0.f, 0.f, 0.f}; }
;             const f32x4 w0 = *(const LAS f32x4*)(cw + col), w1 = *(const LAS f32x4*)(cw + 768 + col), w2 = *(const LAS f32x4*)(cw + 1536 + col);
; #pragma unroll
;             for (int r = 0; r < 4; ++r) { f32x4 y = w0 * x[r] + w1 * x[r + 1] + w2 * x[r + 2];
	v_fma_f32 v53, v47, s5, -v53
	v_fmac_f32_e32 v53, 0x3377d1cf, v47
	v_fmac_f32_e32 v53, 0x3f317217, v47
	v_cmp_lt_f32_e64 s[40:41], |v47|, s6
	s_nop 1
	v_cndmask_b32_e64 v47, v47, v53, s[40:41]
	v_cndmask_b32_e32 v53, 0, v193, vcc
	v_sub_f32_e32 v47, v47, v53
	v_sub_f32_e32 v46, v46, v47
	v_mul_f32_e32 v46, 0x3d800000, v46
	v_cvt_pk_bf16_f32 v46, v46, v46
	global_store_short v[48:49], v46, off offset:896
	v_min_f32_e32 v46, 0, v44
	v_mul_f32_e64 v44, |v44|, s4
	v_exp_f32_e32 v44, v44
	v_and_b32_e32 v48, 0xffff0000, v39
	v_add_f32_e32 v44, 1.0, v44
	v_cmp_gt_f32_e32 vcc, s21, v44
	s_nop 1
	v_cndmask_b32_e64 v47, 0, 32, vcc
	v_ldexp_f32 v44, v44, v47
	v_log_f32_e32 v44, v44
	s_nop 0
	v_mul_f32_e32 v47, 0x3f317217, v44
	v_fma_f32 v47, v44, s5, -v47
	v_fmac_f32_e32 v47, 0x3377d1cf, v44
	v_fmac_f32_e32 v47, 0x3f317217, v44
	v_cmp_lt_f32_e64 s[40:41], |v44|, s6
	s_nop 1
	v_cndmask_b32_e64 v44, v44, v47, s[40:41]
	v_cndmask_b32_e32 v47, 0, v193, vcc
	v_sub_f32_e32 v44, v44, v47
	v_sub_f32_e32 v44, v46, v44
	v_mul_f32_e32 v44, 0x3d800000, v44
	v_cvt_pk_bf16_f32 v44, v44, v44
	global_store_short v[50:51], v44, off offset:768
	v_min_f32_e32 v44, 0, v45
	v_mul_f32_e64 v45, |v45|, s4
	v_exp_f32_e32 v45, v45
	v_lshlrev_b32_e32 v47, 16, v39
	v_add_f32_e32 v45, 1.0, v45
	v_cmp_gt_f32_e32 vcc, s21, v45
	s_nop 1
	v_cndmask_b32_e64 v46, 0, 32, vcc
	v_ldexp_f32 v45, v45, v46
	v_log_f32_e32 v45, v45
	s_nop 0
	v_mul_f32_e32 v46, 0x3f317217, v45
	v_fma_f32 v46, v45, s5, -v46
	s_cselect_b64 s[4:5], -1, 0
	s_cmp_gt_u32 s9, s1
	v_cmp_lt_f32_e64 s[40:41], |v45|, s6
	s_cselect_b64 s[6:7], -1, 0
	v_fmac_f32_e32 v46, 0x3377d1cf, v45
	s_or_b64 s[6:7], s[4:5], s[6:7]
	v_fmac_f32_e32 v46, 0x3f317217, v45
	s_cmp_lt_u32 s9, s8
	v_cndmask_b32_e64 v45, v45, v46, s[40:41]
	v_cndmask_b32_e32 v46, 0, v193, vcc
	s_cselect_b64 s[4:5], -1, 0
	s_cmp_ge_u32 s9, s1
	v_sub_f32_e32 v45, v45, v46
	s_cselect_b64 s[14:15], -1, 0
	v_sub_f32_e32 v44, v44, v45
	s_or_b64 s[4:5], s[4:5], s[14:15]
	v_mul_f32_e32 v44, 0x3d800000, v44
	s_cmp_le_u32 s10, s8
	s_cselect_b64 s[14:15], -1, 0
	s_cmp_gt_u32 s10, s1
	v_cvt_pk_bf16_f32 v44, v44, v44
	s_cselect_b64 s[10:11], -1, 0
	global_store_short v[50:51], v44, off offset:896
	v_lshlrev_b32_e32 v46, 16, v38
	v_and_b32_e32 v38, 0xffff0000, v38
	s_or_b64 s[14:15], s[14:15], s[10:11]
	s_add_i32 s10, s9, 5
	v_cndmask_b32_e64 v39, v38, 0, s[4:5]
	v_cndmask_b32_e64 v38, v46, 0, s[4:5]
	v_lshlrev_b32_e32 v46, 16, v42
	v_and_b32_e32 v42, 0xffff0000, v42
	s_cmp_le_u32 s10, s8
	ds_read_b128 v[74:77], v117 offset:58368
	ds_read_b128 v[78:81], v117 offset:61440
	ds_read_b128 v[82:85], v117 offset:64512
	v_cndmask_b32_e64 v49, v48, 0, s[4:5]
	v_cndmask_b32_e64 v48, v47, 0, s[4:5]
	v_lshlrev_b32_e32 v47, 16, v43
	v_and_b32_e32 v43, 0xffff0000, v43
	v_cndmask_b32_e64 v87, v42, 0, s[4:5]
	v_cndmask_b32_e64 v86, v46, 0, s[4:5]
	v_lshlrev_b32_e32 v42, 16, v32
	v_and_b32_e32 v32, 0xffff0000, v32
	v_lshlrev_b32_e32 v46, 16, v33
	s_cselect_b64 s[8:9], -1, 0
	s_cmp_gt_u32 s10, s1
	v_cndmask_b32_e64 v89, v43, 0, s[4:5]
	v_and_b32_e32 v43, 0xffff0000, v33
	v_cndmask_b32_e64 v33, v32, 0, s[14:15]
	v_cndmask_b32_e64 v32, v42, 0, s[14:15]
	v_cndmask_b32_e64 v42, v46, 0, s[14:15]
	v_lshlrev_b32_e32 v46, 16, v36
	s_cselect_b64 s[10:11], -1, 0
	v_lshlrev_b32_e32 v44, 16, v40
	v_and_b32_e32 v45, 0xffff0000, v40
	v_cndmask_b32_e64 v88, v47, 0, s[4:5]
	v_and_b32_e32 v36, 0xffff0000, v36
	v_lshlrev_b32_e32 v47, 16, v37
	v_and_b32_e32 v37, 0xffff0000, v37
	v_cndmask_b32_e64 v68, v46, 0, s[4:5]
	s_or_b64 s[26:27], s[8:9], s[10:11]
	v_and_b32_e32 v46, 0xffff0000, v31
	v_lshlrev_b32_e32 v40, 16, v41
	v_and_b32_e32 v41, 0xffff0000, v41
	v_cndmask_b32_e64 v45, v45, 0, s[6:7]
	v_cndmask_b32_e64 v44, v44, 0, s[6:7]
	v_cndmask_b32_e64 v69, v36, 0, s[4:5]
	v_cndmask_b32_e64 v71, v37, 0, s[4:5]
	v_cndmask_b32_e64 v70, v47, 0, s[4:5]
	v_lshlrev_b32_e32 v36, 16, v30
	v_and_b32_e32 v30, 0xffff0000, v30
	v_lshlrev_b32_e32 v37, 16, v31
	v_cndmask_b32_e64 v73, v46, 0, s[26:27]
	s_waitcnt lgkmcnt(1)
	v_pk_mul_f32 v[46:47], v[38:39], v[78:79]
	v_cndmask_b32_e64 v41, v41, 0, s[6:7]
	v_cndmask_b32_e64 v40, v40, 0, s[6:7]
	v_cndmask_b32_e64 v31, v30, 0, s[26:27]
	v_cndmask_b32_e64 v30, v36, 0, s[26:27]
	v_cndmask_b32_e64 v72, v37, 0, s[26:27]
	v_pk_mul_f32 v[36:37], v[48:49], v[80:81]
	v_pk_fma_f32 v[44:45], v[44:45], v[74:75], v[46:47]
	v_pk_fma_f32 v[36:37], v[40:41], v[76:77], v[36:37]
	s_waitcnt lgkmcnt(0)
; #define LAS __attribute__((address_space(3)))
; __device__ __forceinline__ float siluf_(float x) { return x / (1.f + __expf(-x)); }
; __device__ __forceinline__ f32x4 bf4(u32x2 v) { return (f32x4){lo_bf(v.x), hi_bf(v.x), lo_bf(v.y), hi_bf(v.y)}; }
; __device__ __forceinline__ void ph_prep_tok(CArgs& a, int l, LAS unsigned char* lds, int gw, int ngw) {
;     ...
;         for (int g = 0; g < 3; ++g) { const int col = g * 256 + 4 * lane;
;             f32x4 x[6];
; #pragma unroll
;             for (int r = 0; r < 6; ++r) { const int t = tpos + r - 1; x[r] = (t >= lo && t < hi) ? bf4(xr[g][r]) : (f32x4){0.f, 0.f, 0.f, 0.f}; }
;             const f32x4 w0 = *(const LAS f32x4*)(cw + col), w1 = *(const LAS f32x4*)(cw + 768 + col), w2 = *(const LAS f32x4*)(cw + 1536 + col);
; #pragma unroll
;             for (int r = 0; r < 4; ++r) { f32x4 y = w0 * x[r] + w1 * x[r + 1] + w2 * x[r + 2];
;                 y[0] = siluf_(y[0]); y[1] = siluf_(y[1]); y[2] = siluf_(y[2]); y[3] = siluf_(y[3]);
;                 if (g == 0) { qv[r] = y; sq[r] = (y[0] * y[0] + y[1] * y[1]) + (y[2] * y[2] + y[3] * y[3]); }
;                 else if (g == 1) { kv[r] = y; sk[r] = (y[0] * y[0] + y[1] * y[1]) + (y[2] * y[2] + y[3] * y[3]); }
	v_pk_fma_f32 v[40:41], v[86:87], v[82:83], v[44:45]
	v_pk_fma_f32 v[36:37], v[88:89], v[84:85], v[36:37]
	v_mul_f32_e32 v44, 0xbfb8aa3b, v40
	v_mul_f32_e32 v45, 0xbfb8aa3b, v41
	v_exp_f32_e32 v44, v44
	v_exp_f32_e32 v45, v45
	v_cndmask_b32_e64 v43, v43, 0, s[14:15]
	s_mov_b32 s1, 0x5e000000
	v_pk_add_f32 v[44:45], v[44:45], 1.0 op_sel_hi:[1,0]
	s_nop 0
	v_div_scale_f32 v46, s[8:9], v45, v45, v41
	v_rcp_f32_e32 v47, v46
	s_nop 0
	v_fma_f32 v50, -v46, v47, 1.0
	v_fmac_f32_e32 v47, v50, v47
	v_div_scale_f32 v50, vcc, v41, v45, v41
	v_mul_f32_e32 v51, v50, v47
	v_fma_f32 v52, -v46, v51, v50
	v_fmac_f32_e32 v51, v52, v47
	v_fma_f32 v46, -v46, v51, v50
	v_div_fmas_f32 v46, v46, v47, v51
	v_div_fixup_f32 v47, v46, v45, v41
	v_div_scale_f32 v41, s[8:9], v44, v44, v40
	v_rcp_f32_e32 v45, v41
	s_nop 0
	v_fma_f32 v46, -v41, v45, 1.0
	v_fmac_f32_e32 v45, v46, v45
	v_div_scale_f32 v46, vcc, v40, v44, v40
	v_mul_f32_e32 v50, v46, v45
	v_fma_f32 v51, -v41, v50, v46
	v_fmac_f32_e32 v50, v51, v45
	v_fma_f32 v41, -v41, v50, v46
	v_div_fmas_f32 v41, v41, v45, v50
	v_div_fixup_f32 v46, v41, v44, v40
	v_mul_f32_e32 v40, 0xbfb8aa3b, v36
	v_mul_f32_e32 v41, 0xbfb8aa3b, v37
	v_exp_f32_e32 v40, v40
	v_exp_f32_e32 v41, v41
	s_nop 0
	v_pk_add_f32 v[40:41], v[40:41], 1.0 op_sel_hi:[1,0]
	s_nop 0
	v_div_scale_f32 v44, s[8:9], v41, v41, v37
	v_rcp_f32_e32 v45, v44
	s_nop 0
	v_fma_f32 v50, -v44, v45, 1.0
	v_fmac_f32_e32 v45, v50, v45
	v_div_scale_f32 v50, vcc, v37, v41, v37
	v_mul_f32_e32 v51, v50, v45
	v_fma_f32 v52, -v44, v51, v50
	v_fmac_f32_e32 v51, v52, v45
	v_fma_f32 v44, -v44, v51, v50
	v_div_fmas_f32 v44, v44, v45, v51
	v_div_fixup_f32 v51, v44, v41, v37
	v_div_scale_f32 v37, s[8:9], v40, v40, v36
	v_rcp_f32_e32 v41, v37
	s_nop 0
	v_fma_f32 v44, -v37, v41, 1.0
	v_fmac_f32_e32 v41, v44, v41
	v_div_scale_f32 v44, vcc, v36, v40, v36
	v_mul_f32_e32 v45, v44, v41
	v_fma_f32 v50, -v37, v45, v44
	v_fmac_f32_e32 v45, v50, v41
	v_fma_f32 v37, -v37, v45, v44
	v_div_fmas_f32 v37, v37, v41, v45
	v_div_fixup_f32 v50, v37, v40, v36
	v_mov_b32_e32 v40, v47
	v_mov_b32_e32 v41, v51
	v_mov_b32_e32 v36, v46
	v_mov_b32_e32 v37, v50
	v_pk_mul_f32 v[40:41], v[40:41], v[40:41]
	s_nop 0
	v_pk_fma_f32 v[54:55], v[36:37], v[36:37], v[40:41]
	v_pk_mul_f32 v[40:41], v[86:87], v[78:79]
	v_pk_mul_f32 v[36:37], v[88:89], v[80:81]
	v_pk_fma_f32 v[38:39], v[38:39], v[74:75], v[40:41]
	v_pk_fma_f32 v[36:37], v[48:49], v[76:77], v[36:37]
	v_pk_fma_f32 v[38:39], v[32:33], v[82:83], v[38:39]
	v_pk_fma_f32 v[36:37], v[42:43], v[84:85], v[36:37]
	v_mul_f32_e32 v40, 0xbfb8aa3b, v38
	v_mul_f32_e32 v41, 0xbfb8aa3b, v39
	v_exp_f32_e32 v40, v40
	v_exp_f32_e32 v41, v41
	s_nop 0
	v_pk_add_f32 v[40:41], v[40:41], 1.0 op_sel_hi:[1,0]
	s_nop 0
	v_div_scale_f32 v44, s[8:9], v41, v41, v39
	v_rcp_f32_e32 v45, v44
	s_nop 0
	v_fma_f32 v48, -v44, v45, 1.0
	v_fmac_f32_e32 v45, v48, v45
	v_div_scale_f32 v48, vcc, v39, v41, v39
	v_mul_f32_e32 v49, v48, v45
	v_fma_f32 v52, -v44, v49, v48
	v_fmac_f32_e32 v49, v52, v45
	v_fma_f32 v44, -v44, v49, v48
	v_div_fmas_f32 v44, v44, v45, v49
	v_div_fixup_f32 v41, v44, v41, v39
	v_div_scale_f32 v39, s[8:9], v40, v40, v38
	v_rcp_f32_e32 v44, v39
	s_nop 0
	v_fma_f32 v45, -v39, v44, 1.0
	v_fmac_f32_e32 v44, v45, v44
	v_div_scale_f32 v45, vcc, v38, v40, v38
	v_mul_f32_e32 v48, v45, v44
	v_fma_f32 v49, -v39, v48, v45
	v_fmac_f32_e32 v48, v49, v44
	v_fma_f32 v39, -v39, v48, v45
	v_div_fmas_f32 v39, v39, v44, v48
	v_div_fixup_f32 v40, v39, v40, v38
	v_mul_f32_e32 v38, 0xbfb8aa3b, v36
	v_mul_f32_e32 v39, 0xbfb8aa3b, v37
	v_exp_f32_e32 v38, v38
	v_exp_f32_e32 v39, v39
	s_nop 0
	v_pk_add_f32 v[38:39], v[38:39], 1.0 op_sel_hi:[1,0]
	s_nop 0
	v_div_scale_f32 v44, s[8:9], v39, v39, v37
	v_rcp_f32_e32 v45, v44
	s_nop 0
	v_fma_f32 v48, -v44, v45, 1.0
	v_fmac_f32_e32 v45, v48, v45
	v_div_scale_f32 v48, vcc, v37, v39, v37
	v_mul_f32_e32 v49, v48, v45
	v_fma_f32 v52, -v44, v49, v48
	v_fmac_f32_e32 v49, v52, v45
	v_fma_f32 v44, -v44, v49, v48
	v_div_fmas_f32 v44, v44, v45, v49
	v_div_fixup_f32 v45, v44, v39, v37
	v_div_scale_f32 v37, s[8:9], v38, v38, v36
	v_rcp_f32_e32 v39, v37
	s_nop 0
	v_fma_f32 v44, -v37, v39, 1.0
	v_fmac_f32_e32 v39, v44, v39
	v_div_scale_f32 v44, vcc, v36, v38, v36
	v_mul_f32_e32 v48, v44, v39
	v_fma_f32 v49, -v37, v48, v44
	v_fmac_f32_e32 v48, v49, v39
	v_fma_f32 v37, -v37, v48, v44
	v_div_fmas_f32 v37, v37, v39, v48
	v_div_fixup_f32 v44, v37, v38, v36
	v_mov_b32_e32 v38, v41
	v_mov_b32_e32 v39, v45
	v_mov_b32_e32 v36, v40
	v_mov_b32_e32 v37, v44
	v_pk_mul_f32 v[38:39], v[38:39], v[38:39]
	s_nop 0
	v_pk_fma_f32 v[52:53], v[36:37], v[36:37], v[38:39]
	v_pk_mul_f32 v[36:37], v[42:43], v[80:81]
	v_pk_mul_f32 v[38:39], v[32:33], v[78:79]
	v_pk_fma_f32 v[36:37], v[88:89], v[76:77], v[36:37]
	v_pk_fma_f32 v[38:39], v[86:87], v[74:75], v[38:39]
	v_pk_fma_f32 v[48:49], v[70:71], v[84:85], v[36:37]
	v_pk_fma_f32 v[36:37], v[68:69], v[82:83], v[38:39]
	v_pk_mul_f32 v[68:69], v[68:69], v[78:79]
	v_mul_f32_e32 v38, 0xbfb8aa3b, v36
	v_mul_f32_e32 v39, 0xbfb8aa3b, v37
	v_exp_f32_e32 v38, v38
	v_exp_f32_e32 v39, v39
	v_pk_fma_f32 v[32:33], v[32:33], v[74:75], v[68:69]
	v_pk_mul_f32 v[70:71], v[70:71], v[80:81]
	v_pk_fma_f32 v[30:31], v[30:31], v[82:83], v[32:33]
	v_pk_add_f32 v[38:39], v[38:39], 1.0 op_sel_hi:[1,0]
	v_mul_f32_e32 v32, 0xbfb8aa3b, v30
	v_div_scale_f32 v86, s[8:9], v39, v39, v37
	v_rcp_f32_e32 v87, v86
	v_mul_f32_e32 v33, 0xbfb8aa3b, v31
	v_exp_f32_e32 v32, v32
	v_exp_f32_e32 v33, v33
	v_fma_f32 v88, -v86, v87, 1.0
	v_fmac_f32_e32 v87, v88, v87
	v_div_scale_f32 v88, vcc, v37, v39, v37
	v_mul_f32_e32 v89, v88, v87
	v_fma_f32 v90, -v86, v89, v88
	v_fmac_f32_e32 v89, v90, v87
; #define LAS __attribute__((address_space(3)))
; __device__ __forceinline__ float siluf_(float x) { return x / (1.f + __expf(-x)); }
; __device__ __forceinline__ f32x4 bf4(u32x2 v) { return (f32x4){lo_bf(v.x), hi_bf(v.x), lo_bf(v.y), hi_bf(v.y)}; }
; __device__ __forceinline__ void ph_prep_tok(CArgs& a, int l, LAS unsigned char* lds, int gw, int ngw) {
;     ...
;         for (int g = 0; g < 3; ++g) { const int col = g * 256 + 4 * lane;
;             f32x4 x[6];
; #pragma unroll
;             for (int r = 0; r < 6; ++r) { const int t = tpos + r - 1; x[r] = (t >= lo && t < hi) ? bf4(xr[g][r]) : (f32x4){0.f, 0.f, 0.f, 0.f}; }
;             const f32x4 w0 = *(const LAS f32x4*)(cw + col), w1 = *(const LAS f32x4*)(cw + 768 + col), w2 = *(const LAS f32x4*)(cw + 1536 + col);
; #pragma unroll
;             for (int r = 0; r < 4; ++r) { f32x4 y = w0 * x[r] + w1 * x[r + 1] + w2 * x[r + 2];
;                 y[0] = siluf_(y[0]); y[1] = siluf_(y[1]); y[2] = siluf_(y[2]); y[3] = siluf_(y[3]);
;                 if (g == 0) { qv[r] = y; sq[r] = (y[0] * y[0] + y[1] * y[1]) + (y[2] * y[2] + y[3] * y[3]); }
;                 else if (g == 1) { kv[r] = y; sk[r] = (y[0] * y[0] + y[1] * y[1]) + (y[2] * y[2] + y[3] * y[3]); }
	v_fma_f32 v86, -v86, v89, v88
	v_div_fmas_f32 v86, v86, v87, v89
	v_div_fixup_f32 v37, v86, v39, v37
	v_div_scale_f32 v39, s[8:9], v38, v38, v36
	v_rcp_f32_e32 v86, v39
	v_pk_add_f32 v[32:33], v[32:33], 1.0 op_sel_hi:[1,0]
	v_pk_fma_f32 v[42:43], v[42:43], v[76:77], v[70:71]
	v_div_scale_f32 v68, s[8:9], v33, v33, v31
	v_fma_f32 v87, -v39, v86, 1.0
	v_fmac_f32_e32 v86, v87, v86
	v_div_scale_f32 v87, vcc, v36, v38, v36
	v_mul_f32_e32 v88, v87, v86
	v_fma_f32 v89, -v39, v88, v87
	v_fmac_f32_e32 v88, v89, v86
	v_fma_f32 v39, -v39, v88, v87
	v_div_fmas_f32 v39, v39, v86, v88
	v_div_fixup_f32 v36, v39, v38, v36
	v_mul_f32_e32 v38, 0xbfb8aa3b, v48
	v_mul_f32_e32 v39, 0xbfb8aa3b, v49
	v_exp_f32_e32 v38, v38
	v_exp_f32_e32 v39, v39
	v_rcp_f32_e32 v69, v68
	v_pk_fma_f32 v[42:43], v[72:73], v[84:85], v[42:43]
	v_and_b32_e32 v74, 0xffff0000, v63
	v_pk_add_f32 v[38:39], v[38:39], 1.0 op_sel_hi:[1,0]
	v_fma_f32 v70, -v68, v69, 1.0
	v_div_scale_f32 v86, s[8:9], v39, v39, v49
	v_rcp_f32_e32 v87, v86
	v_fmac_f32_e32 v69, v70, v69
	v_fma_f32 v88, -v86, v87, 1.0
	v_fmac_f32_e32 v87, v88, v87
	v_div_scale_f32 v88, vcc, v49, v39, v49
	v_mul_f32_e32 v89, v88, v87
	v_fma_f32 v90, -v86, v89, v88
	v_fmac_f32_e32 v89, v90, v87
	v_fma_f32 v86, -v86, v89, v88
	v_div_fmas_f32 v86, v86, v87, v89
	v_div_fixup_f32 v39, v86, v39, v49
	v_div_scale_f32 v49, s[8:9], v38, v38, v48
	v_rcp_f32_e32 v86, v49
	s_nop 0
	v_fma_f32 v87, -v49, v86, 1.0
	v_fmac_f32_e32 v86, v87, v86
	v_div_scale_f32 v87, vcc, v48, v38, v48
	v_mul_f32_e32 v88, v87, v86
	v_fma_f32 v89, -v49, v88, v87
	v_fmac_f32_e32 v88, v89, v86
	v_fma_f32 v49, -v49, v88, v87
	v_div_fmas_f32 v49, v49, v86, v88
	v_div_scale_f32 v70, vcc, v31, v33, v31
	v_mul_f32_e32 v71, v70, v69
	v_fma_f32 v72, -v68, v71, v70
	v_fmac_f32_e32 v71, v72, v69
	v_fma_f32 v68, -v68, v71, v70
	v_div_fmas_f32 v68, v68, v69, v71
	v_div_fixup_f32 v31, v68, v33, v31
	v_div_scale_f32 v33, s[8:9], v32, v32, v30
	v_rcp_f32_e32 v68, v33
	v_div_fixup_f32 v38, v49, v38, v48
	v_mov_b32_e32 v86, v37
	v_mov_b32_e32 v87, v39
	v_fma_f32 v69, -v33, v68, 1.0
	v_fmac_f32_e32 v68, v69, v68
	v_div_scale_f32 v69, vcc, v30, v32, v30
	v_mul_f32_e32 v70, v69, v68
	v_fma_f32 v71, -v33, v70, v69
	v_fmac_f32_e32 v70, v71, v68
	v_fma_f32 v33, -v33, v70, v69
	v_div_fmas_f32 v33, v33, v68, v70
	v_div_fixup_f32 v30, v33, v32, v30
	v_mul_f32_e32 v32, 0xbfb8aa3b, v42
	v_mul_f32_e32 v33, 0xbfb8aa3b, v43
	v_exp_f32_e32 v32, v32
	v_exp_f32_e32 v33, v33
	v_mov_b32_e32 v48, v36
	v_mov_b32_e32 v49, v38
	v_pk_mul_f32 v[86:87], v[86:87], v[86:87]
	v_pk_add_f32 v[32:33], v[32:33], 1.0 op_sel_hi:[1,0]
	v_pk_fma_f32 v[48:49], v[48:49], v[48:49], v[86:87]
	v_div_scale_f32 v68, s[8:9], v33, v33, v43
	v_rcp_f32_e32 v69, v68
	v_cndmask_b32_e64 v89, v74, 0, s[4:5]
	v_fma_f32 v70, -v68, v69, 1.0
	v_fmac_f32_e32 v69, v70, v69
	v_div_scale_f32 v70, vcc, v43, v33, v43
	v_mul_f32_e32 v71, v70, v69
	v_fma_f32 v72, -v68, v71, v70
	v_fmac_f32_e32 v71, v72, v69
	v_fma_f32 v68, -v68, v71, v70
	v_div_fmas_f32 v68, v68, v69, v71
	v_div_fixup_f32 v33, v68, v33, v43
	v_div_scale_f32 v43, s[8:9], v32, v32, v42
	v_rcp_f32_e32 v68, v43
	v_and_b32_e32 v72, 0xffff0000, v65
	v_cndmask_b32_e64 v73, v72, 0, s[4:5]
	v_fma_f32 v69, -v43, v68, 1.0
	v_fmac_f32_e32 v68, v69, v68
	v_div_scale_f32 v69, vcc, v42, v32, v42
	v_mul_f32_e32 v70, v69, v68
	v_fma_f32 v71, -v43, v70, v69
	v_fmac_f32_e32 v70, v71, v68
	v_fma_f32 v43, -v43, v70, v69
	v_div_fmas_f32 v43, v43, v68, v70
	v_lshlrev_b32_e32 v70, 16, v64
	v_and_b32_e32 v64, 0xffff0000, v64
	v_lshlrev_b32_e32 v71, 16, v65
	v_cndmask_b32_e64 v65, v64, 0, s[4:5]
	v_cndmask_b32_e64 v64, v70, 0, s[4:5]
	v_cndmask_b32_e64 v72, v71, 0, s[4:5]
	v_lshlrev_b32_e32 v70, 16, v62
	v_and_b32_e32 v62, 0xffff0000, v62
	v_lshlrev_b32_e32 v71, 16, v63
	v_cndmask_b32_e64 v63, v62, 0, s[4:5]
	v_cndmask_b32_e64 v62, v70, 0, s[4:5]
	v_cndmask_b32_e64 v88, v71, 0, s[4:5]
	v_lshlrev_b32_e32 v70, 16, v60
	v_and_b32_e32 v60, 0xffff0000, v60
	v_lshlrev_b32_e32 v71, 16, v61
	v_and_b32_e32 v61, 0xffff0000, v61
	v_cndmask_b32_e64 v91, v60, 0, s[14:15]
	v_cndmask_b32_e64 v93, v61, 0, s[14:15]
	v_lshlrev_b32_e32 v60, 16, v58
	v_and_b32_e32 v58, 0xffff0000, v58
	v_lshlrev_b32_e32 v61, 16, v59
	v_and_b32_e32 v59, 0xffff0000, v59
	v_cndmask_b32_e64 v95, v58, 0, s[4:5]
	v_cndmask_b32_e64 v97, v59, 0, s[4:5]
	v_lshlrev_b32_e32 v58, 16, v56
	v_and_b32_e32 v56, 0xffff0000, v56
	v_lshlrev_b32_e32 v59, 16, v57
	v_and_b32_e32 v57, 0xffff0000, v57
	v_cndmask_b32_e64 v99, v56, 0, s[26:27]
	v_cndmask_b32_e64 v98, v58, 0, s[26:27]
	v_cndmask_b32_e64 v101, v57, 0, s[26:27]
	v_cndmask_b32_e64 v100, v59, 0, s[26:27]
	ds_read_b128 v[56:59], v117 offset:59392
	ds_read_b128 v[80:83], v117 offset:62464
	v_cndmask_b32_e64 v94, v60, 0, s[4:5]
	v_lshl_add_u32 v60, v111, 2, v116
	v_div_fixup_f32 v32, v43, v32, v42
	v_mov_b32_e32 v68, v31
	v_mov_b32_e32 v69, v33
	ds_read_b128 v[84:87], v60
	v_mov_b32_e32 v42, v30
	v_mov_b32_e32 v43, v32
	v_pk_mul_f32 v[68:69], v[68:69], v[68:69]
	v_cndmask_b32_e64 v90, v70, 0, s[14:15]
	v_pk_fma_f32 v[42:43], v[42:43], v[42:43], v[68:69]
	v_lshlrev_b32_e32 v68, 16, v66
	v_and_b32_e32 v69, 0xffff0000, v66
	v_lshlrev_b32_e32 v66, 16, v67
	v_and_b32_e32 v67, 0xffff0000, v67
	v_cndmask_b32_e64 v69, v69, 0, s[6:7]
	v_cndmask_b32_e64 v68, v68, 0, s[6:7]
	v_cndmask_b32_e64 v92, v71, 0, s[14:15]
	s_waitcnt lgkmcnt(1)
	v_pk_mul_f32 v[70:71], v[64:65], v[80:81]
	v_cndmask_b32_e64 v67, v67, 0, s[6:7]
	v_cndmask_b32_e64 v66, v66, 0, s[6:7]
	v_cndmask_b32_e64 v96, v61, 0, s[4:5]
	v_pk_mul_f32 v[60:61], v[72:73], v[82:83]
	v_pk_fma_f32 v[68:69], v[68:69], v[56:57], v[70:71]
	v_pk_fma_f32 v[60:61], v[66:67], v[58:59], v[60:61]
	s_waitcnt lgkmcnt(0)
; #define LAS __attribute__((address_space(3)))
; __device__ __forceinline__ float siluf_(float x) { return x / (1.f + __expf(-x)); }
; __device__ __forceinline__ f32x4 bf4(u32x2 v) { return (f32x4){lo_bf(v.x), hi_bf(v.x), lo_bf(v.y), hi_bf(v.y)}; }
; __device__ __forceinline__ void ph_prep_tok(CArgs& a, int l, LAS unsigned char* lds, int gw, int ngw) {
;     ...
;         for (int g = 0; g < 3; ++g) { const int col = g * 256 + 4 * lane;
;             f32x4 x[6];
; #pragma unroll
;             for (int r = 0; r < 6; ++r) { const int t = tpos + r - 1; x[r] = (t >= lo && t < hi) ? bf4(xr[g][r]) : (f32x4){0.f, 0.f, 0.f, 0.f}; }
;             const f32x4 w0 = *(const LAS f32x4*)(cw + col), w1 = *(const LAS f32x4*)(cw + 768 + col), w2 = *(const LAS f32x4*)(cw + 1536 + col);
; #pragma unroll
;             for (int r = 0; r < 4; ++r) { f32x4 y = w0 * x[r] + w1 * x[r + 1] + w2 * x[r + 2];
;                 y[0] = siluf_(y[0]); y[1] = siluf_(y[1]); y[2] = siluf_(y[2]); y[3] = siluf_(y[3]);
;                 if (g == 0) { qv[r] = y; sq[r] = (y[0] * y[0] + y[1] * y[1]) + (y[2] * y[2] + y[3] * y[3]); }
;                 else if (g == 1) { kv[r] = y; sk[r] = (y[0] * y[0] + y[1] * y[1]) + (y[2] * y[2] + y[3] * y[3]); }
	v_pk_fma_f32 v[66:67], v[62:63], v[84:85], v[68:69]
	v_pk_fma_f32 v[60:61], v[88:89], v[86:87], v[60:61]
	v_mul_f32_e32 v68, 0xbfb8aa3b, v66
	v_mul_f32_e32 v69, 0xbfb8aa3b, v67
	v_exp_f32_e32 v68, v68
	v_exp_f32_e32 v69, v69
	s_nop 0
	v_pk_add_f32 v[68:69], v[68:69], 1.0 op_sel_hi:[1,0]
	s_nop 0
	v_div_scale_f32 v70, s[8:9], v69, v69, v67
	v_rcp_f32_e32 v71, v70
	s_nop 0
	v_fma_f32 v74, -v70, v71, 1.0
	v_fmac_f32_e32 v71, v74, v71
	v_div_scale_f32 v74, vcc, v67, v69, v67
	v_mul_f32_e32 v75, v74, v71
	v_fma_f32 v76, -v70, v75, v74
	v_fmac_f32_e32 v75, v76, v71
	v_fma_f32 v70, -v70, v75, v74
	v_div_fmas_f32 v70, v70, v71, v75
	v_div_fixup_f32 v71, v70, v69, v67
	v_div_scale_f32 v67, s[8:9], v68, v68, v66
	v_rcp_f32_e32 v69, v67
	s_nop 0
	v_fma_f32 v70, -v67, v69, 1.0
	v_fmac_f32_e32 v69, v70, v69
	v_div_scale_f32 v70, vcc, v66, v68, v66
	v_mul_f32_e32 v74, v70, v69
	v_fma_f32 v75, -v67, v74, v70
	v_fmac_f32_e32 v74, v75, v69
	v_fma_f32 v67, -v67, v74, v70
	v_div_fmas_f32 v67, v67, v69, v74
	v_div_fixup_f32 v70, v67, v68, v66
	v_mul_f32_e32 v66, 0xbfb8aa3b, v60
	v_mul_f32_e32 v67, 0xbfb8aa3b, v61
	v_exp_f32_e32 v66, v66
	v_exp_f32_e32 v67, v67
	s_nop 0
	v_pk_add_f32 v[66:67], v[66:67], 1.0 op_sel_hi:[1,0]
	s_nop 0
	v_div_scale_f32 v68, s[8:9], v67, v67, v61
	v_rcp_f32_e32 v69, v68
	s_nop 0
	v_fma_f32 v74, -v68, v69, 1.0
	v_fmac_f32_e32 v69, v74, v69
	v_div_scale_f32 v74, vcc, v61, v67, v61
	v_mul_f32_e32 v75, v74, v69
	v_fma_f32 v76, -v68, v75, v74
	v_fmac_f32_e32 v75, v76, v69
	v_fma_f32 v68, -v68, v75, v74
	v_div_fmas_f32 v68, v68, v69, v75
	v_div_fixup_f32 v75, v68, v67, v61
	v_div_scale_f32 v61, s[8:9], v66, v66, v60
	v_rcp_f32_e32 v67, v61
	s_nop 0
	v_fma_f32 v68, -v61, v67, 1.0
	v_fmac_f32_e32 v67, v68, v67
	v_div_scale_f32 v68, vcc, v60, v66, v60
	v_mul_f32_e32 v69, v68, v67
	v_fma_f32 v74, -v61, v69, v68
	v_fmac_f32_e32 v69, v74, v67
	v_fma_f32 v61, -v61, v69, v68
	v_div_fmas_f32 v61, v61, v67, v69
	v_div_fixup_f32 v74, v61, v66, v60
	v_mov_b32_e32 v66, v71
	v_mov_b32_e32 v67, v75
	v_mov_b32_e32 v60, v70
	v_mov_b32_e32 v61, v74
	v_pk_mul_f32 v[66:67], v[66:67], v[66:67]
	s_nop 0
	v_pk_fma_f32 v[78:79], v[60:61], v[60:61], v[66:67]
	v_pk_mul_f32 v[66:67], v[62:63], v[80:81]
	v_pk_mul_f32 v[60:61], v[88:89], v[82:83]
	v_pk_fma_f32 v[64:65], v[64:65], v[56:57], v[66:67]
	v_pk_fma_f32 v[60:61], v[72:73], v[58:59], v[60:61]
	v_pk_fma_f32 v[64:65], v[90:91], v[84:85], v[64:65]
	v_pk_fma_f32 v[60:61], v[92:93], v[86:87], v[60:61]
	v_mul_f32_e32 v66, 0xbfb8aa3b, v64
	v_mul_f32_e32 v67, 0xbfb8aa3b, v65
	v_exp_f32_e32 v66, v66
	v_exp_f32_e32 v67, v67
	s_nop 0
	v_pk_add_f32 v[66:67], v[66:67], 1.0 op_sel_hi:[1,0]
	s_nop 0
	v_div_scale_f32 v68, s[8:9], v67, v67, v65
	v_rcp_f32_e32 v69, v68
	s_nop 0
	v_fma_f32 v72, -v68, v69, 1.0
	v_fmac_f32_e32 v69, v72, v69
	v_div_scale_f32 v72, vcc, v65, v67, v65
	v_mul_f32_e32 v73, v72, v69
	v_fma_f32 v76, -v68, v73, v72
	v_fmac_f32_e32 v73, v76, v69
	v_fma_f32 v68, -v68, v73, v72
	v_div_fmas_f32 v68, v68, v69, v73
	v_div_fixup_f32 v65, v68, v67, v65
	v_div_scale_f32 v67, s[8:9], v66, v66, v64
	v_rcp_f32_e32 v68, v67
	s_nop 0
	v_fma_f32 v69, -v67, v68, 1.0
	v_fmac_f32_e32 v68, v69, v68
	v_div_scale_f32 v69, vcc, v64, v66, v64
	v_mul_f32_e32 v72, v69, v68
	v_fma_f32 v73, -v67, v72, v69
	v_fmac_f32_e32 v72, v73, v68
	v_fma_f32 v67, -v67, v72, v69
	v_div_fmas_f32 v67, v67, v68, v72
	v_div_fixup_f32 v64, v67, v66, v64
	v_mul_f32_e32 v66, 0xbfb8aa3b, v60
	v_mul_f32_e32 v67, 0xbfb8aa3b, v61
	v_exp_f32_e32 v66, v66
	v_exp_f32_e32 v67, v67
	s_nop 0
	v_pk_add_f32 v[66:67], v[66:67], 1.0 op_sel_hi:[1,0]
	s_nop 0
	v_div_scale_f32 v68, s[8:9], v67, v67, v61
	v_rcp_f32_e32 v69, v68
	s_nop 0
	v_fma_f32 v72, -v68, v69, 1.0
	v_fmac_f32_e32 v69, v72, v69
	v_div_scale_f32 v72, vcc, v61, v67, v61
	v_mul_f32_e32 v73, v72, v69
	v_fma_f32 v76, -v68, v73, v72
	v_fmac_f32_e32 v73, v76, v69
	v_fma_f32 v68, -v68, v73, v72
	v_div_fmas_f32 v68, v68, v69, v73
	v_div_fixup_f32 v67, v68, v67, v61
	v_div_scale_f32 v61, s[8:9], v66, v66, v60
	v_rcp_f32_e32 v68, v61
	s_nop 0
	v_fma_f32 v69, -v61, v68, 1.0
	v_fmac_f32_e32 v68, v69, v68
	v_div_scale_f32 v69, vcc, v60, v66, v60
	v_mul_f32_e32 v72, v69, v68
	v_fma_f32 v73, -v61, v72, v69
	v_fmac_f32_e32 v72, v73, v68
	v_fma_f32 v61, -v61, v72, v69
	v_div_fmas_f32 v61, v61, v68, v72
	v_div_fixup_f32 v66, v61, v66, v60
	v_mov_b32_e32 v68, v65
	v_mov_b32_e32 v69, v67
	v_mov_b32_e32 v60, v64
	v_mov_b32_e32 v61, v66
	v_pk_mul_f32 v[68:69], v[68:69], v[68:69]
	s_nop 0
	v_pk_fma_f32 v[76:77], v[60:61], v[60:61], v[68:69]
	v_pk_mul_f32 v[60:61], v[92:93], v[82:83]
	v_pk_mul_f32 v[68:69], v[90:91], v[80:81]
	v_pk_fma_f32 v[60:61], v[88:89], v[58:59], v[60:61]
	v_pk_fma_f32 v[62:63], v[62:63], v[56:57], v[68:69]
	v_pk_fma_f32 v[68:69], v[96:97], v[86:87], v[60:61]
	v_pk_fma_f32 v[60:61], v[94:95], v[84:85], v[62:63]
	v_pk_mul_f32 v[80:81], v[94:95], v[80:81]
	v_mul_f32_e32 v62, 0xbfb8aa3b, v60
	v_mul_f32_e32 v63, 0xbfb8aa3b, v61
	v_exp_f32_e32 v62, v62
	v_exp_f32_e32 v63, v63
	v_pk_fma_f32 v[56:57], v[90:91], v[56:57], v[80:81]
	v_pk_add_f32 v[62:63], v[62:63], 1.0 op_sel_hi:[1,0]
	s_nop 0
	v_div_scale_f32 v72, s[8:9], v63, v63, v61
	v_rcp_f32_e32 v73, v72
	v_pk_fma_f32 v[56:57], v[98:99], v[84:85], v[56:57]
	v_fma_f32 v88, -v72, v73, 1.0
	v_fmac_f32_e32 v73, v88, v73
	v_div_scale_f32 v88, vcc, v61, v63, v61
	v_mul_f32_e32 v89, v88, v73
	v_fma_f32 v102, -v72, v89, v88
	v_fmac_f32_e32 v89, v102, v73
	v_fma_f32 v72, -v72, v89, v88
	v_div_fmas_f32 v72, v72, v73, v89
	v_div_fixup_f32 v61, v72, v63, v61
	v_div_scale_f32 v63, s[8:9], v62, v62, v60
	v_rcp_f32_e32 v72, v63
	s_nop 0
	v_fma_f32 v73, -v63, v72, 1.0
; #define LAS __attribute__((address_space(3)))
; __device__ __forceinline__ float siluf_(float x) { return x / (1.f + __expf(-x)); }
; __device__ __forceinline__ f32x4 bf4(u32x2 v) { return (f32x4){lo_bf(v.x), hi_bf(v.x), lo_bf(v.y), hi_bf(v.y)}; }
; __device__ __forceinline__ void ph_prep_tok(CArgs& a, int l, LAS unsigned char* lds, int gw, int ngw) {
;     ...
;         for (int g = 0; g < 3; ++g) { const int col = g * 256 + 4 * lane;
;             f32x4 x[6];
; #pragma unroll
;             for (int r = 0; r < 6; ++r) { const int t = tpos + r - 1; x[r] = (t >= lo && t < hi) ? bf4(xr[g][r]) : (f32x4){0.f, 0.f, 0.f, 0.f}; }
;             const f32x4 w0 = *(const LAS f32x4*)(cw + col), w1 = *(const LAS f32x4*)(cw + 768 + col), w2 = *(const LAS f32x4*)(cw + 1536 + col);
; #pragma unroll
;             for (int r = 0; r < 4; ++r) { f32x4 y = w0 * x[r] + w1 * x[r + 1] + w2 * x[r + 2];
;                 y[0] = siluf_(y[0]); y[1] = siluf_(y[1]); y[2] = siluf_(y[2]); y[3] = siluf_(y[3]);
;                 if (g == 0) { qv[r] = y; sq[r] = (y[0] * y[0] + y[1] * y[1]) + (y[2] * y[2] + y[3] * y[3]); }
;                 else if (g == 1) { kv[r] = y; sk[r] = (y[0] * y[0] + y[1] * y[1]) + (y[2] * y[2] + y[3] * y[3]); }
	v_fmac_f32_e32 v72, v73, v72
	v_div_scale_f32 v73, vcc, v60, v62, v60
	v_mul_f32_e32 v88, v73, v72
	v_fma_f32 v89, -v63, v88, v73
	v_fmac_f32_e32 v88, v89, v72
	v_fma_f32 v63, -v63, v88, v73
	v_div_fmas_f32 v63, v63, v72, v88
	v_div_fixup_f32 v60, v63, v62, v60
	v_mul_f32_e32 v62, 0xbfb8aa3b, v68
	v_mul_f32_e32 v63, 0xbfb8aa3b, v69
	v_exp_f32_e32 v62, v62
	v_exp_f32_e32 v63, v63
	s_nop 0
	v_pk_add_f32 v[62:63], v[62:63], 1.0 op_sel_hi:[1,0]
	s_nop 0
	v_div_scale_f32 v72, s[8:9], v63, v63, v69
	v_rcp_f32_e32 v73, v72
	s_nop 0
	v_fma_f32 v88, -v72, v73, 1.0
	v_fmac_f32_e32 v73, v88, v73
	v_div_scale_f32 v88, vcc, v69, v63, v69
	v_mul_f32_e32 v89, v88, v73
	v_fma_f32 v102, -v72, v89, v88
	v_fmac_f32_e32 v89, v102, v73
	v_fma_f32 v72, -v72, v89, v88
	v_div_fmas_f32 v72, v72, v73, v89
	v_div_fixup_f32 v63, v72, v63, v69
	v_div_scale_f32 v69, s[8:9], v62, v62, v68
	v_rcp_f32_e32 v72, v69
	s_nop 0
	v_fma_f32 v73, -v69, v72, 1.0
	v_fmac_f32_e32 v72, v73, v72
	v_div_scale_f32 v73, vcc, v68, v62, v68
	v_mul_f32_e32 v88, v73, v72
	v_fma_f32 v89, -v69, v88, v73
	v_fmac_f32_e32 v88, v89, v72
	v_fma_f32 v69, -v69, v88, v73
	v_div_fmas_f32 v69, v69, v72, v88
	v_div_fixup_f32 v62, v69, v62, v68
	v_mov_b32_e32 v72, v61
	v_mov_b32_e32 v73, v63
	v_mov_b32_e32 v68, v60
	v_mov_b32_e32 v69, v62
	v_pk_mul_f32 v[72:73], v[72:73], v[72:73]
	s_nop 0
	v_pk_fma_f32 v[72:73], v[68:69], v[68:69], v[72:73]
	v_pk_mul_f32 v[68:69], v[96:97], v[82:83]
	s_nop 0
	v_pk_fma_f32 v[58:59], v[92:93], v[58:59], v[68:69]
	v_mul_f32_e32 v68, 0xbfb8aa3b, v56
	v_mul_f32_e32 v69, 0xbfb8aa3b, v57
	v_exp_f32_e32 v68, v68
	v_exp_f32_e32 v69, v69
	v_pk_fma_f32 v[58:59], v[100:101], v[86:87], v[58:59]
	v_pk_add_f32 v[68:69], v[68:69], 1.0 op_sel_hi:[1,0]
	s_nop 0
	v_div_scale_f32 v80, s[8:9], v69, v69, v57
	v_rcp_f32_e32 v81, v80
	s_nop 0
	v_fma_f32 v82, -v80, v81, 1.0
	v_fmac_f32_e32 v81, v82, v81
	v_div_scale_f32 v82, vcc, v57, v69, v57
	v_mul_f32_e32 v83, v82, v81
	v_fma_f32 v84, -v80, v83, v82
	v_fmac_f32_e32 v83, v84, v81
	v_fma_f32 v80, -v80, v83, v82
	v_div_fmas_f32 v80, v80, v81, v83
	v_div_fixup_f32 v57, v80, v69, v57
	v_div_scale_f32 v69, s[8:9], v68, v68, v56
	v_rcp_f32_e32 v80, v69
	s_nop 0
	v_fma_f32 v81, -v69, v80, 1.0
	v_fmac_f32_e32 v80, v81, v80
	v_div_scale_f32 v81, vcc, v56, v68, v56
	v_mul_f32_e32 v82, v81, v80
	v_fma_f32 v83, -v69, v82, v81
	v_fmac_f32_e32 v82, v83, v80
	v_fma_f32 v69, -v69, v82, v81
	v_div_fmas_f32 v69, v69, v80, v82
	v_div_fixup_f32 v56, v69, v68, v56
	v_mul_f32_e32 v68, 0xbfb8aa3b, v58
	v_mul_f32_e32 v69, 0xbfb8aa3b, v59
	v_exp_f32_e32 v68, v68
	v_exp_f32_e32 v69, v69
	s_nop 0
	v_pk_add_f32 v[68:69], v[68:69], 1.0 op_sel_hi:[1,0]
	s_nop 0
	v_div_scale_f32 v80, s[8:9], v69, v69, v59
	v_rcp_f32_e32 v81, v80
	s_nop 0
	v_fma_f32 v82, -v80, v81, 1.0
	v_fmac_f32_e32 v81, v82, v81
	v_div_scale_f32 v82, vcc, v59, v69, v59
	v_mul_f32_e32 v83, v82, v81
	v_fma_f32 v84, -v80, v83, v82
	v_fmac_f32_e32 v83, v84, v81
	v_fma_f32 v80, -v80, v83, v82
	v_div_fmas_f32 v80, v80, v81, v83
	v_div_fixup_f32 v59, v80, v69, v59
	v_div_scale_f32 v69, s[8:9], v68, v68, v58
	v_rcp_f32_e32 v80, v69
	s_nop 0
	v_fma_f32 v81, -v69, v80, 1.0
	v_fmac_f32_e32 v80, v81, v80
	v_div_scale_f32 v81, vcc, v58, v68, v58
	v_mul_f32_e32 v82, v81, v80
	v_fma_f32 v83, -v69, v82, v81
	v_fmac_f32_e32 v82, v83, v80
	v_fma_f32 v69, -v69, v82, v81
	v_div_fmas_f32 v69, v69, v80, v82
	v_div_fixup_f32 v58, v69, v68, v58
	v_mov_b32_e32 v80, v57
	v_mov_b32_e32 v81, v59
	v_mov_b32_e32 v68, v56
	v_mov_b32_e32 v69, v58
	v_pk_mul_f32 v[80:81], v[80:81], v[80:81]
	s_nop 0
	v_pk_fma_f32 v[68:69], v[68:69], v[68:69], v[80:81]
	v_lshlrev_b32_e32 v80, 16, v12
	v_and_b32_e32 v12, 0xffff0000, v12
	v_lshlrev_b32_e32 v81, 16, v13
	v_and_b32_e32 v13, 0xffff0000, v13
	v_cndmask_b32_e64 v101, v12, 0, s[6:7]
	v_cndmask_b32_e64 v103, v13, 0, s[6:7]
	v_lshlrev_b32_e32 v12, 16, v10
	v_and_b32_e32 v10, 0xffff0000, v10
	v_lshlrev_b32_e32 v13, 16, v11
	v_and_b32_e32 v11, 0xffff0000, v11
	v_cndmask_b32_e64 v97, v11, 0, s[4:5]
	v_cndmask_b32_e64 v99, v10, 0, s[4:5]
	v_lshlrev_b32_e32 v10, 16, v8
	v_and_b32_e32 v8, 0xffff0000, v8
	v_lshlrev_b32_e32 v11, 16, v9
	v_and_b32_e32 v9, 0xffff0000, v9
	v_cndmask_b32_e64 v93, v9, 0, s[4:5]
	v_cndmask_b32_e64 v95, v8, 0, s[4:5]
	v_lshlrev_b32_e32 v8, 16, v6
	v_and_b32_e32 v6, 0xffff0000, v6
	v_lshlrev_b32_e32 v9, 16, v7
	v_and_b32_e32 v7, 0xffff0000, v7
	v_cndmask_b32_e64 v102, v81, 0, s[6:7]
	v_cndmask_b32_e64 v81, v7, 0, s[14:15]
	v_cndmask_b32_e64 v83, v6, 0, s[14:15]
	v_lshlrev_b32_e32 v6, 16, v4
	v_and_b32_e32 v4, 0xffff0000, v4
	v_lshlrev_b32_e32 v7, 16, v5
	v_and_b32_e32 v5, 0xffff0000, v5
	v_cndmask_b32_e64 v87, v5, 0, s[4:5]
	v_cndmask_b32_e64 v89, v4, 0, s[4:5]
	v_lshlrev_b32_e32 v4, 16, v2
	v_and_b32_e32 v2, 0xffff0000, v2
	v_lshlrev_b32_e32 v5, 16, v3
	v_and_b32_e32 v3, 0xffff0000, v3
	v_cndmask_b32_e64 v100, v80, 0, s[6:7]
	v_cndmask_b32_e64 v80, v9, 0, s[14:15]
	v_cndmask_b32_e64 v82, v8, 0, s[14:15]
	v_cndmask_b32_e64 v86, v7, 0, s[4:5]
	v_cndmask_b32_e64 v88, v6, 0, s[4:5]
	v_cndmask_b32_e64 v85, v3, 0, s[26:27]
	v_cndmask_b32_e64 v84, v5, 0, s[26:27]
	v_cndmask_b32_e64 v91, v2, 0, s[26:27]
	v_cndmask_b32_e64 v90, v4, 0, s[26:27]
	ds_read_b128 v[2:5], v117 offset:60416
	ds_read_b128 v[6:9], v117 offset:63488
	v_cndmask_b32_e64 v94, v10, 0, s[4:5]
	v_lshl_add_u32 v10, v112, 2, v116
	v_cndmask_b32_e64 v96, v13, 0, s[4:5]
	v_cndmask_b32_e64 v98, v12, 0, s[4:5]
	v_cndmask_b32_e64 v92, v11, 0, s[4:5]
	ds_read_b128 v[10:13], v10
	s_waitcnt lgkmcnt(1)
	v_pk_mul_f32 v[118:119], v[96:97], v[8:9]
	v_pk_mul_f32 v[116:117], v[98:99], v[6:7]
	v_pk_fma_f32 v[102:103], v[102:103], v[4:5], v[118:119]
	v_pk_fma_f32 v[100:101], v[100:101], v[2:3], v[116:117]
	s_waitcnt lgkmcnt(0)
; #define LAS __attribute__((address_space(3)))
; __device__ __forceinline__ unsigned pk2(float lo, float hi) { return f2bf(lo) | (f2bf(hi) << 16); }
; __device__ __forceinline__ float siluf_(float x) { return x / (1.f + __expf(-x)); }
; __device__ __forceinline__ f32x4 bf4(u32x2 v) { return (f32x4){lo_bf(v.x), hi_bf(v.x), lo_bf(v.y), hi_bf(v.y)}; }
; __device__ __forceinline__ void ph_prep_tok(CArgs& a, int l, LAS unsigned char* lds, int gw, int ngw) {
;     ...
;         for (int g = 0; g < 3; ++g) { const int col = g * 256 + 4 * lane;
;             f32x4 x[6];
; #pragma unroll
;             for (int r = 0; r < 6; ++r) { const int t = tpos + r - 1; x[r] = (t >= lo && t < hi) ? bf4(xr[g][r]) : (f32x4){0.f, 0.f, 0.f, 0.f}; }
;             const f32x4 w0 = *(const LAS f32x4*)(cw + col), w1 = *(const LAS f32x4*)(cw + 768 + col), w2 = *(const LAS f32x4*)(cw + 1536 + col);
; #pragma unroll
;             for (int r = 0; r < 4; ++r) { f32x4 y = w0 * x[r] + w1 * x[r + 1] + w2 * x[r + 2];
;                 y[0] = siluf_(y[0]); y[1] = siluf_(y[1]); y[2] = siluf_(y[2]); y[3] = siluf_(y[3]);
;                 if (g == 0) { qv[r] = y; sq[r] = (y[0] * y[0] + y[1] * y[1]) + (y[2] * y[2] + y[3] * y[3]); }
;                 else if (g == 1) { kv[r] = y; sk[r] = (y[0] * y[0] + y[1] * y[1]) + (y[2] * y[2] + y[3] * y[3]); }
;                 else *(u32x2*)((bf16*)DV + (size_t)(row0 + r) * 256 + 4 * lane) = (u32x2){pk2(y[0], y[1]), pk2(y[2], y[3])}; } }
	v_pk_fma_f32 v[102:103], v[92:93], v[12:13], v[102:103]
	v_pk_fma_f32 v[100:101], v[94:95], v[10:11], v[100:101]
	v_mul_f32_e32 v116, 0xbfb8aa3b, v103
	v_exp_f32_e32 v117, v116
	v_mul_f32_e32 v116, 0xbfb8aa3b, v102
	v_exp_f32_e32 v119, v116
	v_mul_f32_e32 v116, 0xbfb8aa3b, v101
	v_exp_f32_e32 v116, v116
	v_mul_f32_e32 v118, 0xbfb8aa3b, v100
	v_exp_f32_e32 v118, v118
	s_mov_b32 s6, 0x358637bd
	v_pk_add_f32 v[116:117], v[116:117], 1.0 op_sel_hi:[1,0]
	s_nop 0
	v_div_scale_f32 v120, s[4:5], v116, v116, v101
	v_rcp_f32_e32 v121, v120
	s_nop 0
	v_fma_f32 v122, -v120, v121, 1.0
	v_fmac_f32_e32 v121, v122, v121
	v_div_scale_f32 v122, vcc, v101, v116, v101
	v_mul_f32_e32 v123, v122, v121
	v_fma_f32 v124, -v120, v123, v122
	v_fmac_f32_e32 v123, v124, v121
	v_fma_f32 v120, -v120, v123, v122
	v_div_fmas_f32 v120, v120, v121, v123
	v_div_fixup_f32 v101, v120, v116, v101
	v_div_scale_f32 v116, s[4:5], v117, v117, v103
	v_rcp_f32_e32 v120, v116
	s_nop 0
	v_fma_f32 v121, -v116, v120, 1.0
	v_fmac_f32_e32 v120, v121, v120
	v_div_scale_f32 v121, vcc, v103, v117, v103
	v_mul_f32_e32 v122, v121, v120
	v_fma_f32 v123, -v116, v122, v121
	v_fmac_f32_e32 v122, v123, v120
	v_fma_f32 v116, -v116, v122, v121
	v_div_fmas_f32 v116, v116, v120, v122
	v_div_fixup_f32 v103, v116, v117, v103
	v_pk_add_f32 v[116:117], v[118:119], 1.0 op_sel_hi:[1,0]
	s_nop 0
	v_div_scale_f32 v118, s[4:5], v116, v116, v100
	v_rcp_f32_e32 v119, v118
	s_nop 0
	v_fma_f32 v120, -v118, v119, 1.0
	v_fmac_f32_e32 v119, v120, v119
	v_div_scale_f32 v120, vcc, v100, v116, v100
	v_mul_f32_e32 v121, v120, v119
	v_fma_f32 v122, -v118, v121, v120
	v_fmac_f32_e32 v121, v122, v119
	v_fma_f32 v118, -v118, v121, v120
	v_div_fmas_f32 v118, v118, v119, v121
	v_div_fixup_f32 v100, v118, v116, v100
	v_div_scale_f32 v116, s[4:5], v117, v117, v102
	v_rcp_f32_e32 v118, v116
	s_nop 0
	v_fma_f32 v119, -v116, v118, 1.0
	v_fmac_f32_e32 v118, v119, v118
	v_div_scale_f32 v119, vcc, v102, v117, v102
	v_mul_f32_e32 v120, v119, v118
	v_fma_f32 v121, -v116, v120, v119
	v_fmac_f32_e32 v120, v121, v118
	v_fma_f32 v116, -v116, v120, v119
	v_div_fmas_f32 v116, v116, v118, v120
	v_div_fixup_f32 v102, v116, v117, v102
	v_and_b32_sdwa v116, v102, v169 dst_sel:DWORD dst_unused:UNUSED_PAD src0_sel:WORD_1 src1_sel:DWORD
	v_and_b32_sdwa v117, v100, v169 dst_sel:DWORD dst_unused:UNUSED_PAD src0_sel:WORD_1 src1_sel:DWORD
	v_add3_u32 v100, v100, v117, s81
	v_add3_u32 v102, v102, v116, s81
	v_and_b32_sdwa v116, v103, v169 dst_sel:DWORD dst_unused:UNUSED_PAD src0_sel:WORD_1 src1_sel:DWORD
	v_and_b32_sdwa v117, v101, v169 dst_sel:DWORD dst_unused:UNUSED_PAD src0_sel:WORD_1 src1_sel:DWORD
	v_add3_u32 v103, v103, v116, s81
	v_add3_u32 v101, v101, v117, s81
	v_and_b32_e32 v103, 0xffff0000, v103
	v_and_b32_e32 v101, 0xffff0000, v101
	v_or_b32_sdwa v103, v103, v102 dst_sel:DWORD dst_unused:UNUSED_PAD src0_sel:DWORD src1_sel:WORD_1
	v_or_b32_sdwa v102, v101, v100 dst_sel:DWORD dst_unused:UNUSED_PAD src0_sel:DWORD src1_sel:WORD_1
	v_lshl_add_u64 v[100:101], s[2:3], 0, v[20:21]
	v_add_co_u32_e32 v116, vcc, s1, v100
	s_nop 1
	v_addc_co_u32_e32 v117, vcc, 0, v101, vcc
	global_store_dwordx2 v[116:117], v[102:103], off
	v_pk_mul_f32 v[116:117], v[92:93], v[8:9]
	v_pk_mul_f32 v[102:103], v[94:95], v[6:7]
	v_pk_fma_f32 v[96:97], v[96:97], v[4:5], v[116:117]
	v_pk_fma_f32 v[98:99], v[98:99], v[2:3], v[102:103]
	v_pk_fma_f32 v[96:97], v[80:81], v[12:13], v[96:97]
	v_pk_fma_f32 v[98:99], v[82:83], v[10:11], v[98:99]
	v_mul_f32_e32 v102, 0xbfb8aa3b, v97
	v_exp_f32_e32 v103, v102
	v_mul_f32_e32 v102, 0xbfb8aa3b, v96
	v_exp_f32_e32 v117, v102
	v_mul_f32_e32 v102, 0xbfb8aa3b, v99
	v_exp_f32_e32 v102, v102
	v_mul_f32_e32 v116, 0xbfb8aa3b, v98
	v_exp_f32_e32 v116, v116
	v_pk_add_f32 v[102:103], v[102:103], 1.0 op_sel_hi:[1,0]
	s_nop 0
	v_div_scale_f32 v118, s[4:5], v102, v102, v99
	v_rcp_f32_e32 v119, v118
	s_nop 0
	v_fma_f32 v120, -v118, v119, 1.0
	v_fmac_f32_e32 v119, v120, v119
	v_div_scale_f32 v120, vcc, v99, v102, v99
	v_mul_f32_e32 v121, v120, v119
	v_fma_f32 v122, -v118, v121, v120
	v_fmac_f32_e32 v121, v122, v119
	v_fma_f32 v118, -v118, v121, v120
	v_div_fmas_f32 v118, v118, v119, v121
	v_div_fixup_f32 v99, v118, v102, v99
	v_div_scale_f32 v102, s[4:5], v103, v103, v97
	v_rcp_f32_e32 v118, v102
	s_nop 0
	v_fma_f32 v119, -v102, v118, 1.0
	v_fmac_f32_e32 v118, v119, v118
	v_div_scale_f32 v119, vcc, v97, v103, v97
	v_mul_f32_e32 v120, v119, v118
	v_fma_f32 v121, -v102, v120, v119
	v_fmac_f32_e32 v120, v121, v118
	v_fma_f32 v102, -v102, v120, v119
	v_div_fmas_f32 v102, v102, v118, v120
	v_div_fixup_f32 v97, v102, v103, v97
	v_pk_add_f32 v[102:103], v[116:117], 1.0 op_sel_hi:[1,0]
	s_nop 0
	v_div_scale_f32 v116, s[4:5], v102, v102, v98
	v_rcp_f32_e32 v117, v116
	s_nop 0
	v_fma_f32 v118, -v116, v117, 1.0
	v_fmac_f32_e32 v117, v118, v117
	v_div_scale_f32 v118, vcc, v98, v102, v98
	v_mul_f32_e32 v119, v118, v117
	v_fma_f32 v120, -v116, v119, v118
	v_fmac_f32_e32 v119, v120, v117
	v_fma_f32 v116, -v116, v119, v118
	v_div_fmas_f32 v116, v116, v117, v119
	v_div_fixup_f32 v98, v116, v102, v98
	v_div_scale_f32 v102, s[4:5], v103, v103, v96
	v_rcp_f32_e32 v116, v102
	s_nop 0
	v_fma_f32 v117, -v102, v116, 1.0
	v_fmac_f32_e32 v116, v117, v116
	v_div_scale_f32 v117, vcc, v96, v103, v96
	v_mul_f32_e32 v118, v117, v116
	v_fma_f32 v119, -v102, v118, v117
	v_fmac_f32_e32 v118, v119, v116
	v_fma_f32 v102, -v102, v118, v117
	v_div_fmas_f32 v102, v102, v116, v118
	v_div_fixup_f32 v96, v102, v103, v96
	v_and_b32_sdwa v102, v96, v169 dst_sel:DWORD dst_unused:UNUSED_PAD src0_sel:WORD_1 src1_sel:DWORD
	v_and_b32_sdwa v103, v98, v169 dst_sel:DWORD dst_unused:UNUSED_PAD src0_sel:WORD_1 src1_sel:DWORD
; __device__ __forceinline__ unsigned pk2(float lo, float hi) { return f2bf(lo) | (f2bf(hi) << 16); }
; __device__ __forceinline__ float siluf_(float x) { return x / (1.f + __expf(-x)); }
; __device__ __forceinline__ void ph_prep_tok(CArgs& a, int l, LAS unsigned char* lds, int gw, int ngw) {
;     ...
;             for (int r = 0; r < 4; ++r) { f32x4 y = w0 * x[r] + w1 * x[r + 1] + w2 * x[r + 2];
;                 y[0] = siluf_(y[0]); y[1] = siluf_(y[1]); y[2] = siluf_(y[2]); y[3] = siluf_(y[3]);
;                 if (g == 0) { qv[r] = y; sq[r] = (y[0] * y[0] + y[1] * y[1]) + (y[2] * y[2] + y[3] * y[3]); }
;                 else if (g == 1) { kv[r] = y; sk[r] = (y[0] * y[0] + y[1] * y[1]) + (y[2] * y[2] + y[3] * y[3]); }
;                 else *(u32x2*)((bf16*)DV + (size_t)(row0 + r) * 256 + 4 * lane) = (u32x2){pk2(y[0], y[1]), pk2(y[2], y[3])}; } }
	v_add3_u32 v96, v96, v102, s81
	v_and_b32_sdwa v102, v97, v169 dst_sel:DWORD dst_unused:UNUSED_PAD src0_sel:WORD_1 src1_sel:DWORD
	v_add3_u32 v98, v98, v103, s81
	v_and_b32_sdwa v103, v99, v169 dst_sel:DWORD dst_unused:UNUSED_PAD src0_sel:WORD_1 src1_sel:DWORD
	v_add3_u32 v97, v97, v102, s81
	v_add3_u32 v99, v99, v103, s81
	v_and_b32_e32 v97, 0xffff0000, v97
	v_and_b32_e32 v99, 0xffff0000, v99
	v_or_b32_sdwa v103, v97, v96 dst_sel:DWORD dst_unused:UNUSED_PAD src0_sel:DWORD src1_sel:WORD_1
	v_lshl_add_u64 v[96:97], s[2:3], 0, v[16:17]
	v_or_b32_sdwa v102, v99, v98 dst_sel:DWORD dst_unused:UNUSED_PAD src0_sel:DWORD src1_sel:WORD_1
	v_add_co_u32_e32 v98, vcc, s1, v96
	v_pk_mul_f32 v[116:117], v[80:81], v[8:9]
	s_nop 0
	v_addc_co_u32_e32 v99, vcc, 0, v97, vcc
	v_pk_fma_f32 v[92:93], v[92:93], v[4:5], v[116:117]
	global_store_dwordx2 v[98:99], v[102:103], off offset:512
	v_pk_mul_f32 v[102:103], v[82:83], v[6:7]
	v_pk_fma_f32 v[92:93], v[86:87], v[12:13], v[92:93]
	v_pk_fma_f32 v[94:95], v[94:95], v[2:3], v[102:103]
	v_mul_f32_e32 v102, 0xbfb8aa3b, v93
	v_pk_fma_f32 v[94:95], v[88:89], v[10:11], v[94:95]
	v_exp_f32_e32 v103, v102
	v_mul_f32_e32 v102, 0xbfb8aa3b, v92
	v_exp_f32_e32 v117, v102
	v_mul_f32_e32 v102, 0xbfb8aa3b, v95
	v_exp_f32_e32 v102, v102
	v_mul_f32_e32 v116, 0xbfb8aa3b, v94
	v_exp_f32_e32 v116, v116
	v_pk_mul_f32 v[8:9], v[86:87], v[8:9]
	v_pk_add_f32 v[102:103], v[102:103], 1.0 op_sel_hi:[1,0]
	v_pk_fma_f32 v[4:5], v[80:81], v[4:5], v[8:9]
	v_div_scale_f32 v118, s[4:5], v102, v102, v95
	v_rcp_f32_e32 v119, v118
	v_pk_mul_f32 v[6:7], v[88:89], v[6:7]
	v_pk_fma_f32 v[4:5], v[84:85], v[12:13], v[4:5]
	v_pk_fma_f32 v[2:3], v[82:83], v[2:3], v[6:7]
	v_fma_f32 v120, -v118, v119, 1.0
	v_fmac_f32_e32 v119, v120, v119
	v_div_scale_f32 v120, vcc, v95, v102, v95
	v_mul_f32_e32 v121, v120, v119
	v_fma_f32 v122, -v118, v121, v120
	v_fmac_f32_e32 v121, v122, v119
	v_fma_f32 v118, -v118, v121, v120
	v_div_fmas_f32 v118, v118, v119, v121
	v_div_fixup_f32 v95, v118, v102, v95
	v_div_scale_f32 v102, s[4:5], v103, v103, v93
	v_rcp_f32_e32 v118, v102
	v_mul_f32_e32 v6, 0xbfb8aa3b, v5
	v_pk_fma_f32 v[2:3], v[90:91], v[10:11], v[2:3]
	v_exp_f32_e32 v7, v6
	v_fma_f32 v119, -v102, v118, 1.0
	v_fmac_f32_e32 v118, v119, v118
	v_div_scale_f32 v119, vcc, v93, v103, v93
	v_mul_f32_e32 v120, v119, v118
	v_fma_f32 v121, -v102, v120, v119
	v_fmac_f32_e32 v120, v121, v118
	v_fma_f32 v102, -v102, v120, v119
	v_div_fmas_f32 v102, v102, v118, v120
	v_div_fixup_f32 v93, v102, v103, v93
	v_pk_add_f32 v[102:103], v[116:117], 1.0 op_sel_hi:[1,0]
	v_mul_f32_e32 v6, 0xbfb8aa3b, v4
	v_div_scale_f32 v116, s[4:5], v102, v102, v94
	v_rcp_f32_e32 v117, v116
	v_exp_f32_e32 v9, v6
	v_mul_f32_e32 v6, 0xbfb8aa3b, v3
	v_exp_f32_e32 v6, v6
	v_fma_f32 v118, -v116, v117, 1.0
	v_fmac_f32_e32 v117, v118, v117
	v_div_scale_f32 v118, vcc, v94, v102, v94
	v_mul_f32_e32 v119, v118, v117
	v_fma_f32 v120, -v116, v119, v118
	v_fmac_f32_e32 v119, v120, v117
	v_fma_f32 v116, -v116, v119, v118
	v_div_fmas_f32 v116, v116, v117, v119
	v_div_fixup_f32 v94, v116, v102, v94
	v_div_scale_f32 v102, s[4:5], v103, v103, v92
	v_rcp_f32_e32 v116, v102
	v_pk_add_f32 v[6:7], v[6:7], 1.0 op_sel_hi:[1,0]
	v_mul_f32_e32 v8, 0xbfb8aa3b, v2
	v_div_scale_f32 v10, s[4:5], v6, v6, v3
	v_fma_f32 v117, -v102, v116, 1.0
	v_fmac_f32_e32 v116, v117, v116
	v_div_scale_f32 v117, vcc, v92, v103, v92
	v_rcp_f32_e32 v11, v10
	v_mul_f32_e32 v118, v117, v116
	v_fma_f32 v119, -v102, v118, v117
	v_fmac_f32_e32 v118, v119, v116
	v_fma_f32 v102, -v102, v118, v117
	v_fma_f32 v12, -v10, v11, 1.0
	v_div_fmas_f32 v102, v102, v116, v118
	v_fmac_f32_e32 v11, v12, v11
	v_div_scale_f32 v12, vcc, v3, v6, v3
	v_mul_f32_e32 v13, v12, v11
	v_fma_f32 v80, -v10, v13, v12
	v_fmac_f32_e32 v13, v80, v11
	v_fma_f32 v10, -v10, v13, v12
	v_div_fmas_f32 v10, v10, v11, v13
	v_div_fixup_f32 v3, v10, v6, v3
	v_div_scale_f32 v6, s[4:5], v7, v7, v5
	v_rcp_f32_e32 v10, v6
	v_exp_f32_e32 v8, v8
	v_div_fixup_f32 v92, v102, v103, v92
	v_and_b32_sdwa v102, v92, v169 dst_sel:DWORD dst_unused:UNUSED_PAD src0_sel:WORD_1 src1_sel:DWORD
	v_fma_f32 v11, -v6, v10, 1.0
	v_fmac_f32_e32 v10, v11, v10
	v_div_scale_f32 v11, vcc, v5, v7, v5
	v_mul_f32_e32 v12, v11, v10
	v_fma_f32 v13, -v6, v12, v11
	v_fmac_f32_e32 v12, v13, v10
	v_fma_f32 v6, -v6, v12, v11
	v_div_fmas_f32 v6, v6, v10, v12
	v_div_fixup_f32 v5, v6, v7, v5
	v_pk_add_f32 v[6:7], v[8:9], 1.0 op_sel_hi:[1,0]
	v_and_b32_sdwa v103, v94, v169 dst_sel:DWORD dst_unused:UNUSED_PAD src0_sel:WORD_1 src1_sel:DWORD
	v_div_scale_f32 v8, s[4:5], v6, v6, v2
	v_rcp_f32_e32 v9, v8
	v_add3_u32 v94, v94, v103, s81
	v_add3_u32 v92, v92, v102, s81
	v_and_b32_sdwa v102, v93, v169 dst_sel:DWORD dst_unused:UNUSED_PAD src0_sel:WORD_1 src1_sel:DWORD
	v_fma_f32 v10, -v8, v9, 1.0
	v_fmac_f32_e32 v9, v10, v9
	v_div_scale_f32 v10, vcc, v2, v6, v2
	v_mul_f32_e32 v11, v10, v9
	v_fma_f32 v12, -v8, v11, v10
	v_fmac_f32_e32 v11, v12, v9
	v_fma_f32 v8, -v8, v11, v10
	v_div_fmas_f32 v8, v8, v9, v11
	v_div_fixup_f32 v2, v8, v6, v2
	v_div_scale_f32 v6, s[4:5], v7, v7, v4
	v_rcp_f32_e32 v8, v6
	v_and_b32_sdwa v103, v95, v169 dst_sel:DWORD dst_unused:UNUSED_PAD src0_sel:WORD_1 src1_sel:DWORD
	v_add3_u32 v93, v93, v102, s81
	v_add3_u32 v95, v95, v103, s81
	v_fma_f32 v9, -v6, v8, 1.0
	v_fmac_f32_e32 v8, v9, v8
	v_div_scale_f32 v9, vcc, v4, v7, v4
	v_mul_f32_e32 v10, v9, v8
	v_fma_f32 v11, -v6, v10, v9
	v_fmac_f32_e32 v10, v11, v8
	v_fma_f32 v6, -v6, v10, v9
	v_div_fmas_f32 v6, v6, v8, v10
	v_div_fixup_f32 v4, v6, v7, v4
	v_and_b32_sdwa v6, v4, v169 dst_sel:DWORD dst_unused:UNUSED_PAD src0_sel:WORD_1 src1_sel:DWORD
; __device__ __forceinline__ unsigned pk2(float lo, float hi) { return f2bf(lo) | (f2bf(hi) << 16); }
; __device__ __forceinline__ float row16_sum(float v) { v += dpp_f<0xB1>(v); v += dpp_f<0x4E>(v); v += dpp_f<0x141>(v); v += dpp_f<0x140>(v); return v; }
; __device__ __forceinline__ void ph_prep_tok(CArgs& a, int l, LAS unsigned char* lds, int gw, int ngw) {
;     ...
;                 else *(u32x2*)((bf16*)DV + (size_t)(row0 + r) * 256 + 4 * lane) = (u32x2){pk2(y[0], y[1]), pk2(y[2], y[3])}; } }
; #pragma unroll
;         for (int r = 0; r < 4; ++r) { const float rq = rsqrtf(row16_sum(sq[r]) + 1e-6f) * 0.125f, rk = rsqrtf(row16_sum(sk[r]) + 1e-6f);
;             const f32x4 qn = qv[r] * rq, kn = kv[r] * rk;
;             *(u32x2*)((bf16*)(a.ws + WS_CKD + CD_QB) + (size_t)(row0 + r) * 256 + 4 * lane) = (u32x2){pk2(qn[0], qn[1]), pk2(qn[2], qn[3])};
;             *(u32x2*)((bf16*)(a.ws + WS_CKD + CD_KB) + (size_t)(row0 + r) * 256 + 4 * lane) = (u32x2){pk2(kn[0], kn[1]), pk2(kn[2], kn[3])}; }
	v_and_b32_sdwa v7, v2, v169 dst_sel:DWORD dst_unused:UNUSED_PAD src0_sel:WORD_1 src1_sel:DWORD
	v_add3_u32 v2, v2, v7, s81
	v_add3_u32 v4, v4, v6, s81
	v_and_b32_sdwa v6, v5, v169 dst_sel:DWORD dst_unused:UNUSED_PAD src0_sel:WORD_1 src1_sel:DWORD
	v_and_b32_sdwa v7, v3, v169 dst_sel:DWORD dst_unused:UNUSED_PAD src0_sel:WORD_1 src1_sel:DWORD
	v_add3_u32 v5, v5, v6, s81
	v_add3_u32 v3, v3, v7, s81
	v_and_b32_e32 v5, 0xffff0000, v5
	v_and_b32_e32 v6, 0xffff0000, v3
	v_or_b32_sdwa v3, v5, v4 dst_sel:DWORD dst_unused:UNUSED_PAD src0_sel:DWORD src1_sel:WORD_1
	v_or_b32_sdwa v2, v6, v2 dst_sel:DWORD dst_unused:UNUSED_PAD src0_sel:DWORD src1_sel:WORD_1
	global_store_dwordx2 v[98:99], v[2:3], off offset:1536
	v_mov_b32_e32 v2, v78
	v_mov_b32_e32 v3, v54
	v_mov_b32_e32 v54, v79
	v_pk_add_f32 v[2:3], v[2:3], v[54:55]
	s_mov_b32 s1, 0x73e00000
	v_and_b32_e32 v93, 0xffff0000, v93
	v_mov_b32_dpp v5, v3 quad_perm:[1,0,3,2] row_mask:0xf bank_mask:0xf bound_ctrl:1
	v_mov_b32_dpp v4, v2 quad_perm:[1,0,3,2] row_mask:0xf bank_mask:0xf bound_ctrl:1
	v_pk_add_f32 v[2:3], v[2:3], v[4:5]
	v_and_b32_e32 v95, 0xffff0000, v95
	v_or_b32_sdwa v93, v93, v92 dst_sel:DWORD dst_unused:UNUSED_PAD src0_sel:DWORD src1_sel:WORD_1
	v_mov_b32_dpp v5, v3 quad_perm:[2,3,0,1] row_mask:0xf bank_mask:0xf bound_ctrl:1
	v_mov_b32_dpp v4, v2 quad_perm:[2,3,0,1] row_mask:0xf bank_mask:0xf bound_ctrl:1
	v_pk_add_f32 v[2:3], v[2:3], v[4:5]
	v_or_b32_sdwa v92, v95, v94 dst_sel:DWORD dst_unused:UNUSED_PAD src0_sel:DWORD src1_sel:WORD_1
	global_store_dwordx2 v[98:99], v[92:93], off offset:1024
	v_mov_b32_dpp v5, v3 row_half_mirror row_mask:0xf bank_mask:0xf bound_ctrl:1
	v_mov_b32_dpp v4, v2 row_half_mirror row_mask:0xf bank_mask:0xf bound_ctrl:1
	v_pk_add_f32 v[2:3], v[2:3], v[4:5]
	s_mov_b32 s4, 0x72c00000
	s_nop 0
	v_mov_b32_dpp v5, v3 row_mirror row_mask:0xf bank_mask:0xf bound_ctrl:1
	v_mov_b32_dpp v4, v2 row_mirror row_mask:0xf bank_mask:0xf bound_ctrl:1
	v_pk_add_f32 v[2:3], v[2:3], v[4:5]
	s_nop 0
	v_pk_add_f32 v[2:3], v[2:3], s[6:7] op_sel_hi:[1,0]
	s_nop 0
	v_mul_f32_e32 v4, 0x4b800000, v3
	v_cmp_gt_f32_e64 s[40:41], s21, v3
	v_cmp_gt_f32_e32 vcc, s21, v2
	s_nop 0
	v_cndmask_b32_e64 v3, v3, v4, s[40:41]
	v_rsq_f32_e32 v3, v3
	s_nop 0
	v_mul_f32_e32 v4, 0x45800000, v3
	v_cndmask_b32_e64 v3, v3, v4, s[40:41]
	v_mul_f32_e32 v4, 0x3e000000, v3
	v_mul_f32_e32 v3, 0x4b800000, v2
	v_pk_mul_f32 v[6:7], v[50:51], v[4:5] op_sel_hi:[1,0]
	v_pk_mul_f32 v[4:5], v[46:47], v[4:5] op_sel_hi:[1,0]
	v_cndmask_b32_e32 v2, v2, v3, vcc
	v_rsq_f32_e32 v2, v2
	v_cvt_pk_bf16_f32 v4, v4, v5
	v_mul_f32_e32 v3, 0x45800000, v2
	v_cndmask_b32_e32 v2, v2, v3, vcc
	v_cvt_pk_bf16_f32 v5, v6, v7
	v_add_co_u32_e32 v6, vcc, s1, v100
	v_pk_mul_f32 v[8:9], v[74:75], v[2:3] op_sel_hi:[1,0]
	v_pk_mul_f32 v[2:3], v[70:71], v[2:3] op_sel_hi:[1,0]
	v_addc_co_u32_e32 v7, vcc, 0, v101, vcc
	global_store_dwordx2 v[6:7], v[4:5], off
	v_cvt_pk_bf16_f32 v2, v2, v3
	v_cvt_pk_bf16_f32 v3, v8, v9
	v_add_co_u32_e32 v4, vcc, s4, v100
	s_nop 1
	v_addc_co_u32_e32 v5, vcc, 0, v101, vcc
	global_store_dwordx2 v[4:5], v[2:3], off
	v_mov_b32_e32 v2, v76
	v_mov_b32_e32 v3, v52
	v_mov_b32_e32 v52, v77
	v_pk_add_f32 v[2:3], v[2:3], v[52:53]
	s_nop 1
	v_mov_b32_dpp v5, v3 quad_perm:[1,0,3,2] row_mask:0xf bank_mask:0xf bound_ctrl:1
	v_mov_b32_dpp v4, v2 quad_perm:[1,0,3,2] row_mask:0xf bank_mask:0xf bound_ctrl:1
	v_pk_add_f32 v[2:3], v[2:3], v[4:5]
	s_nop 1
	v_mov_b32_dpp v5, v3 quad_perm:[2,3,0,1] row_mask:0xf bank_mask:0xf bound_ctrl:1
	v_mov_b32_dpp v4, v2 quad_perm:[2,3,0,1] row_mask:0xf bank_mask:0xf bound_ctrl:1
	v_pk_add_f32 v[2:3], v[2:3], v[4:5]
	s_nop 1
	v_mov_b32_dpp v5, v3 row_half_mirror row_mask:0xf bank_mask:0xf bound_ctrl:1
	v_mov_b32_dpp v4, v2 row_half_mirror row_mask:0xf bank_mask:0xf bound_ctrl:1
	v_pk_add_f32 v[2:3], v[2:3], v[4:5]
	s_nop 1
	v_mov_b32_dpp v5, v3 row_mirror row_mask:0xf bank_mask:0xf bound_ctrl:1
	v_mov_b32_dpp v4, v2 row_mirror row_mask:0xf bank_mask:0xf bound_ctrl:1
	v_pk_add_f32 v[2:3], v[2:3], v[4:5]
	s_nop 0
	v_pk_add_f32 v[2:3], v[2:3], s[6:7] op_sel_hi:[1,0]
	s_nop 0
	v_mul_f32_e32 v4, 0x4b800000, v3
	v_cmp_gt_f32_e64 s[40:41], s21, v3
	v_cmp_gt_f32_e32 vcc, s21, v2
	s_nop 0
	v_cndmask_b32_e64 v3, v3, v4, s[40:41]
	v_rsq_f32_e32 v3, v3
	s_nop 0
	v_mul_f32_e32 v4, 0x45800000, v3
	v_cndmask_b32_e64 v3, v3, v4, s[40:41]
	v_mul_f32_e32 v4, 0x3e000000, v3
	v_mul_f32_e32 v3, 0x4b800000, v2
	v_pk_mul_f32 v[6:7], v[44:45], v[4:5] op_sel_hi:[1,0]
	v_pk_mul_f32 v[4:5], v[40:41], v[4:5] op_sel_hi:[1,0]
	v_cndmask_b32_e32 v2, v2, v3, vcc
	v_rsq_f32_e32 v2, v2
	v_cvt_pk_bf16_f32 v4, v4, v5
	v_mul_f32_e32 v3, 0x45800000, v2
	v_cndmask_b32_e32 v2, v2, v3, vcc
	v_cvt_pk_bf16_f32 v5, v6, v7
	v_add_co_u32_e32 v6, vcc, s1, v96
	v_pk_mul_f32 v[8:9], v[66:67], v[2:3] op_sel_hi:[1,0]
	v_pk_mul_f32 v[2:3], v[64:65], v[2:3] op_sel_hi:[1,0]
	v_addc_co_u32_e32 v7, vcc, 0, v97, vcc
	global_store_dwordx2 v[6:7], v[4:5], off offset:512
	v_cvt_pk_bf16_f32 v2, v2, v3
	v_cvt_pk_bf16_f32 v3, v8, v9
	v_add_co_u32_e32 v4, vcc, s4, v96
	s_nop 1
	v_addc_co_u32_e32 v5, vcc, 0, v97, vcc
	global_store_dwordx2 v[4:5], v[2:3], off offset:512
	v_mov_b32_e32 v2, v72
	v_mov_b32_e32 v3, v48
	v_mov_b32_e32 v48, v73
	v_pk_add_f32 v[2:3], v[2:3], v[48:49]
	s_nop 1
	v_mov_b32_dpp v9, v3 quad_perm:[1,0,3,2] row_mask:0xf bank_mask:0xf bound_ctrl:1
	v_mov_b32_dpp v8, v2 quad_perm:[1,0,3,2] row_mask:0xf bank_mask:0xf bound_ctrl:1
	v_pk_add_f32 v[2:3], v[2:3], v[8:9]
	s_nop 1
	v_mov_b32_dpp v9, v3 quad_perm:[2,3,0,1] row_mask:0xf bank_mask:0xf bound_ctrl:1
	v_mov_b32_dpp v8, v2 quad_perm:[2,3,0,1] row_mask:0xf bank_mask:0xf bound_ctrl:1
; __device__ __forceinline__ float bf2f(unsigned v) { return __uint_as_float(v << 16); }
; __device__ __forceinline__ unsigned pk2(float lo, float hi) { return f2bf(lo) | (f2bf(hi) << 16); }
; __device__ __forceinline__ float sigmoidf_(float x) { return 1.f / (1.f + __expf(-x)); }
; __device__ __forceinline__ float softplusf_(float x) { return fmaxf(x, 0.f) + __logf(1.f + __expf(-fabsf(x))); }
; __device__ __forceinline__ float row16_sum(float v) { v += dpp_f<0xB1>(v); v += dpp_f<0x4E>(v); v += dpp_f<0x141>(v); v += dpp_f<0x140>(v); return v; }
; __device__ __forceinline__ void ph_prep_tok(CArgs& a, int l, LAS unsigned char* lds, int gw, int ngw) {
;     ...
;         for (int r = 0; r < 4; ++r) { const float rq = rsqrtf(row16_sum(sq[r]) + 1e-6f) * 0.125f, rk = rsqrtf(row16_sum(sk[r]) + 1e-6f);
;             const f32x4 qn = qv[r] * rq, kn = kv[r] * rk;
;             *(u32x2*)((bf16*)(a.ws + WS_CKD + CD_QB) + (size_t)(row0 + r) * 256 + 4 * lane) = (u32x2){pk2(qn[0], qn[1]), pk2(qn[2], qn[3])};
;             *(u32x2*)((bf16*)(a.ws + WS_CKD + CD_KB) + (size_t)(row0 + r) * 256 + 4 * lane) = (u32x2){pk2(kn[0], kn[1]), pk2(kn[2], kn[3])}; }
;         if (lane < 16) { const float af = bf2f(gb4[0]), ab = bf2f(gb4[1]), bfv = bf2f(gb4[2]), bbv = bf2f(gb4[3]);
;             const float gf = eaf * softplusf_(af + dtf), gb = eab * softplusf_(ab + dtb);
;             *(f32x4*)(DG + (size_t)(row0 + gr) * 16 + 4 * gh) = (f32x4){sigmoidf_(bfv), gf, sigmoidf_(bbv), gb}; }
	v_pk_add_f32 v[2:3], v[2:3], v[8:9]
	s_nop 1
	v_mov_b32_dpp v9, v3 row_half_mirror row_mask:0xf bank_mask:0xf bound_ctrl:1
	v_mov_b32_dpp v8, v2 row_half_mirror row_mask:0xf bank_mask:0xf bound_ctrl:1
	v_pk_add_f32 v[2:3], v[2:3], v[8:9]
	s_nop 1
	v_mov_b32_dpp v9, v3 row_mirror row_mask:0xf bank_mask:0xf bound_ctrl:1
	v_mov_b32_dpp v8, v2 row_mirror row_mask:0xf bank_mask:0xf bound_ctrl:1
	v_pk_add_f32 v[2:3], v[2:3], v[8:9]
	s_nop 0
	v_pk_add_f32 v[2:3], v[2:3], s[6:7] op_sel_hi:[1,0]
	s_nop 0
	v_mul_f32_e32 v8, 0x4b800000, v3
	v_cmp_gt_f32_e64 s[40:41], s21, v3
	v_cmp_gt_f32_e32 vcc, s21, v2
	s_nop 0
	v_cndmask_b32_e64 v3, v3, v8, s[40:41]
	v_rsq_f32_e32 v3, v3
	s_nop 0
	v_mul_f32_e32 v8, 0x45800000, v3
	v_cndmask_b32_e64 v3, v3, v8, s[40:41]
	v_mul_f32_e32 v8, 0x3e000000, v3
	v_mul_f32_e32 v3, 0x4b800000, v2
	v_cndmask_b32_e32 v2, v2, v3, vcc
	v_pk_mul_f32 v[10:11], v[38:39], v[8:9] op_sel_hi:[1,0]
	v_pk_mul_f32 v[8:9], v[36:37], v[8:9] op_sel_hi:[1,0]
	v_rsq_f32_e32 v2, v2
	v_cvt_pk_bf16_f32 v8, v8, v8
	v_lshrrev_b32_e32 v8, 16, v8
	v_cvt_pk_bf16_f32 v9, v9, v9
	v_and_or_b32 v8, v9, s80, v8
	v_mul_f32_e32 v3, 0x45800000, v2
	v_cndmask_b32_e32 v2, v2, v3, vcc
	v_pk_mul_f32 v[12:13], v[62:63], v[2:3] op_sel_hi:[1,0]
	v_pk_mul_f32 v[2:3], v[60:61], v[2:3] op_sel_hi:[1,0]
	v_cvt_pk_bf16_f32 v9, v10, v11
	global_store_dwordx2 v[6:7], v[8:9], off offset:1024
	v_cvt_pk_bf16_f32 v2, v2, v3
	v_cvt_pk_bf16_f32 v3, v12, v12
	v_bfe_u32 v8, v13, 16, 1
	v_lshrrev_b32_e32 v3, 16, v3
	v_add3_u32 v8, v13, v8, s81
	v_and_or_b32 v3, v8, s80, v3
	global_store_dwordx2 v[4:5], v[2:3], off offset:1024
	v_mov_b32_e32 v2, v68
	v_mov_b32_e32 v3, v42
	v_mov_b32_e32 v42, v69
	v_pk_add_f32 v[2:3], v[2:3], v[42:43]
	s_nop 1
	v_mov_b32_dpp v9, v3 quad_perm:[1,0,3,2] row_mask:0xf bank_mask:0xf bound_ctrl:1
	v_mov_b32_dpp v8, v2 quad_perm:[1,0,3,2] row_mask:0xf bank_mask:0xf bound_ctrl:1
	v_pk_add_f32 v[2:3], v[2:3], v[8:9]
	s_nop 1
	v_mov_b32_dpp v9, v3 quad_perm:[2,3,0,1] row_mask:0xf bank_mask:0xf bound_ctrl:1
	v_mov_b32_dpp v8, v2 quad_perm:[2,3,0,1] row_mask:0xf bank_mask:0xf bound_ctrl:1
	v_pk_add_f32 v[2:3], v[2:3], v[8:9]
	s_nop 1
	v_mov_b32_dpp v9, v3 row_half_mirror row_mask:0xf bank_mask:0xf bound_ctrl:1
	v_mov_b32_dpp v8, v2 row_half_mirror row_mask:0xf bank_mask:0xf bound_ctrl:1
	v_pk_add_f32 v[2:3], v[2:3], v[8:9]
	s_nop 1
	v_mov_b32_dpp v9, v3 row_mirror row_mask:0xf bank_mask:0xf bound_ctrl:1
	v_mov_b32_dpp v8, v2 row_mirror row_mask:0xf bank_mask:0xf bound_ctrl:1
	v_pk_add_f32 v[2:3], v[2:3], v[8:9]
	s_nop 0
	v_pk_add_f32 v[2:3], v[2:3], s[6:7] op_sel_hi:[1,0]
	s_nop 0
	v_mul_f32_e32 v8, 0x4b800000, v3
	v_cmp_gt_f32_e64 s[40:41], s21, v3
	v_cmp_gt_f32_e32 vcc, s21, v2
	s_nop 0
	v_cndmask_b32_e64 v3, v3, v8, s[40:41]
	v_rsq_f32_e32 v3, v3
	s_nop 0
	v_mul_f32_e32 v8, 0x45800000, v3
	v_cndmask_b32_e64 v3, v3, v8, s[40:41]
	v_mul_f32_e32 v8, 0x3e000000, v3
	v_mul_f32_e32 v3, 0x4b800000, v2
	v_cndmask_b32_e32 v2, v2, v3, vcc
	v_pk_mul_f32 v[10:11], v[32:33], v[8:9] op_sel_hi:[1,0]
	v_pk_mul_f32 v[8:9], v[30:31], v[8:9] op_sel_hi:[1,0]
	v_rsq_f32_e32 v2, v2
	v_cvt_pk_bf16_f32 v8, v8, v8
	v_lshrrev_b32_e32 v8, 16, v8
	v_cvt_pk_bf16_f32 v9, v9, v9
	v_and_or_b32 v8, v9, s80, v8
	v_mul_f32_e32 v3, 0x45800000, v2
	v_cvt_pk_bf16_f32 v9, v10, v10
	v_bfe_u32 v10, v11, 16, 1
	v_cndmask_b32_e32 v2, v2, v3, vcc
	v_lshrrev_b32_e32 v9, 16, v9
	v_add3_u32 v10, v11, v10, s81
	v_pk_mul_f32 v[12:13], v[58:59], v[2:3] op_sel_hi:[1,0]
	v_pk_mul_f32 v[2:3], v[56:57], v[2:3] op_sel_hi:[1,0]
	v_and_or_b32 v9, v10, s80, v9
	global_store_dwordx2 v[6:7], v[8:9], off offset:1536
	v_cvt_pk_bf16_f32 v2, v2, v3
	v_cvt_pk_bf16_f32 v3, v12, v12
	v_bfe_u32 v6, v13, 16, 1
	v_lshrrev_b32_e32 v3, 16, v3
	v_add3_u32 v6, v13, v6, s81
	v_and_or_b32 v3, v6, s80, v3
	global_store_dwordx2 v[4:5], v[2:3], off offset:1536
	s_and_saveexec_b64 s[4:5], s[38:39]
	s_cbranch_execz .LBB0_301
	v_lshlrev_b32_e32 v2, 16, v34
	v_add_f32_e32 v2, v1, v2
	s_mov_b32 s1, 0xbfb8aa3b
	v_max_f32_e32 v3, 0, v2
	v_mul_f32_e64 v2, |v2|, s1
	v_exp_f32_e32 v2, v2
	s_mov_b32 s6, 0x3f317217
	s_mov_b32 s7, 0x7f800000
	v_lshlrev_b32_e32 v4, 16, v113
	v_add_f32_e32 v2, 1.0, v2
	v_cmp_gt_f32_e32 vcc, s21, v2
	v_lshlrev_b32_e32 v6, 16, v114
	v_lshlrev_b32_e32 v7, 16, v115
	v_cndmask_b32_e64 v5, 0, 32, vcc
	v_ldexp_f32 v2, v2, v5
	v_log_f32_e32 v2, v2
	s_nop 0
	v_mul_f32_e32 v5, 0x3f317217, v2
	v_fma_f32 v5, v2, s6, -v5
	v_fmac_f32_e32 v5, 0x3377d1cf, v2
	v_fmac_f32_e32 v5, 0x3f317217, v2
	v_cmp_lt_f32_e64 s[40:41], |v2|, s7
	s_nop 1
	v_cndmask_b32_e64 v2, v2, v5, s[40:41]
	v_cndmask_b32_e32 v5, 0, v193, vcc
	v_sub_f32_e32 v2, v2, v5
	v_add_f32_e32 v2, v3, v2
	v_mul_f32_e64 v3, v2, -v105
	v_add_f32_e32 v2, v104, v4
	v_max_f32_e32 v4, 0, v2
	v_mul_f32_e64 v2, |v2|, s1
	v_exp_f32_e32 v2, v2
	s_nop 0
	v_add_f32_e32 v2, 1.0, v2
	v_cmp_gt_f32_e32 vcc, s21, v2
	s_nop 1
	v_cndmask_b32_e64 v5, 0, 32, vcc
	v_ldexp_f32 v2, v2, v5
	v_log_f32_e32 v2, v2
	s_nop 0
	v_mul_f32_e32 v5, 0x3f317217, v2
	v_fma_f32 v5, v2, s6, -v5
	v_fmac_f32_e32 v5, 0x3377d1cf, v2
	v_fmac_f32_e32 v5, 0x3f317217, v2
	v_cmp_lt_f32_e64 s[40:41], |v2|, s7
	s_nop 1
	v_cndmask_b32_e64 v2, v2, v5, s[40:41]
	v_cndmask_b32_e32 v5, 0, v193, vcc
	v_sub_f32_e32 v2, v2, v5
	v_add_f32_e32 v2, v4, v2
	v_mul_f32_e64 v5, v2, -v106
	v_mul_f32_e32 v2, 0xbfb8aa3b, v6
	v_exp_f32_e32 v2, v2
	s_nop 0
	v_add_f32_e32 v2, 1.0, v2
	v_div_scale_f32 v4, s[6:7], v2, v2, 1.0
	v_rcp_f32_e32 v6, v4
	s_nop 0
	v_fma_f32 v8, -v4, v6, 1.0
	v_fmac_f32_e32 v6, v8, v6
	v_div_scale_f32 v8, vcc, 1.0, v2, 1.0
	v_mul_f32_e32 v9, v8, v6
	v_fma_f32 v10, -v4, v9, v8
	v_fmac_f32_e32 v9, v10, v6
	v_fma_f32 v4, -v4, v9, v8
	v_div_fmas_f32 v4, v4, v6, v9
	v_div_fixup_f32 v2, v4, v2, 1.0
	v_mul_f32_e32 v4, 0xbfb8aa3b, v7
	v_exp_f32_e32 v4, v4
	s_nop 0
	v_add_f32_e32 v4, 1.0, v4
	v_div_scale_f32 v6, s[6:7], v4, v4, 1.0
	v_rcp_f32_e32 v7, v6
	s_nop 0
	v_fma_f32 v8, -v6, v7, 1.0
	v_fmac_f32_e32 v7, v8, v7
	v_div_scale_f32 v8, vcc, 1.0, v4, 1.0
	v_mul_f32_e32 v9, v8, v7
	v_fma_f32 v10, -v6, v9, v8
	v_fmac_f32_e32 v9, v10, v7
	v_fma_f32 v6, -v6, v9, v8
	v_div_fmas_f32 v6, v6, v7, v9
	v_div_fixup_f32 v4, v6, v4, 1.0
	v_add_u32_e32 v6, s0, v107
	v_ashrrev_i32_e32 v7, 31, v6
	v_lshlrev_b64 v[6:7], 6, v[6:7]
	v_lshl_add_u64 v[6:7], v[14:15], 0, v[6:7]
	global_store_dwordx4 v[6:7], v[2:5], off
	s_branch .LBB0_301

; #define LAS __attribute__((address_space(3)))
; __device__ __forceinline__ unsigned f2bf(float f) { unsigned u = __float_as_uint(f); return (u + 0x7fffu + ((u >> 16) & 1u)) >> 16; }
; __device__ __forceinline__ u32x2 cvt4(f32x4 v) { return (u32x2){pk2(v[0], v[1]), pk2(v[2], v[3])}; }
; __device__ __forceinline__ void gla_s2(CArgs& a, int u, LAS unsigned char* ub, int w, int lane) {
;     const int fr = lane & 15, kg = lane >> 4;
;     bf16* FT = (bf16*)(a.ws + WS_CKA + CA_FT) + (size_t)u * 4096; bf16* UT = (bf16*)(a.ws + WS_CKA + CA_UT) + (size_t)u * 2048;
;     LAS bf16* QE = (LAS bf16*)ub; LAS bf16* KE = QE + 2560; LAS bf16* KTT = KE + 2560; LAS bf16* VT = KTT + 2304;
;     const int It = w & 3, vh = w >> 2;
;     const bf16x8 qf = *(const LAS bf16x8*)(QE + (16 * It + fr) * 40 + 8 * kg);
;     f32x4 st[4];
; #pragma unroll
;     for (int Jt = 0; Jt < 4; ++Jt) { const bf16x8 kf = *(const LAS bf16x8*)(KE + (16 * Jt + fr) * 40 + 8 * kg);
;         st[Jt] = __builtin_amdgcn_mfma_f32_16x16x32_bf16(kf, qf, (f32x4){0.f, 0.f, 0.f, 0.f}, 0, 0, 0);
; #pragma unroll
;         for (int e = 0; e < 4; ++e) st[Jt][e] = (16 * Jt + 4 * kg + e <= 16 * It + fr) ? st[Jt][e] : 0.f; }
;     const bf16x8 Sb01 = frag2(cvt4(st[0]), cvt4(st[1])), Sb23 = frag2(cvt4(st[2]), cvt4(st[3]));
;     bf16* ftp = FT + (4 * kg) * 64 + 16 * It + fr;
; #pragma unroll
;     for (int vv = 0; vv < 2; ++vv) { const int Vt = 2 * vh + vv; const LAS bf16* vr = VT + (16 * Vt + fr) * 72 + 4 * kg;
;         f32x4 f = (f32x4){0.f, 0.f, 0.f, 0.f};
;         f = __builtin_amdgcn_mfma_f32_16x16x32_bf16(frag2(*(const LAS u32x2*)vr, *(const LAS u32x2*)(vr + 16)), Sb01, f, 0, 0, 0);
;         f = __builtin_amdgcn_mfma_f32_16x16x32_bf16(frag2(*(const LAS u32x2*)(vr + 32), *(const LAS u32x2*)(vr + 48)), Sb23, f, 0, 0, 0);
; #pragma unroll
;         for (int e = 0; e < 4; ++e) ftp[(16 * Vt + e) * 64] = (bf16)f2bf(f[e]); }
;     const int kt = w & 1, Vu = w >> 1;
;     f32x4 uu = (f32x4){0.f, 0.f, 0.f, 0.f};
; #pragma unroll
;     for (int s = 0; s < 2; ++s) uu = __builtin_amdgcn_mfma_f32_16x16x32_bf16(*(const LAS bf16x8*)(KTT + (16 * kt + fr) * 72 + 32 * s + 8 * kg), *(const LAS bf16x8*)(VT + (16 * Vu + fr) * 72 + 32 * s + 8 * kg), uu, 0, 0, 0);
;     *(u32x2*)(UT + (16 * Vu + fr) * 32 + 16 * kt + 4 * kg) = cvt4(uu);
; }
.LBB0_369:
	v_and_b32_e32 v7, 15, v1
	v_and_b32_e32 v2, -16, v1
	v_or_b32_e32 v4, s68, v7
	v_add_u32_e32 v2, 0, v2
	v_mad_u32_u24 v5, v4, s33, v2
	ds_read_b128 v[8:11], v5 offset:24064
	v_mad_u32_u24 v5, v7, s33, v2
	ds_read_b128 v[12:15], v5 offset:29184
	v_ashrrev_i32_e32 v3, 4, v1
	v_lshlrev_b32_e32 v6, 2, v3
	v_cmp_le_i32_e32 vcc, v6, v4
	v_add_u32_e32 v20, 16, v6
	s_waitcnt vmcnt(13)
	v_add_u32_e32 v24, 32, v6
	s_waitcnt lgkmcnt(0)
	v_mfma_f32_16x16x32_bf16 v[12:15], v[12:15], v[8:11], 0
	s_add_i32 s54, s54, 2
	s_lshl_b64 s[2:3], s[78:79], 13
	s_add_u32 s2, s31, s2
	s_waitcnt vmcnt(9)
	s_nop 3
	v_cndmask_b32_e32 v16, 0, v12, vcc
	v_cmp_lt_i32_e32 vcc, v6, v4
	v_or_b32_e32 v12, 2, v6
	s_addc_u32 s3, s44, s3
	v_cndmask_b32_e32 v17, 0, v13, vcc
	v_cmp_le_i32_e32 vcc, v12, v4
	v_or_b32_e32 v12, 3, v6
	s_mov_b32 s27, s79
	v_cndmask_b32_e32 v18, 0, v14, vcc
	v_cmp_le_i32_e32 vcc, v12, v4
	v_lshlrev_b32_e32 v34, 1, v7
	s_mov_b32 s29, s79
	v_cndmask_b32_e32 v19, 0, v15, vcc
	ds_read_b128 v[12:15], v5 offset:30464
	s_waitcnt lgkmcnt(0)
	v_mfma_f32_16x16x32_bf16 v[12:15], v[12:15], v[8:11], 0
	v_cmp_le_i32_e32 vcc, v20, v4
	s_nop 6
	v_cndmask_b32_e32 v20, 0, v12, vcc
	v_add_u32_e32 v12, 17, v6
	v_cmp_le_i32_e32 vcc, v12, v4
	v_add_u32_e32 v12, 18, v6
	s_nop 0
	v_cndmask_b32_e32 v21, 0, v13, vcc
	v_cmp_le_i32_e32 vcc, v12, v4
	v_add_u32_e32 v12, 19, v6
	s_nop 0
	v_cndmask_b32_e32 v22, 0, v14, vcc
	v_cmp_le_i32_e32 vcc, v12, v4
	s_nop 1
	v_cndmask_b32_e32 v23, 0, v15, vcc
	ds_read_b128 v[12:15], v5 offset:31744
	s_waitcnt lgkmcnt(0)
	v_mfma_f32_16x16x32_bf16 v[12:15], v[12:15], v[8:11], 0
	v_cmp_le_i32_e32 vcc, v24, v4
	s_nop 6
	v_cndmask_b32_e32 v24, 0, v12, vcc
	v_add_u32_e32 v12, 33, v6
	v_cmp_le_i32_e32 vcc, v12, v4
	v_add_u32_e32 v12, 34, v6
	s_nop 0
	v_cndmask_b32_e32 v25, 0, v13, vcc
	v_cmp_le_i32_e32 vcc, v12, v4
	v_add_u32_e32 v12, 35, v6
	s_nop 0
	v_cndmask_b32_e32 v26, 0, v14, vcc
	v_cmp_le_i32_e32 vcc, v12, v4
	s_nop 1
	v_cndmask_b32_e32 v27, 0, v15, vcc
	ds_read_b128 v[12:15], v5 offset:33024
	s_waitcnt lgkmcnt(0)
	v_mfma_f32_16x16x32_bf16 v[8:11], v[12:15], v[8:11], 0
	v_add_u32_e32 v5, 48, v6
	v_cmp_le_i32_e32 vcc, v5, v4
	s_nop 3
	s_nop 1
	v_cndmask_b32_e32 v5, 0, v8, vcc
	v_add_u32_e32 v8, 49, v6
	v_cmp_le_i32_e32 vcc, v8, v4
	v_add_u32_e32 v8, 50, v6
	s_nop 0
	v_cndmask_b32_e32 v14, 0, v9, vcc
	v_cmp_le_i32_e32 vcc, v8, v4
	v_add_u32_e32 v8, 51, v6
	s_nop 0
	v_cndmask_b32_e32 v15, 0, v10, vcc
	v_cmp_le_i32_e32 vcc, v8, v4
	v_cvt_pk_bf16_f32 v8, v16, v17
	v_cvt_pk_bf16_f32 v9, v18, v19
	v_cndmask_b32_e32 v4, 0, v11, vcc
	v_cvt_pk_bf16_f32 v10, v20, v21
	v_cvt_pk_bf16_f32 v11, v22, v23
	v_cvt_pk_bf16_f32 v12, v24, v25
	v_cvt_pk_bf16_f32 v13, v26, v27
	v_cvt_pk_bf16_f32 v14, v5, v14
	v_cvt_pk_bf16_f32 v15, v15, v4
	v_lshlrev_b32_e32 v4, 8, v3
	v_ashrrev_i32_e32 v5, 31, v4
	v_lshl_add_u32 v24, v3, 3, 0
	v_or_b32_e32 v3, s45, v7
	v_lshl_add_u64 v[4:5], v[4:5], 1, s[2:3]
	v_mad_u64_u32 v[16:17], s[2:3], v3, s75, v[24:25]
	v_add_u32_e32 v3, 0x9800, v16
	ds_read2_b64 v[16:19], v3 offset1:4
	ds_read2_b64 v[20:23], v3 offset0:8 offset1:12
	s_waitcnt lgkmcnt(1)
	v_mfma_f32_16x16x32_bf16 v[16:19], v[16:19], v[8:11], 0
	v_lshl_add_u64 v[4:5], v[4:5], 0, s[26:27]
	v_lshl_add_u64 v[4:5], v[4:5], 0, v[34:35]
	s_waitcnt lgkmcnt(0)
	v_mfma_f32_16x16x32_bf16 v[16:19], v[20:23], v[12:15], v[16:19]
	v_lshl_add_u64 v[20:21], s[92:93], 1, v[4:5]
	s_nop 6
	v_cvt_pk_bf16_f32 v3, v16, v16
	global_store_short v[20:21], v3, off
	v_cvt_pk_bf16_f32 v3, v17, v17
	global_store_short v[20:21], v3, off offset:128
	v_cvt_pk_bf16_f32 v3, v18, v18
	global_store_short v[20:21], v3, off offset:256
	v_cvt_pk_bf16_f32 v3, v19, v19
	global_store_short v[20:21], v3, off offset:384
	v_or_b32_e32 v3, s47, v7
	v_mad_u64_u32 v[16:17], s[2:3], v3, s75, v[24:25]
	v_add_u32_e32 v3, 0x9800, v16
	ds_read2_b64 v[16:19], v3 offset1:4
	s_waitcnt lgkmcnt(0)
	v_mfma_f32_16x16x32_bf16 v[8:11], v[16:19], v[8:11], 0
	ds_read2_b64 v[16:19], v3 offset0:8 offset1:12
	s_waitcnt lgkmcnt(0)
	v_mfma_f32_16x16x32_bf16 v[8:11], v[16:19], v[12:15], v[8:11]
	v_lshl_add_u64 v[12:13], s[94:95], 1, v[4:5]
	s_nop 6
	v_cvt_pk_bf16_f32 v3, v8, v8
	global_store_short v[12:13], v3, off
	v_cvt_pk_bf16_f32 v3, v9, v9
	v_lshl_add_u64 v[8:9], s[96:97], 1, v[4:5]
	global_store_short v[8:9], v3, off
	v_cvt_pk_bf16_f32 v3, v10, v10
	v_lshl_add_u64 v[8:9], s[58:59], 1, v[4:5]
	global_store_short v[8:9], v3, off
	v_cvt_pk_bf16_f32 v3, v11, v11
	v_lshl_add_u64 v[4:5], s[4:5], 1, v[4:5]
	global_store_short v[4:5], v3, off
	v_or_b32_e32 v3, s67, v7
	v_mad_u32_u24 v14, v3, s75, v2
	v_or_b32_e32 v3, s46, v7
	v_mad_u64_u32 v[8:9], s[2:3], v3, s75, v[2:3]
	ds_read_b128 v[2:5], v14 offset:34304
	ds_read_b128 v[10:13], v8 offset:38912
	s_waitcnt lgkmcnt(0)
	v_mfma_f32_16x16x32_bf16 v[2:5], v[2:5], v[10:13], 0
	ds_read_b128 v[10:13], v14 offset:34368
	ds_read_b128 v[14:17], v8 offset:38976
	s_add_u32 s2, s74, s76
	s_addc_u32 s3, s22, s77
	s_waitcnt lgkmcnt(0)
	v_mfma_f32_16x16x32_bf16 v[2:5], v[10:13], v[14:17], v[2:5]
	s_add_i32 s9, s9, 2
	s_addk_i32 s20, 0x80
	s_addk_i32 s0, 0xff80
	s_nop 4
	v_cvt_pk_bf16_f32 v2, v2, v2
	v_lshrrev_b32_e32 v2, 16, v2
	v_cvt_pk_bf16_f32 v3, v3, v3
	v_and_or_b32 v2, v3, s80, v2
	v_cvt_pk_bf16_f32 v3, v4, v5
	v_lshl_or_b32 v4, v7, 5, s23
	v_ashrrev_i32_e32 v5, 31, v4
	v_lshl_add_u64 v[4:5], v[4:5], 1, s[2:3]
	v_lshl_add_u64 v[4:5], v[4:5], 0, s[28:29]
	v_ashrrev_i32_e32 v7, 31, v6
	v_lshl_add_u64 v[4:5], v[6:7], 1, v[4:5]
	s_addk_i32 s55, 0xff80
	s_andn2_b64 vcc, exec, s[48:49]
	global_store_dwordx2 v[4:5], v[2:3], off
	s_cbranch_vccz .LBB0_1679

; #define LAS __attribute__((address_space(3)))
; __device__ __forceinline__ u32x2 cvt4(f32x4 v) { return (u32x2){pk2(v[0], v[1]), pk2(v[2], v[3])}; }
; __device__ __forceinline__ void gla_fetch(CArgs& a, int u, int w, int lane, GlaIn& in) {
;     ...
;     if (w < 4) { const int k = lane & 31, half = lane >> 5; const int src_off = (w == 0 || w == 2) ? 0 : 128;
; #pragma unroll
; __device__ __forceinline__ void gla_s2(CArgs& a, int u, LAS unsigned char* ub, int w, int lane) {
;     const int fr = lane & 15, kg = lane >> 4;
;     bf16* FT = (bf16*)(a.ws + WS_CKA + CA_FT) + (size_t)u * 4096; bf16* UT = (bf16*)(a.ws + WS_CKA + CA_UT) + (size_t)u * 2048;
;     LAS bf16* QE = (LAS bf16*)ub; LAS bf16* KE = QE + 2560; LAS bf16* KTT = KE + 2560; LAS bf16* VT = KTT + 2304;
;     const int It = w & 3, vh = w >> 2;
;     const bf16x8 qf = *(const LAS bf16x8*)(QE + (16 * It + fr) * 40 + 8 * kg);
;     f32x4 st[4];
; #pragma unroll
;     for (int Jt = 0; Jt < 4; ++Jt) { const bf16x8 kf = *(const LAS bf16x8*)(KE + (16 * Jt + fr) * 40 + 8 * kg);
;         st[Jt] = __builtin_amdgcn_mfma_f32_16x16x32_bf16(kf, qf, (f32x4){0.f, 0.f, 0.f, 0.f}, 0, 0, 0);
; #pragma unroll
;         for (int e = 0; e < 4; ++e) st[Jt][e] = (16 * Jt + 4 * kg + e <= 16 * It + fr) ? st[Jt][e] : 0.f; }
;     const bf16x8 Sb01 = frag2(cvt4(st[0]), cvt4(st[1])), Sb23 = frag2(cvt4(st[2]), cvt4(st[3]));
;     bf16* ftp = FT + (4 * kg) * 64 + 16 * It + fr;
; #pragma unroll
;     for (int vv = 0; vv < 2; ++vv) { const int Vt = 2 * vh + vv; const LAS bf16* vr = VT + (16 * Vt + fr) * 72 + 4 * kg;
;         f32x4 f = (f32x4){0.f, 0.f, 0.f, 0.f};
;         f = __builtin_amdgcn_mfma_f32_16x16x32_bf16(frag2(*(const LAS u32x2*)vr, *(const LAS u32x2*)(vr + 16)), Sb01, f, 0, 0, 0);
;         f = __builtin_amdgcn_mfma_f32_16x16x32_bf16(frag2(*(const LAS u32x2*)(vr + 32), *(const LAS u32x2*)(vr + 48)), Sb23, f, 0, 0, 0);
; #pragma unroll
;         for (int e = 0; e < 4; ++e) ftp[(16 * Vt + e) * 64] = (bf16)f2bf(f[e]); }
;     const int kt = w & 1, Vu = w >> 1;
;     f32x4 uu = (f32x4){0.f, 0.f, 0.f, 0.f};
; #pragma unroll
;     for (int s = 0; s < 2; ++s) uu = __builtin_amdgcn_mfma_f32_16x16x32_bf16(*(const LAS bf16x8*)(KTT + (16 * kt + fr) * 72 + 32 * s + 8 * kg), *(const LAS bf16x8*)(VT + (16 * Vu + fr) * 72 + 32 * s + 8 * kg), uu, 0, 0, 0);
;     *(u32x2*)(UT + (16 * Vu + fr) * 32 + 16 * kt + 4 * kg) = cvt4(uu);
; }
.LBB0_1022:
	global_load_ushort v159, v[2:3], off
	global_load_ushort v158, v[4:5], off
	global_load_ushort v60, v[6:7], off
	global_load_ushort v59, v[8:9], off
	global_load_ushort v58, v[10:11], off
	global_load_ushort v57, v[12:13], off
	global_load_ushort v56, v[14:15], off
	global_load_ushort v55, v[16:17], off
	global_load_ushort v54, v[18:19], off
	global_load_ushort v53, v[22:23], off
	global_load_ushort v43, v[24:25], off
	s_nop 0
	global_load_ushort v24, v[26:27], off
	global_load_ushort v23, v[28:29], off
	global_load_ushort v22, v[30:31], off
	global_load_ushort v18, v[32:33], off
	global_load_ushort v16, v[20:21], off
	v_or_b32_e32 v9, s68, v34
	v_add_u32_e32 v8, 0, v161
	v_mad_u32_u24 v2, v9, s33, v8
	v_mad_u32_u24 v14, v34, s33, v8
	ds_read_b128 v[2:5], v2
	ds_read_b128 v[10:13], v14 offset:5120
	v_ashrrev_i32_e32 v7, 4, v1
	v_lshlrev_b32_e32 v6, 2, v7
	v_cmp_le_i32_e32 vcc, v6, v9
	v_add_u32_e32 v21, 16, v6
	s_waitcnt lgkmcnt(0)
	v_mfma_f32_16x16x32_bf16 v[10:13], v[10:13], v[2:5], 0
	v_add_u32_e32 v28, 32, v6
	s_lshl_b64 s[2:3], s[78:79], 13
	s_add_u32 s2, s31, s2
	s_nop 4
	v_cndmask_b32_e32 v15, 0, v10, vcc
	v_cmp_lt_i32_e32 vcc, v6, v9
	v_or_b32_e32 v10, 2, v6
	s_addc_u32 s3, s44, s3
	v_cndmask_b32_e32 v17, 0, v11, vcc
	v_cmp_le_i32_e32 vcc, v10, v9
	v_or_b32_e32 v10, 3, v6
	s_lshl_b32 s26, s68, 1
	v_cndmask_b32_e32 v19, 0, v12, vcc
	v_cmp_le_i32_e32 vcc, v10, v9
	s_mov_b32 s27, s79
	s_nop 0
	v_cndmask_b32_e32 v20, 0, v13, vcc
	ds_read_b128 v[10:13], v14 offset:6400
	s_waitcnt lgkmcnt(0)
	v_mfma_f32_16x16x32_bf16 v[10:13], v[10:13], v[2:5], 0
	v_cmp_le_i32_e32 vcc, v21, v9
	s_nop 6
	v_cndmask_b32_e32 v21, 0, v10, vcc
	v_add_u32_e32 v10, 17, v6
	v_cmp_le_i32_e32 vcc, v10, v9
	v_add_u32_e32 v10, 18, v6
	s_nop 0
	v_cndmask_b32_e32 v25, 0, v11, vcc
	v_cmp_le_i32_e32 vcc, v10, v9
	v_add_u32_e32 v10, 19, v6
	s_nop 0
	v_cndmask_b32_e32 v26, 0, v12, vcc
	v_cmp_le_i32_e32 vcc, v10, v9
	s_nop 1
	v_cndmask_b32_e32 v27, 0, v13, vcc
	ds_read_b128 v[10:13], v14 offset:7680
	s_waitcnt lgkmcnt(0)
	v_mfma_f32_16x16x32_bf16 v[10:13], v[10:13], v[2:5], 0
	v_cmp_le_i32_e32 vcc, v28, v9
	s_nop 6
	v_cndmask_b32_e32 v28, 0, v10, vcc
	v_add_u32_e32 v10, 33, v6
	v_cmp_le_i32_e32 vcc, v10, v9
	v_add_u32_e32 v10, 34, v6
	s_nop 0
	v_cndmask_b32_e32 v29, 0, v11, vcc
	v_cmp_le_i32_e32 vcc, v10, v9
	v_add_u32_e32 v10, 35, v6
	s_nop 0
	v_cndmask_b32_e32 v30, 0, v12, vcc
	v_cmp_le_i32_e32 vcc, v10, v9
	s_nop 1
	v_cndmask_b32_e32 v31, 0, v13, vcc
	ds_read_b128 v[10:13], v14 offset:8960
	s_waitcnt lgkmcnt(0)
	v_mfma_f32_16x16x32_bf16 v[2:5], v[10:13], v[2:5], 0
	v_add_u32_e32 v10, 48, v6
	v_cmp_le_i32_e32 vcc, v10, v9
	s_nop 3
	s_nop 1
	v_cndmask_b32_e32 v12, 0, v2, vcc
	v_add_u32_e32 v2, 49, v6
	v_cmp_le_i32_e32 vcc, v2, v9
	v_add_u32_e32 v2, 50, v6
	s_nop 0
	v_cndmask_b32_e32 v13, 0, v3, vcc
	v_cmp_le_i32_e32 vcc, v2, v9
	v_add_u32_e32 v2, 51, v6
	s_nop 0
	v_cndmask_b32_e32 v14, 0, v4, vcc
	v_cmp_le_i32_e32 vcc, v2, v9
	v_cvt_pk_bf16_f32 v2, v15, v17
	v_cvt_pk_bf16_f32 v3, v19, v20
	v_cndmask_b32_e32 v9, 0, v5, vcc
	v_cvt_pk_bf16_f32 v4, v21, v25
	v_cvt_pk_bf16_f32 v5, v26, v27
	v_cvt_pk_bf16_f32 v10, v28, v29
	v_cvt_pk_bf16_f32 v11, v30, v31
	v_cvt_pk_bf16_f32 v12, v12, v13
	v_cvt_pk_bf16_f32 v13, v14, v14
	v_bfe_u32 v14, v9, 16, 1
	v_add3_u32 v9, v9, v14, s81
	v_lshlrev_b32_e32 v14, 8, v7
	v_ashrrev_i32_e32 v15, 31, v14
	v_lshl_add_u32 v20, v7, 3, 0
	v_or_b32_e32 v7, s45, v34
	v_lshl_add_u64 v[14:15], v[14:15], 1, s[2:3]
	v_mad_u64_u32 v[26:27], s[2:3], v7, s75, v[20:21]
	v_add_u32_e32 v7, 0x3800, v26
	ds_read2_b64 v[26:29], v7 offset0:64 offset1:68
	ds_read2_b64 v[30:33], v7 offset0:72 offset1:76
	s_waitcnt lgkmcnt(1)
	v_mfma_f32_16x16x32_bf16 v[26:29], v[26:29], v[2:5], 0
	v_lshrrev_b32_e32 v13, 16, v13
	v_and_or_b32 v13, v9, s80, v13
	v_lshl_add_u64 v[14:15], v[14:15], 0, s[26:27]
	v_lshl_add_u64 v[14:15], v[34:35], 1, v[14:15]
	s_waitcnt lgkmcnt(0)
	v_mfma_f32_16x16x32_bf16 v[26:29], v[30:33], v[10:13], v[26:29]
	v_lshl_add_u64 v[30:31], s[92:93], 1, v[14:15]
	s_nop 6
	v_cvt_pk_bf16_f32 v7, v26, v26
	global_store_short v[30:31], v7, off
	v_cvt_pk_bf16_f32 v7, v27, v27
	global_store_short v[30:31], v7, off offset:128
	v_cvt_pk_bf16_f32 v7, v28, v28
	global_store_short v[30:31], v7, off offset:256
	v_cvt_pk_bf16_f32 v7, v29, v29
	global_store_short v[30:31], v7, off offset:384
	v_or_b32_e32 v7, s47, v34
	v_mad_u64_u32 v[20:21], s[2:3], v7, s75, v[20:21]
	v_add_u32_e32 v7, 0x3800, v20
	ds_read2_b64 v[26:29], v7 offset0:64 offset1:68
	s_waitcnt lgkmcnt(0)
	v_mfma_f32_16x16x32_bf16 v[2:5], v[26:29], v[2:5], 0
	ds_read2_b64 v[26:29], v7 offset0:72 offset1:76
	s_waitcnt lgkmcnt(0)
	v_mfma_f32_16x16x32_bf16 v[2:5], v[26:29], v[10:13], v[2:5]
	v_lshl_add_u64 v[10:11], s[94:95], 1, v[14:15]
	s_nop 6
	v_cvt_pk_bf16_f32 v2, v2, v2
	global_store_short v[10:11], v2, off
	v_cvt_pk_bf16_f32 v7, v3, v3
	v_lshl_add_u64 v[2:3], s[96:97], 1, v[14:15]
	global_store_short v[2:3], v7, off
	v_cvt_pk_bf16_f32 v4, v4, v4
	v_lshl_add_u64 v[2:3], s[58:59], 1, v[14:15]
	global_store_short v[2:3], v4, off
	v_cvt_pk_bf16_f32 v4, v5, v5
	v_lshl_add_u64 v[2:3], s[4:5], 1, v[14:15]
	global_store_short v[2:3], v4, off
	v_or_b32_e32 v2, s67, v34
	v_mad_u32_u24 v7, v2, s75, v8
	v_or_b32_e32 v2, s46, v34
	v_mad_u64_u32 v[8:9], s[2:3], v2, s75, v[8:9]
	ds_read_b128 v[2:5], v7 offset:10240
	ds_read_b128 v[10:13], v8 offset:14848
	s_waitcnt lgkmcnt(0)
	v_mfma_f32_16x16x32_bf16 v[2:5], v[2:5], v[10:13], 0
	ds_read_b128 v[10:13], v7 offset:10304
	ds_read_b128 v[26:29], v8 offset:14912
	s_add_u32 s2, s74, s28
	s_addc_u32 s3, s22, s29
	s_waitcnt lgkmcnt(0)
	v_mfma_f32_16x16x32_bf16 v[2:5], v[10:13], v[26:29], v[2:5]
	s_lshl_b32 s28, s67, 1
	s_mov_b32 s29, s79
	s_and_b64 vcc, s[38:39], exec
	s_nop 4
	v_cvt_pk_bf16_f32 v2, v2, v3
	v_cvt_pk_bf16_f32 v3, v4, v5
	v_lshl_or_b32 v4, v34, 5, s23
	v_ashrrev_i32_e32 v5, 31, v4
	v_lshl_add_u64 v[4:5], v[4:5], 1, s[2:3]
	v_lshl_add_u64 v[4:5], v[4:5], 0, s[28:29]
	v_ashrrev_i32_e32 v7, 31, v6
	v_lshl_add_u64 v[4:5], v[6:7], 1, v[4:5]
	s_mov_b64 s[2:3], -1
	global_store_dwordx2 v[4:5], v[2:3], off
	s_cbranch_vccz .LBB0_1024
	v_and_or_b32 v2, v1, 15, s34
	v_and_b32_e32 v3, 0x7ffffff0, v1
	v_mul_lo_u32 v2, v2, s75
	v_lshlrev_b32_e32 v3, 1, v3
	s_mov_b32 s2, 0x5040100
	v_add3_u32 v6, 0, v2, v3
	s_waitcnt vmcnt(17)
	v_perm_b32 v5, v55, v56, s2
	v_perm_b32 v4, v57, v58, s2
	v_perm_b32 v3, v59, v60, s2
	v_perm_b32 v2, v158, v159, s2
	ds_write_b128 v6, v[2:5] offset:38912
	s_waitcnt vmcnt(9)
	v_perm_b32 v5, v16, v18, s2
	v_perm_b32 v4, v22, v23, s2
	v_perm_b32 v3, v24, v43, s2
	v_perm_b32 v2, v53, v54, s2
	ds_write_b128 v6, v[2:5] offset:38928
	s_mov_b64 s[2:3], 0

; #define LAS __attribute__((address_space(3)))
; __device__ __forceinline__ void gdn_fetch(CArgs& a, int u, int w, int lane, GdnIn& in) {
;     const int chain = u / 36, n = u % 36, b = chain >> 3, h = (chain >> 1) & 3, dir = chain & 1;
;     const int r0 = scan_row(b, dir, n * 64), step = dir ? -1 : 1, fr = lane & 15, kg = lane >> 4;
;     const float* DQ = (const float*)(a.ws + WS_MIX + MX_DQ) + h * 64; const float* DK = (const float*)(a.ws + WS_MIX + MX_DK) + h * 64; const float* DV = (const float*)(a.ws + WS_MIX + MX_DV) + h * 64;
;     const float* DG = (const float*)(a.ws + WS_MIX + MX_DG);
;     const bf16* KB = (const bf16*)(a.ws + WS_CKD + CD_KB) + (ptrdiff_t)r0 * 256 + h * 64; const bf16* QB = (const bf16*)(a.ws + WS_CKD + CD_QB) + (ptrdiff_t)r0 * 256 + h * 64;
;     const ptrdiff_t ldt = (ptrdiff_t)step * 256;
;     const bool isW = w >= 4; const int c0 = 16 * (w & 3), I1 = w >> 1;
;     in.g2 = *(const f32x2*)(DG + (size_t)(r0 + step * lane) * 16 + h * 4 + dir * 2);
; #pragma unroll
;     for (int s = 0; s < 2; ++s) { in.ak[s] = *(const bf16x8*)(KB + (ptrdiff_t)(16 * I1 + fr) * ldt + 32 * s + 8 * kg); in.aq[s] = *(const bf16x8*)(QB + (ptrdiff_t)(16 * I1 + fr) * ldt + 32 * s + 8 * kg);
; #pragma unroll
; __device__ __forceinline__ void gdn_s23(CArgs& a, int u, const GdnIn2& in, LAS unsigned char* ub, LAS unsigned char* dwb, int w, int lane, float cl) {
;     ...
;     { const int blk = lane >> 4, c = lane & 15; float T[16];
; #pragma unroll
;       for (int hb = 0; hb < 4; ++hb) {
;           u32x4 arow[4][2];
; #pragma unroll
;           for (int rr = 0; rr < 4; ++rr) { const int r = 4 * hb + rr; arow[rr][0] = *(const LAS u32x4*)(AB + (16 * blk + r) * 72 + 16 * blk); if (hb >= 2) arow[rr][1] = *(const LAS u32x4*)(AB + (16 * blk + r) * 72 + 16 * blk + 8); }
;           asm volatile("s_waitcnt lgkmcnt(0)" ::: "memory");
; #pragma unroll
;           for (int rr = 0; rr < 4; ++rr) { const int r = 4 * hb + rr; float t = (r == c) ? 1.f : 0.f;
;               float t2 = 0.f;
; #pragma unroll
;               for (int j = 0; j < r; ++j) { const unsigned wv = arow[rr][j >> 3][(j >> 1) & 3]; const float av = (j & 1) ? hi_bf(wv) : lo_bf(wv); if (j & 1) t2 -= av * T[j]; else t -= av * T[j]; }
;               t += t2;
;               T[r] = t; DW[(blk * 16 + r) * 16 + c] = (bf16)f2bf(t); } } }
.LBB0_1723:
	s_bfe_u32 s76, s9, 0x20001
	s_cmp_eq_u32 s27, 0
	s_cselect_b64 s[52:53], -1, 0
	s_and_b64 s[48:49], s[52:53], exec
	s_cselect_b32 s77, 1, -1
	s_ashr_i32 s3, s2, 31
	s_lshl_b64 s[48:49], s[2:3], 9
	v_readlane_b32 s3, v251, 14
	s_add_u32 s3, s3, s48
	v_readlane_b32 s54, v249, 10
	s_addc_u32 s55, s54, s49
	s_lshl_b32 s62, s76, 7
	s_add_u32 s54, s3, s62
	s_addc_u32 s55, s55, 0
	s_add_u32 s3, s37, s48
	s_addc_u32 s49, s72, s49
	v_mul_lo_u32 v46, v110, s77
	s_add_u32 s48, s3, s62
	v_add_u32_e32 v46, s2, v46
	s_addc_u32 s49, s49, 0
	v_ashrrev_i32_e32 v47, 31, v46
	s_and_b64 s[62:63], s[52:53], exec
	s_movk_i32 s3, 0xff00
	v_lshlrev_b64 v[46:47], 6, v[46:47]
	s_cselect_b32 s62, 0x100, s3
	v_lshl_add_u64 v[46:47], s[6:7], 0, v[46:47]
	s_lshl_b32 s78, s76, 4
	v_lshl_add_u64 v[46:47], v[46:47], 0, s[78:79]
	s_lshl_b32 s78, s27, 3
	v_lshl_add_u64 v[46:47], v[46:47], 0, s[78:79]
	global_load_dwordx2 v[114:115], v[46:47], off
	v_or_b32_e32 v46, s42, v119
	v_ashrrev_i32_e32 v50, 1, v110
	v_mad_i64_i32 v[46:47], s[2:3], s62, v46, 0
	v_and_b32_e32 v50, -8, v50
	v_lshlrev_b64 v[46:47], 1, v[46:47]
	v_ashrrev_i32_e32 v51, 31, v50
	v_lshl_add_u64 v[48:49], s[54:55], 0, v[46:47]
	v_lshlrev_b64 v[50:51], 1, v[50:51]
	v_lshl_add_u64 v[46:47], s[48:49], 0, v[46:47]
	v_lshl_add_u64 v[52:53], v[48:49], 0, v[50:51]
	v_lshl_add_u64 v[54:55], v[46:47], 0, v[50:51]
	v_lshl_add_u64 v[50:51], s[54:55], 0, v[50:51]
	v_mul_hi_i32_i24_e32 v57, s62, v32
	v_mul_i32_i24_e32 v56, s62, v32
	v_lshl_add_u64 v[66:67], v[56:57], 1, v[50:51]
	v_mul_hi_i32_i24_e32 v57, s62, v33
	v_mul_i32_i24_e32 v56, s62, v33
	v_lshl_add_u64 v[32:33], v[56:57], 1, v[50:51]
	v_ashrrev_i32_e32 v111, 31, v110
	global_load_dwordx4 v[58:61], v[52:53], off
	global_load_dwordx4 v[46:49], v[54:55], off
	global_load_dwordx4 v[70:73], v[66:67], off
	global_load_dwordx4 v[62:65], v[32:33], off
	s_nop 0
	global_load_dwordx4 v[50:53], v[52:53], off offset:64
	s_nop 0
	global_load_dwordx4 v[54:57], v[54:55], off offset:64
	s_nop 0
	global_load_dwordx4 v[74:77], v[66:67], off offset:64
	s_nop 0
	global_load_dwordx4 v[66:69], v[32:33], off offset:64
	v_lshl_add_u64 v[32:33], v[110:111], 1, s[54:55]
	s_mul_hi_i32 s3, s62, s73
	s_mul_i32 s2, s62, s73
	v_lshl_add_u64 v[86:87], s[2:3], 1, v[32:33]
	s_mul_hi_i32 s3, s62, s16
	s_mul_i32 s2, s62, s16
	global_load_ushort v131, v[86:87], off
	v_lshl_add_u64 v[86:87], s[2:3], 1, v[32:33]
	s_mul_hi_i32 s3, s62, s17
	s_mul_i32 s2, s62, s17
	global_load_ushort v133, v[86:87], off
	v_lshl_add_u64 v[86:87], s[2:3], 1, v[32:33]
	s_mul_hi_i32 s3, s62, s35
	s_mul_i32 s2, s62, s35
	global_load_ushort v135, v[86:87], off
	v_lshl_add_u64 v[86:87], s[2:3], 1, v[32:33]
	s_mul_hi_i32 s3, s62, s14
	s_mul_i32 s2, s62, s14
	global_load_ushort v137, v[86:87], off
	v_lshl_add_u64 v[86:87], s[2:3], 1, v[32:33]
	s_mul_hi_i32 s3, s62, s82
	s_mul_i32 s2, s62, s82
	global_load_ushort v111, v[86:87], off
	v_lshl_add_u64 v[86:87], s[2:3], 1, v[32:33]
	s_mul_hi_i32 s3, s62, s83
	s_mul_i32 s2, s62, s83
	global_load_ushort v132, v[86:87], off
	v_lshl_add_u64 v[86:87], s[2:3], 1, v[32:33]
	s_mul_hi_i32 s3, s62, s10
	s_mul_i32 s2, s62, s10
	v_lshl_add_u64 v[32:33], s[2:3], 1, v[32:33]
	v_and_b32_e32 v85, -16, v110
	global_load_ushort v134, v[86:87], off
	global_load_ushort v136, v[32:33], off
	v_lshl_add_u32 v32, v85, 1, 0
	v_mad_u64_u32 v[154:155], s[2:3], v85, s75, v[32:33]
	ds_read_b128 v[86:89], v154 offset:432
	s_waitcnt lgkmcnt(0)
	ds_read2_b32 v[88:89], v154 offset0:36 offset1:72
	v_cmp_eq_u32_e32 vcc, 0, v119
	v_lshlrev_b32_e32 v33, 5, v110
	v_lshlrev_b32_e32 v118, 1, v119
	v_cndmask_b32_e64 v116, 0, 1.0, vcc
	v_and_b32_e32 v33, 0xfffffe00, v33
	v_cmp_eq_u32_e32 vcc, 1, v119
	v_add3_u32 v158, s8, v118, v33
	s_waitcnt lgkmcnt(0)
	v_lshlrev_b32_e32 v88, 16, v88
	v_cndmask_b32_e64 v33, 0, 1.0, vcc
	v_fma_f32 v159, -v116, v88, v33
	v_cvt_pk_bf16_f32 v33, v159, v159
	v_cmp_eq_u32_e32 vcc, 2, v119
	s_waitcnt lgkmcnt(0)
	ds_write_b16 v158, v33 offset:55328
	v_lshlrev_b32_e32 v88, 16, v89
	v_cndmask_b32_e64 v33, 0, 1.0, vcc
	v_fma_f32 v33, -v116, v88, v33
	v_and_b32_e32 v88, 0xffff0000, v89
	v_fma_f32 v88, -v159, v88, 0
	v_add_f32_e32 v161, v33, v88
	v_cvt_pk_bf16_f32 v33, v161, v161
	v_cmp_eq_u32_e32 vcc, 3, v119
	ds_write_b16 v158, v33 offset:55360
	v_lshlrev_b32_e32 v88, 16, v86
	v_cndmask_b32_e64 v33, 0, 1.0, vcc
	v_fma_f32 v33, -v116, v88, v33
	v_and_b32_e32 v86, 0xffff0000, v86
	v_lshlrev_b32_e32 v87, 16, v87
	v_fma_f32 v86, -v159, v86, 0
	v_fma_f32 v33, -v161, v87, v33
	v_add_f32_e32 v162, v86, v33
	v_cvt_pk_bf16_f32 v33, v162, v162
	ds_write_b16_d16_hi v158, v116 offset:55296
	ds_write_b16 v158, v33 offset:55392
	ds_read_b128 v[86:89], v154 offset:576
	ds_read_b128 v[94:97], v154 offset:720
	ds_read_b128 v[98:101], v154 offset:864
	ds_read_b128 v[102:105], v154 offset:1008
	v_cmp_eq_u32_e32 vcc, 4, v119
	s_waitcnt lgkmcnt(3)
	v_lshlrev_b32_e32 v88, 16, v86
	v_and_b32_e32 v86, 0xffff0000, v86
	v_cndmask_b32_e64 v33, 0, 1.0, vcc
	v_fma_f32 v33, -v116, v88, v33
	v_fma_f32 v86, -v159, v86, 0
	v_lshlrev_b32_e32 v88, 16, v87
	v_and_b32_e32 v87, 0xffff0000, v87
	v_fma_f32 v33, -v161, v88, v33
	v_fma_f32 v86, -v162, v87, v86
	v_add_f32_e32 v163, v86, v33
	v_cvt_pk_bf16_f32 v33, v163, v163
	v_cmp_eq_u32_e32 vcc, 5, v119
	s_waitcnt lgkmcnt(0)
	ds_write_b16 v158, v33 offset:55424
	s_waitcnt lgkmcnt(3)
	v_lshlrev_b32_e32 v86, 16, v94
	v_cndmask_b32_e64 v33, 0, 1.0, vcc
	v_fma_f32 v33, -v116, v86, v33
	v_and_b32_e32 v86, 0xffff0000, v94
	v_lshlrev_b32_e32 v87, 16, v95
	v_fma_f32 v86, -v159, v86, 0
	v_fma_f32 v33, -v161, v87, v33
	v_and_b32_e32 v87, 0xffff0000, v95
	v_fma_f32 v86, -v162, v87, v86
	v_lshlrev_b32_e32 v87, 16, v96
	v_fma_f32 v33, -v163, v87, v33
	v_add_f32_e32 v178, v86, v33
	v_cvt_pk_bf16_f32 v33, v178, v178
	v_cmp_eq_u32_e32 vcc, 6, v119
	ds_write_b16 v158, v33 offset:55456
	s_waitcnt lgkmcnt(3)
; #define LAS __attribute__((address_space(3)))
; __device__ __forceinline__ unsigned f2bf(float f) { unsigned u = __float_as_uint(f); return (u + 0x7fffu + ((u >> 16) & 1u)) >> 16; }
; __device__ __forceinline__ float lo_bf(unsigned w) { return __uint_as_float(w << 16); }
; __device__ __forceinline__ float hi_bf(unsigned w) { return __uint_as_float(w & 0xffff0000u); }
; __device__ __forceinline__ void gdn_s23(CArgs& a, int u, const GdnIn2& in, LAS unsigned char* ub, LAS unsigned char* dwb, int w, int lane, float cl) {
;     ...
;     { const int blk = lane >> 4, c = lane & 15; float T[16];
; #pragma unroll
;       for (int hb = 0; hb < 4; ++hb) {
;           u32x4 arow[4][2];
; #pragma unroll
;           for (int rr = 0; rr < 4; ++rr) { const int r = 4 * hb + rr; arow[rr][0] = *(const LAS u32x4*)(AB + (16 * blk + r) * 72 + 16 * blk); if (hb >= 2) arow[rr][1] = *(const LAS u32x4*)(AB + (16 * blk + r) * 72 + 16 * blk + 8); }
;           asm volatile("s_waitcnt lgkmcnt(0)" ::: "memory");
; #pragma unroll
;           for (int rr = 0; rr < 4; ++rr) { const int r = 4 * hb + rr; float t = (r == c) ? 1.f : 0.f;
;               float t2 = 0.f;
; #pragma unroll
;               for (int j = 0; j < r; ++j) { const unsigned wv = arow[rr][j >> 3][(j >> 1) & 3]; const float av = (j & 1) ? hi_bf(wv) : lo_bf(wv); if (j & 1) t2 -= av * T[j]; else t -= av * T[j]; }
;               t += t2;
;               T[r] = t; DW[(blk * 16 + r) * 16 + c] = (bf16)f2bf(t); } } }
	v_lshlrev_b32_e32 v86, 16, v98
	v_cndmask_b32_e64 v33, 0, 1.0, vcc
	v_fma_f32 v33, -v116, v86, v33
	v_and_b32_e32 v86, 0xffff0000, v98
	v_lshlrev_b32_e32 v87, 16, v99
	v_fma_f32 v86, -v159, v86, 0
	v_fma_f32 v33, -v161, v87, v33
	v_and_b32_e32 v87, 0xffff0000, v99
	v_fma_f32 v86, -v162, v87, v86
	v_lshlrev_b32_e32 v87, 16, v100
	v_fma_f32 v33, -v163, v87, v33
	v_and_b32_e32 v87, 0xffff0000, v100
	v_fma_f32 v86, -v178, v87, v86
	v_add_f32_e32 v179, v33, v86
	v_cvt_pk_bf16_f32 v33, v179, v179
	v_cmp_eq_u32_e32 vcc, 7, v119
	ds_write_b16 v158, v33 offset:55488
	s_waitcnt lgkmcnt(3)
	v_lshlrev_b32_e32 v86, 16, v102
	v_cndmask_b32_e64 v33, 0, 1.0, vcc
	v_fma_f32 v33, -v116, v86, v33
	v_and_b32_e32 v86, 0xffff0000, v102
	v_lshlrev_b32_e32 v87, 16, v103
	v_fma_f32 v86, -v159, v86, 0
	v_fma_f32 v33, -v161, v87, v33
	v_and_b32_e32 v87, 0xffff0000, v103
	v_fma_f32 v86, -v162, v87, v86
	v_lshlrev_b32_e32 v87, 16, v104
	v_fma_f32 v33, -v163, v87, v33
	v_and_b32_e32 v87, 0xffff0000, v104
	v_fma_f32 v86, -v178, v87, v86
	v_lshlrev_b32_e32 v87, 16, v105
	v_fma_f32 v33, -v179, v87, v33
	v_add_f32_e32 v180, v86, v33
	v_cvt_pk_bf16_f32 v33, v180, v180
	ds_write_b16 v158, v33 offset:55520
	ds_read_b128 v[86:89], v154 offset:1152
	ds_read_b128 v[94:97], v154 offset:1296
	ds_read_b128 v[98:101], v154 offset:1440
	ds_read_b128 v[102:105], v154 offset:1584
	ds_read_b128 v[106:109], v154 offset:1600
	v_add_u32_e32 v33, 0x400, v154
	v_cmp_eq_u32_e32 vcc, 8, v119
	s_waitcnt lgkmcnt(0)
	ds_read2_b32 v[108:109], v33 offset0:72 offset1:108
	v_lshlrev_b32_e32 v155, 16, v86
	v_cndmask_b32_e64 v33, 0, 1.0, vcc
	v_and_b32_e32 v86, 0xffff0000, v86
	v_fma_f32 v33, -v116, v155, v33
	v_fma_f32 v86, -v159, v86, 0
	v_lshlrev_b32_e32 v155, 16, v87
	v_and_b32_e32 v87, 0xffff0000, v87
	v_fma_f32 v33, -v161, v155, v33
	v_fma_f32 v86, -v162, v87, v86
	v_lshlrev_b32_e32 v87, 16, v88
	v_fma_f32 v33, -v163, v87, v33
	v_and_b32_e32 v87, 0xffff0000, v88
	v_fma_f32 v86, -v178, v87, v86
	v_lshlrev_b32_e32 v87, 16, v89
	v_fma_f32 v33, -v179, v87, v33
	v_and_b32_e32 v87, 0xffff0000, v89
	v_fma_f32 v86, -v180, v87, v86
	v_add_f32_e32 v181, v33, v86
	v_cvt_pk_bf16_f32 v33, v181, v181
	v_cmp_eq_u32_e32 vcc, 9, v119
	s_waitcnt lgkmcnt(0)
	ds_write_b16 v158, v33 offset:55552
	v_lshlrev_b32_e32 v86, 16, v94
	v_cndmask_b32_e64 v33, 0, 1.0, vcc
	v_fma_f32 v33, -v116, v86, v33
	v_and_b32_e32 v86, 0xffff0000, v94
	v_lshlrev_b32_e32 v87, 16, v95
	v_fma_f32 v86, -v159, v86, 0
	v_fma_f32 v33, -v161, v87, v33
	v_and_b32_e32 v87, 0xffff0000, v95
	v_fma_f32 v86, -v162, v87, v86
	v_lshlrev_b32_e32 v87, 16, v96
	v_fma_f32 v33, -v163, v87, v33
	v_and_b32_e32 v87, 0xffff0000, v96
	v_fma_f32 v86, -v178, v87, v86
	v_lshlrev_b32_e32 v87, 16, v97
	v_fma_f32 v33, -v179, v87, v33
	v_and_b32_e32 v87, 0xffff0000, v97
	v_fma_f32 v86, -v180, v87, v86
	s_waitcnt lgkmcnt(1)
	v_lshlrev_b32_e32 v87, 16, v108
	v_fma_f32 v33, -v181, v87, v33
	v_add_f32_e32 v108, v86, v33
	v_cvt_pk_bf16_f32 v33, v108, v108
	v_cmp_eq_u32_e32 vcc, 10, v119
	ds_write_b16 v158, v33 offset:55584
	v_lshlrev_b32_e32 v86, 16, v98
	v_cndmask_b32_e64 v33, 0, 1.0, vcc
	v_fma_f32 v33, -v116, v86, v33
	v_and_b32_e32 v86, 0xffff0000, v98
	v_lshlrev_b32_e32 v87, 16, v99
	v_fma_f32 v86, -v159, v86, 0
	v_fma_f32 v33, -v161, v87, v33
	v_and_b32_e32 v87, 0xffff0000, v99
	v_fma_f32 v86, -v162, v87, v86
	v_lshlrev_b32_e32 v87, 16, v100
	v_fma_f32 v33, -v163, v87, v33
	v_and_b32_e32 v87, 0xffff0000, v100
	v_fma_f32 v86, -v178, v87, v86
	v_lshlrev_b32_e32 v87, 16, v101
	v_fma_f32 v33, -v179, v87, v33
	v_and_b32_e32 v87, 0xffff0000, v101
	v_fma_f32 v86, -v180, v87, v86
	v_lshlrev_b32_e32 v87, 16, v109
	v_fma_f32 v33, -v181, v87, v33
	v_and_b32_e32 v87, 0xffff0000, v109
	v_fma_f32 v86, -v108, v87, v86
	v_add_f32_e32 v109, v33, v86
	v_cvt_pk_bf16_f32 v33, v109, v109
	v_cmp_eq_u32_e32 vcc, 11, v119
	ds_write_b16 v158, v33 offset:55616
	v_lshlrev_b32_e32 v86, 16, v102
	v_cndmask_b32_e64 v33, 0, 1.0, vcc
	v_fma_f32 v33, -v116, v86, v33
	v_and_b32_e32 v86, 0xffff0000, v102
	v_lshlrev_b32_e32 v87, 16, v103
	v_fma_f32 v86, -v159, v86, 0
	v_fma_f32 v33, -v161, v87, v33
	v_and_b32_e32 v87, 0xffff0000, v103
	v_fma_f32 v86, -v162, v87, v86
	v_lshlrev_b32_e32 v87, 16, v104
	v_fma_f32 v33, -v163, v87, v33
	v_and_b32_e32 v87, 0xffff0000, v104
	v_fma_f32 v86, -v178, v87, v86
	v_lshlrev_b32_e32 v87, 16, v105
	v_fma_f32 v33, -v179, v87, v33
	v_and_b32_e32 v87, 0xffff0000, v105
	v_fma_f32 v86, -v180, v87, v86
	v_lshlrev_b32_e32 v87, 16, v106
	v_fma_f32 v33, -v181, v87, v33
	v_and_b32_e32 v87, 0xffff0000, v106
	v_fma_f32 v86, -v108, v87, v86
	v_lshlrev_b32_e32 v87, 16, v107
	v_fma_f32 v33, -v109, v87, v33
	v_add_f32_e32 v182, v86, v33
	v_cvt_pk_bf16_f32 v33, v182, v182
	ds_write_b16 v158, v33 offset:55648
	ds_read_b128 v[86:89], v154 offset:1728
	ds_read_b128 v[94:97], v154 offset:1744
	v_or_b32_e32 v33, 15, v110
	v_mad_u64_u32 v[32:33], s[2:3], v33, s75, v[32:33]
	v_cmp_eq_u32_e32 vcc, 12, v119
	s_waitcnt lgkmcnt(0)
	ds_read_b128 v[96:99], v154 offset:1872
	ds_read_b128 v[100:103], v154 offset:1888
	ds_read_b128 v[104:107], v154 offset:2016
	ds_read_b128 v[154:157], v154 offset:2032
	ds_read_b128 v[170:173], v32
	ds_read_b128 v[174:177], v32 offset:16
	v_cndmask_b32_e64 v32, 0, 1.0, vcc
	v_lshlrev_b32_e32 v33, 16, v86
	v_fma_f32 v32, -v116, v33, v32
	v_and_b32_e32 v33, 0xffff0000, v86
	v_lshlrev_b32_e32 v86, 16, v87
	v_fma_f32 v33, -v159, v33, 0
	v_fma_f32 v32, -v161, v86, v32
	v_and_b32_e32 v86, 0xffff0000, v87
	v_fma_f32 v33, -v162, v86, v33
	v_lshlrev_b32_e32 v86, 16, v88
	v_fma_f32 v32, -v163, v86, v32
	v_and_b32_e32 v86, 0xffff0000, v88
	v_fma_f32 v33, -v178, v86, v33
	v_lshlrev_b32_e32 v86, 16, v89
	v_fma_f32 v32, -v179, v86, v32
	v_and_b32_e32 v86, 0xffff0000, v89
	v_fma_f32 v33, -v180, v86, v33
	v_lshlrev_b32_e32 v86, 16, v94
	v_fma_f32 v32, -v181, v86, v32
	v_and_b32_e32 v86, 0xffff0000, v94
	v_fma_f32 v33, -v108, v86, v33
	v_lshlrev_b32_e32 v86, 16, v95
	v_fma_f32 v32, -v109, v86, v32
	v_and_b32_e32 v86, 0xffff0000, v95
	v_fma_f32 v33, -v182, v86, v33
	v_add_f32_e32 v32, v33, v32
	v_cvt_pk_bf16_f32 v33, v32, v32
	v_cmp_eq_u32_e32 vcc, 13, v119
	s_waitcnt lgkmcnt(0)
; #define LAS __attribute__((address_space(3)))
; __device__ __forceinline__ void gdn_s23(CArgs& a, int u, const GdnIn2& in, LAS unsigned char* ub, LAS unsigned char* dwb, int w, int lane, float cl) {
;     ...
;     { const int blk = lane >> 4, c = lane & 15; float T[16];
; #pragma unroll
;       for (int hb = 0; hb < 4; ++hb) {
;           u32x4 arow[4][2];
; #pragma unroll
;           for (int rr = 0; rr < 4; ++rr) { const int r = 4 * hb + rr; arow[rr][0] = *(const LAS u32x4*)(AB + (16 * blk + r) * 72 + 16 * blk); if (hb >= 2) arow[rr][1] = *(const LAS u32x4*)(AB + (16 * blk + r) * 72 + 16 * blk + 8); }
;           asm volatile("s_waitcnt lgkmcnt(0)" ::: "memory");
; #pragma unroll
;           for (int rr = 0; rr < 4; ++rr) { const int r = 4 * hb + rr; float t = (r == c) ? 1.f : 0.f;
;               float t2 = 0.f;
; #pragma unroll
;               for (int j = 0; j < r; ++j) { const unsigned wv = arow[rr][j >> 3][(j >> 1) & 3]; const float av = (j & 1) ? hi_bf(wv) : lo_bf(wv); if (j & 1) t2 -= av * T[j]; else t -= av * T[j]; }
;               t += t2;
;               T[r] = t; DW[(blk * 16 + r) * 16 + c] = (bf16)f2bf(t); } } }
;     asm volatile("s_waitcnt lgkmcnt(0)" ::: "memory");
;     f32x4 X[4];
; #pragma unroll
;     for (int I = 0; I < 4; ++I) {
;         const f32x4 br = *(const LAS f32x4*)(GT + 16 * I + 4 * kg), er = *(const LAS f32x4*)(GT + 128 + 16 * I + 4 * kg);
;         const f32x4 Rf = (f32x4){__uint_as_float(in.R[I].x << 16), __uint_as_float(in.R[I].y << 16), __uint_as_float(in.R[I].z << 16), __uint_as_float(in.R[I].w << 16)};
;         f32x4 acc = isW ? br * er * Rf : br * Rf;
; #pragma unroll
;         for (int P = 0; 2 * P < I; ++P) {
;             const u32x2 alo = *(const LAS u32x2*)(AB + (16 * I + fr) * 72 + 32 * P + 4 * kg);
;             const u32x2 ahi = (2 * P + 1 < I) ? *(const LAS u32x2*)(AB + (16 * I + fr) * 72 + 32 * P + 16 + 4 * kg) : (u32x2){0u, 0u};
;             const u32x2 xlo = cvt4(-X[2 * P]); const u32x2 xhi = (2 * P + 1 < I) ? cvt4(-X[2 * P + 1]) : (u32x2){0u, 0u};
;             acc = __builtin_amdgcn_mfma_f32_16x16x32_bf16(frag2(alo, ahi), frag2(xlo, xhi), acc, 0, 0, 0); }
;         const u32x2 dlo = *(const LAS u32x2*)(DW + (I * 16 + fr) * 16 + 4 * kg);
;         X[I] = __builtin_amdgcn_mfma_f32_16x16x32_bf16(frag2(dlo, (u32x2){0u, 0u}), frag2(cvt4(acc), (u32x2){0u, 0u}), (f32x4){0.f, 0.f, 0.f, 0.f}, 0, 0, 0);
	ds_write_b16 v158, v33 offset:55680
	s_waitcnt lgkmcnt(6)
	v_lshlrev_b32_e32 v86, 16, v96
	v_cndmask_b32_e64 v33, 0, 1.0, vcc
	v_fma_f32 v33, -v116, v86, v33
	v_and_b32_e32 v86, 0xffff0000, v96
	v_lshlrev_b32_e32 v87, 16, v97
	v_fma_f32 v86, -v159, v86, 0
	v_fma_f32 v33, -v161, v87, v33
	v_and_b32_e32 v87, 0xffff0000, v97
	v_fma_f32 v86, -v162, v87, v86
	v_lshlrev_b32_e32 v87, 16, v98
	v_fma_f32 v33, -v163, v87, v33
	v_and_b32_e32 v87, 0xffff0000, v98
	v_fma_f32 v86, -v178, v87, v86
	v_lshlrev_b32_e32 v87, 16, v99
	v_fma_f32 v33, -v179, v87, v33
	v_and_b32_e32 v87, 0xffff0000, v99
	v_fma_f32 v86, -v180, v87, v86
	s_waitcnt lgkmcnt(5)
	v_lshlrev_b32_e32 v87, 16, v100
	v_fma_f32 v33, -v181, v87, v33
	v_and_b32_e32 v87, 0xffff0000, v100
	v_fma_f32 v86, -v108, v87, v86
	v_lshlrev_b32_e32 v87, 16, v101
	v_fma_f32 v33, -v109, v87, v33
	v_and_b32_e32 v87, 0xffff0000, v101
	v_fma_f32 v86, -v182, v87, v86
	v_lshlrev_b32_e32 v87, 16, v102
	v_fma_f32 v33, -v32, v87, v33
	v_add_f32_e32 v33, v86, v33
	v_cvt_pk_bf16_f32 v86, v33, v33
	v_cmp_eq_u32_e32 vcc, 14, v119
	ds_write_b16 v158, v86 offset:55712
	s_waitcnt lgkmcnt(5)
	v_lshlrev_b32_e32 v87, 16, v104
	v_cndmask_b32_e64 v86, 0, 1.0, vcc
	v_fma_f32 v86, -v116, v87, v86
	v_and_b32_e32 v87, 0xffff0000, v104
	v_lshlrev_b32_e32 v88, 16, v105
	v_fma_f32 v87, -v159, v87, 0
	v_fma_f32 v86, -v161, v88, v86
	v_and_b32_e32 v88, 0xffff0000, v105
	v_fma_f32 v87, -v162, v88, v87
	v_lshlrev_b32_e32 v88, 16, v106
	v_fma_f32 v86, -v163, v88, v86
	v_and_b32_e32 v88, 0xffff0000, v106
	v_fma_f32 v87, -v178, v88, v87
	v_lshlrev_b32_e32 v88, 16, v107
	v_fma_f32 v86, -v179, v88, v86
	v_and_b32_e32 v88, 0xffff0000, v107
	v_fma_f32 v87, -v180, v88, v87
	s_waitcnt lgkmcnt(4)
	v_lshlrev_b32_e32 v88, 16, v154
	v_fma_f32 v86, -v181, v88, v86
	v_and_b32_e32 v88, 0xffff0000, v154
	v_fma_f32 v87, -v108, v88, v87
	v_lshlrev_b32_e32 v88, 16, v155
	v_fma_f32 v86, -v109, v88, v86
	v_and_b32_e32 v88, 0xffff0000, v155
	v_fma_f32 v87, -v182, v88, v87
	v_lshlrev_b32_e32 v88, 16, v156
	v_fma_f32 v86, -v32, v88, v86
	v_and_b32_e32 v88, 0xffff0000, v156
	v_fma_f32 v87, -v33, v88, v87
	v_add_f32_e32 v86, v86, v87
	v_cvt_pk_bf16_f32 v87, v86, v86
	v_cmp_eq_u32_e32 vcc, 15, v119
	ds_write_b16 v158, v87 offset:55744
	s_waitcnt lgkmcnt(4)
	v_lshlrev_b32_e32 v88, 16, v170
	v_cndmask_b32_e64 v87, 0, 1.0, vcc
	v_fma_f32 v87, -v116, v88, v87
	v_and_b32_e32 v88, 0xffff0000, v170
	v_lshlrev_b32_e32 v89, 16, v171
	v_fma_f32 v88, -v159, v88, 0
	v_fma_f32 v87, -v161, v89, v87
	v_and_b32_e32 v89, 0xffff0000, v171
	v_fma_f32 v88, -v162, v89, v88
	v_lshlrev_b32_e32 v89, 16, v172
	v_fma_f32 v87, -v163, v89, v87
	v_and_b32_e32 v89, 0xffff0000, v172
	v_fma_f32 v88, -v178, v89, v88
	v_lshlrev_b32_e32 v89, 16, v173
	v_fma_f32 v87, -v179, v89, v87
	v_and_b32_e32 v89, 0xffff0000, v173
	v_fma_f32 v88, -v180, v89, v88
	s_waitcnt lgkmcnt(3)
	v_lshlrev_b32_e32 v89, 16, v174
	v_fma_f32 v87, -v181, v89, v87
	v_and_b32_e32 v89, 0xffff0000, v174
	v_fma_f32 v88, -v108, v89, v88
	v_lshlrev_b32_e32 v89, 16, v175
	v_fma_f32 v87, -v109, v89, v87
	v_and_b32_e32 v89, 0xffff0000, v175
	v_fma_f32 v88, -v182, v89, v88
	v_lshlrev_b32_e32 v89, 16, v176
	v_fma_f32 v32, -v32, v89, v87
	v_and_b32_e32 v87, 0xffff0000, v176
	v_fma_f32 v33, -v33, v87, v88
	v_lshlrev_b32_e32 v87, 16, v177
	v_fma_f32 v32, -v86, v87, v32
	v_add_f32_e32 v32, v33, v32
	v_cvt_pk_bf16_f32 v32, v32, v32
	ds_write_b16 v158, v32 offset:55776
	s_waitcnt lgkmcnt(0)
	v_add_u32_e32 v157, s8, v85
	ds_read_b128 v[94:97], v157 offset:57344
	ds_read_b128 v[86:89], v157 offset:57856
	v_ashrrev_i32_e32 v123, 4, v110
	v_lshlrev_b32_e32 v104, 3, v123
	v_lshlrev_b32_e32 v33, 16, v82
	v_lshlrev_b32_e32 v82, 16, v83
	v_lshlrev_b32_e32 v83, 16, v84
	s_waitcnt lgkmcnt(0)
	v_pk_mul_f32 v[84:85], v[96:97], v[88:89]
	v_pk_mul_f32 v[98:99], v[94:95], v[86:87]
	v_sub_u32_e32 v158, v157, v104
	v_lshlrev_b32_e32 v32, 16, v34
	v_cndmask_b32_e64 v85, v97, v85, s[38:39]
	v_cndmask_b32_e64 v84, v96, v84, s[38:39]
	v_cndmask_b32_e64 v95, v95, v99, s[38:39]
	v_cndmask_b32_e64 v94, v94, v98, s[38:39]
	v_pk_mul_f32 v[84:85], v[84:85], v[82:83]
	v_pk_mul_f32 v[82:83], v[94:95], v[32:33]
	v_lshl_add_u32 v32, v119, 5, v158
	ds_read_b64 v[32:33], v32 offset:55296
	v_cvt_pk_bf16_f32 v82, v82, v82
	v_bfe_u32 v94, v83, 16, 1
	v_mov_b32_e32 v34, v35
	v_lshrrev_b32_e32 v82, 16, v82
	v_add3_u32 v83, v83, v94, s81
	v_and_or_b32 v82, v83, s80, v82
	v_cvt_pk_bf16_f32 v83, v84, v85
	v_mov_b32_e32 v84, v35
	v_mov_b32_e32 v85, v35
	v_or_b32_e32 v156, 16, v119
	v_add_u32_e32 v154, 0, v104
	s_waitcnt lgkmcnt(0)
	v_mfma_f32_16x16x32_bf16 v[94:97], v[32:35], v[82:85], 0
	ds_read_b128 v[98:101], v157 offset:57408
	ds_read_b128 v[82:85], v157 offset:57920
	v_lshlrev_b32_e32 v32, 16, v78
	s_waitcnt vmcnt(27)
	v_lshlrev_b32_e32 v33, 16, v79
	s_waitcnt vmcnt(26)
	v_lshlrev_b32_e32 v78, 16, v80
	s_waitcnt vmcnt(25)
	v_lshlrev_b32_e32 v79, 16, v81
	s_waitcnt lgkmcnt(0)
	v_pk_mul_f32 v[80:81], v[100:101], v[84:85]
	v_pk_mul_f32 v[102:103], v[98:99], v[82:83]
	v_cndmask_b32_e64 v81, v101, v81, s[38:39]
	v_cndmask_b32_e64 v80, v100, v80, s[38:39]
	v_cndmask_b32_e64 v99, v99, v103, s[38:39]
	v_cndmask_b32_e64 v98, v98, v102, s[38:39]
	v_xor_b32_e32 v100, 0x80000000, v95
	v_pk_mul_f32 v[80:81], v[80:81], v[78:79]
	v_pk_mul_f32 v[78:79], v[98:99], v[32:33]
	v_xor_b32_e32 v99, 0x80000000, v94
	v_bfe_u32 v101, v100, 16, 1
	v_add3_u32 v100, v100, v101, s81
	v_bfe_u32 v101, v99, 16, 1
	v_add3_u32 v99, v99, v101, s81
	v_mad_u32_u24 v159, v156, s75, v154
	v_xor_b32_e32 v98, 0x80000000, v97
	v_lshrrev_b32_e32 v99, 16, v99
	ds_read_b64 v[32:33], v159
	v_xor_b32_e32 v34, 0x80000000, v96
	v_and_or_b32 v106, v100, s80, v99
	v_cvt_pk_bf16_f32 v98, v98, v98
	v_bfe_u32 v99, v34, 16, 1
	v_add3_u32 v34, v34, v99, s81
	v_lshrrev_b32_e32 v34, 16, v34
	v_and_or_b32 v107, v98, s80, v34
	v_mov_b32_e32 v34, v35
	v_mov_b32_e32 v108, v35
	v_mov_b32_e32 v109, v35
	v_or_b32_e32 v155, 32, v119
	s_ashr_i32 s27, s26, 31
	s_waitcnt lgkmcnt(0)
; #define LAS __attribute__((address_space(3)))
; __device__ __forceinline__ void gdn_s23(CArgs& a, int u, const GdnIn2& in, LAS unsigned char* ub, LAS unsigned char* dwb, int w, int lane, float cl) {
;     ...
;     f32x4 X[4];
; #pragma unroll
;     for (int I = 0; I < 4; ++I) {
;         const f32x4 br = *(const LAS f32x4*)(GT + 16 * I + 4 * kg), er = *(const LAS f32x4*)(GT + 128 + 16 * I + 4 * kg);
;         const f32x4 Rf = (f32x4){__uint_as_float(in.R[I].x << 16), __uint_as_float(in.R[I].y << 16), __uint_as_float(in.R[I].z << 16), __uint_as_float(in.R[I].w << 16)};
;         f32x4 acc = isW ? br * er * Rf : br * Rf;
; #pragma unroll
;         for (int P = 0; 2 * P < I; ++P) {
;             const u32x2 alo = *(const LAS u32x2*)(AB + (16 * I + fr) * 72 + 32 * P + 4 * kg);
;             const u32x2 ahi = (2 * P + 1 < I) ? *(const LAS u32x2*)(AB + (16 * I + fr) * 72 + 32 * P + 16 + 4 * kg) : (u32x2){0u, 0u};
;             const u32x2 xlo = cvt4(-X[2 * P]); const u32x2 xhi = (2 * P + 1 < I) ? cvt4(-X[2 * P + 1]) : (u32x2){0u, 0u};
;             acc = __builtin_amdgcn_mfma_f32_16x16x32_bf16(frag2(alo, ahi), frag2(xlo, xhi), acc, 0, 0, 0); }
;         const u32x2 dlo = *(const LAS u32x2*)(DW + (I * 16 + fr) * 16 + 4 * kg);
;         X[I] = __builtin_amdgcn_mfma_f32_16x16x32_bf16(frag2(dlo, (u32x2){0u, 0u}), frag2(cvt4(acc), (u32x2){0u, 0u}), (f32x4){0.f, 0.f, 0.f, 0.f}, 0, 0, 0);
;     }
;     const bf16x8 Xb01 = frag2(cvt4(X[0]), cvt4(X[1])), Xb23 = frag2(cvt4(X[2]), cvt4(X[3]));
;     const float ecl = __expf(cl);
;     bf16* ftp = FTo + (c0 + fr) * 64 + 4 * kg; bf16* btp = BTo + (c0 + fr) * 64 + 4 * kg; bf16* ep = Eo + (4 * kg) * 64 + c0 + fr; bf16* mp = Mo + (4 * kg) * 64 + c0 + fr;
; #pragma unroll
;     for (int t4 = 0; t4 < 4; ++t4) {
;         const LAS bf16* ar = ATT + (16 * t4 + fr) * 72 + 4 * kg; const LAS bf16* kr = KTT + (16 * t4 + fr) * 72 + 4 * kg;
;         f32x4 pa = (f32x4){0.f, 0.f, 0.f, 0.f}, pk = (f32x4){0.f, 0.f, 0.f, 0.f};
;         pa = __builtin_amdgcn_mfma_f32_16x16x32_bf16(frag2(*(const LAS u32x2*)ar, *(const LAS u32x2*)(ar + 16)), Xb01, pa, 0, 0, 0);
;         pa = __builtin_amdgcn_mfma_f32_16x16x32_bf16(frag2(*(const LAS u32x2*)(ar + 32), *(const LAS u32x2*)(ar + 48)), Xb23, pa, 0, 0, 0);
;         pk = __builtin_amdgcn_mfma_f32_16x16x32_bf16(frag2(*(const LAS u32x2*)kr, *(const LAS u32x2*)(kr + 16)), Xb01, pk, 0, 0, 0);
	v_mfma_f32_16x16x32_bf16 v[78:81], v[32:35], v[106:109], v[78:81]
	v_lshl_add_u32 v32, v156, 5, v158
	ds_read_b64 v[32:33], v32 offset:55296
	s_lshl_b64 s[76:77], s[26:27], 13
	s_add_u32 s62, s85, s76
	s_addc_u32 s63, s64, s77
	s_nop 2
	v_cvt_pk_bf16_f32 v78, v78, v78
	v_bfe_u32 v98, v79, 16, 1
	v_lshrrev_b32_e32 v78, 16, v78
	v_add3_u32 v79, v79, v98, s81
	v_and_or_b32 v78, v79, s80, v78
	v_cvt_pk_bf16_f32 v79, v80, v81
	v_mov_b32_e32 v80, v35
	v_mov_b32_e32 v81, v35
	s_add_u32 s48, s71, s76
	s_addc_u32 s49, s18, s77
	s_waitcnt lgkmcnt(0)
	v_mfma_f32_16x16x32_bf16 v[98:101], v[32:35], v[78:81], 0
	ds_read_b128 v[102:105], v157 offset:57472
	ds_read_b128 v[78:81], v157 offset:57984
	s_waitcnt vmcnt(24)
	v_lshlrev_b32_e32 v32, 16, v90
	s_waitcnt vmcnt(23)
	v_lshlrev_b32_e32 v33, 16, v91
	s_waitcnt vmcnt(22)
	v_lshlrev_b32_e32 v90, 16, v92
	s_waitcnt vmcnt(21)
	v_lshlrev_b32_e32 v91, 16, v93
	s_waitcnt lgkmcnt(0)
	v_pk_mul_f32 v[92:93], v[104:105], v[80:81]
	v_pk_mul_f32 v[108:109], v[102:103], v[78:79]
	v_cndmask_b32_e64 v93, v105, v93, s[38:39]
	v_cndmask_b32_e64 v92, v104, v92, s[38:39]
	v_cndmask_b32_e64 v103, v103, v109, s[38:39]
	v_cndmask_b32_e64 v102, v102, v108, s[38:39]
	v_pk_mul_f32 v[92:93], v[92:93], v[90:91]
	v_pk_mul_f32 v[90:91], v[102:103], v[32:33]
	v_add_u32_e32 v32, 0x800, v159
	v_xor_b32_e32 v108, 0x80000000, v99
	ds_read2_b64 v[102:105], v32 offset0:32 offset1:36
	v_xor_b32_e32 v34, 0x80000000, v98
	v_xor_b32_e32 v33, 0x80000000, v101
	v_xor_b32_e32 v32, 0x80000000, v100
	v_cvt_pk_bf16_f32 v108, v34, v108
	v_cvt_pk_bf16_f32 v109, v32, v33
	v_lshl_add_u32 v32, v155, 5, v158
	ds_read_b64 v[32:33], v32 offset:55296
	s_waitcnt lgkmcnt(1)
	v_mfma_f32_16x16x32_bf16 v[90:93], v[102:105], v[106:109], v[90:93]
	v_mov_b32_e32 v34, v35
	s_add_u32 s2, s19, s76
	v_lshlrev_b32_e32 v116, 2, v123
	s_addc_u32 s3, s66, s77
	s_add_u32 s54, s21, s76
	s_nop 2
	v_cvt_pk_bf16_f32 v90, v90, v90
	v_bfe_u32 v102, v91, 16, 1
	v_lshrrev_b32_e32 v90, 16, v90
	v_add3_u32 v91, v91, v102, s81
	v_and_or_b32 v90, v91, s80, v90
	v_cvt_pk_bf16_f32 v91, v92, v93
	v_mov_b32_e32 v92, v35
	v_mov_b32_e32 v93, v35
	s_addc_u32 s55, s70, s77
	s_mov_b64 s[76:77], -1
	s_waitcnt lgkmcnt(0)
	v_mfma_f32_16x16x32_bf16 v[102:105], v[32:35], v[90:93], 0
	ds_read_b128 v[170:173], v157 offset:57536
	ds_read_b128 v[90:93], v157 offset:58048
	s_waitcnt vmcnt(20)
	v_lshlrev_b32_e32 v32, 16, v117
	s_waitcnt vmcnt(19)
	v_lshlrev_b32_e32 v33, 16, v120
	s_waitcnt vmcnt(18)
	v_lshlrev_b32_e32 v120, 16, v121
	s_waitcnt vmcnt(17)
	v_lshlrev_b32_e32 v121, 16, v122
	s_waitcnt lgkmcnt(0)
	v_pk_mul_f32 v[174:175], v[170:171], v[90:91]
	v_pk_mul_f32 v[162:163], v[172:173], v[92:93]
	v_cndmask_b32_e64 v171, v171, v175, s[38:39]
	v_cndmask_b32_e64 v170, v170, v174, s[38:39]
	v_pk_mul_f32 v[170:171], v[170:171], v[32:33]
	v_add_u32_e32 v32, 0x1000, v159
	ds_read2_b64 v[174:177], v32 offset0:64 offset1:68
	v_cndmask_b32_e64 v163, v173, v163, s[38:39]
	v_cndmask_b32_e64 v162, v172, v162, s[38:39]
	v_pk_mul_f32 v[172:173], v[162:163], v[120:121]
	v_xor_b32_e32 v121, 0x80000000, v103
	v_xor_b32_e32 v120, 0x80000000, v102
	v_cvt_pk_bf16_f32 v121, v121, v121
	v_cvt_pk_bf16_f32 v120, v120, v120
	v_xor_b32_e32 v117, 0x80000000, v105
	v_lshrrev_b32_e32 v120, 16, v120
	s_waitcnt lgkmcnt(0)
	v_mfma_f32_16x16x32_bf16 v[106:109], v[174:177], v[106:109], v[170:173]
	ds_read_b64 v[32:33], v159 offset:4672
	v_xor_b32_e32 v34, 0x80000000, v104
	v_or_b32_e32 v157, 48, v119
	v_and_or_b32 v170, v121, s80, v120
	v_cvt_pk_bf16_f32 v171, v34, v117
	v_mov_b32_e32 v34, v35
	v_mov_b32_e32 v172, v35
	v_mov_b32_e32 v173, v35
	s_andn2_b64 vcc, exec, s[60:61]
	s_waitcnt lgkmcnt(0)
	v_mfma_f32_16x16x32_bf16 v[106:109], v[32:35], v[170:173], v[106:109]
	v_lshl_add_u32 v32, v157, 5, v158
	ds_read_b64 v[32:33], v32 offset:55296
	s_nop 5
	v_cvt_pk_bf16_f32 v106, v106, v107
	v_cvt_pk_bf16_f32 v107, v108, v109
	v_mov_b32_e32 v108, v35
	v_mov_b32_e32 v109, v35
	v_ashrrev_i32_e32 v117, 31, v116
	s_waitcnt lgkmcnt(0)
	v_mfma_f32_16x16x32_bf16 v[106:109], v[32:35], v[106:109], 0
	v_cvt_pk_bf16_f32 v94, v94, v95
	v_cvt_pk_bf16_f32 v95, v96, v97
	v_cvt_pk_bf16_f32 v96, v98, v99
	v_cvt_pk_bf16_f32 v97, v100, v101
	v_cvt_pk_bf16_f32 v98, v102, v103
	v_cvt_pk_bf16_f32 v99, v104, v105
	s_nop 1
	v_cvt_pk_bf16_f32 v100, v106, v107
	v_lshlrev_b32_e32 v34, 7, v45
	v_cvt_pk_bf16_f32 v101, v108, v109
	v_lshl_add_u64 v[32:33], s[48:49], 0, v[34:35]
	v_lshlrev_b64 v[102:103], 1, v[116:117]
	v_lshl_add_u64 v[120:121], v[32:33], 0, v[102:103]
	v_lshl_add_u64 v[32:33], s[54:55], 0, v[34:35]
	v_mul_u32_u24_e32 v34, 0x48, v119
	v_lshl_add_u32 v34, v34, 1, v154
	v_add_u32_e32 v106, 0x2000, v34
	v_lshl_add_u64 v[32:33], v[32:33], 0, v[102:103]
	ds_read2_b64 v[102:105], v106 offset0:128 offset1:132
	ds_read2_b64 v[106:109], v106 offset0:136 offset1:140
	s_waitcnt lgkmcnt(1)
	v_mfma_f32_16x16x32_bf16 v[102:105], v[102:105], v[94:97], 0
	v_add_u32_e32 v34, 0x4800, v34
	ds_read2_b64 v[170:173], v34 offset0:8 offset1:12
	s_waitcnt lgkmcnt(1)
	v_mfma_f32_16x16x32_bf16 v[102:105], v[106:109], v[98:101], v[102:105]
	ds_read2_b64 v[106:109], v34 offset1:4
	v_cndmask_b32_e64 v34, 0, 1, s[60:61]
	v_cmp_ne_u32_e64 s[48:49], 1, v34
	s_waitcnt lgkmcnt(0)
	v_mfma_f32_16x16x32_bf16 v[106:109], v[106:109], v[94:97], 0
	v_mfma_f32_16x16x32_bf16 v[106:109], v[170:173], v[98:101], v[106:109]
	s_cbranch_vccnz .LBB0_1725
	s_nop 0
	v_cvt_pk_bf16_f32 v158, v102, v103
	v_cvt_pk_bf16_f32 v159, v104, v105
	global_store_dwordx2 v[120:121], v[158:159], off
	s_nop 2
	v_cvt_pk_bf16_f32 v158, v106, v107
	v_cvt_pk_bf16_f32 v34, v108, v108
	v_bfe_u32 v117, v109, 16, 1
	v_lshrrev_b32_e32 v34, 16, v34
	v_add3_u32 v117, v109, v117, s81
	v_and_or_b32 v159, v117, s80, v34
	s_mov_b64 s[76:77], 0
	global_store_dwordx2 v[32:33], v[158:159], off

; #define LAS __attribute__((address_space(3)))
; __device__ __forceinline__ u32x2 cvt4(f32x4 v) { return (u32x2){pk2(v[0], v[1]), pk2(v[2], v[3])}; }
; __device__ __forceinline__ void gdn_s23(CArgs& a, int u, const GdnIn2& in, LAS unsigned char* ub, LAS unsigned char* dwb, int w, int lane, float cl) {
;     ...
;     for (int t4 = 0; t4 < 4; ++t4) {
;         const LAS bf16* ar = ATT + (16 * t4 + fr) * 72 + 4 * kg; const LAS bf16* kr = KTT + (16 * t4 + fr) * 72 + 4 * kg;
;         f32x4 pa = (f32x4){0.f, 0.f, 0.f, 0.f}, pk = (f32x4){0.f, 0.f, 0.f, 0.f};
;         pa = __builtin_amdgcn_mfma_f32_16x16x32_bf16(frag2(*(const LAS u32x2*)ar, *(const LAS u32x2*)(ar + 16)), Xb01, pa, 0, 0, 0);
;         pa = __builtin_amdgcn_mfma_f32_16x16x32_bf16(frag2(*(const LAS u32x2*)(ar + 32), *(const LAS u32x2*)(ar + 48)), Xb23, pa, 0, 0, 0);
;         pk = __builtin_amdgcn_mfma_f32_16x16x32_bf16(frag2(*(const LAS u32x2*)kr, *(const LAS u32x2*)(kr + 16)), Xb01, pk, 0, 0, 0);
;         pk = __builtin_amdgcn_mfma_f32_16x16x32_bf16(frag2(*(const LAS u32x2*)(kr + 32), *(const LAS u32x2*)(kr + 48)), Xb23, pk, 0, 0, 0);
;         if (!isW) {
;             *(u32x2*)(ftp + 16 * t4) = cvt4(pa);
;             *(u32x2*)(btp + 16 * t4) = cvt4(pk);
.LBB0_1727:
	v_mul_u32_u24_e32 v86, 0x48, v156
	v_lshl_add_u32 v106, v86, 1, v154
	v_add_u32_e32 v102, 0x2000, v106
	ds_read2_b64 v[86:89], v102 offset0:128 offset1:132
	ds_read2_b64 v[102:105], v102 offset0:136 offset1:140
	v_add_u32_e32 v106, 0x4800, v106
	s_mov_b64 s[2:3], -1
	s_and_b64 vcc, exec, s[48:49]
	s_waitcnt lgkmcnt(1)
	v_mfma_f32_16x16x32_bf16 v[86:89], v[86:89], v[94:97], 0
	s_waitcnt lgkmcnt(0)
	v_mfma_f32_16x16x32_bf16 v[86:89], v[102:105], v[98:101], v[86:89]
	ds_read2_b64 v[102:105], v106 offset1:4
	ds_read2_b64 v[106:109], v106 offset0:8 offset1:12
	s_waitcnt lgkmcnt(1)
	v_mfma_f32_16x16x32_bf16 v[102:105], v[102:105], v[94:97], 0
	s_waitcnt lgkmcnt(0)
	v_mfma_f32_16x16x32_bf16 v[102:105], v[106:109], v[98:101], v[102:105]
	s_cbranch_vccnz .LBB0_1729
	s_nop 0
	v_cvt_pk_bf16_f32 v106, v86, v87
	v_cvt_pk_bf16_f32 v107, v88, v89
	global_store_dwordx2 v[120:121], v[106:107], off offset:32
	s_nop 2
	v_cvt_pk_bf16_f32 v106, v102, v103
	v_cvt_pk_bf16_f32 v107, v104, v104
	v_bfe_u32 v108, v105, 16, 1
	v_lshrrev_b32_e32 v107, 16, v107
	v_add3_u32 v108, v105, v108, s81
	v_and_or_b32 v107, v108, s80, v107
	s_mov_b64 s[2:3], 0
	global_store_dwordx2 v[32:33], v[106:107], off offset:32

; #define LAS __attribute__((address_space(3)))
; __device__ __forceinline__ u32x2 cvt4(f32x4 v) { return (u32x2){pk2(v[0], v[1]), pk2(v[2], v[3])}; }
; __device__ __forceinline__ void gdn_s23(CArgs& a, int u, const GdnIn2& in, LAS unsigned char* ub, LAS unsigned char* dwb, int w, int lane, float cl) {
;     ...
;     for (int t4 = 0; t4 < 4; ++t4) {
;         const LAS bf16* ar = ATT + (16 * t4 + fr) * 72 + 4 * kg; const LAS bf16* kr = KTT + (16 * t4 + fr) * 72 + 4 * kg;
;         f32x4 pa = (f32x4){0.f, 0.f, 0.f, 0.f}, pk = (f32x4){0.f, 0.f, 0.f, 0.f};
;         pa = __builtin_amdgcn_mfma_f32_16x16x32_bf16(frag2(*(const LAS u32x2*)ar, *(const LAS u32x2*)(ar + 16)), Xb01, pa, 0, 0, 0);
;         pa = __builtin_amdgcn_mfma_f32_16x16x32_bf16(frag2(*(const LAS u32x2*)(ar + 32), *(const LAS u32x2*)(ar + 48)), Xb23, pa, 0, 0, 0);
;         pk = __builtin_amdgcn_mfma_f32_16x16x32_bf16(frag2(*(const LAS u32x2*)kr, *(const LAS u32x2*)(kr + 16)), Xb01, pk, 0, 0, 0);
;         pk = __builtin_amdgcn_mfma_f32_16x16x32_bf16(frag2(*(const LAS u32x2*)(kr + 32), *(const LAS u32x2*)(kr + 48)), Xb23, pk, 0, 0, 0);
;         if (!isW) {
;             *(u32x2*)(ftp + 16 * t4) = cvt4(pa);
;             *(u32x2*)(btp + 16 * t4) = cvt4(pk);
.LBB0_1731:
	v_mul_u32_u24_e32 v82, 0x48, v155
	s_nop 3
	v_lshl_add_u32 v102, v82, 1, v154
	v_add_u32_e32 v86, 0x2000, v102
	ds_read2_b64 v[82:85], v86 offset0:128 offset1:132
	ds_read2_b64 v[86:89], v86 offset0:136 offset1:140
	v_add_u32_e32 v102, 0x4800, v102
	s_mov_b64 s[2:3], -1
	s_and_b64 vcc, exec, s[48:49]
	s_waitcnt lgkmcnt(1)
	v_mfma_f32_16x16x32_bf16 v[82:85], v[82:85], v[94:97], 0
	s_waitcnt lgkmcnt(0)
	v_mfma_f32_16x16x32_bf16 v[82:85], v[86:89], v[98:101], v[82:85]
	ds_read2_b64 v[86:89], v102 offset1:4
	ds_read2_b64 v[102:105], v102 offset0:8 offset1:12
	s_waitcnt lgkmcnt(1)
	v_mfma_f32_16x16x32_bf16 v[86:89], v[86:89], v[94:97], 0
	s_waitcnt lgkmcnt(0)
	v_mfma_f32_16x16x32_bf16 v[86:89], v[102:105], v[98:101], v[86:89]
	s_cbranch_vccnz .LBB0_1733
	s_nop 0
	v_cvt_pk_bf16_f32 v102, v82, v83
	v_cvt_pk_bf16_f32 v103, v84, v85
	global_store_dwordx2 v[120:121], v[102:103], off offset:64
	s_nop 2
	v_cvt_pk_bf16_f32 v102, v86, v87
	v_cvt_pk_bf16_f32 v103, v88, v88
	v_bfe_u32 v104, v89, 16, 1
	v_lshrrev_b32_e32 v103, 16, v103
	v_add3_u32 v104, v89, v104, s81
	v_and_or_b32 v103, v104, s80, v103
	s_mov_b64 s[2:3], 0
	global_store_dwordx2 v[32:33], v[102:103], off offset:64

; #define LAS __attribute__((address_space(3)))
; __device__ __forceinline__ unsigned f2bf(float f) { unsigned u = __float_as_uint(f); return (u + 0x7fffu + ((u >> 16) & 1u)) >> 16; }
; __device__ __forceinline__ u32x2 cvt4(f32x4 v) { return (u32x2){pk2(v[0], v[1]), pk2(v[2], v[3])}; }
; __device__ __forceinline__ void gdn_s23(CArgs& a, int u, const GdnIn2& in, LAS unsigned char* ub, LAS unsigned char* dwb, int w, int lane, float cl) {
;     ...
;     for (int t4 = 0; t4 < 4; ++t4) {
;         const LAS bf16* ar = ATT + (16 * t4 + fr) * 72 + 4 * kg; const LAS bf16* kr = KTT + (16 * t4 + fr) * 72 + 4 * kg;
;         f32x4 pa = (f32x4){0.f, 0.f, 0.f, 0.f}, pk = (f32x4){0.f, 0.f, 0.f, 0.f};
;         pa = __builtin_amdgcn_mfma_f32_16x16x32_bf16(frag2(*(const LAS u32x2*)ar, *(const LAS u32x2*)(ar + 16)), Xb01, pa, 0, 0, 0);
;         pa = __builtin_amdgcn_mfma_f32_16x16x32_bf16(frag2(*(const LAS u32x2*)(ar + 32), *(const LAS u32x2*)(ar + 48)), Xb23, pa, 0, 0, 0);
;         pk = __builtin_amdgcn_mfma_f32_16x16x32_bf16(frag2(*(const LAS u32x2*)kr, *(const LAS u32x2*)(kr + 16)), Xb01, pk, 0, 0, 0);
;         pk = __builtin_amdgcn_mfma_f32_16x16x32_bf16(frag2(*(const LAS u32x2*)(kr + 32), *(const LAS u32x2*)(kr + 48)), Xb23, pk, 0, 0, 0);
;         if (!isW) {
;             *(u32x2*)(ftp + 16 * t4) = cvt4(pa);
;             *(u32x2*)(btp + 16 * t4) = cvt4(pk);
;         } else {
;             const f32x4 ec = *(const LAS f32x4*)(GT + 128 + 16 * t4 + 4 * kg);
; #pragma unroll
;             for (int e = 0; e < 4; ++e) { const int row = 16 * t4 + 4 * kg + e, col = c0 + fr;
;                 ep[(16 * t4 + e) * 64] = (bf16)f2bf(ec[e] * __uint_as_float(in.Qv[t4][e] << 16) - pa[e]);
;                 mp[(16 * t4 + e) * 64] = (bf16)f2bf((row == col ? ecl : 0.f) - pk[e]); }
;         }
;     }
.LBB0_1735:
	v_mul_u32_u24_e32 v78, 0x48, v157
	s_nop 3
	v_lshl_add_u32 v86, v78, 1, v154
	v_add_u32_e32 v82, 0x2000, v86
	ds_read2_b64 v[78:81], v82 offset0:128 offset1:132
	ds_read2_b64 v[82:85], v82 offset0:136 offset1:140
	v_add_u32_e32 v86, 0x4800, v86
	s_mov_b64 s[2:3], -1
	s_and_b64 vcc, exec, s[48:49]
	s_waitcnt lgkmcnt(1)
	v_mfma_f32_16x16x32_bf16 v[78:81], v[78:81], v[94:97], 0
	s_waitcnt lgkmcnt(0)
	v_mfma_f32_16x16x32_bf16 v[78:81], v[82:85], v[98:101], v[78:81]
	ds_read2_b64 v[82:85], v86 offset1:4
	ds_read2_b64 v[86:89], v86 offset0:8 offset1:12
	s_waitcnt lgkmcnt(1)
	v_mfma_f32_16x16x32_bf16 v[82:85], v[82:85], v[94:97], 0
	s_waitcnt lgkmcnt(0)
	v_mfma_f32_16x16x32_bf16 v[82:85], v[86:89], v[98:101], v[82:85]
	s_cbranch_vccnz .LBB0_1737
	s_nop 0
	v_cvt_pk_bf16_f32 v86, v78, v79
	v_cvt_pk_bf16_f32 v87, v80, v81
	global_store_dwordx2 v[120:121], v[86:87], off offset:96
	s_nop 2
	v_cvt_pk_bf16_f32 v86, v82, v83
	v_cvt_pk_bf16_f32 v87, v84, v84
	v_bfe_u32 v88, v85, 16, 1
	v_lshrrev_b32_e32 v87, 16, v87
	v_add3_u32 v88, v85, v88, s81
	v_and_or_b32 v87, v88, s80, v87
	s_mov_b64 s[2:3], 0
	global_store_dwordx2 v[32:33], v[86:87], off offset:96
.LBB0_1737:
	s_andn2_b64 vcc, exec, s[2:3]
	s_cbranch_vccnz .LBB0_1739
	v_fma_f32 v32, v140, v90, -v78
	v_cvt_pk_bf16_f32 v78, v32, v32
	v_add_co_u32_e32 v32, vcc, 0x1000, v122
	v_add_u32_e32 v86, 48, v116
	s_nop 0
	v_addc_co_u32_e32 v33, vcc, 0, v123, vcc
	v_cmp_eq_u32_e32 vcc, v86, v45
	global_store_short v[32:33], v78, off offset:2048
	v_fma_f32 v79, v138, v91, -v79
	v_cndmask_b32_e32 v78, 0, v34, vcc
	v_sub_f32_e32 v78, v78, v82
	v_add_co_u32_e32 v86, vcc, 0x1000, v118
	v_cvt_pk_bf16_f32 v78, v78, v78
	s_nop 0
	v_addc_co_u32_e32 v87, vcc, 0, v119, vcc
	global_store_short v[86:87], v78, off offset:2048
	v_add_u32_e32 v78, 49, v116
	v_cmp_eq_u32_e32 vcc, v78, v45
	v_cvt_pk_bf16_f32 v79, v79, v79
	s_nop 0
	v_cndmask_b32_e32 v78, 0, v34, vcc
	v_sub_f32_e32 v78, v78, v83
	global_store_short_d16_hi v[32:33], v79, off offset:2176
	v_cvt_pk_bf16_f32 v78, v78, v78
	global_store_short v[86:87], v78, off offset:2176
	v_add_u32_e32 v78, 50, v116
	v_fma_f32 v79, v141, v92, -v80
	v_cmp_eq_u32_e32 vcc, v78, v45
	v_cvt_pk_bf16_f32 v79, v79, v79
	s_nop 0
	v_cndmask_b32_e32 v78, 0, v34, vcc
	v_sub_f32_e32 v78, v78, v84
	global_store_short v[32:33], v79, off offset:2304
	v_cvt_pk_bf16_f32 v78, v78, v78
	v_fma_f32 v79, v139, v93, -v81
	global_store_short v[86:87], v78, off offset:2304
	v_add_u32_e32 v78, 51, v116
	v_bfe_u32 v80, v79, 16, 1
	v_add3_u32 v79, v79, v80, s81
	v_cmp_eq_u32_e32 vcc, v78, v45
	global_store_short_d16_hi v[32:33], v79, off offset:2432
	s_nop 0
	v_cndmask_b32_e32 v32, 0, v34, vcc
	v_sub_f32_e32 v32, v32, v85
	v_bfe_u32 v33, v32, 16, 1
	v_add3_u32 v32, v32, v33, s81
	global_store_short_d16_hi v[86:87], v32, off offset:2432

; #define LAS __attribute__((address_space(3)))
; __device__ __forceinline__ unsigned f2bf(float f) { unsigned u = __float_as_uint(f); return (u + 0x7fffu + ((u >> 16) & 1u)) >> 16; }
; __device__ __forceinline__ float rdlane_f(float v, int l) { return __builtin_bit_cast(float, __builtin_amdgcn_readlane(__builtin_bit_cast(int, v), l)); }
; __device__ __forceinline__ float gdn_s1(const GdnIn& in, LAS unsigned char* ub, LAS unsigned char* dwb, int w, int lane) {
;     const int fr = lane & 15, kg = lane >> 4, I1 = w >> 1;
;     LAS bf16* AB = (LAS bf16*)ub; LAS bf16* ATT = AB + 4608; LAS bf16* KTT = ATT + 4608; LAS float* GT = (LAS float*)(dwb + 2048);
;     float beta = in.g2.x, cum = in.g2.y;
; #pragma unroll
;     for (int o = 1; o < 64; o <<= 1) { const float t = __shfl_up(cum, o); if (lane >= o) cum += t; }
;     const float cl = rdlane_f(cum, 63);
;     GT[lane] = beta; GT[64 + lane] = cum; GT[128 + lane] = __expf(cum);
;     asm volatile("s_waitcnt lgkmcnt(0)" ::: "memory");
;     { const f32x4 ci = *(const LAS f32x4*)(GT + 64 + 16 * I1 + 4 * kg), bi = *(const LAS f32x4*)(GT + 16 * I1 + 4 * kg);
; #pragma unroll
;       for (int jj = 0; jj < 2; ++jj) { const int J = 2 * (w & 1) + jj;
;           f32x4 ck = (f32x4){0.f, 0.f, 0.f, 0.f}, cq = (f32x4){0.f, 0.f, 0.f, 0.f};
; #pragma unroll
;           for (int s = 0; s < 2; ++s) { ck = __builtin_amdgcn_mfma_f32_16x16x32_bf16(in.ak[s], in.bk[jj][s], ck, 0, 0, 0); cq = __builtin_amdgcn_mfma_f32_16x16x32_bf16(in.aq[s], in.bk[jj][s], cq, 0, 0, 0); }
;           const int j = 16 * J + fr; const float cj = GT[64 + j];
; #pragma unroll
;           for (int e = 0; e < 4; ++e) { const int i = 16 * I1 + 4 * kg + e; const float gm = __expf(fminf(ci[e] - cj, 0.f));
;               AB[i * 72 + j] = (bf16)f2bf(j < i ? bi[e] * ck[e] * gm : 0.f); ATT[i * 72 + j] = (bf16)f2bf(j <= i ? cq[e] * gm : 0.f); } } }
.Lgf2b_done:
.LBB0_1775:
	s_waitcnt vmcnt(32)
	v_mov_b32_e32 v33, v115
	s_waitcnt vmcnt(29)
	v_mfma_f32_16x16x32_bf16 v[86:89], v[58:61], v[70:73], 0
	s_movk_i32 s2, 0x48
	v_add_f32_dpp v33, v33, v33 row_shr:1 row_mask:0xf bank_mask:0xf
	s_cmp_gt_u32 s0, 33
	v_mfma_f32_16x16x32_bf16 v[70:73], v[46:49], v[70:73], 0
	v_add_f32_dpp v33, v33, v33 row_shr:2 row_mask:0xf bank_mask:0xf
	s_cselect_b64 s[50:51], -1, 0
	s_nop 1
	v_add_f32_dpp v33, v33, v33 row_shr:4 row_mask:0xf bank_mask:0xf
	s_mov_b64 s[62:63], 0x40000
	s_waitcnt vmcnt(25)
	v_add_f32_dpp v33, v33, v33 row_shr:8 row_mask:0xf bank_mask:0xf
	v_mfma_f32_16x16x32_bf16 v[86:89], v[50:53], v[74:77], v[86:89]
	s_nop 1
	v_add_f32_dpp v33, v33, v33 row_bcast:15 row_mask:0xa bank_mask:0xf
	v_mfma_f32_16x16x32_bf16 v[70:73], v[54:57], v[74:77], v[70:73]
	v_mfma_f32_16x16x32_bf16 v[46:49], v[46:49], v[62:65], 0
	v_add_f32_dpp v33, v33, v33 row_bcast:31 row_mask:0xc bank_mask:0xf
	v_mfma_f32_16x16x32_bf16 v[58:61], v[58:61], v[62:65], 0
	v_mul_f32_e32 v78, 0x3fb8aa3b, v33
	v_exp_f32_e32 v78, v78
	v_lshl_add_u32 v32, v110, 2, s8
	ds_write2st64_b32 v32, v114, v33 offset0:224 offset1:225
	v_add_u32_e32 v114, s42, v34
	ds_write_b32 v32, v78 offset:57856
	s_waitcnt lgkmcnt(0)
	v_lshl_add_u32 v32, v34, 2, s30
	ds_read_b128 v[82:85], v32 offset:57600
	ds_read_b128 v[78:81], v32 offset:57344
	v_or_b32_e32 v32, s43, v106
	v_lshl_add_u32 v34, v32, 2, s8
	v_add_u32_e32 v34, 0xe000, v34
	ds_read2_b32 v[74:75], v34 offset0:64 offset1:80
	s_waitcnt lgkmcnt(1)
	v_mul_f32_e32 v76, v78, v86
	v_cmp_lt_i32_e32 vcc, v32, v114
	s_waitcnt vmcnt(24)
	v_mfma_f32_16x16x32_bf16 v[46:49], v[54:57], v[66:69], v[46:49]
	v_readlane_b32 s9, v33, 63
	s_waitcnt lgkmcnt(0)
	v_sub_f32_e32 v34, v82, v74
	v_min_f32_e32 v34, 0, v34
	v_mul_f32_e32 v34, 0x3fb8aa3b, v34
	v_exp_f32_e32 v34, v34
	v_sub_f32_e32 v54, v82, v75
	v_min_f32_e32 v54, 0, v54
	v_mfma_f32_16x16x32_bf16 v[50:53], v[50:53], v[66:69], v[58:61]
	v_mul_f32_e32 v76, v76, v34
	v_cndmask_b32_e32 v76, 0, v76, vcc
	v_cmp_gt_i32_e32 vcc, v32, v114
	v_mul_f32_e32 v34, v70, v34
	s_nop 0
	v_cndmask_b32_e64 v34, v34, 0, vcc
	v_cvt_pk_bf16_f32 v86, v76, v76
	v_mad_u64_u32 v[76:77], s[2:3], v114, s2, v[32:33]
	v_lshl_add_u32 v76, v76, 1, 0
	v_cvt_pk_bf16_f32 v34, v34, v34
	ds_write_b16 v76, v34 offset:36864
	v_sub_f32_e32 v34, v83, v74
	v_min_f32_e32 v34, 0, v34
	v_mul_f32_e32 v34, 0x3fb8aa3b, v34
	v_exp_f32_e32 v34, v34
	v_mul_f32_e32 v77, v79, v87
	v_or_b32_e32 v70, 1, v114
	ds_write_b16 v76, v86 offset:27648
	v_mul_f32_e32 v77, v77, v34
	v_cndmask_b32_e64 v77, v77, 0, vcc
	v_mul_f32_e32 v34, v71, v34
	v_cmp_le_i32_e32 vcc, v32, v70
	v_cvt_pk_bf16_f32 v77, v77, v77
	s_nop 0
	v_cndmask_b32_e32 v34, 0, v34, vcc
	v_cvt_pk_bf16_f32 v34, v34, v34
	ds_write_b16 v76, v34 offset:37008
	v_sub_f32_e32 v34, v84, v74
	v_min_f32_e32 v34, 0, v34
	v_mul_f32_e32 v34, 0x3fb8aa3b, v34
	v_exp_f32_e32 v34, v34
	ds_write_b16 v76, v77 offset:27792
	v_or_b32_e32 v71, 2, v114
	v_mul_f32_e32 v77, v80, v88
	v_cmp_lt_i32_e32 vcc, v32, v71
	v_mul_f32_e32 v77, v77, v34
	v_mul_f32_e32 v34, v72, v34
	v_cndmask_b32_e32 v77, 0, v77, vcc
	v_cmp_le_i32_e32 vcc, v32, v71
	v_mul_f32_e32 v54, 0x3fb8aa3b, v54
	v_exp_f32_e32 v54, v54
	v_cndmask_b32_e32 v34, 0, v34, vcc
	v_cvt_pk_bf16_f32 v34, v34, v34
	ds_write_b16 v76, v34 offset:37152
	v_sub_f32_e32 v34, v85, v74
	v_min_f32_e32 v34, 0, v34
	v_mul_f32_e32 v34, 0x3fb8aa3b, v34
	v_exp_f32_e32 v34, v34
	v_or_b32_e32 v72, 3, v114
	v_mul_f32_e32 v74, v81, v89
	v_cmp_lt_i32_e32 vcc, v32, v72
	v_mul_f32_e32 v74, v74, v34
	v_mul_f32_e32 v34, v73, v34
	v_cndmask_b32_e32 v74, 0, v74, vcc
	v_cmp_le_i32_e32 vcc, v32, v72
	v_mul_f32_e32 v50, v78, v50
	v_mul_f32_e32 v50, v50, v54
	v_cndmask_b32_e32 v34, 0, v34, vcc
	v_cvt_pk_bf16_f32 v34, v34, v34
	ds_write_b16_d16_hi v76, v34 offset:37296
	v_or_b32_e32 v34, 16, v32
	v_cmp_lt_i32_e32 vcc, v34, v114
	v_mul_f32_e32 v46, v46, v54
	v_bfe_u32 v86, v77, 16, 1
	v_cndmask_b32_e32 v50, 0, v50, vcc
	v_cmp_gt_i32_e32 vcc, v34, v114
	v_cvt_pk_bf16_f32 v50, v50, v50
	ds_write_b16 v76, v50 offset:27680
	v_cndmask_b32_e64 v46, v46, 0, vcc
	v_cvt_pk_bf16_f32 v46, v46, v46
	ds_write_b16 v76, v46 offset:36896
	v_sub_f32_e32 v46, v83, v75
	v_min_f32_e32 v46, 0, v46
	v_mul_f32_e32 v46, 0x3fb8aa3b, v46
	v_exp_f32_e32 v46, v46
	v_mul_f32_e32 v50, v79, v51
	v_add3_u32 v77, v77, v86, s81
	ds_write_b16_d16_hi v76, v77 offset:27936
	v_mul_f32_e32 v50, v50, v46
	v_cndmask_b32_e64 v50, v50, 0, vcc
	v_mul_f32_e32 v46, v47, v46
	v_cmp_le_i32_e32 vcc, v34, v70
	v_cvt_pk_bf16_f32 v50, v50, v50
	s_nop 0
	v_cndmask_b32_e32 v46, 0, v46, vcc
	v_cvt_pk_bf16_f32 v46, v46, v46
	ds_write_b16 v76, v46 offset:37040
	v_sub_f32_e32 v46, v84, v75
	v_min_f32_e32 v46, 0, v46
	v_mul_f32_e32 v46, 0x3fb8aa3b, v46
	v_exp_f32_e32 v46, v46
	v_mul_f32_e32 v47, v80, v52
	v_cmp_lt_i32_e32 vcc, v34, v71
	ds_write_b16 v76, v50 offset:27824
	v_mul_f32_e32 v47, v47, v46
	v_cndmask_b32_e32 v47, 0, v47, vcc
	v_mul_f32_e32 v46, v48, v46
	v_cmp_le_i32_e32 vcc, v34, v71
	v_cvt_pk_bf16_f32 v47, v47, v47
	ds_write_b16 v76, v47 offset:27968
	v_cndmask_b32_e32 v46, 0, v46, vcc
	v_cvt_pk_bf16_f32 v46, v46, v46
	ds_write_b16 v76, v46 offset:37184
	v_sub_f32_e32 v46, v85, v75
	v_min_f32_e32 v46, 0, v46
	v_mul_f32_e32 v46, 0x3fb8aa3b, v46
	v_exp_f32_e32 v46, v46
	v_mul_f32_e32 v47, v81, v53
	v_cmp_lt_i32_e32 vcc, v34, v72
	v_bfe_u32 v77, v74, 16, 1
	v_mul_f32_e32 v47, v47, v46
	v_cndmask_b32_e32 v47, 0, v47, vcc
	v_mul_f32_e32 v46, v49, v46
	v_cmp_le_i32_e32 vcc, v34, v72
	v_cvt_pk_bf16_f32 v47, v47, v47
	ds_write_b16 v76, v47 offset:28112
	v_cndmask_b32_e32 v46, 0, v46, vcc
	v_add3_u32 v74, v74, v77, s81
	v_cvt_pk_bf16_f32 v46, v46, v46
	ds_write_b16_d16_hi v76, v74 offset:28080
	ds_write_b16 v76, v46 offset:37328
	v_mov_b32_e32 v33, s84
	ds_read_b128 v[46:49], v33 offset:57600
	ds_read_b128 v[50:53], v33 offset:57616
	s_waitcnt vmcnt(20)
; #define LAS __attribute__((address_space(3)))
; __device__ __forceinline__ unsigned f2bf(float f) { unsigned u = __float_as_uint(f); return (u + 0x7fffu + ((u >> 16) & 1u)) >> 16; }
; __device__ __forceinline__ void gdn_fetch2(CArgs& a, int u, int w, int lane, GdnIn2& in) {
;     const int chain = u / 36, n = u % 36, b = chain >> 3, h = (chain >> 1) & 3, dir = chain & 1;
;     const int r0 = scan_row(b, dir, n * 64), step = dir ? -1 : 1, fr = lane & 15, kg = lane >> 4;
;     const bf16* QBh = (const bf16*)(a.ws + WS_CKD + CD_QB) + h * 64; const bf16* KBh = (const bf16*)(a.ws + WS_CKD + CD_KB) + h * 64; const bf16* VBh = (const bf16*)(a.ws + WS_MIX + MX_DV) + h * 64;
;     const bool isW = w >= 4; const int c0 = 16 * (w & 3);
; #pragma unroll
;     for (int I = 0; I < 4; ++I)
; #pragma unroll
;         for (int e = 0; e < 4; ++e) { const size_t ro = (size_t)(r0 + step * (16 * I + 4 * kg + e)) * 256 + c0 + fr; in.R[I][e] = isW ? (unsigned)KBh[ro] : (unsigned)VBh[ro]; in.Qv[I][e] = isW ? (unsigned)QBh[ro] : 0u; }
; }
; __device__ __forceinline__ float gdn_s1(const GdnIn& in, LAS unsigned char* ub, LAS unsigned char* dwb, int w, int lane) {
;     ...
;     { const f32x4 c8a = *(const LAS f32x4*)(GT + 64 + 8 * w), c8b = *(const LAS f32x4*)(GT + 64 + 8 * w + 4);
; #pragma unroll
;       for (int tt = 0; tt < 8; ++tt) KTT[lane * 72 + 8 * w + tt] = (bf16)f2bf(__uint_as_float(in.kt8[tt] << 16) * __expf(cl - (tt < 4 ? c8a[tt & 3] : c8b[tt & 3]))); }
;     asm volatile("s_waitcnt lgkmcnt(0)" ::: "memory");
	v_lshlrev_b32_e32 v55, 16, v137
	v_lshlrev_b32_e32 v54, 16, v135
	v_lshlrev_b32_e32 v57, 16, v133
	s_waitcnt lgkmcnt(1)
	v_sub_f32_e32 v46, s9, v46
	v_sub_f32_e32 v47, s9, v47
	v_sub_f32_e32 v48, s9, v48
	v_sub_f32_e32 v49, s9, v49
	v_mul_f32_e32 v46, 0x3fb8aa3b, v46
	v_mul_f32_e32 v47, 0x3fb8aa3b, v47
	v_mul_f32_e32 v48, 0x3fb8aa3b, v48
	v_mul_f32_e32 v49, 0x3fb8aa3b, v49
	v_exp_f32_e32 v46, v46
	v_exp_f32_e32 v47, v47
	v_exp_f32_e32 v48, v48
	v_exp_f32_e32 v49, v49
	s_waitcnt lgkmcnt(0)
	v_sub_f32_e32 v50, s9, v50
	v_sub_f32_e32 v51, s9, v51
	v_sub_f32_e32 v52, s9, v52
	v_sub_f32_e32 v53, s9, v53
	v_mul_f32_e32 v50, 0x3fb8aa3b, v50
	v_mul_f32_e32 v51, 0x3fb8aa3b, v51
	v_mul_f32_e32 v52, 0x3fb8aa3b, v52
	v_mul_f32_e32 v53, 0x3fb8aa3b, v53
	v_lshlrev_b32_e32 v56, 16, v131
	v_exp_f32_e32 v50, v50
	v_exp_f32_e32 v51, v51
	v_exp_f32_e32 v52, v52
	v_exp_f32_e32 v53, v53
	v_pk_mul_f32 v[46:47], v[46:47], v[56:57]
	v_pk_mul_f32 v[48:49], v[48:49], v[54:55]
	v_bfe_u32 v56, v47, 16, 1
	v_bfe_u32 v54, v49, 16, 1
	v_bfe_u32 v55, v48, 16, 1
	v_bfe_u32 v57, v46, 16, 1
	v_add3_u32 v57, v46, v57, s81
	v_add3_u32 v56, v47, v56, s81
	v_add3_u32 v55, v48, v55, s81
	v_add3_u32 v54, v49, v54, s81
	s_waitcnt vmcnt(16)
	v_lshlrev_b32_e32 v47, 16, v136
	v_lshlrev_b32_e32 v46, 16, v134
	v_lshlrev_b32_e32 v49, 16, v132
	v_lshlrev_b32_e32 v48, 16, v111
	v_pk_mul_f32 v[48:49], v[50:51], v[48:49]
	v_pk_mul_f32 v[46:47], v[52:53], v[46:47]
	v_bfe_u32 v52, v49, 16, 1
	v_bfe_u32 v50, v47, 16, 1
	v_bfe_u32 v51, v46, 16, 1
	v_bfe_u32 v53, v48, 16, 1
	v_mul_lo_u32 v33, v110, s75
	v_add3_u32 v48, v48, v53, s81
	v_add3_u32 v52, v49, v52, s81
	v_add3_u32 v46, v46, v51, s81
	v_add3_u32 v47, v47, v50, s81
	s_mov_b32 s2, 0x7060302
	v_add_u32_e32 v33, s11, v33
	v_perm_b32 v49, v47, v46, s2
	v_perm_b32 v48, v52, v48, s2
	v_perm_b32 v47, v54, v55, s2
	v_perm_b32 v46, v56, v57, s2
	ds_write_b128 v33, v[46:49] offset:46080
	s_waitcnt lgkmcnt(0)
	s_and_b64 vcc, exec, s[50:51]
	s_waitcnt lgkmcnt(0)
	s_barrier
	s_waitcnt vmcnt(0)
	v_lshlrev_b32_e32 v103, 16, v103
	v_lshlrev_b32_e32 v102, 16, v102
	v_lshlrev_b32_e32 v105, 16, v105
	v_lshlrev_b32_e32 v104, 16, v104
	v_lshlrev_b32_e32 v99, 16, v99
	v_lshlrev_b32_e32 v98, 16, v98
	v_lshlrev_b32_e32 v101, 16, v101
	v_lshlrev_b32_e32 v100, 16, v100
	v_lshlrev_b32_e32 v96, 16, v96
	v_lshlrev_b32_e32 v94, 16, v94
	v_lshlrev_b32_e32 v97, 16, v97
	v_lshlrev_b32_e32 v95, 16, v95
	v_lshlrev_b32_e32 v92, 16, v92
	v_lshlrev_b32_e32 v90, 16, v90
	v_lshlrev_b32_e32 v93, 16, v93
	v_lshlrev_b32_e32 v91, 16, v91
	s_cbranch_vccnz .LBB0_1781
	s_add_i32 s2, s26, 2
	s_mul_hi_i32 s3, s2, 0x38e38e39
	s_lshr_b32 s20, s3, 31
	s_ashr_i32 s3, s3, 3
	s_add_i32 s3, s3, s20
	s_mul_i32 s20, s3, 36
	s_sub_i32 s2, s2, s20
	s_ashr_i32 s36, s3, 3
	s_and_b32 s20, s3, 1
	s_lshl_b32 s29, s2, 6
	s_cmp_gt_i32 s2, 3
	s_mov_b64 s[26:27], -1
	s_cbranch_scc0 .LBB0_1778
	s_add_i32 s2, s29, 0xffffff00
	s_lshl_b32 s26, s36, 11
	s_sub_i32 s27, 0x8ff, s29
	s_cmp_eq_u32 s20, 0
	s_cselect_b32 s2, s2, s27
	s_add_i32 s2, s26, s2
	s_addk_i32 s2, 0x1000
	s_mov_b64 s[26:27], 0

; #define LAS __attribute__((address_space(3)))
; __device__ __forceinline__ unsigned f2bf(float f) { unsigned u = __float_as_uint(f); return (u + 0x7fffu + ((u >> 16) & 1u)) >> 16; }
; __device__ __forceinline__ float lo_bf(unsigned w) { return __uint_as_float(w << 16); }
; __device__ __forceinline__ float hi_bf(unsigned w) { return __uint_as_float(w & 0xffff0000u); }
; __device__ __forceinline__ void gdn_s23(CArgs& a, int u, const GdnIn2& in, LAS unsigned char* ub, LAS unsigned char* dwb, int w, int lane, float cl) {
;     ...
;     { const int blk = lane >> 4, c = lane & 15; float T[16];
; #pragma unroll
;       for (int hb = 0; hb < 4; ++hb) {
;           u32x4 arow[4][2];
; #pragma unroll
;           for (int rr = 0; rr < 4; ++rr) { const int r = 4 * hb + rr; arow[rr][0] = *(const LAS u32x4*)(AB + (16 * blk + r) * 72 + 16 * blk); if (hb >= 2) arow[rr][1] = *(const LAS u32x4*)(AB + (16 * blk + r) * 72 + 16 * blk + 8); }
;           asm volatile("s_waitcnt lgkmcnt(0)" ::: "memory");
; #pragma unroll
;           for (int rr = 0; rr < 4; ++rr) { const int r = 4 * hb + rr; float t = (r == c) ? 1.f : 0.f;
;               float t2 = 0.f;
; #pragma unroll
;               for (int j = 0; j < r; ++j) { const unsigned wv = arow[rr][j >> 3][(j >> 1) & 3]; const float av = (j & 1) ? hi_bf(wv) : lo_bf(wv); if (j & 1) t2 -= av * T[j]; else t -= av * T[j]; }
;               t += t2;
;               T[r] = t; DW[(blk * 16 + r) * 16 + c] = (bf16)f2bf(t); } } }
.LBB0_1781:
	v_and_b32_e32 v76, -16, v110
	v_lshl_add_u32 v32, v76, 1, 0
	v_mad_u64_u32 v[66:67], s[2:3], v76, s75, v[32:33]
	ds_read_b128 v[46:49], v66 offset:28080
	v_add_u32_e32 v33, 0x6c00, v66
	s_waitcnt lgkmcnt(0)
	ds_read2_b32 v[48:49], v33 offset0:36 offset1:72
	v_cmp_eq_u32_e32 vcc, 0, v106
	v_lshlrev_b32_e32 v33, 5, v110
	v_lshlrev_b32_e32 v34, 1, v106
	v_cndmask_b32_e64 v77, 0, 1.0, vcc
	v_and_b32_e32 v33, 0xfffffe00, v33
	v_cmp_eq_u32_e32 vcc, 1, v106
	v_add3_u32 v78, s8, v34, v33
	s_waitcnt lgkmcnt(0)
	v_lshlrev_b32_e32 v48, 16, v48
	v_cndmask_b32_e64 v33, 0, 1.0, vcc
	v_fma_f32 v79, -v77, v48, v33
	v_cvt_pk_bf16_f32 v33, v79, v79
	v_cmp_eq_u32_e32 vcc, 2, v106
	s_waitcnt lgkmcnt(0)
	ds_write_b16 v78, v33 offset:55328
	v_lshlrev_b32_e32 v48, 16, v49
	v_cndmask_b32_e64 v33, 0, 1.0, vcc
	v_fma_f32 v33, -v77, v48, v33
	v_and_b32_e32 v48, 0xffff0000, v49
	v_fma_f32 v48, -v79, v48, 0
	v_add_f32_e32 v80, v33, v48
	v_cvt_pk_bf16_f32 v33, v80, v80
	v_cmp_eq_u32_e32 vcc, 3, v106
	ds_write_b16 v78, v33 offset:55360
	v_lshlrev_b32_e32 v48, 16, v46
	v_cndmask_b32_e64 v33, 0, 1.0, vcc
	v_fma_f32 v33, -v77, v48, v33
	v_and_b32_e32 v46, 0xffff0000, v46
	v_lshlrev_b32_e32 v47, 16, v47
	v_fma_f32 v46, -v79, v46, 0
	v_fma_f32 v33, -v80, v47, v33
	v_add_f32_e32 v81, v46, v33
	v_cvt_pk_bf16_f32 v33, v81, v81
	ds_write_b16_d16_hi v78, v77 offset:55296
	ds_write_b16 v78, v33 offset:55392
	ds_read_b128 v[46:49], v66 offset:28224
	s_waitcnt lgkmcnt(0)
	ds_read_b128 v[48:51], v66 offset:28368
	ds_read_b128 v[52:55], v66 offset:28512
	ds_read_b128 v[56:59], v66 offset:28656
	v_cmp_eq_u32_e32 vcc, 4, v106
	s_waitcnt lgkmcnt(0)
	v_ashrrev_i32_e32 v82, 4, v110
	s_waitcnt lgkmcnt(2)
	v_lshlrev_b32_e32 v51, 16, v46
	v_cndmask_b32_e64 v33, 0, 1.0, vcc
	v_and_b32_e32 v46, 0xffff0000, v46
	v_fma_f32 v33, -v77, v51, v33
	v_fma_f32 v46, -v79, v46, 0
	v_lshlrev_b32_e32 v51, 16, v47
	v_and_b32_e32 v47, 0xffff0000, v47
	v_fma_f32 v33, -v80, v51, v33
	v_fma_f32 v46, -v81, v47, v46
	v_add_f32_e32 v83, v46, v33
	v_cvt_pk_bf16_f32 v33, v83, v83
	v_cmp_eq_u32_e32 vcc, 5, v106
	ds_write_b16 v78, v33 offset:55424
	v_lshlrev_b32_e32 v46, 16, v48
	v_cndmask_b32_e64 v33, 0, 1.0, vcc
	v_fma_f32 v33, -v77, v46, v33
	v_and_b32_e32 v46, 0xffff0000, v48
	v_lshlrev_b32_e32 v47, 16, v49
	v_fma_f32 v46, -v79, v46, 0
	v_fma_f32 v33, -v80, v47, v33
	v_and_b32_e32 v47, 0xffff0000, v49
	v_fma_f32 v46, -v81, v47, v46
	v_lshlrev_b32_e32 v47, 16, v50
	v_fma_f32 v33, -v83, v47, v33
	v_add_f32_e32 v84, v46, v33
	v_cvt_pk_bf16_f32 v33, v84, v84
	v_cmp_eq_u32_e32 vcc, 6, v106
	ds_write_b16 v78, v33 offset:55456
	s_waitcnt lgkmcnt(3)
	v_lshlrev_b32_e32 v46, 16, v52
	v_cndmask_b32_e64 v33, 0, 1.0, vcc
	v_fma_f32 v33, -v77, v46, v33
	v_and_b32_e32 v46, 0xffff0000, v52
	v_lshlrev_b32_e32 v47, 16, v53
	v_fma_f32 v46, -v79, v46, 0
	v_fma_f32 v33, -v80, v47, v33
	v_and_b32_e32 v47, 0xffff0000, v53
	v_fma_f32 v46, -v81, v47, v46
	v_lshlrev_b32_e32 v47, 16, v54
	v_fma_f32 v33, -v83, v47, v33
	v_and_b32_e32 v47, 0xffff0000, v54
	v_fma_f32 v46, -v84, v47, v46
	v_add_f32_e32 v85, v33, v46
	v_cvt_pk_bf16_f32 v33, v85, v85
	v_cmp_eq_u32_e32 vcc, 7, v106
	ds_write_b16 v78, v33 offset:55488
	s_waitcnt lgkmcnt(3)
	v_lshlrev_b32_e32 v46, 16, v56
	v_cndmask_b32_e64 v33, 0, 1.0, vcc
	v_fma_f32 v33, -v77, v46, v33
	v_and_b32_e32 v46, 0xffff0000, v56
	v_lshlrev_b32_e32 v47, 16, v57
	v_fma_f32 v46, -v79, v46, 0
	v_fma_f32 v33, -v80, v47, v33
	v_and_b32_e32 v47, 0xffff0000, v57
	v_fma_f32 v46, -v81, v47, v46
	v_lshlrev_b32_e32 v47, 16, v58
	v_fma_f32 v33, -v83, v47, v33
	v_and_b32_e32 v47, 0xffff0000, v58
	v_fma_f32 v46, -v84, v47, v46
	v_lshlrev_b32_e32 v47, 16, v59
	v_fma_f32 v33, -v85, v47, v33
	v_add_f32_e32 v86, v46, v33
	v_cvt_pk_bf16_f32 v33, v86, v86
	ds_write_b16 v78, v33 offset:55520
	ds_read_b128 v[46:49], v66 offset:28800
	ds_read_b128 v[50:53], v66 offset:28944
	ds_read_b128 v[54:57], v66 offset:29088
	ds_read_b128 v[58:61], v66 offset:29232
	ds_read_b128 v[62:65], v66 offset:29248
	v_add_u32_e32 v33, 0x7000, v66
	v_cmp_eq_u32_e32 vcc, 8, v106
	s_waitcnt lgkmcnt(0)
	ds_read2_b32 v[64:65], v33 offset0:72 offset1:108
	v_lshlrev_b32_e32 v67, 16, v46
	v_cndmask_b32_e64 v33, 0, 1.0, vcc
	v_and_b32_e32 v46, 0xffff0000, v46
	v_fma_f32 v33, -v77, v67, v33
	v_fma_f32 v46, -v79, v46, 0
	v_lshlrev_b32_e32 v67, 16, v47
	v_and_b32_e32 v47, 0xffff0000, v47
	v_fma_f32 v33, -v80, v67, v33
	v_fma_f32 v46, -v81, v47, v46
	v_lshlrev_b32_e32 v47, 16, v48
	v_fma_f32 v33, -v83, v47, v33
	v_and_b32_e32 v47, 0xffff0000, v48
	v_fma_f32 v46, -v84, v47, v46
	v_lshlrev_b32_e32 v47, 16, v49
	v_fma_f32 v33, -v85, v47, v33
	v_and_b32_e32 v47, 0xffff0000, v49
	v_fma_f32 v46, -v86, v47, v46
	v_add_f32_e32 v87, v33, v46
	v_cvt_pk_bf16_f32 v33, v87, v87
	v_cmp_eq_u32_e32 vcc, 9, v106
	s_waitcnt lgkmcnt(0)
	ds_write_b16 v78, v33 offset:55552
	v_lshlrev_b32_e32 v46, 16, v50
	v_cndmask_b32_e64 v33, 0, 1.0, vcc
	v_fma_f32 v33, -v77, v46, v33
	v_and_b32_e32 v46, 0xffff0000, v50
	v_lshlrev_b32_e32 v47, 16, v51
	v_fma_f32 v46, -v79, v46, 0
	v_fma_f32 v33, -v80, v47, v33
	v_and_b32_e32 v47, 0xffff0000, v51
	v_fma_f32 v46, -v81, v47, v46
	v_lshlrev_b32_e32 v47, 16, v52
	v_fma_f32 v33, -v83, v47, v33
	v_and_b32_e32 v47, 0xffff0000, v52
	v_fma_f32 v46, -v84, v47, v46
	v_lshlrev_b32_e32 v47, 16, v53
	v_fma_f32 v33, -v85, v47, v33
	v_and_b32_e32 v47, 0xffff0000, v53
	v_fma_f32 v46, -v86, v47, v46
	s_waitcnt lgkmcnt(1)
; #define LAS __attribute__((address_space(3)))
; __device__ __forceinline__ unsigned f2bf(float f) { unsigned u = __float_as_uint(f); return (u + 0x7fffu + ((u >> 16) & 1u)) >> 16; }
; __device__ __forceinline__ float lo_bf(unsigned w) { return __uint_as_float(w << 16); }
; __device__ __forceinline__ float hi_bf(unsigned w) { return __uint_as_float(w & 0xffff0000u); }
; __device__ __forceinline__ void gdn_s23(CArgs& a, int u, const GdnIn2& in, LAS unsigned char* ub, LAS unsigned char* dwb, int w, int lane, float cl) {
;     ...
;     { const int blk = lane >> 4, c = lane & 15; float T[16];
; #pragma unroll
;       for (int hb = 0; hb < 4; ++hb) {
;           u32x4 arow[4][2];
; #pragma unroll
;           for (int rr = 0; rr < 4; ++rr) { const int r = 4 * hb + rr; arow[rr][0] = *(const LAS u32x4*)(AB + (16 * blk + r) * 72 + 16 * blk); if (hb >= 2) arow[rr][1] = *(const LAS u32x4*)(AB + (16 * blk + r) * 72 + 16 * blk + 8); }
;           asm volatile("s_waitcnt lgkmcnt(0)" ::: "memory");
; #pragma unroll
;           for (int rr = 0; rr < 4; ++rr) { const int r = 4 * hb + rr; float t = (r == c) ? 1.f : 0.f;
;               float t2 = 0.f;
; #pragma unroll
;               for (int j = 0; j < r; ++j) { const unsigned wv = arow[rr][j >> 3][(j >> 1) & 3]; const float av = (j & 1) ? hi_bf(wv) : lo_bf(wv); if (j & 1) t2 -= av * T[j]; else t -= av * T[j]; }
;               t += t2;
;               T[r] = t; DW[(blk * 16 + r) * 16 + c] = (bf16)f2bf(t); } } }
	v_lshlrev_b32_e32 v47, 16, v64
	v_fma_f32 v33, -v87, v47, v33
	v_add_f32_e32 v88, v46, v33
	v_cvt_pk_bf16_f32 v33, v88, v88
	v_cmp_eq_u32_e32 vcc, 10, v106
	ds_write_b16 v78, v33 offset:55584
	v_lshlrev_b32_e32 v46, 16, v54
	v_cndmask_b32_e64 v33, 0, 1.0, vcc
	v_fma_f32 v33, -v77, v46, v33
	v_and_b32_e32 v46, 0xffff0000, v54
	v_lshlrev_b32_e32 v47, 16, v55
	v_fma_f32 v46, -v79, v46, 0
	v_fma_f32 v33, -v80, v47, v33
	v_and_b32_e32 v47, 0xffff0000, v55
	v_fma_f32 v46, -v81, v47, v46
	v_lshlrev_b32_e32 v47, 16, v56
	v_fma_f32 v33, -v83, v47, v33
	v_and_b32_e32 v47, 0xffff0000, v56
	v_fma_f32 v46, -v84, v47, v46
	v_lshlrev_b32_e32 v47, 16, v57
	v_fma_f32 v33, -v85, v47, v33
	v_and_b32_e32 v47, 0xffff0000, v57
	v_fma_f32 v46, -v86, v47, v46
	v_lshlrev_b32_e32 v47, 16, v65
	v_fma_f32 v33, -v87, v47, v33
	v_and_b32_e32 v47, 0xffff0000, v65
	v_fma_f32 v46, -v88, v47, v46
	v_add_f32_e32 v89, v33, v46
	v_cvt_pk_bf16_f32 v33, v89, v89
	v_cmp_eq_u32_e32 vcc, 11, v106
	ds_write_b16 v78, v33 offset:55616
	v_lshlrev_b32_e32 v46, 16, v58
	v_cndmask_b32_e64 v33, 0, 1.0, vcc
	v_fma_f32 v33, -v77, v46, v33
	v_and_b32_e32 v46, 0xffff0000, v58
	v_lshlrev_b32_e32 v47, 16, v59
	v_fma_f32 v46, -v79, v46, 0
	v_fma_f32 v33, -v80, v47, v33
	v_and_b32_e32 v47, 0xffff0000, v59
	v_fma_f32 v46, -v81, v47, v46
	v_lshlrev_b32_e32 v47, 16, v60
	v_fma_f32 v33, -v83, v47, v33
	v_and_b32_e32 v47, 0xffff0000, v60
	v_fma_f32 v46, -v84, v47, v46
	v_lshlrev_b32_e32 v47, 16, v61
	v_fma_f32 v33, -v85, v47, v33
	v_and_b32_e32 v47, 0xffff0000, v61
	v_fma_f32 v46, -v86, v47, v46
	v_lshlrev_b32_e32 v47, 16, v62
	v_fma_f32 v33, -v87, v47, v33
	v_and_b32_e32 v47, 0xffff0000, v62
	v_fma_f32 v46, -v88, v47, v46
	v_lshlrev_b32_e32 v47, 16, v63
	v_fma_f32 v33, -v89, v47, v33
	v_add_f32_e32 v111, v46, v33
	v_cvt_pk_bf16_f32 v33, v111, v111
	ds_write_b16 v78, v33 offset:55648
	ds_read_b128 v[46:49], v66 offset:29376
	ds_read_b128 v[50:53], v66 offset:29392
	v_or_b32_e32 v33, 15, v110
	v_mad_u64_u32 v[32:33], s[2:3], v33, s75, v[32:33]
	v_cmp_eq_u32_e32 vcc, 12, v106
	s_waitcnt lgkmcnt(0)
	ds_read_b128 v[52:55], v66 offset:29520
	ds_read_b128 v[56:59], v66 offset:29536
	ds_read_b128 v[60:63], v66 offset:29664
	ds_read_b128 v[64:67], v66 offset:29680
	ds_read_b128 v[68:71], v32 offset:27648
	ds_read_b128 v[72:75], v32 offset:27664
	v_cndmask_b32_e64 v32, 0, 1.0, vcc
	v_lshlrev_b32_e32 v33, 16, v46
	v_fma_f32 v32, -v77, v33, v32
	v_and_b32_e32 v33, 0xffff0000, v46
	v_lshlrev_b32_e32 v46, 16, v47
	v_fma_f32 v33, -v79, v33, 0
	v_fma_f32 v32, -v80, v46, v32
	v_and_b32_e32 v46, 0xffff0000, v47
	v_fma_f32 v33, -v81, v46, v33
	v_lshlrev_b32_e32 v46, 16, v48
	v_fma_f32 v32, -v83, v46, v32
	v_and_b32_e32 v46, 0xffff0000, v48
	v_fma_f32 v33, -v84, v46, v33
	v_lshlrev_b32_e32 v46, 16, v49
	v_fma_f32 v32, -v85, v46, v32
	v_and_b32_e32 v46, 0xffff0000, v49
	v_fma_f32 v33, -v86, v46, v33
	v_lshlrev_b32_e32 v46, 16, v50
	v_fma_f32 v32, -v87, v46, v32
	v_and_b32_e32 v46, 0xffff0000, v50
	v_fma_f32 v33, -v88, v46, v33
	v_lshlrev_b32_e32 v46, 16, v51
	v_fma_f32 v32, -v89, v46, v32
	v_and_b32_e32 v46, 0xffff0000, v51
	v_fma_f32 v33, -v111, v46, v33
	v_add_f32_e32 v32, v33, v32
	v_cvt_pk_bf16_f32 v33, v32, v32
	v_cmp_eq_u32_e32 vcc, 13, v106
	s_waitcnt lgkmcnt(0)
	ds_write_b16 v78, v33 offset:55680
	s_waitcnt lgkmcnt(6)
	v_lshlrev_b32_e32 v46, 16, v52
	v_cndmask_b32_e64 v33, 0, 1.0, vcc
	v_fma_f32 v33, -v77, v46, v33
	v_and_b32_e32 v46, 0xffff0000, v52
	v_lshlrev_b32_e32 v47, 16, v53
	v_fma_f32 v46, -v79, v46, 0
	v_fma_f32 v33, -v80, v47, v33
	v_and_b32_e32 v47, 0xffff0000, v53
	v_fma_f32 v46, -v81, v47, v46
	v_lshlrev_b32_e32 v47, 16, v54
	v_fma_f32 v33, -v83, v47, v33
	v_and_b32_e32 v47, 0xffff0000, v54
	v_fma_f32 v46, -v84, v47, v46
	v_lshlrev_b32_e32 v47, 16, v55
	v_fma_f32 v33, -v85, v47, v33
	v_and_b32_e32 v47, 0xffff0000, v55
	v_fma_f32 v46, -v86, v47, v46
	s_waitcnt lgkmcnt(5)
	v_lshlrev_b32_e32 v47, 16, v56
	v_fma_f32 v33, -v87, v47, v33
	v_and_b32_e32 v47, 0xffff0000, v56
	v_fma_f32 v46, -v88, v47, v46
	v_lshlrev_b32_e32 v47, 16, v57
	v_fma_f32 v33, -v89, v47, v33
	v_and_b32_e32 v47, 0xffff0000, v57
	v_fma_f32 v46, -v111, v47, v46
	v_lshlrev_b32_e32 v47, 16, v58
	v_fma_f32 v33, -v32, v47, v33
	v_add_f32_e32 v33, v46, v33
	v_cvt_pk_bf16_f32 v46, v33, v33
	v_cmp_eq_u32_e32 vcc, 14, v106
	ds_write_b16 v78, v46 offset:55712
	s_waitcnt lgkmcnt(5)
	v_lshlrev_b32_e32 v47, 16, v60
	v_cndmask_b32_e64 v46, 0, 1.0, vcc
	v_fma_f32 v46, -v77, v47, v46
	v_and_b32_e32 v47, 0xffff0000, v60
	v_lshlrev_b32_e32 v48, 16, v61
	v_fma_f32 v47, -v79, v47, 0
	v_fma_f32 v46, -v80, v48, v46
	v_and_b32_e32 v48, 0xffff0000, v61
	v_fma_f32 v47, -v81, v48, v47
	v_lshlrev_b32_e32 v48, 16, v62
	v_fma_f32 v46, -v83, v48, v46
	v_and_b32_e32 v48, 0xffff0000, v62
	v_fma_f32 v47, -v84, v48, v47
	v_lshlrev_b32_e32 v48, 16, v63
	v_fma_f32 v46, -v85, v48, v46
	v_and_b32_e32 v48, 0xffff0000, v63
	v_fma_f32 v47, -v86, v48, v47
	s_waitcnt lgkmcnt(4)
	v_lshlrev_b32_e32 v48, 16, v64
	v_fma_f32 v46, -v87, v48, v46
	v_and_b32_e32 v48, 0xffff0000, v64
	v_fma_f32 v47, -v88, v48, v47
	v_lshlrev_b32_e32 v48, 16, v65
	v_fma_f32 v46, -v89, v48, v46
	v_and_b32_e32 v48, 0xffff0000, v65
	v_fma_f32 v47, -v111, v48, v47
	v_lshlrev_b32_e32 v48, 16, v66
	v_fma_f32 v46, -v32, v48, v46
	v_and_b32_e32 v48, 0xffff0000, v66
	v_fma_f32 v47, -v33, v48, v47
	v_add_f32_e32 v46, v46, v47
	v_cvt_pk_bf16_f32 v47, v46, v46
	v_cmp_eq_u32_e32 vcc, 15, v106
	ds_write_b16 v78, v47 offset:55744
	s_waitcnt lgkmcnt(4)
; #define LAS __attribute__((address_space(3)))
; __device__ __forceinline__ unsigned f2bf(float f) { unsigned u = __float_as_uint(f); return (u + 0x7fffu + ((u >> 16) & 1u)) >> 16; }
; __device__ __forceinline__ float lo_bf(unsigned w) { return __uint_as_float(w << 16); }
; __device__ __forceinline__ float hi_bf(unsigned w) { return __uint_as_float(w & 0xffff0000u); }
; __device__ __forceinline__ u32x2 cvt4(f32x4 v) { return (u32x2){pk2(v[0], v[1]), pk2(v[2], v[3])}; }
; __device__ __forceinline__ void gdn_s23(CArgs& a, int u, const GdnIn2& in, LAS unsigned char* ub, LAS unsigned char* dwb, int w, int lane, float cl) {
;     ...
;           for (int rr = 0; rr < 4; ++rr) { const int r = 4 * hb + rr; float t = (r == c) ? 1.f : 0.f;
;               float t2 = 0.f;
; #pragma unroll
;               for (int j = 0; j < r; ++j) { const unsigned wv = arow[rr][j >> 3][(j >> 1) & 3]; const float av = (j & 1) ? hi_bf(wv) : lo_bf(wv); if (j & 1) t2 -= av * T[j]; else t -= av * T[j]; }
;               t += t2;
;               T[r] = t; DW[(blk * 16 + r) * 16 + c] = (bf16)f2bf(t); } } }
;     asm volatile("s_waitcnt lgkmcnt(0)" ::: "memory");
;     f32x4 X[4];
; #pragma unroll
;     for (int I = 0; I < 4; ++I) {
;         const f32x4 br = *(const LAS f32x4*)(GT + 16 * I + 4 * kg), er = *(const LAS f32x4*)(GT + 128 + 16 * I + 4 * kg);
;         const f32x4 Rf = (f32x4){__uint_as_float(in.R[I].x << 16), __uint_as_float(in.R[I].y << 16), __uint_as_float(in.R[I].z << 16), __uint_as_float(in.R[I].w << 16)};
;         f32x4 acc = isW ? br * er * Rf : br * Rf;
; #pragma unroll
;         for (int P = 0; 2 * P < I; ++P) {
;             const u32x2 alo = *(const LAS u32x2*)(AB + (16 * I + fr) * 72 + 32 * P + 4 * kg);
;             const u32x2 ahi = (2 * P + 1 < I) ? *(const LAS u32x2*)(AB + (16 * I + fr) * 72 + 32 * P + 16 + 4 * kg) : (u32x2){0u, 0u};
;             const u32x2 xlo = cvt4(-X[2 * P]); const u32x2 xhi = (2 * P + 1 < I) ? cvt4(-X[2 * P + 1]) : (u32x2){0u, 0u};
;             acc = __builtin_amdgcn_mfma_f32_16x16x32_bf16(frag2(alo, ahi), frag2(xlo, xhi), acc, 0, 0, 0); }
;         const u32x2 dlo = *(const LAS u32x2*)(DW + (I * 16 + fr) * 16 + 4 * kg);
;         X[I] = __builtin_amdgcn_mfma_f32_16x16x32_bf16(frag2(dlo, (u32x2){0u, 0u}), frag2(cvt4(acc), (u32x2){0u, 0u}), (f32x4){0.f, 0.f, 0.f, 0.f}, 0, 0, 0);
	v_lshlrev_b32_e32 v48, 16, v68
	v_cndmask_b32_e64 v47, 0, 1.0, vcc
	v_fma_f32 v47, -v77, v48, v47
	v_and_b32_e32 v48, 0xffff0000, v68
	v_lshlrev_b32_e32 v49, 16, v69
	v_fma_f32 v48, -v79, v48, 0
	v_fma_f32 v47, -v80, v49, v47
	v_and_b32_e32 v49, 0xffff0000, v69
	v_fma_f32 v48, -v81, v49, v48
	v_lshlrev_b32_e32 v49, 16, v70
	v_fma_f32 v47, -v83, v49, v47
	v_and_b32_e32 v49, 0xffff0000, v70
	v_fma_f32 v48, -v84, v49, v48
	v_lshlrev_b32_e32 v49, 16, v71
	v_fma_f32 v47, -v85, v49, v47
	v_and_b32_e32 v49, 0xffff0000, v71
	v_fma_f32 v48, -v86, v49, v48
	s_waitcnt lgkmcnt(3)
	v_lshlrev_b32_e32 v49, 16, v72
	v_fma_f32 v47, -v87, v49, v47
	v_and_b32_e32 v49, 0xffff0000, v72
	v_fma_f32 v48, -v88, v49, v48
	v_lshlrev_b32_e32 v49, 16, v73
	v_fma_f32 v47, -v89, v49, v47
	v_and_b32_e32 v49, 0xffff0000, v73
	v_fma_f32 v48, -v111, v49, v48
	v_lshlrev_b32_e32 v49, 16, v74
	v_fma_f32 v32, -v32, v49, v47
	v_and_b32_e32 v47, 0xffff0000, v74
	v_fma_f32 v33, -v33, v47, v48
	v_lshlrev_b32_e32 v47, 16, v75
	v_fma_f32 v32, -v46, v47, v32
	v_add_f32_e32 v32, v33, v32
	v_cvt_pk_bf16_f32 v32, v32, v32
	ds_write_b16 v78, v32 offset:55776
	s_waitcnt lgkmcnt(0)
	v_add_u32_e32 v79, s8, v76
	ds_read_b128 v[46:49], v79 offset:57344
	ds_read_b128 v[54:57], v79 offset:57856
	v_lshlrev_b32_e32 v70, 3, v82
	v_sub_u32_e32 v33, v79, v70
	s_waitcnt vmcnt(15)
	v_lshlrev_b32_e32 v50, 16, v123
	s_waitcnt vmcnt(14)
	v_lshlrev_b32_e32 v51, 16, v139
	s_waitcnt lgkmcnt(0)
	v_pk_mul_f32 v[60:61], v[46:47], v[54:55]
	v_pk_mul_f32 v[58:59], v[48:49], v[56:57]
	v_cndmask_b32_e64 v47, v47, v61, s[38:39]
	v_cndmask_b32_e64 v46, v46, v60, s[38:39]
	v_pk_mul_f32 v[50:51], v[46:47], v[50:51]
	v_lshl_add_u32 v46, v106, 5, v33
	ds_read_b64 v[46:47], v46 offset:55296
	v_cndmask_b32_e64 v48, v48, v58, s[38:39]
	s_waitcnt vmcnt(13)
	v_lshlrev_b32_e32 v52, 16, v141
	s_waitcnt vmcnt(12)
	v_lshlrev_b32_e32 v53, 16, v142
	v_cndmask_b32_e64 v49, v49, v59, s[38:39]
	v_pk_mul_f32 v[52:53], v[48:49], v[52:53]
	v_mov_b32_e32 v48, v35
	v_mov_b32_e32 v49, v35
	v_cvt_pk_bf16_f32 v50, v50, v51
	v_cvt_pk_bf16_f32 v51, v52, v53
	v_mov_b32_e32 v52, v35
	v_mov_b32_e32 v53, v35
	s_waitcnt vmcnt(9)
	v_lshlrev_b32_e32 v60, 16, v138
	s_waitcnt vmcnt(8)
	v_lshlrev_b32_e32 v61, 16, v140
	s_waitcnt lgkmcnt(0)
	v_mfma_f32_16x16x32_bf16 v[62:65], v[46:49], v[50:53], 0
	ds_read_b128 v[46:49], v79 offset:57408
	ds_read_b128 v[50:53], v79 offset:57920
	v_or_b32_e32 v89, 16, v106
	v_add_u32_e32 v86, 0, v70
	v_lshlrev_b32_e32 v58, 16, v121
	v_lshlrev_b32_e32 v59, 16, v122
	s_waitcnt lgkmcnt(0)
	v_pk_mul_f32 v[66:67], v[48:49], v[52:53]
	v_pk_mul_f32 v[68:69], v[46:47], v[50:51]
	v_cndmask_b32_e64 v49, v49, v67, s[38:39]
	v_xor_b32_e32 v67, 0x80000000, v63
	v_cndmask_b32_e64 v48, v48, v66, s[38:39]
	v_cndmask_b32_e64 v46, v46, v68, s[38:39]
	v_xor_b32_e32 v66, 0x80000000, v62
	v_bfe_u32 v68, v67, 16, 1
	v_add3_u32 v67, v67, v68, s81
	v_bfe_u32 v68, v66, 16, 1
	v_add3_u32 v66, v66, v68, s81
	v_cndmask_b32_e64 v47, v47, v69, s[38:39]
	v_pk_mul_f32 v[48:49], v[48:49], v[60:61]
	v_mad_u32_u24 v78, v89, s75, v86
	v_xor_b32_e32 v61, 0x80000000, v65
	v_lshrrev_b32_e32 v66, 16, v66
	v_pk_mul_f32 v[46:47], v[46:47], v[58:59]
	ds_read_b64 v[58:59], v78 offset:27648
	v_xor_b32_e32 v60, 0x80000000, v64
	v_and_or_b32 v74, v67, s80, v66
	v_cvt_pk_bf16_f32 v75, v60, v61
	v_mov_b32_e32 v60, v35
	v_mov_b32_e32 v61, v35
	v_mov_b32_e32 v76, v35
	v_mov_b32_e32 v77, v35
	s_waitcnt vmcnt(7)
	v_lshlrev_b32_e32 v70, 16, v107
	s_waitcnt vmcnt(6)
	v_lshlrev_b32_e32 v71, 16, v108
	s_waitcnt lgkmcnt(0)
	v_mfma_f32_16x16x32_bf16 v[46:49], v[58:61], v[74:77], v[46:49]
	v_lshl_add_u32 v58, v89, 5, v33
	ds_read_b64 v[58:59], v58 offset:55296
	s_waitcnt vmcnt(5)
	v_lshlrev_b32_e32 v72, 16, v109
	s_waitcnt vmcnt(4)
	v_lshlrev_b32_e32 v73, 16, v117
	v_or_b32_e32 v88, 32, v106
	s_nop 0
	v_cvt_pk_bf16_f32 v46, v46, v46
	v_bfe_u32 v66, v47, 16, 1
	v_lshrrev_b32_e32 v46, 16, v46
	v_add3_u32 v47, v47, v66, s81
	v_and_or_b32 v46, v47, s80, v46
	v_cvt_pk_bf16_f32 v47, v48, v49
	v_mov_b32_e32 v48, v35
	v_mov_b32_e32 v49, v35
	s_waitcnt vmcnt(1)
	v_lshlrev_b32_e32 v84, 16, v119
	s_waitcnt vmcnt(0)
	v_lshlrev_b32_e32 v85, 16, v120
	s_waitcnt lgkmcnt(0)
	v_mfma_f32_16x16x32_bf16 v[66:69], v[58:61], v[46:49], 0
	ds_read_b128 v[46:49], v79 offset:57472
	ds_read_b128 v[58:61], v79 offset:57984
	v_or_b32_e32 v87, 48, v106
	s_ashr_i32 s29, s28, 31
	s_lshl_b64 s[52:53], s[28:29], 13
	s_add_u32 s26, s85, s52
	s_waitcnt lgkmcnt(0)
; #define LAS __attribute__((address_space(3)))
; __device__ __forceinline__ void gdn_s23(CArgs& a, int u, const GdnIn2& in, LAS unsigned char* ub, LAS unsigned char* dwb, int w, int lane, float cl) {
;     ...
;     f32x4 X[4];
; #pragma unroll
;     for (int I = 0; I < 4; ++I) {
;         const f32x4 br = *(const LAS f32x4*)(GT + 16 * I + 4 * kg), er = *(const LAS f32x4*)(GT + 128 + 16 * I + 4 * kg);
;         const f32x4 Rf = (f32x4){__uint_as_float(in.R[I].x << 16), __uint_as_float(in.R[I].y << 16), __uint_as_float(in.R[I].z << 16), __uint_as_float(in.R[I].w << 16)};
;         f32x4 acc = isW ? br * er * Rf : br * Rf;
; #pragma unroll
;         for (int P = 0; 2 * P < I; ++P) {
;             const u32x2 alo = *(const LAS u32x2*)(AB + (16 * I + fr) * 72 + 32 * P + 4 * kg);
;             const u32x2 ahi = (2 * P + 1 < I) ? *(const LAS u32x2*)(AB + (16 * I + fr) * 72 + 32 * P + 16 + 4 * kg) : (u32x2){0u, 0u};
;             const u32x2 xlo = cvt4(-X[2 * P]); const u32x2 xhi = (2 * P + 1 < I) ? cvt4(-X[2 * P + 1]) : (u32x2){0u, 0u};
;             acc = __builtin_amdgcn_mfma_f32_16x16x32_bf16(frag2(alo, ahi), frag2(xlo, xhi), acc, 0, 0, 0); }
;         const u32x2 dlo = *(const LAS u32x2*)(DW + (I * 16 + fr) * 16 + 4 * kg);
;         X[I] = __builtin_amdgcn_mfma_f32_16x16x32_bf16(frag2(dlo, (u32x2){0u, 0u}), frag2(cvt4(acc), (u32x2){0u, 0u}), (f32x4){0.f, 0.f, 0.f, 0.f}, 0, 0, 0);
;     }
;     const bf16x8 Xb01 = frag2(cvt4(X[0]), cvt4(X[1])), Xb23 = frag2(cvt4(X[2]), cvt4(X[3]));
;     const float ecl = __expf(cl);
;     bf16* ftp = FTo + (c0 + fr) * 64 + 4 * kg; bf16* btp = BTo + (c0 + fr) * 64 + 4 * kg; bf16* ep = Eo + (4 * kg) * 64 + c0 + fr; bf16* mp = Mo + (4 * kg) * 64 + c0 + fr;
; #pragma unroll
;     for (int t4 = 0; t4 < 4; ++t4) {
;         const LAS bf16* ar = ATT + (16 * t4 + fr) * 72 + 4 * kg; const LAS bf16* kr = KTT + (16 * t4 + fr) * 72 + 4 * kg;
;         f32x4 pa = (f32x4){0.f, 0.f, 0.f, 0.f}, pk = (f32x4){0.f, 0.f, 0.f, 0.f};
;         pa = __builtin_amdgcn_mfma_f32_16x16x32_bf16(frag2(*(const LAS u32x2*)ar, *(const LAS u32x2*)(ar + 16)), Xb01, pa, 0, 0, 0);
;         pa = __builtin_amdgcn_mfma_f32_16x16x32_bf16(frag2(*(const LAS u32x2*)(ar + 32), *(const LAS u32x2*)(ar + 48)), Xb23, pa, 0, 0, 0);
;         pk = __builtin_amdgcn_mfma_f32_16x16x32_bf16(frag2(*(const LAS u32x2*)kr, *(const LAS u32x2*)(kr + 16)), Xb01, pk, 0, 0, 0);
	v_pk_mul_f32 v[80:81], v[46:47], v[58:59]
	v_pk_mul_f32 v[76:77], v[48:49], v[60:61]
	v_cndmask_b32_e64 v47, v47, v81, s[38:39]
	v_cndmask_b32_e64 v46, v46, v80, s[38:39]
	v_cndmask_b32_e64 v49, v49, v77, s[38:39]
	v_cndmask_b32_e64 v48, v48, v76, s[38:39]
	v_pk_mul_f32 v[46:47], v[46:47], v[70:71]
	v_add_u32_e32 v70, 0x7000, v78
	v_xor_b32_e32 v81, 0x80000000, v67
	v_pk_mul_f32 v[48:49], v[48:49], v[72:73]
	ds_read2_b64 v[70:73], v70 offset0:160 offset1:164
	v_xor_b32_e32 v76, 0x80000000, v66
	v_xor_b32_e32 v80, 0x80000000, v69
	v_xor_b32_e32 v77, 0x80000000, v68
	v_cvt_pk_bf16_f32 v76, v76, v81
	v_cvt_pk_bf16_f32 v77, v77, v80
	v_lshlrev_b32_e32 v81, 16, v118
	s_addc_u32 s27, s64, s53
	s_waitcnt lgkmcnt(0)
	v_mfma_f32_16x16x32_bf16 v[46:49], v[70:73], v[74:77], v[46:49]
	v_lshl_add_u32 v70, v88, 5, v33
	ds_read_b64 v[70:71], v70 offset:55296
	v_mov_b32_e32 v72, v35
	v_mov_b32_e32 v73, v35
	v_lshl_add_u32 v33, v87, 5, v33
	s_nop 2
	v_cvt_pk_bf16_f32 v46, v46, v47
	v_cvt_pk_bf16_f32 v47, v48, v49
	v_mov_b32_e32 v48, v35
	v_mov_b32_e32 v49, v35
	v_lshlrev_b32_e32 v80, 16, v116
	s_add_u32 s28, s71, s52
	s_waitcnt lgkmcnt(0)
	v_mfma_f32_16x16x32_bf16 v[70:73], v[70:73], v[46:49], 0
	ds_read_b128 v[126:129], v79 offset:57536
	ds_read_b128 v[46:49], v79 offset:58048
	v_add_u32_e32 v79, 0x7800, v78
	ds_read2_b64 v[118:121], v79 offset0:192 offset1:196
	ds_read_b64 v[78:79], v78 offset:32320
	s_nop 2
	v_xor_b32_e32 v83, 0x80000000, v70
	s_waitcnt lgkmcnt(2)
	v_pk_mul_f32 v[108:109], v[128:129], v[48:49]
	v_pk_mul_f32 v[114:115], v[126:127], v[46:47]
	v_cndmask_b32_e64 v109, v129, v109, s[38:39]
	v_cndmask_b32_e64 v108, v128, v108, s[38:39]
	v_pk_mul_f32 v[116:117], v[108:109], v[84:85]
	v_xor_b32_e32 v84, 0x80000000, v71
	v_bfe_u32 v85, v84, 16, 1
	v_add3_u32 v84, v84, v85, s81
	v_cndmask_b32_e64 v115, v127, v115, s[38:39]
	v_cndmask_b32_e64 v114, v126, v114, s[38:39]
	v_cvt_pk_bf16_f32 v83, v83, v83
	v_pk_mul_f32 v[114:115], v[114:115], v[80:81]
	v_xor_b32_e32 v81, 0x80000000, v73
	v_lshrrev_b32_e32 v83, 16, v83
	s_waitcnt lgkmcnt(1)
	v_mfma_f32_16x16x32_bf16 v[74:77], v[118:121], v[74:77], v[114:117]
	v_xor_b32_e32 v80, 0x80000000, v72
	s_addc_u32 s29, s18, s53
	s_add_u32 s2, s19, s52
	v_and_or_b32 v114, v84, s80, v83
	v_cvt_pk_bf16_f32 v81, v81, v81
	v_cvt_pk_bf16_f32 v80, v80, v80
	v_lshrrev_b32_e32 v80, 16, v80
	v_and_or_b32 v115, v81, s80, v80
	v_mov_b32_e32 v80, v35
	v_mov_b32_e32 v81, v35
	v_mov_b32_e32 v116, v35
	v_mov_b32_e32 v117, v35
	v_lshlrev_b32_e32 v32, 2, v82
	s_addc_u32 s3, s66, s53
	s_waitcnt lgkmcnt(0)
	v_mfma_f32_16x16x32_bf16 v[74:77], v[78:81], v[114:117], v[74:77]
	ds_read_b64 v[78:79], v33 offset:55296
	s_add_u32 s52, s21, s52
	s_addc_u32 s53, s70, s53
	s_and_b64 vcc, exec, s[48:49]
	s_nop 3
	v_cvt_pk_bf16_f32 v74, v74, v75
	v_cvt_pk_bf16_f32 v75, v76, v77
	v_cvt_pk_bf16_f32 v62, v62, v63
	v_cvt_pk_bf16_f32 v63, v64, v65
	v_cvt_pk_bf16_f32 v64, v66, v67
	v_cvt_pk_bf16_f32 v65, v68, v69
	v_mov_b32_e32 v76, v35
	v_mov_b32_e32 v77, v35
	s_waitcnt lgkmcnt(0)
	s_nop 0
	v_mfma_f32_16x16x32_bf16 v[74:77], v[78:81], v[74:77], 0
	v_cvt_pk_bf16_f32 v66, v70, v71
	v_cvt_pk_bf16_f32 v67, v72, v73
	s_nop 5
	v_cvt_pk_bf16_f32 v68, v74, v75
	v_cvt_pk_bf16_f32 v69, v76, v77
	v_ashrrev_i32_e32 v33, 31, v32
	v_lshlrev_b32_e32 v70, 7, v45
	v_mov_b32_e32 v71, v35
	v_lshlrev_b64 v[74:75], 1, v[32:33]
	v_mul_u32_u24_e32 v33, 0x48, v106
	v_lshl_add_u64 v[72:73], s[28:29], 0, v[70:71]
	v_lshl_add_u64 v[70:71], s[52:53], 0, v[70:71]
	v_lshl_add_u32 v33, v33, 1, v86
	v_lshl_add_u64 v[80:81], v[72:73], 0, v[74:75]
	v_lshl_add_u64 v[78:79], v[70:71], 0, v[74:75]
	v_add_u32_e32 v74, 0x9000, v33
	ds_read2_b64 v[70:73], v74 offset1:4
	ds_read2_b64 v[74:77], v74 offset0:8 offset1:12
	s_waitcnt lgkmcnt(1)
	v_mfma_f32_16x16x32_bf16 v[70:73], v[70:73], v[62:65], 0
	v_add_u32_e32 v33, 0xb000, v33
	ds_read2_b64 v[106:109], v33 offset0:136 offset1:140
	s_mov_b64 s[28:29], -1
	s_waitcnt lgkmcnt(1)
	v_mfma_f32_16x16x32_bf16 v[70:73], v[74:77], v[66:69], v[70:73]
	ds_read2_b64 v[74:77], v33 offset0:128 offset1:132
	s_waitcnt lgkmcnt(0)
	v_mfma_f32_16x16x32_bf16 v[74:77], v[74:77], v[62:65], 0
	v_mfma_f32_16x16x32_bf16 v[74:77], v[106:109], v[66:69], v[74:77]
	s_cbranch_vccnz .LBB0_1783
	s_nop 2
	v_cvt_pk_bf16_f32 v84, v70, v71
	v_cvt_pk_bf16_f32 v85, v72, v73
	global_store_dwordx2 v[80:81], v[84:85], off
	s_nop 0
	v_cvt_pk_bf16_f32 v84, v74, v75
	v_cvt_pk_bf16_f32 v85, v76, v77
	s_mov_b64 s[28:29], 0
	global_store_dwordx2 v[78:79], v[84:85], off

; #define LAS __attribute__((address_space(3)))
; __device__ __forceinline__ u32x2 cvt4(f32x4 v) { return (u32x2){pk2(v[0], v[1]), pk2(v[2], v[3])}; }
; __device__ __forceinline__ void gdn_s23(CArgs& a, int u, const GdnIn2& in, LAS unsigned char* ub, LAS unsigned char* dwb, int w, int lane, float cl) {
;     ...
;     for (int t4 = 0; t4 < 4; ++t4) {
;         const LAS bf16* ar = ATT + (16 * t4 + fr) * 72 + 4 * kg; const LAS bf16* kr = KTT + (16 * t4 + fr) * 72 + 4 * kg;
;         f32x4 pa = (f32x4){0.f, 0.f, 0.f, 0.f}, pk = (f32x4){0.f, 0.f, 0.f, 0.f};
;         pa = __builtin_amdgcn_mfma_f32_16x16x32_bf16(frag2(*(const LAS u32x2*)ar, *(const LAS u32x2*)(ar + 16)), Xb01, pa, 0, 0, 0);
;         pa = __builtin_amdgcn_mfma_f32_16x16x32_bf16(frag2(*(const LAS u32x2*)(ar + 32), *(const LAS u32x2*)(ar + 48)), Xb23, pa, 0, 0, 0);
;         pk = __builtin_amdgcn_mfma_f32_16x16x32_bf16(frag2(*(const LAS u32x2*)kr, *(const LAS u32x2*)(kr + 16)), Xb01, pk, 0, 0, 0);
;         pk = __builtin_amdgcn_mfma_f32_16x16x32_bf16(frag2(*(const LAS u32x2*)(kr + 32), *(const LAS u32x2*)(kr + 48)), Xb23, pk, 0, 0, 0);
;         if (!isW) {
;             *(u32x2*)(ftp + 16 * t4) = cvt4(pa);
;             *(u32x2*)(btp + 16 * t4) = cvt4(pk);
.LBB0_1785:
	v_mul_u32_u24_e32 v34, 0x48, v89
	v_lshl_add_u32 v34, v34, 1, v86
	v_add_u32_e32 v70, 0x9000, v34
	ds_read2_b64 v[54:57], v70 offset1:4
	ds_read2_b64 v[70:73], v70 offset0:8 offset1:12
	v_add_u32_e32 v34, 0xb000, v34
	ds_read2_b64 v[74:77], v34 offset0:136 offset1:140
	s_mov_b64 s[2:3], -1
	s_and_b64 vcc, exec, s[48:49]
	s_waitcnt lgkmcnt(2)
	v_mfma_f32_16x16x32_bf16 v[54:57], v[54:57], v[62:65], 0
	s_waitcnt lgkmcnt(1)
	v_mfma_f32_16x16x32_bf16 v[54:57], v[70:73], v[66:69], v[54:57]
	ds_read2_b64 v[70:73], v34 offset0:128 offset1:132
	s_waitcnt lgkmcnt(0)
	v_mfma_f32_16x16x32_bf16 v[70:73], v[70:73], v[62:65], 0
	v_mfma_f32_16x16x32_bf16 v[70:73], v[74:77], v[66:69], v[70:73]
	s_cbranch_vccnz .LBB0_1787
	s_nop 2
	v_cvt_pk_bf16_f32 v74, v54, v55
	v_cvt_pk_bf16_f32 v75, v56, v57
	global_store_dwordx2 v[80:81], v[74:75], off offset:32
	s_nop 0
	v_cvt_pk_bf16_f32 v74, v70, v71
	v_cvt_pk_bf16_f32 v34, v72, v72
	v_lshrrev_b32_e32 v34, 16, v34
	v_cvt_pk_bf16_f32 v75, v73, v73
	v_and_or_b32 v75, v75, s80, v34
	s_mov_b64 s[2:3], 0
	global_store_dwordx2 v[78:79], v[74:75], off offset:32

; #define LAS __attribute__((address_space(3)))
; __device__ __forceinline__ u32x2 cvt4(f32x4 v) { return (u32x2){pk2(v[0], v[1]), pk2(v[2], v[3])}; }
; __device__ __forceinline__ void gdn_s23(CArgs& a, int u, const GdnIn2& in, LAS unsigned char* ub, LAS unsigned char* dwb, int w, int lane, float cl) {
;     ...
;     for (int t4 = 0; t4 < 4; ++t4) {
;         const LAS bf16* ar = ATT + (16 * t4 + fr) * 72 + 4 * kg; const LAS bf16* kr = KTT + (16 * t4 + fr) * 72 + 4 * kg;
;         f32x4 pa = (f32x4){0.f, 0.f, 0.f, 0.f}, pk = (f32x4){0.f, 0.f, 0.f, 0.f};
;         pa = __builtin_amdgcn_mfma_f32_16x16x32_bf16(frag2(*(const LAS u32x2*)ar, *(const LAS u32x2*)(ar + 16)), Xb01, pa, 0, 0, 0);
;         pa = __builtin_amdgcn_mfma_f32_16x16x32_bf16(frag2(*(const LAS u32x2*)(ar + 32), *(const LAS u32x2*)(ar + 48)), Xb23, pa, 0, 0, 0);
;         pk = __builtin_amdgcn_mfma_f32_16x16x32_bf16(frag2(*(const LAS u32x2*)kr, *(const LAS u32x2*)(kr + 16)), Xb01, pk, 0, 0, 0);
;         pk = __builtin_amdgcn_mfma_f32_16x16x32_bf16(frag2(*(const LAS u32x2*)(kr + 32), *(const LAS u32x2*)(kr + 48)), Xb23, pk, 0, 0, 0);
;         if (!isW) {
;             *(u32x2*)(ftp + 16 * t4) = cvt4(pa);
;             *(u32x2*)(btp + 16 * t4) = cvt4(pk);
.LBB0_1789:
	v_mul_u32_u24_e32 v34, 0x48, v88
	v_lshl_add_u32 v34, v34, 1, v86
	v_add_u32_e32 v54, 0x9000, v34
	ds_read2_b64 v[50:53], v54 offset1:4
	ds_read2_b64 v[54:57], v54 offset0:8 offset1:12
	v_add_u32_e32 v34, 0xb000, v34
	ds_read2_b64 v[70:73], v34 offset0:136 offset1:140
	s_mov_b64 s[2:3], -1
	s_and_b64 vcc, exec, s[48:49]
	s_waitcnt lgkmcnt(2)
	v_mfma_f32_16x16x32_bf16 v[50:53], v[50:53], v[62:65], 0
	s_waitcnt lgkmcnt(1)
	v_mfma_f32_16x16x32_bf16 v[50:53], v[54:57], v[66:69], v[50:53]
	ds_read2_b64 v[54:57], v34 offset0:128 offset1:132
	s_waitcnt lgkmcnt(0)
	v_mfma_f32_16x16x32_bf16 v[54:57], v[54:57], v[62:65], 0
	v_mfma_f32_16x16x32_bf16 v[54:57], v[70:73], v[66:69], v[54:57]
	s_cbranch_vccnz .LBB0_1791
	s_nop 2
	v_cvt_pk_bf16_f32 v70, v50, v51
	v_cvt_pk_bf16_f32 v71, v52, v53
	global_store_dwordx2 v[80:81], v[70:71], off offset:64
	s_nop 0
	v_cvt_pk_bf16_f32 v70, v54, v55
	v_cvt_pk_bf16_f32 v34, v56, v56
	v_lshrrev_b32_e32 v34, 16, v34
	v_cvt_pk_bf16_f32 v71, v57, v57
	v_and_or_b32 v71, v71, s80, v34
	s_mov_b64 s[2:3], 0
	global_store_dwordx2 v[78:79], v[70:71], off offset:64

; #define LAS __attribute__((address_space(3)))
; __device__ __forceinline__ u32x2 cvt4(f32x4 v) { return (u32x2){pk2(v[0], v[1]), pk2(v[2], v[3])}; }
; __device__ __forceinline__ void gdn_s23(CArgs& a, int u, const GdnIn2& in, LAS unsigned char* ub, LAS unsigned char* dwb, int w, int lane, float cl) {
;     ...
;     for (int t4 = 0; t4 < 4; ++t4) {
;         const LAS bf16* ar = ATT + (16 * t4 + fr) * 72 + 4 * kg; const LAS bf16* kr = KTT + (16 * t4 + fr) * 72 + 4 * kg;
;         f32x4 pa = (f32x4){0.f, 0.f, 0.f, 0.f}, pk = (f32x4){0.f, 0.f, 0.f, 0.f};
;         pa = __builtin_amdgcn_mfma_f32_16x16x32_bf16(frag2(*(const LAS u32x2*)ar, *(const LAS u32x2*)(ar + 16)), Xb01, pa, 0, 0, 0);
;         pa = __builtin_amdgcn_mfma_f32_16x16x32_bf16(frag2(*(const LAS u32x2*)(ar + 32), *(const LAS u32x2*)(ar + 48)), Xb23, pa, 0, 0, 0);
;         pk = __builtin_amdgcn_mfma_f32_16x16x32_bf16(frag2(*(const LAS u32x2*)kr, *(const LAS u32x2*)(kr + 16)), Xb01, pk, 0, 0, 0);
;         pk = __builtin_amdgcn_mfma_f32_16x16x32_bf16(frag2(*(const LAS u32x2*)(kr + 32), *(const LAS u32x2*)(kr + 48)), Xb23, pk, 0, 0, 0);
;         if (!isW) {
;             *(u32x2*)(ftp + 16 * t4) = cvt4(pa);
;             *(u32x2*)(btp + 16 * t4) = cvt4(pk);
.LBB0_1793:
	v_mul_u32_u24_e32 v34, 0x48, v87
	v_lshl_add_u32 v34, v34, 1, v86
	v_add_u32_e32 v58, 0x9000, v34
	ds_read2_b64 v[50:53], v58 offset1:4
	ds_read2_b64 v[58:61], v58 offset0:8 offset1:12
	v_add_u32_e32 v34, 0xb000, v34
	ds_read2_b64 v[54:57], v34 offset0:128 offset1:132
	s_and_b64 vcc, exec, s[48:49]
	s_mov_b64 s[2:3], -1
	s_waitcnt lgkmcnt(2)
	v_mfma_f32_16x16x32_bf16 v[50:53], v[50:53], v[62:65], 0
	s_waitcnt lgkmcnt(1)
	v_mfma_f32_16x16x32_bf16 v[50:53], v[58:61], v[66:69], v[50:53]
	ds_read2_b64 v[58:61], v34 offset0:136 offset1:140
	s_waitcnt lgkmcnt(1)
	v_mfma_f32_16x16x32_bf16 v[54:57], v[54:57], v[62:65], 0
	s_waitcnt lgkmcnt(0)
	v_mfma_f32_16x16x32_bf16 v[54:57], v[58:61], v[66:69], v[54:57]
	s_cbranch_vccnz .LBB0_1795
	s_nop 1
	v_cvt_pk_bf16_f32 v58, v50, v51
	v_cvt_pk_bf16_f32 v59, v52, v53
	global_store_dwordx2 v[80:81], v[58:59], off offset:96
	s_nop 1
	v_cvt_pk_bf16_f32 v58, v54, v55
	v_cvt_pk_bf16_f32 v34, v56, v56
	v_lshrrev_b32_e32 v34, 16, v34
	v_cvt_pk_bf16_f32 v59, v57, v57
	v_and_or_b32 v59, v59, s80, v34
	global_store_dwordx2 v[78:79], v[58:59], off offset:96
	s_cbranch_execnz .LBB0_1682
	s_branch .LBB0_1796

; #define LAS __attribute__((address_space(3)))
; __device__ __forceinline__ unsigned f2bf(float f) { unsigned u = __float_as_uint(f); return (u + 0x7fffu + ((u >> 16) & 1u)) >> 16; }
; __device__ __forceinline__ void gdn_s23(CArgs& a, int u, const GdnIn2& in, LAS unsigned char* ub, LAS unsigned char* dwb, int w, int lane, float cl) {
;     ...
;         } else {
;             const f32x4 ec = *(const LAS f32x4*)(GT + 128 + 16 * t4 + 4 * kg);
; #pragma unroll
;             for (int e = 0; e < 4; ++e) { const int row = 16 * t4 + 4 * kg + e, col = c0 + fr;
;                 ep[(16 * t4 + e) * 64] = (bf16)f2bf(ec[e] * __uint_as_float(in.Qv[t4][e] << 16) - pa[e]);
;                 mp[(16 * t4 + e) * 64] = (bf16)f2bf((row == col ? ecl : 0.f) - pk[e]); }
;         }
.LBB0_1796:
	v_add_co_u32_e32 v58, vcc, 0x1000, v84
	v_add_u32_e32 v34, 48, v32
	s_nop 0
	v_addc_co_u32_e32 v59, vcc, 0, v85, vcc
	v_fma_f32 v46, v92, v46, -v50
	v_cmp_eq_u32_e32 vcc, v34, v45
	v_cvt_pk_bf16_f32 v46, v46, v46
	s_nop 0
	v_cndmask_b32_e32 v34, 0, v33, vcc
	v_sub_f32_e32 v34, v34, v54
	global_store_short_d16_hi v[58:59], v46, off offset:2048
	v_add_co_u32_e32 v60, vcc, 0x1000, v82
	v_cvt_pk_bf16_f32 v34, v34, v34
	s_nop 0
	v_addc_co_u32_e32 v61, vcc, 0, v83, vcc
	global_store_short v[60:61], v34, off offset:2048
	v_add_u32_e32 v34, 49, v32
	v_fma_f32 v46, v90, v47, -v51
	v_cmp_eq_u32_e32 vcc, v34, v45
	v_cvt_pk_bf16_f32 v46, v46, v46
	s_nop 0
	v_cndmask_b32_e32 v34, 0, v33, vcc
	v_sub_f32_e32 v34, v34, v55
	global_store_short v[58:59], v46, off offset:2176
	v_cvt_pk_bf16_f32 v34, v34, v34
	global_store_short v[60:61], v34, off offset:2176
	v_add_u32_e32 v34, 50, v32
	v_fma_f32 v46, v93, v48, -v52
	v_cmp_eq_u32_e32 vcc, v34, v45
	v_cvt_pk_bf16_f32 v46, v46, v46
	s_nop 0
	v_cndmask_b32_e32 v34, 0, v33, vcc
	v_sub_f32_e32 v34, v34, v56
	v_add_u32_e32 v32, 51, v32
	global_store_short_d16_hi v[58:59], v46, off offset:2304
	v_cmp_eq_u32_e32 vcc, v32, v45
	v_cvt_pk_bf16_f32 v34, v34, v34
	global_store_short v[60:61], v34, off offset:2304
	v_cndmask_b32_e32 v32, 0, v33, vcc
	v_fma_f32 v34, v91, v49, -v53
	v_sub_f32_e32 v32, v32, v57
	v_bfe_u32 v46, v34, 16, 1
	v_bfe_u32 v33, v32, 16, 1
	v_add3_u32 v34, v34, v46, s81
	v_add3_u32 v32, v32, v33, s81
	global_store_short_d16_hi v[58:59], v34, off offset:2432
	global_store_short_d16_hi v[60:61], v32, off offset:2432
	s_branch .LBB0_1682

; #define LAS __attribute__((address_space(3)))
; __device__ __forceinline__ unsigned f2bf(float f) { unsigned u = __float_as_uint(f); return (u + 0x7fffu + ((u >> 16) & 1u)) >> 16; }
; __device__ __forceinline__ float lo_bf(unsigned w) { return __uint_as_float(w << 16); }
; __device__ __forceinline__ float hi_bf(unsigned w) { return __uint_as_float(w & 0xffff0000u); }
; __device__ __forceinline__ u32x2 cvt4(f32x4 v) { return (u32x2){pk2(v[0], v[1]), pk2(v[2], v[3])}; }
; __device__ __forceinline__ void gla_seq_block(CArgs& a, int chain, LAS unsigned char* lds, int w, int lane) {
;     ...
;         for (int n = 0; n < 36; ++n) {
;             const LAS unsigned char* sl = lds + (n % 3) * SLOT; const int r0 = scan_row(b, dir, n * 64);
;             const bf16x8 Sb = frag2(cvt4(S[0]), cvt4(S[1]));
;             f32x4 o[4];
; #pragma unroll
;             for (int t = 0; t < 4; ++t) { const u32x2 ff = *(const LAS u32x2*)(sl + 5120 + v * 144 + (16 * t + 4 * kg) * 2);
;                 o[t] = (f32x4){lo_bf(ff.x), hi_bf(ff.x), lo_bf(ff.y), hi_bf(ff.y)};
;                 const LAS unsigned char* qr = sl + (16 * t + fr) * 80 + 4 * kg * 2;
;                 o[t] = __builtin_amdgcn_mfma_f32_16x16x32_bf16(frag2(*(const LAS u32x2*)qr, *(const LAS u32x2*)(qr + 32)), Sb, o[t], 0, 0, 0); }
; #pragma unroll
;             for (int kt = 0; kt < 2; ++kt) { const f32x4 d4 = *(const LAS f32x4*)(sl + 19456 + (16 * kt + 4 * kg) * 4); const u32x2 u2 = *(const LAS u32x2*)(sl + 14336 + v * 80 + (16 * kt + 4 * kg) * 2);
;                 S[kt] = d4 * S[kt] + (f32x4){lo_bf(u2.x), hi_bf(u2.x), lo_bf(u2.y), hi_bf(u2.y)}; }
;             { bf16* gp = GO + (ptrdiff_t)(r0 + step * 4 * kg) * 256 + h * 64 + v; const ptrdiff_t sd = (ptrdiff_t)step * 256;
; #pragma unroll
;               for (int t = 0; t < 4; ++t)
; #pragma unroll
;                   for (int e = 0; e < 4; ++e) gp[(16 * t + e) * sd] = (bf16)f2bf(o[t][e]); }
;             __syncthreads();
.LBB0_1801:
	s_mul_i32 s2, s51, 0xab
	s_bfe_u32 s2, s2, 0x70009
	v_cvt_pk_bf16_f32 v28, v16, v17
	s_mul_i32 s2, s2, 3
	s_sub_i32 s2, s51, s2
	s_and_b32 s2, s2, 0xff
	v_cvt_pk_bf16_f32 v29, v18, v19
	s_mulk_i32 s2, 0x4c80
	s_add_i32 s2, s2, 0
	v_cvt_pk_bf16_f32 v30, v12, v13
	v_add_u32_e32 v8, s2, v21
	v_add_u32_e32 v33, v8, v24
	ds_read2_b64 v[36:39], v33 offset1:4
	v_cvt_pk_bf16_f32 v31, v14, v15
	v_add_u32_e32 v2, v8, v20
	v_add_u32_e32 v32, 0x1000, v2
	ds_read2_b64 v[4:7], v32 offset0:128 offset1:132
	v_add_u32_e32 v34, s2, v22
	s_add_i32 s51, s51, 1
	s_sub_i32 s50, s50, 64
	s_add_i32 s9, s9, 64
	s_waitcnt lgkmcnt(0)
	v_lshlrev_b32_e32 v2, 16, v4
	v_and_b32_e32 v3, 0xffff0000, v4
	v_lshlrev_b32_e32 v4, 16, v5
	v_and_b32_e32 v5, 0xffff0000, v5
	s_cmp_lg_u32 s50, -1
	s_nop 0
	v_mfma_f32_16x16x32_bf16 v[2:5], v[36:39], v[28:31], v[2:5]
	v_lshlrev_b32_e32 v36, 16, v6
	v_and_b32_e32 v37, 0xffff0000, v6
	v_lshlrev_b32_e32 v38, 16, v7
	v_and_b32_e32 v39, 0xffff0000, v7
	ds_read2_b64 v[6:9], v33 offset0:160 offset1:164
	s_waitcnt lgkmcnt(0)
	v_mfma_f32_16x16x32_bf16 v[6:9], v[6:9], v[28:31], v[36:39]
	s_nop 2
	ds_read2_b64 v[36:39], v32 offset0:136 offset1:140
	v_add_u32_e32 v32, 0x800, v33
	ds_read2_b64 v[44:47], v32 offset0:64 offset1:68
	s_waitcnt lgkmcnt(1)
	v_lshlrev_b32_e32 v40, 16, v36
	v_and_b32_e32 v41, 0xffff0000, v36
	v_lshlrev_b32_e32 v42, 16, v37
	v_and_b32_e32 v43, 0xffff0000, v37
	v_lshlrev_b32_e32 v36, 16, v38
	v_and_b32_e32 v37, 0xffff0000, v38
	s_waitcnt lgkmcnt(0)
	v_mfma_f32_16x16x32_bf16 v[40:43], v[44:47], v[28:31], v[40:43]
	ds_read2_b64 v[44:47], v32 offset0:224 offset1:228
	v_lshlrev_b32_e32 v38, 16, v39
	v_and_b32_e32 v39, 0xffff0000, v39
	v_add_u32_e32 v32, s2, v25
	s_waitcnt lgkmcnt(0)
	v_mfma_f32_16x16x32_bf16 v[28:31], v[44:47], v[28:31], v[36:39]
	s_nop 2
	ds_read_b128 v[36:39], v32 offset:19456
	v_add_u32_e32 v32, v34, v21
	ds_read_b64 v[32:33], v32 offset:14336
	s_waitcnt lgkmcnt(0)
	v_lshlrev_b32_e32 v44, 16, v32
	v_and_b32_e32 v45, 0xffff0000, v32
	v_lshlrev_b32_e32 v32, 16, v33
	v_and_b32_e32 v33, 0xffff0000, v33
	v_pk_fma_f32 v[18:19], v[38:39], v[18:19], v[32:33]
	v_add_u32_e32 v32, s2, v26
	v_pk_fma_f32 v[16:17], v[36:37], v[16:17], v[44:45]
	ds_read_b128 v[36:39], v32 offset:19456
	v_add_u32_e32 v32, v34, v27
	ds_read_b64 v[32:33], v32 offset:14336
	v_cvt_pk_bf16_f32 v2, v2, v2
	s_waitcnt lgkmcnt(0)
	v_lshlrev_b32_e32 v44, 16, v32
	v_and_b32_e32 v45, 0xffff0000, v32
	v_lshlrev_b32_e32 v32, 16, v33
	v_and_b32_e32 v33, 0xffff0000, v33
	v_pk_fma_f32 v[14:15], v[38:39], v[14:15], v[32:33]
	v_add_u32_e32 v32, s52, v23
	v_ashrrev_i32_e32 v33, 31, v32
	v_lshlrev_b64 v[32:33], 9, v[32:33]
	v_lshl_add_u64 v[32:33], v[10:11], 0, v[32:33]
	global_store_short v[32:33], v2, off
	v_bfe_u32 v2, v3, 16, 1
	v_add3_u32 v34, v3, v2, s81
	v_lshl_add_u64 v[2:3], v[32:33], 0, s[28:29]
	global_store_short_d16_hi v[2:3], v34, off
	v_cvt_pk_bf16_f32 v4, v4, v4
	v_lshl_add_u64 v[2:3], v[2:3], 0, s[28:29]
	global_store_short_d16_hi v[2:3], v4, off
	v_cvt_pk_bf16_f32 v4, v5, v5
	v_lshl_add_u64 v[2:3], v[2:3], 0, s[28:29]
	global_store_short v[2:3], v4, off
	v_cvt_pk_bf16_f32 v4, v6, v6
	v_lshl_add_u64 v[2:3], v[2:3], 0, s[48:49]
	global_store_short v[2:3], v4, off
	v_cvt_pk_bf16_f32 v4, v7, v7
	v_lshl_add_u64 v[2:3], v[2:3], 0, s[28:29]
	global_store_short v[2:3], v4, off
	v_cvt_pk_bf16_f32 v4, v8, v8
	v_lshl_add_u64 v[2:3], v[2:3], 0, s[28:29]
	global_store_short v[2:3], v4, off
	v_cvt_pk_bf16_f32 v4, v9, v9
	v_lshl_add_u64 v[2:3], v[2:3], 0, s[28:29]
	global_store_short v[2:3], v4, off
	v_cvt_pk_bf16_f32 v4, v40, v40
	v_lshl_add_u64 v[2:3], v[2:3], 0, s[48:49]
	global_store_short v[2:3], v4, off
	v_cvt_pk_bf16_f32 v4, v41, v41
	v_lshl_add_u64 v[2:3], v[2:3], 0, s[28:29]
	global_store_short v[2:3], v4, off
	v_cvt_pk_bf16_f32 v4, v42, v42
	v_lshl_add_u64 v[2:3], v[2:3], 0, s[28:29]
	global_store_short v[2:3], v4, off
	v_cvt_pk_bf16_f32 v4, v43, v43
	v_lshl_add_u64 v[2:3], v[2:3], 0, s[28:29]
	global_store_short v[2:3], v4, off
	v_cvt_pk_bf16_f32 v4, v28, v28
	v_lshl_add_u64 v[2:3], v[2:3], 0, s[48:49]
	global_store_short v[2:3], v4, off
	v_cvt_pk_bf16_f32 v4, v29, v29
	v_lshl_add_u64 v[2:3], v[2:3], 0, s[28:29]
	global_store_short v[2:3], v4, off
	v_cvt_pk_bf16_f32 v4, v30, v30
	v_lshl_add_u64 v[2:3], v[2:3], 0, s[28:29]
	global_store_short v[2:3], v4, off
	v_bfe_u32 v4, v31, 16, 1
	v_pk_fma_f32 v[12:13], v[36:37], v[12:13], v[44:45]
	v_add3_u32 v4, v31, v4, s81
	v_lshl_add_u64 v[2:3], v[2:3], 0, s[28:29]
	global_store_short_d16_hi v[2:3], v4, off
	s_barrier
	s_cbranch_scc0 .LBB0_1806

; #define LAS __attribute__((address_space(3)))
; __device__ __forceinline__ unsigned f2bf(float f) { unsigned u = __float_as_uint(f); return (u + 0x7fffu + ((u >> 16) & 1u)) >> 16; }
; __device__ __forceinline__ float lo_bf(unsigned w) { return __uint_as_float(w << 16); }
; __device__ __forceinline__ float hi_bf(unsigned w) { return __uint_as_float(w & 0xffff0000u); }
; __device__ __forceinline__ u32x2 cvt4(f32x4 v) { return (u32x2){pk2(v[0], v[1]), pk2(v[2], v[3])}; }
; __device__ __forceinline__ void gdn_seq_block(CArgs& a, int chain, LAS unsigned char* lds, int w, int lane) {
;     ...
;         for (int n = 0; n < 36; ++n) {
;             const LAS unsigned char* sl = lds + (n % 3) * SLOT; const int r0 = scan_row(b, dir, n * 64);
;             bf16x8 Sb[2];
; #pragma unroll
;             for (int s = 0; s < 2; ++s) Sb[s] = frag2(cvt4(S[2 * s]), cvt4(S[2 * s + 1]));
;             f32x4 o[4];
; #pragma unroll
;             for (int t = 0; t < 4; ++t) {
;                 const u32x2 ff = *(const LAS u32x2*)(sl + 27648 + v * 144 + (16 * t + 4 * kg) * 2);
;                 o[t] = (f32x4){lo_bf(ff.x), hi_bf(ff.x), lo_bf(ff.y), hi_bf(ff.y)};
;                 const u32x2 bb2 = *(const LAS u32x2*)(sl + 18432 + v * 144 + (16 * t + 4 * kg) * 2);
;                 f32x4 sn = (f32x4){lo_bf(bb2.x), hi_bf(bb2.x), lo_bf(bb2.y), hi_bf(bb2.y)};
; #pragma unroll
;                 for (int s = 0; s < 2; ++s) { const LAS unsigned char* er = sl + 9216 + (16 * t + fr) * 144 + (32 * s + 4 * kg) * 2; const LAS unsigned char* mr = sl + (16 * t + fr) * 144 + (32 * s + 4 * kg) * 2;
;                     o[t] = __builtin_amdgcn_mfma_f32_16x16x32_bf16(frag2(*(const LAS u32x2*)er, *(const LAS u32x2*)(er + 32)), Sb[s], o[t], 0, 0, 0);
;                     sn = __builtin_amdgcn_mfma_f32_16x16x32_bf16(frag2(*(const LAS u32x2*)mr, *(const LAS u32x2*)(mr + 32)), Sb[s], sn, 0, 0, 0); }
;                 S[t] = sn; }
;             { bf16* dp = DO + (ptrdiff_t)(r0 + step * 4 * kg) * 256 + h * 64 + v; const ptrdiff_t sd = (ptrdiff_t)step * 256;
; #pragma unroll
;               for (int t = 0; t < 4; ++t)
; #pragma unroll
;                   for (int e = 0; e < 4; ++e) dp[(16 * t + e) * sd] = (bf16)f2bf(o[t][e]); }
;             __syncthreads();
.LBB0_1885:
	v_cvt_pk_bf16_f32 v2, v10, v11
	v_cvt_pk_bf16_f32 v3, v12, v13
	s_mul_i32 s2, s50, 0xab
	s_bfe_u32 s2, s2, 0x70009
	v_cvt_pk_bf16_f32 v4, v14, v15
	s_mul_i32 s2, s2, 3
	s_sub_i32 s2, s50, s2
	s_and_b32 s2, s2, 0xff
	v_cvt_pk_bf16_f32 v5, v16, v17
	s_mul_i32 s2, s2, 0x9000
	s_add_i32 s2, s2, 0
	v_cvt_pk_bf16_f32 v6, v22, v23
	v_add3_u32 v16, s2, v34, v38
	v_add_u32_e32 v41, 0x4800, v16
	ds_read2_b64 v[20:23], v41 offset1:4
	v_cvt_pk_bf16_f32 v7, v24, v25
	v_cvt_pk_bf16_f32 v8, v30, v31
	v_add3_u32 v54, s2, v40, v38
	v_cvt_pk_bf16_f32 v9, v32, v32
	v_add_u32_e32 v32, 0x6800, v16
	s_waitcnt lgkmcnt(0)
	v_lshlrev_b32_e32 v16, 16, v20
	v_and_b32_e32 v17, 0xffff0000, v20
	v_add_u32_e32 v20, 0x2000, v54
	ds_read2_b64 v[24:27], v20 offset0:128 offset1:132
	ds_read2_b64 v[12:15], v32 offset0:128 offset1:132
	v_lshrrev_b32_e32 v9, 16, v9
	v_cvt_pk_bf16_f32 v10, v33, v33
	v_and_or_b32 v9, v10, s80, v9
	s_waitcnt lgkmcnt(0)
	v_lshlrev_b32_e32 v10, 16, v12
	v_and_b32_e32 v11, 0xffff0000, v12
	v_lshlrev_b32_e32 v12, 16, v13
	v_and_b32_e32 v13, 0xffff0000, v13
	v_lshlrev_b32_e32 v18, 16, v21
	v_and_b32_e32 v19, 0xffff0000, v21
	v_mfma_f32_16x16x32_bf16 v[10:13], v[24:27], v[2:5], v[10:13]
	ds_read2_b64 v[24:27], v54 offset1:4
	v_add_u32_e32 v33, 0x2800, v54
	ds_read2_b64 v[28:31], v33 offset0:160 offset1:164
	s_waitcnt lgkmcnt(1)
	v_mfma_f32_16x16x32_bf16 v[24:27], v[24:27], v[2:5], v[16:19]
	s_nop 2
	ds_read2_b64 v[16:19], v20 offset0:136 offset1:140
	ds_read2_b64 v[42:45], v41 offset0:8 offset1:12
	v_add_u32_e32 v41, 0x3800, v54
	s_waitcnt lgkmcnt(1)
	v_mfma_f32_16x16x32_bf16 v[18:21], v[16:19], v[6:9], v[10:13]
	s_nop 2
	ds_read2_b64 v[10:13], v54 offset0:8 offset1:12
	v_lshlrev_b32_e32 v16, 16, v23
	v_and_b32_e32 v17, 0xffff0000, v23
	s_waitcnt lgkmcnt(0)
	v_mfma_f32_16x16x32_bf16 v[10:13], v[10:13], v[6:9], v[24:27]
	s_nop 2
	v_lshlrev_b32_e32 v24, 16, v14
	v_and_b32_e32 v25, 0xffff0000, v14
	v_lshlrev_b32_e32 v26, 16, v15
	v_and_b32_e32 v27, 0xffff0000, v15
	v_lshlrev_b32_e32 v14, 16, v22
	v_and_b32_e32 v15, 0xffff0000, v22
	v_mfma_f32_16x16x32_bf16 v[22:25], v[28:31], v[2:5], v[24:27]
	v_add_u32_e32 v30, 0x800, v54
	v_lshlrev_b32_e32 v46, 16, v42
	v_and_b32_e32 v47, 0xffff0000, v42
	ds_read2_b64 v[26:29], v30 offset0:32 offset1:36
	s_waitcnt lgkmcnt(0)
	v_mfma_f32_16x16x32_bf16 v[14:17], v[26:29], v[2:5], v[14:17]
	ds_read2_b64 v[26:29], v33 offset0:168 offset1:172
	v_lshlrev_b32_e32 v48, 16, v43
	v_and_b32_e32 v49, 0xffff0000, v43
	s_waitcnt lgkmcnt(0)
	v_mfma_f32_16x16x32_bf16 v[26:29], v[26:29], v[6:9], v[22:25]
	s_nop 2
	ds_read2_b64 v[22:25], v30 offset0:40 offset1:44
	ds_read2_b64 v[30:33], v32 offset0:136 offset1:140
	v_lshlrev_b32_e32 v42, 16, v44
	s_waitcnt lgkmcnt(1)
	v_mfma_f32_16x16x32_bf16 v[14:17], v[22:25], v[6:9], v[14:17]
	s_waitcnt lgkmcnt(0)
	v_lshlrev_b32_e32 v22, 16, v30
	v_and_b32_e32 v23, 0xffff0000, v30
	v_add_u32_e32 v30, 0x3000, v54
	ds_read2_b64 v[50:53], v30 offset0:192 offset1:196
	v_lshlrev_b32_e32 v24, 16, v31
	v_and_b32_e32 v25, 0xffff0000, v31
	v_add_u32_e32 v31, 0x1000, v54
	v_add_u32_e32 v54, 0x1800, v54
	s_waitcnt lgkmcnt(0)
	v_mfma_f32_16x16x32_bf16 v[22:25], v[50:53], v[2:5], v[22:25]
	ds_read2_b64 v[50:53], v31 offset0:64 offset1:68
	v_and_b32_e32 v43, 0xffff0000, v44
	v_lshlrev_b32_e32 v44, 16, v45
	s_waitcnt lgkmcnt(0)
	v_mfma_f32_16x16x32_bf16 v[46:49], v[50:53], v[2:5], v[46:49]
	ds_read2_b64 v[50:53], v30 offset0:200 offset1:204
	v_lshlrev_b32_e32 v30, 16, v32
	v_and_b32_e32 v45, 0xffff0000, v45
	s_waitcnt lgkmcnt(0)
	v_mfma_f32_16x16x32_bf16 v[50:53], v[50:53], v[6:9], v[22:25]
	s_nop 2
	ds_read2_b64 v[22:25], v31 offset0:72 offset1:76
	v_and_b32_e32 v31, 0xffff0000, v32
	v_lshlrev_b32_e32 v32, 16, v33
	s_waitcnt lgkmcnt(0)
	v_mfma_f32_16x16x32_bf16 v[22:25], v[22:25], v[6:9], v[46:49]
	s_nop 2
	ds_read2_b64 v[46:49], v41 offset0:224 offset1:228
	v_and_b32_e32 v33, 0xffff0000, v33
	s_add_i32 s50, s50, 1
	s_sub_i32 s36, s36, 64
	s_waitcnt lgkmcnt(0)
	v_mfma_f32_16x16x32_bf16 v[30:33], v[46:49], v[2:5], v[30:33]
	ds_read2_b64 v[46:49], v54 offset0:96 offset1:100
	s_add_i32 s0, s0, 64
	s_cmp_eq_u32 s36, -1
	s_waitcnt lgkmcnt(0)
	v_mfma_f32_16x16x32_bf16 v[2:5], v[46:49], v[2:5], v[42:45]
	s_nop 2
	ds_read2_b64 v[42:45], v41 offset0:232 offset1:236
	s_waitcnt lgkmcnt(0)
	v_mfma_f32_16x16x32_bf16 v[42:45], v[42:45], v[6:9], v[30:33]
	s_nop 2
	ds_read2_b64 v[30:33], v54 offset0:104 offset1:108
	s_waitcnt lgkmcnt(0)
	v_mfma_f32_16x16x32_bf16 v[30:33], v[30:33], v[6:9], v[2:5]
	s_nop 2
	v_add_u32_e32 v2, s51, v39
	v_ashrrev_i32_e32 v3, 31, v2
	v_lshlrev_b64 v[2:3], 9, v[2:3]
	v_lshl_add_u64 v[2:3], v[36:37], 0, v[2:3]
	v_cvt_pk_bf16_f32 v4, v18, v18
	global_store_short v[2:3], v4, off
	v_cvt_pk_bf16_f32 v4, v19, v19
	v_lshl_add_u64 v[2:3], v[2:3], 0, s[28:29]
	global_store_short v[2:3], v4, off
	v_cvt_pk_bf16_f32 v4, v20, v20
	v_lshl_add_u64 v[2:3], v[2:3], 0, s[28:29]
	global_store_short v[2:3], v4, off
	v_cvt_pk_bf16_f32 v4, v21, v21
	v_lshl_add_u64 v[2:3], v[2:3], 0, s[28:29]
	global_store_short v[2:3], v4, off
	v_cvt_pk_bf16_f32 v4, v26, v26
	v_lshl_add_u64 v[2:3], v[2:3], 0, s[48:49]
	global_store_short v[2:3], v4, off
	v_cvt_pk_bf16_f32 v4, v27, v27
	v_lshl_add_u64 v[2:3], v[2:3], 0, s[28:29]
	global_store_short v[2:3], v4, off
	v_cvt_pk_bf16_f32 v4, v28, v28
	v_lshl_add_u64 v[2:3], v[2:3], 0, s[28:29]
	global_store_short v[2:3], v4, off
	v_cvt_pk_bf16_f32 v4, v29, v29
	v_lshl_add_u64 v[2:3], v[2:3], 0, s[28:29]
	global_store_short v[2:3], v4, off
	v_cvt_pk_bf16_f32 v4, v50, v50
	v_lshl_add_u64 v[2:3], v[2:3], 0, s[48:49]
	global_store_short v[2:3], v4, off
	v_cvt_pk_bf16_f32 v4, v51, v51
	v_lshl_add_u64 v[2:3], v[2:3], 0, s[28:29]
	global_store_short v[2:3], v4, off
	v_cvt_pk_bf16_f32 v4, v52, v52
	v_lshl_add_u64 v[2:3], v[2:3], 0, s[28:29]
	global_store_short v[2:3], v4, off
	v_cvt_pk_bf16_f32 v4, v53, v53
	v_lshl_add_u64 v[2:3], v[2:3], 0, s[28:29]
	global_store_short v[2:3], v4, off
	v_cvt_pk_bf16_f32 v4, v42, v42
	v_lshl_add_u64 v[2:3], v[2:3], 0, s[48:49]
	global_store_short v[2:3], v4, off
	v_cvt_pk_bf16_f32 v4, v43, v43
	v_lshl_add_u64 v[2:3], v[2:3], 0, s[28:29]
	global_store_short v[2:3], v4, off
	v_cvt_pk_bf16_f32 v4, v44, v44
	v_lshl_add_u64 v[2:3], v[2:3], 0, s[28:29]
	global_store_short v[2:3], v4, off
	v_bfe_u32 v4, v45, 16, 1
	v_add3_u32 v4, v45, v4, s81
	v_lshl_add_u64 v[2:3], v[2:3], 0, s[28:29]
	global_store_short_d16_hi v[2:3], v4, off
	s_barrier
	s_cbranch_scc1 .LBB0_1890

; #define LAS __attribute__((address_space(3)))
; __device__ __forceinline__ unsigned f2bf(float f) { unsigned u = __float_as_uint(f); return (u + 0x7fffu + ((u >> 16) & 1u)) >> 16; }
; template <int L>
; __device__ __forceinline__ void hyena_unit(CArgs& a, int l, int c, LAS unsigned char* lds) {
;     ...
;     s = wave_sum(s);
;     if (lane == 0) red[w] = s;
;     __syncthreads();
;     float l1 = 0.f;
; #pragma unroll
;     for (int i = 0; i < 8; ++i) l1 += red[i];
;     const float inv = 1.f / l1;
; #pragma unroll
;     for (int q = 0; q < NI; ++q) {
;         const int idx = tid + 512 * q;
;         const bf16 gb = (bf16)f2bf(gv[q] * inv);
;         if (idx < 2 * L + 16) {
; #pragma unroll
;             for (int r = 0; r < 8; ++r) if (idx - r >= 0) *(LAS bf16*)(lds + r * CST + (idx - r) * 2) = gb;
;         }
.LBB0_2065:
	s_or_b64 exec, exec, s[14:15]
	s_waitcnt lgkmcnt(0)
	s_barrier
	ds_read_b128 v[42:45], v35 offset:8704
	ds_read_b128 v[46:49], v35 offset:8720
	s_waitcnt lgkmcnt(1)
	v_add_f32_e32 v42, 0, v42
	v_add_f32_e32 v42, v42, v43
	v_add_f32_e32 v42, v42, v44
	v_add_f32_e32 v42, v42, v45
	s_waitcnt lgkmcnt(0)
	v_add_f32_e32 v42, v42, v46
	v_add_f32_e32 v42, v42, v47
	v_add_f32_e32 v42, v42, v48
	v_add_f32_e32 v42, v42, v49
	v_div_scale_f32 v43, s[14:15], v42, v42, 1.0
	v_rcp_f32_e32 v44, v43
	v_div_scale_f32 v45, vcc, 1.0, v42, 1.0
	v_fma_f32 v46, -v43, v44, 1.0
	v_fmac_f32_e32 v44, v46, v44
	v_mul_f32_e32 v46, v45, v44
	v_fma_f32 v47, -v43, v46, v45
	v_fmac_f32_e32 v46, v47, v44
	v_fma_f32 v43, -v43, v46, v45
	v_div_fmas_f32 v43, v43, v44, v46
	v_div_fixup_f32 v42, v43, v42, 1.0
	v_cmp_gt_i32_e32 vcc, s23, v38
	s_and_saveexec_b64 s[14:15], vcc
	s_cbranch_execz .LBB0_2083
	v_mul_f32_e32 v34, v34, v42
	v_cvt_pk_bf16_f32 v34, v34, v34
	v_lshrrev_b32_e32 v34, 16, v34
	v_cmp_lt_i32_e32 vcc, -1, v38
	s_and_saveexec_b64 s[26:27], vcc
	s_cbranch_execz .LBB0_2075
	v_lshl_add_u32 v43, v38, 1, 0
	ds_write_b16 v43, v34
	s_or_b64 exec, exec, s[26:27]
	v_cmp_lt_i32_e32 vcc, 0, v38
	s_and_saveexec_b64 s[26:27], vcc
	s_cbranch_execnz .LBB0_2076

; #define LAS __attribute__((address_space(3)))
; __device__ __forceinline__ unsigned f2bf(float f) { unsigned u = __float_as_uint(f); return (u + 0x7fffu + ((u >> 16) & 1u)) >> 16; }
; template <int L>
; __device__ __forceinline__ void hyena_unit(CArgs& a, int l, int c, LAS unsigned char* lds) {
;     ...
; #pragma unroll
;     for (int q = 0; q < NI; ++q) {
;         const int idx = tid + 512 * q;
;         const bf16 gb = (bf16)f2bf(gv[q] * inv);
;         if (idx < 2 * L + 16) {
; #pragma unroll
;             for (int r = 0; r < 8; ++r) if (idx - r >= 0) *(LAS bf16*)(lds + r * CST + (idx - r) * 2) = gb;
;         }
.LBB0_2083:
	s_or_b64 exec, exec, s[14:15]
	v_bfe_u32 v34, v38, 4, 2
	v_lshlrev_b32_e32 v34, 3, v34
	v_cmp_gt_i32_e32 vcc, 16, v38
	s_and_saveexec_b64 s[14:15], vcc
	s_cbranch_execz .LBB0_2094
	v_mul_f32_e32 v41, v41, v42
	v_cvt_pk_bf16_f32 v41, v41, v41
	v_lshrrev_b32_e32 v41, 16, v41
	v_cmp_lt_i32_e32 vcc, s35, v38
	s_and_saveexec_b64 s[26:27], vcc
	v_lshl_add_u32 v40, v40, 1, 0
	ds_write_b16 v40, v41
	s_or_b64 exec, exec, s[26:27]
	v_cmp_lt_i32_e32 vcc, s30, v38
	v_lshl_add_u32 v40, v38, 1, 0
	s_and_saveexec_b64 s[26:27], vcc
	s_cbranch_execz .LBB0_2106
	ds_write_b16 v40, v41 offset:2110
	s_or_b64 exec, exec, s[26:27]
	v_cmp_lt_i32_e32 vcc, s36, v38
	s_and_saveexec_b64 s[26:27], vcc
	s_cbranch_execnz .LBB0_2107

; #define LAS __attribute__((address_space(3)))
; __device__ __forceinline__ unsigned pk2(float lo, float hi) { return f2bf(lo) | (f2bf(hi) << 16); }
; template <int L>
; __device__ __forceinline__ void hyena_unit(CArgs& a, int l, int c, LAS unsigned char* lds) {
;     ...
;     const int rr = (8 - (fr & 7)) & 7;
;     const LAS unsigned char* ap = lds + rr * CST + (((8 * kg - fr + L) >> 3) - 2 * w * NTW) * 16;
;     if constexpr (L == SEQ) {
;         static_assert(NTW == 16, "hyena_unit");
;         bf16x8 zn[8], A[16];
; #pragma unroll
;         for (int j = 2; j < 16; ++j) A[j] = *(const LAS bf16x8*)(ap - 32 * j);
; #pragma unroll 1
;         for (int ib = 0; ib < 8; ++ib) {
;             const bf16* zq = zp + 256 * (ib < 7 ? ib + 1 : 7);
; #pragma unroll
;             for (int ii = 0; ii < 8; ++ii) zn[ii] = *(const bf16x8*)(zq + 32 * ii);
; #pragma unroll
;             for (int ii = 0; ii < 8; ++ii) {
;                 A[(16 - 2 * ii) & 15] = *(const LAS bf16x8*)(ap + 64 * ii);
;                 A[(17 - 2 * ii) & 15] = *(const LAS bf16x8*)(ap + 64 * ii - 32);
; #pragma unroll
;                 for (int jj = 0; jj < 16; ++jj) { const int j = (jj + 2) & 15; acc[j] = __builtin_amdgcn_mfma_f32_16x16x32_bf16(A[(j + 16 - 2 * ii) & 15], zc[ii], acc[j], 0, 0, 0); }
;             }
;             ap += 512;
; #pragma unroll
;             for (int ii = 0; ii < 8; ++ii) zc[ii] = zn[ii];
;         }
;     } else {
;         static_assert(L == 256, "hyena_unit");
; #pragma unroll
;         for (int i = 0; i < 8; ++i)
; #pragma unroll
;             for (int j = 0; j < NTW; ++j) acc[j] = __builtin_amdgcn_mfma_f32_16x16x32_bf16(*(const LAS bf16x8*)(ap + (4 * i - 2 * j) * 16), zc[i], acc[j], 0, 0, 0);
;     }
; #pragma unroll
;     for (int j = 0; j < NTW; ++j) *(u32x2*)(YT + 16 * (w * NTW + j) + 4 * kg) = (u32x2){pk2(acc[j][0], acc[j][1]), pk2(acc[j][2], acc[j][3])};
.LBB0_2094:
	s_or_b64 exec, exec, s[14:15]
	v_sub_u32_e32 v39, v34, v39
	v_sub_u32_e32 v40, 0, v38
	v_lshlrev_b32_e32 v39, 1, v39
	v_and_b32_e32 v40, 7, v40
	v_and_b32_e32 v38, 0xffffffc0, v38
	v_and_b32_e32 v39, -16, v39
	v_mul_u32_u24_e32 v40, 0x440, v40
	v_sub_u32_e32 v38, v39, v38
	v_add3_u32 v46, 0, v40, v38
	s_waitcnt lgkmcnt(0)
	s_barrier
	ds_read_b128 v[38:41], v46 offset:480
	ds_read_b128 v[42:45], v46 offset:512
	s_waitcnt vmcnt(7) lgkmcnt(0)
	v_mfma_f32_16x16x32_bf16 v[42:45], v[42:45], v[30:33], 0
	v_mfma_f32_16x16x32_bf16 v[30:33], v[38:41], v[30:33], 0
	ds_read_b128 v[38:41], v46 offset:576
	s_waitcnt vmcnt(6) lgkmcnt(0)
	v_mfma_f32_16x16x32_bf16 v[38:41], v[38:41], v[26:29], v[42:45]
	s_nop 3
	ds_read_b128 v[42:45], v46 offset:544
	s_waitcnt lgkmcnt(0)
	v_mfma_f32_16x16x32_bf16 v[26:29], v[42:45], v[26:29], v[30:33]
	s_nop 2
	ds_read_b128 v[30:33], v46 offset:640
	s_waitcnt vmcnt(5) lgkmcnt(0)
	v_mfma_f32_16x16x32_bf16 v[30:33], v[30:33], v[22:25], v[38:41]
	s_nop 2
	ds_read_b128 v[38:41], v46 offset:608
	s_waitcnt lgkmcnt(0)
	v_mfma_f32_16x16x32_bf16 v[22:25], v[38:41], v[22:25], v[26:29]
	s_nop 2
	ds_read_b128 v[26:29], v46 offset:704
	s_waitcnt vmcnt(4) lgkmcnt(0)
	v_mfma_f32_16x16x32_bf16 v[26:29], v[26:29], v[18:21], v[30:33]
	s_nop 2
	ds_read_b128 v[30:33], v46 offset:672
	s_waitcnt lgkmcnt(0)
	v_mfma_f32_16x16x32_bf16 v[18:21], v[30:33], v[18:21], v[22:25]
	s_nop 2
	ds_read_b128 v[22:25], v46 offset:768
	s_waitcnt vmcnt(3) lgkmcnt(0)
	v_mfma_f32_16x16x32_bf16 v[22:25], v[22:25], v[14:17], v[26:29]
	s_nop 2
	ds_read_b128 v[26:29], v46 offset:736
	s_waitcnt lgkmcnt(0)
	v_mfma_f32_16x16x32_bf16 v[14:17], v[26:29], v[14:17], v[18:21]
	s_nop 2
	ds_read_b128 v[18:21], v46 offset:832
	s_waitcnt vmcnt(2) lgkmcnt(0)
	v_mfma_f32_16x16x32_bf16 v[18:21], v[18:21], v[10:13], v[22:25]
	s_nop 2
	ds_read_b128 v[22:25], v46 offset:800
	s_waitcnt lgkmcnt(0)
	v_mfma_f32_16x16x32_bf16 v[10:13], v[22:25], v[10:13], v[14:17]
	s_nop 2
	ds_read_b128 v[14:17], v46 offset:896
	s_waitcnt vmcnt(1) lgkmcnt(0)
	v_mfma_f32_16x16x32_bf16 v[14:17], v[14:17], v[6:9], v[18:21]
	s_nop 2
	ds_read_b128 v[18:21], v46 offset:864
	s_waitcnt lgkmcnt(0)
	v_mfma_f32_16x16x32_bf16 v[6:9], v[18:21], v[6:9], v[10:13]
	s_nop 2
	ds_read_b128 v[10:13], v46 offset:960
	s_waitcnt vmcnt(0) lgkmcnt(0)
	v_mfma_f32_16x16x32_bf16 v[10:13], v[10:13], v[2:5], v[14:17]
	s_nop 2
	ds_read_b128 v[14:17], v46 offset:928
	s_waitcnt lgkmcnt(0)
	v_mfma_f32_16x16x32_bf16 v[2:5], v[14:17], v[2:5], v[6:9]
	s_nop 2
	v_lshlrev_b32_e32 v8, 5, v1
	v_cvt_pk_bf16_f32 v10, v10, v11
	v_cvt_pk_bf16_f32 v11, v12, v13
	s_nop 1
	v_cvt_pk_bf16_f32 v2, v2, v3
	v_lshl_add_u64 v[6:7], v[36:37], 1, s[6:7]
	v_cvt_pk_bf16_f32 v1, v4, v4
	v_lshl_add_u64 v[6:7], v[6:7], 0, v[34:35]
	v_ashrrev_i32_e32 v9, 31, v8
	v_lshrrev_b32_e32 v1, 16, v1
	v_cvt_pk_bf16_f32 v3, v5, v5
	v_lshl_add_u64 v[6:7], v[8:9], 1, v[6:7]
	v_and_or_b32 v3, v3, s80, v1
	global_store_dwordx2 v[6:7], v[10:11], off
	global_store_dwordx2 v[6:7], v[2:3], off offset:32
	s_barrier
	s_branch .LBB0_2061

; #define LAS __attribute__((address_space(3)))
; __device__ __forceinline__ unsigned f2bf(float f) { unsigned u = __float_as_uint(f); return (u + 0x7fffu + ((u >> 16) & 1u)) >> 16; }
; template <int L>
; __device__ __forceinline__ void hyena_unit(CArgs& a, int l, int c, LAS unsigned char* lds) {
;     ...
;     s = wave_sum(s);
;     if (lane == 0) red[w] = s;
;     __syncthreads();
;     float l1 = 0.f;
; #pragma unroll
;     for (int i = 0; i < 8; ++i) l1 += red[i];
;     const float inv = 1.f / l1;
; #pragma unroll
;     for (int q = 0; q < NI; ++q) {
;         const int idx = tid + 512 * q;
;         const bf16 gb = (bf16)f2bf(gv[q] * inv);
;         if (idx < 2 * L + 16) {
; #pragma unroll
;             for (int r = 0; r < 8; ++r) if (idx - r >= 0) *(LAS bf16*)(lds + r * CST + (idx - r) * 2) = gb;
;         }
.LBB0_2097:
	s_or_b64 exec, exec, s[14:15]
	s_add_i32 s14, 0, 0x10200
	v_mov_b32_e32 v41, s14
	s_waitcnt lgkmcnt(0)
	s_barrier
	ds_read_b128 v[56:59], v41
	v_mov_b32_e32 v55, s50
	s_waitcnt lgkmcnt(0)
	v_add_f32_e32 v41, 0, v56
	v_add_f32_e32 v41, v41, v57
	v_add_f32_e32 v41, v41, v58
	v_add_f32_e32 v41, v41, v59
	ds_read_b128 v[56:59], v55
	s_waitcnt lgkmcnt(0)
	v_add_f32_e32 v41, v41, v56
	v_add_f32_e32 v41, v41, v57
	v_add_f32_e32 v41, v41, v58
	v_add_f32_e32 v41, v41, v59
	v_div_scale_f32 v55, s[14:15], v41, v41, 1.0
	v_rcp_f32_e32 v56, v55
	s_nop 0
	v_fma_f32 v57, -v55, v56, 1.0
	v_fmac_f32_e32 v56, v57, v56
	v_div_scale_f32 v57, vcc, 1.0, v41, 1.0
	v_mul_f32_e32 v58, v57, v56
	v_fma_f32 v59, -v55, v58, v57
	v_fmac_f32_e32 v58, v59, v56
	v_fma_f32 v55, -v55, v58, v57
	v_div_fmas_f32 v55, v55, v56, v58
	v_div_fixup_f32 v41, v55, v41, 1.0
	v_cmp_gt_i32_e32 vcc, s51, v37
	s_and_saveexec_b64 s[14:15], vcc
	s_cbranch_execz .LBB0_2120
	v_mul_f32_e32 v34, v34, v41
	v_cvt_pk_bf16_f32 v34, v34, v34
	v_lshrrev_b32_e32 v34, 16, v34
	v_cmp_lt_i32_e32 vcc, -1, v37
	s_and_saveexec_b64 s[26:27], vcc
	s_cbranch_execz .LBB0_2112
	v_lshl_add_u32 v55, v37, 1, 0
	ds_write_b16 v55, v34
	s_or_b64 exec, exec, s[26:27]
	v_cmp_lt_i32_e32 vcc, 0, v37
	s_and_saveexec_b64 s[26:27], vcc
	s_cbranch_execnz .LBB0_2113

; #define LAS __attribute__((address_space(3)))
; __device__ __forceinline__ unsigned f2bf(float f) { unsigned u = __float_as_uint(f); return (u + 0x7fffu + ((u >> 16) & 1u)) >> 16; }
; template <int L>
; __device__ __forceinline__ void hyena_unit(CArgs& a, int l, int c, LAS unsigned char* lds) {
;     ...
; #pragma unroll
;     for (int q = 0; q < NI; ++q) {
;         const int idx = tid + 512 * q;
;         const bf16 gb = (bf16)f2bf(gv[q] * inv);
;         if (idx < 2 * L + 16) {
; #pragma unroll
;             for (int r = 0; r < 8; ++r) if (idx - r >= 0) *(LAS bf16*)(lds + r * CST + (idx - r) * 2) = gb;
;         }
.LBB0_2120:
	s_or_b64 exec, exec, s[14:15]
	v_bfe_u32 v34, v37, 4, 2
	v_lshlrev_b32_e32 v34, 3, v34
	v_cmp_gt_i32_e32 vcc, s52, v37
	s_and_saveexec_b64 s[14:15], vcc
	s_cbranch_execz .LBB0_2137
	v_mul_f32_e32 v54, v54, v41
	v_cvt_pk_bf16_f32 v54, v54, v54
	v_lshrrev_b32_e32 v54, 16, v54
	v_cmp_lt_i32_e32 vcc, s35, v37
	s_and_saveexec_b64 s[26:27], vcc
	s_cbranch_execz .LBB0_2129
	v_lshl_add_u32 v51, v51, 1, 0
	ds_write_b16 v51, v54
	s_or_b64 exec, exec, s[26:27]
	v_cmp_lt_i32_e32 vcc, s30, v37
	s_and_saveexec_b64 s[26:27], vcc
	s_cbranch_execnz .LBB0_2130

; #define LAS __attribute__((address_space(3)))
; __device__ __forceinline__ unsigned f2bf(float f) { unsigned u = __float_as_uint(f); return (u + 0x7fffu + ((u >> 16) & 1u)) >> 16; }
; template <int L>
; __device__ __forceinline__ void hyena_unit(CArgs& a, int l, int c, LAS unsigned char* lds) {
;     ...
; #pragma unroll
;     for (int q = 0; q < NI; ++q) {
;         const int idx = tid + 512 * q;
;         const bf16 gb = (bf16)f2bf(gv[q] * inv);
;         if (idx < 2 * L + 16) {
; #pragma unroll
;             for (int r = 0; r < 8; ++r) if (idx - r >= 0) *(LAS bf16*)(lds + r * CST + (idx - r) * 2) = gb;
;         }
.LBB0_2137:
	s_or_b64 exec, exec, s[14:15]
	v_cmp_gt_i32_e32 vcc, s53, v37
	s_and_saveexec_b64 s[14:15], vcc
	s_cbranch_execz .LBB0_2154
	v_mul_f32_e32 v51, v53, v41
	v_cvt_pk_bf16_f32 v51, v51, v51
	v_lshrrev_b32_e32 v51, 16, v51
	v_cmp_lt_i32_e32 vcc, s54, v37
	s_and_saveexec_b64 s[26:27], vcc
	s_cbranch_execz .LBB0_2146
	v_lshl_add_u32 v50, v50, 1, 0
	ds_write_b16 v50, v51
	s_or_b64 exec, exec, s[26:27]
	v_cmp_lt_i32_e32 vcc, s21, v37
	s_and_saveexec_b64 s[26:27], vcc
	s_cbranch_execnz .LBB0_2147

; #define LAS __attribute__((address_space(3)))
; __device__ __forceinline__ unsigned f2bf(float f) { unsigned u = __float_as_uint(f); return (u + 0x7fffu + ((u >> 16) & 1u)) >> 16; }
; template <int L>
; __device__ __forceinline__ void hyena_unit(CArgs& a, int l, int c, LAS unsigned char* lds) {
;     ...
; #pragma unroll
;     for (int q = 0; q < NI; ++q) {
;         const int idx = tid + 512 * q;
;         const bf16 gb = (bf16)f2bf(gv[q] * inv);
;         if (idx < 2 * L + 16) {
; #pragma unroll
;             for (int r = 0; r < 8; ++r) if (idx - r >= 0) *(LAS bf16*)(lds + r * CST + (idx - r) * 2) = gb;
;         }
.LBB0_2154:
	s_or_b64 exec, exec, s[14:15]
	v_cmp_gt_i32_e32 vcc, s60, v37
	s_and_saveexec_b64 s[14:15], vcc
	s_cbranch_execz .LBB0_2171
	v_mul_f32_e32 v50, v52, v41
	v_cvt_pk_bf16_f32 v50, v50, v50
	v_lshrrev_b32_e32 v50, 16, v50
	v_cmp_lt_i32_e32 vcc, s61, v37
	s_and_saveexec_b64 s[26:27], vcc
	s_cbranch_execz .LBB0_2163
	v_lshl_add_u32 v48, v48, 1, 0
	ds_write_b16 v48, v50
	s_or_b64 exec, exec, s[26:27]
	v_cmp_lt_i32_e32 vcc, s62, v37
	s_and_saveexec_b64 s[26:27], vcc
	s_cbranch_execnz .LBB0_2164

; #define LAS __attribute__((address_space(3)))
; __device__ __forceinline__ unsigned f2bf(float f) { unsigned u = __float_as_uint(f); return (u + 0x7fffu + ((u >> 16) & 1u)) >> 16; }
; template <int L>
; __device__ __forceinline__ void hyena_unit(CArgs& a, int l, int c, LAS unsigned char* lds) {
;     ...
; #pragma unroll
;     for (int q = 0; q < NI; ++q) {
;         const int idx = tid + 512 * q;
;         const bf16 gb = (bf16)f2bf(gv[q] * inv);
;         if (idx < 2 * L + 16) {
; #pragma unroll
;             for (int r = 0; r < 8; ++r) if (idx - r >= 0) *(LAS bf16*)(lds + r * CST + (idx - r) * 2) = gb;
;         }
.LBB0_2171:
	s_or_b64 exec, exec, s[14:15]
	v_cmp_gt_i32_e32 vcc, s72, v37
	s_and_saveexec_b64 s[14:15], vcc
	s_cbranch_execz .LBB0_2182
	v_mul_f32_e32 v48, v49, v41
	v_cvt_pk_bf16_f32 v48, v48, v48
	v_lshrrev_b32_e32 v48, 16, v48
	v_cmp_lt_i32_e32 vcc, s74, v37
	s_and_saveexec_b64 s[26:27], vcc
	s_cbranch_execz .LBB0_2191
	v_lshl_add_u32 v46, v46, 1, 0
	ds_write_b16 v46, v48
	s_or_b64 exec, exec, s[26:27]
	v_cmp_lt_i32_e32 vcc, s29, v37
	s_and_saveexec_b64 s[26:27], vcc
	s_cbranch_execnz .LBB0_2192

; #define LAS __attribute__((address_space(3)))
; __device__ __forceinline__ unsigned f2bf(float f) { unsigned u = __float_as_uint(f); return (u + 0x7fffu + ((u >> 16) & 1u)) >> 16; }
; template <int L>
; __device__ __forceinline__ void hyena_unit(CArgs& a, int l, int c, LAS unsigned char* lds) {
;     ...
; #pragma unroll
;     for (int q = 0; q < NI; ++q) {
;         const int idx = tid + 512 * q;
;         const bf16 gb = (bf16)f2bf(gv[q] * inv);
;         if (idx < 2 * L + 16) {
; #pragma unroll
;             for (int r = 0; r < 8; ++r) if (idx - r >= 0) *(LAS bf16*)(lds + r * CST + (idx - r) * 2) = gb;
;         }
.LBB0_2182:
	s_or_b64 exec, exec, s[14:15]
	v_cmp_gt_i32_e32 vcc, s84, v37
	s_and_saveexec_b64 s[14:15], vcc
	s_cbranch_execz .LBB0_2205
	v_mul_f32_e32 v46, v47, v41
	v_cvt_pk_bf16_f32 v46, v46, v46
	v_lshrrev_b32_e32 v46, 16, v46
	v_cmp_lt_i32_e32 vcc, s85, v37
	s_and_saveexec_b64 s[26:27], vcc
	s_cbranch_execz .LBB0_2197
	v_lshl_add_u32 v44, v44, 1, 0
	ds_write_b16 v44, v46
	s_or_b64 exec, exec, s[26:27]
	v_cmp_lt_i32_e32 vcc, s86, v37
	s_and_saveexec_b64 s[26:27], vcc
	s_cbranch_execnz .LBB0_2198

; #define LAS __attribute__((address_space(3)))
; __device__ __forceinline__ unsigned f2bf(float f) { unsigned u = __float_as_uint(f); return (u + 0x7fffu + ((u >> 16) & 1u)) >> 16; }
; template <int L>
; __device__ __forceinline__ void hyena_unit(CArgs& a, int l, int c, LAS unsigned char* lds) {
;     ...
; #pragma unroll
;     for (int q = 0; q < NI; ++q) {
;         const int idx = tid + 512 * q;
;         const bf16 gb = (bf16)f2bf(gv[q] * inv);
;         if (idx < 2 * L + 16) {
; #pragma unroll
;             for (int r = 0; r < 8; ++r) if (idx - r >= 0) *(LAS bf16*)(lds + r * CST + (idx - r) * 2) = gb;
;         }
.LBB0_2205:
	s_or_b64 exec, exec, s[14:15]
	v_cmp_gt_i32_e32 vcc, s93, v37
	s_and_saveexec_b64 s[14:15], vcc
	s_cbranch_execz .LBB0_2222
	v_mul_f32_e32 v44, v45, v41
	v_cvt_pk_bf16_f32 v44, v44, v44
	v_lshrrev_b32_e32 v44, 16, v44
	v_cmp_lt_i32_e32 vcc, s94, v37
	s_and_saveexec_b64 s[26:27], vcc
	s_cbranch_execz .LBB0_2210
	v_lshl_add_u32 v42, v42, 1, 0
	ds_write_b16 v42, v44
	s_or_b64 exec, exec, s[26:27]
	v_cmp_lt_i32_e32 vcc, s95, v37
	s_and_saveexec_b64 s[26:27], vcc
	s_cbranch_execnz .LBB0_2211

; #define LAS __attribute__((address_space(3)))
; __device__ __forceinline__ unsigned f2bf(float f) { unsigned u = __float_as_uint(f); return (u + 0x7fffu + ((u >> 16) & 1u)) >> 16; }
; template <int L>
; __device__ __forceinline__ void hyena_unit(CArgs& a, int l, int c, LAS unsigned char* lds) {
;     ...
; #pragma unroll
;     for (int q = 0; q < NI; ++q) {
;         const int idx = tid + 512 * q;
;         const bf16 gb = (bf16)f2bf(gv[q] * inv);
;         if (idx < 2 * L + 16) {
; #pragma unroll
;             for (int r = 0; r < 8; ++r) if (idx - r >= 0) *(LAS bf16*)(lds + r * CST + (idx - r) * 2) = gb;
;         }
.LBB0_2222:
	s_or_b64 exec, exec, s[14:15]
	v_cmp_gt_i32_e32 vcc, s23, v37
	s_and_saveexec_b64 s[14:15], vcc
	s_cbranch_execz .LBB0_2239
	v_mul_f32_e32 v42, v43, v41
	v_cvt_pk_bf16_f32 v42, v42, v42
	s_movk_i32 s16, 0xf1ff
	v_lshrrev_b32_e32 v42, 16, v42
	v_cmp_lt_i32_e32 vcc, s16, v37
	s_and_saveexec_b64 s[26:27], vcc
	v_lshl_add_u32 v40, v40, 1, 0
	ds_write_b16 v40, v42
	s_or_b64 exec, exec, s[26:27]
	s_movk_i32 s16, 0xf200
	v_cmp_lt_i32_e32 vcc, s16, v37
	s_and_saveexec_b64 s[26:27], vcc
	v_lshl_add_u32 v40, v37, 1, 0
	ds_write_b16 v40, v42 offset:15422
	s_or_b64 exec, exec, s[26:27]
	s_movk_i32 s16, 0xf201
	v_cmp_lt_i32_e32 vcc, s16, v37
	s_and_saveexec_b64 s[26:27], vcc
	v_lshl_add_u32 v40, v37, 1, 0
	ds_write_b16 v40, v42 offset:23676
	s_or_b64 exec, exec, s[26:27]
	s_movk_i32 s16, 0xf202
	v_cmp_lt_i32_e32 vcc, s16, v37
	s_and_saveexec_b64 s[26:27], vcc
	v_lshl_add_u32 v40, v37, 1, 0
	ds_write_b16 v40, v42 offset:31930
	s_or_b64 exec, exec, s[26:27]
	s_movk_i32 s16, 0xf203
	v_cmp_lt_i32_e32 vcc, s16, v37
	s_and_saveexec_b64 s[26:27], vcc
	v_lshl_add_u32 v40, v37, 1, 0
	ds_write_b16 v40, v42 offset:40184
	s_or_b64 exec, exec, s[26:27]
	s_movk_i32 s16, 0xf204
	v_cmp_lt_i32_e32 vcc, s16, v37
	s_and_saveexec_b64 s[26:27], vcc
	v_lshl_add_u32 v40, v37, 1, 0
	ds_write_b16 v40, v42 offset:48438
	s_or_b64 exec, exec, s[26:27]
	s_movk_i32 s16, 0xf205
	v_cmp_lt_i32_e32 vcc, s16, v37
	s_and_saveexec_b64 s[26:27], vcc
	v_lshl_add_u32 v40, v37, 1, 0
	ds_write_b16 v40, v42 offset:56692
	s_or_b64 exec, exec, s[26:27]
	s_movk_i32 s16, 0xf206
	v_cmp_lt_i32_e32 vcc, s16, v37
	s_and_b64 exec, exec, vcc
	v_lshl_add_u32 v40, v37, 1, 0
	ds_write_b16 v40, v42 offset:64946
.LBB0_2239:
	s_or_b64 exec, exec, s[14:15]
	v_cmp_gt_i32_e32 vcc, 16, v37
	s_and_saveexec_b64 s[14:15], vcc
	s_cbranch_execz .LBB0_2256
	v_mul_f32_e32 v39, v39, v41
	v_cvt_pk_bf16_f32 v39, v39, v39
	s_movk_i32 s16, 0xefff
	v_lshrrev_b32_e32 v39, 16, v39
	v_cmp_lt_i32_e32 vcc, s16, v37
	s_and_saveexec_b64 s[26:27], vcc
	v_lshl_add_u32 v38, v38, 1, 0
	ds_write_b16 v38, v39
	s_or_b64 exec, exec, s[26:27]
	v_cmp_lt_i32_e32 vcc, s31, v37
	v_lshl_add_u32 v38, v37, 1, 0
	s_and_saveexec_b64 s[26:27], vcc
	ds_write_b16 v38, v39 offset:16446
	s_or_b64 exec, exec, s[26:27]
	s_movk_i32 s16, 0xf001
	v_cmp_lt_i32_e32 vcc, s16, v37
	s_and_saveexec_b64 s[26:27], vcc
	ds_write_b16 v38, v39 offset:24700
	s_or_b64 exec, exec, s[26:27]
	s_movk_i32 s16, 0xf002
	v_cmp_lt_i32_e32 vcc, s16, v37
	s_and_saveexec_b64 s[26:27], vcc
	ds_write_b16 v38, v39 offset:32954
	s_or_b64 exec, exec, s[26:27]
	s_movk_i32 s16, 0xf003
	v_cmp_lt_i32_e32 vcc, s16, v37
	s_and_saveexec_b64 s[26:27], vcc
	ds_write_b16 v38, v39 offset:41208
	s_or_b64 exec, exec, s[26:27]
	s_movk_i32 s16, 0xf004
	v_cmp_lt_i32_e32 vcc, s16, v37
	s_and_saveexec_b64 s[26:27], vcc
	ds_write_b16 v38, v39 offset:49462
	s_or_b64 exec, exec, s[26:27]
	s_movk_i32 s16, 0xf005
	v_cmp_lt_i32_e32 vcc, s16, v37
	s_and_saveexec_b64 s[26:27], vcc
	ds_write_b16 v38, v39 offset:57716
	s_or_b64 exec, exec, s[26:27]
	s_movk_i32 s16, 0xf006
	v_cmp_lt_i32_e32 vcc, s16, v37
	s_and_b64 exec, exec, vcc
	v_add_u32_e32 v38, 0x101b2, v38
	ds_write_b16 v38, v39

; #define LAS __attribute__((address_space(3)))
; template <int L>
; __device__ __forceinline__ void hyena_unit(CArgs& a, int l, int c, LAS unsigned char* lds) {
;     ...
; #pragma unroll
;         for (int j = 2; j < 16; ++j) A[j] = *(const LAS bf16x8*)(ap - 32 * j);
; #pragma unroll 1
;         for (int ib = 0; ib < 8; ++ib) {
;             const bf16* zq = zp + 256 * (ib < 7 ? ib + 1 : 7);
; #pragma unroll
;             for (int ii = 0; ii < 8; ++ii) zn[ii] = *(const bf16x8*)(zq + 32 * ii);
; #pragma unroll
;             for (int ii = 0; ii < 8; ++ii) {
;                 A[(16 - 2 * ii) & 15] = *(const LAS bf16x8*)(ap + 64 * ii);
;                 A[(17 - 2 * ii) & 15] = *(const LAS bf16x8*)(ap + 64 * ii - 32);
; #pragma unroll
;                 for (int jj = 0; jj < 16; ++jj) { const int j = (jj + 2) & 15; acc[j] = __builtin_amdgcn_mfma_f32_16x16x32_bf16(A[(j + 16 - 2 * ii) & 15], zc[ii], acc[j], 0, 0, 0); }
;             }
;             ap += 512;
; #pragma unroll
;             for (int ii = 0; ii < 8; ++ii) zc[ii] = zn[ii];
;         }
.LBB0_2257:
	s_waitcnt vmcnt(1) lgkmcnt(1)
	s_nop 0
	v_mfma_f32_16x16x32_bf16 v[44:47], v[56:59], v[30:33], v[44:47]
	s_cmpk_lg_i32 s14, 0x800
	s_cselect_b32 s78, s14, 0x700
	s_addk_i32 s14, 0x100
	v_mfma_f32_16x16x32_bf16 v[36:39], v[80:83], v[30:33], v[36:39]
	s_cmpk_lg_i32 s14, 0x900
	v_mfma_f32_16x16x32_bf16 v[44:47], v[80:83], v[26:29], v[44:47]
	v_mfma_f32_16x16x32_bf16 v[136:139], v[88:91], v[30:33], v[136:139]
	v_mfma_f32_16x16x32_bf16 v[132:135], v[84:87], v[30:33], v[132:135]
	v_mfma_f32_16x16x32_bf16 v[128:131], v[104:107], v[30:33], v[128:131]
	v_mfma_f32_16x16x32_bf16 v[124:127], v[96:99], v[30:33], v[124:127]
	v_mfma_f32_16x16x32_bf16 v[48:51], v[112:115], v[30:33], v[48:51]
	v_mfma_f32_16x16x32_bf16 v[36:39], v[112:115], v[26:29], v[36:39]
	v_mfma_f32_16x16x32_bf16 v[44:47], v[112:115], v[22:25], v[44:47]
	v_subrev_u32_e32 v112, 32, v161
	s_waitcnt lgkmcnt(0)
	v_mfma_f32_16x16x32_bf16 v[52:55], v[60:63], v[30:33], v[52:55]
	v_mfma_f32_16x16x32_bf16 v[56:59], v[72:75], v[26:29], v[136:139]
	v_mfma_f32_16x16x32_bf16 v[60:63], v[68:71], v[26:29], v[132:135]
	s_nop 1
	ds_read_b128 v[136:139], v112
	ds_read_b128 v[132:135], v161
	v_mfma_f32_16x16x32_bf16 v[128:131], v[88:91], v[26:29], v[128:131]
	v_mfma_f32_16x16x32_bf16 v[124:127], v[84:87], v[26:29], v[124:127]
	v_mfma_f32_16x16x32_bf16 v[140:143], v[68:71], v[30:33], v[140:143]
	v_mfma_f32_16x16x32_bf16 v[40:43], v[76:79], v[30:33], v[40:43]
	v_mfma_f32_16x16x32_bf16 v[52:55], v[76:79], v[26:29], v[52:55]
	v_mfma_f32_16x16x32_bf16 v[76:79], v[72:75], v[22:25], v[128:131]
	v_mfma_f32_16x16x32_bf16 v[80:83], v[68:71], v[22:25], v[124:127]
	v_mfma_f32_16x16x32_bf16 v[144:147], v[72:75], v[30:33], v[144:147]
	s_waitcnt lgkmcnt(0)
	v_mfma_f32_16x16x32_bf16 v[124:127], v[132:135], v[22:25], v[56:59]
	v_mfma_f32_16x16x32_bf16 v[128:131], v[136:139], v[26:29], v[140:143]
	v_mfma_f32_16x16x32_bf16 v[140:143], v[136:139], v[22:25], v[60:63]
	s_nop 2
	ds_read_b128 v[60:63], v161 offset:64
	ds_read_b128 v[56:59], v161 offset:32
	v_mfma_f32_16x16x32_bf16 v[120:123], v[100:103], v[30:33], v[120:123]
	v_mfma_f32_16x16x32_bf16 v[92:95], v[108:111], v[30:33], v[92:95]
	v_mfma_f32_16x16x32_bf16 v[64:67], v[116:119], v[30:33], v[64:67]
	v_mfma_f32_16x16x32_bf16 v[40:43], v[116:119], v[26:29], v[40:43]
	v_mfma_f32_16x16x32_bf16 v[52:55], v[116:119], v[22:25], v[52:55]
	v_mfma_f32_16x16x32_bf16 v[112:115], v[132:135], v[30:33], v[148:151]
	v_mfma_f32_16x16x32_bf16 v[30:33], v[136:139], v[30:33], v[152:155]
	v_mfma_f32_16x16x32_bf16 v[76:79], v[132:135], v[18:21], v[76:79]
	v_mfma_f32_16x16x32_bf16 v[80:83], v[136:139], v[18:21], v[80:83]
	v_mfma_f32_16x16x32_bf16 v[116:119], v[132:135], v[26:29], v[144:147]
	v_mfma_f32_16x16x32_bf16 v[120:123], v[104:107], v[26:29], v[120:123]
	v_mfma_f32_16x16x32_bf16 v[92:95], v[96:99], v[26:29], v[92:95]
	v_mfma_f32_16x16x32_bf16 v[64:67], v[100:103], v[26:29], v[64:67]
	v_mfma_f32_16x16x32_bf16 v[48:51], v[108:111], v[26:29], v[48:51]
	v_mfma_f32_16x16x32_bf16 v[40:43], v[100:103], v[22:25], v[40:43]
	v_mfma_f32_16x16x32_bf16 v[52:55], v[100:103], v[18:21], v[52:55]
	s_waitcnt lgkmcnt(1)
	v_mfma_f32_16x16x32_bf16 v[100:103], v[60:63], v[26:29], v[112:115]
	v_mfma_f32_16x16x32_bf16 v[112:115], v[60:63], v[18:21], v[124:127]
	s_waitcnt lgkmcnt(0)
	v_mfma_f32_16x16x32_bf16 v[26:29], v[56:59], v[26:29], v[30:33]
	v_mfma_f32_16x16x32_bf16 v[30:33], v[56:59], v[22:25], v[128:131]
	v_mfma_f32_16x16x32_bf16 v[124:127], v[60:63], v[14:17], v[76:79]
	v_mfma_f32_16x16x32_bf16 v[128:131], v[56:59], v[14:17], v[80:83]
	s_nop 1
	ds_read_b128 v[76:79], v161 offset:128
	ds_read_b128 v[80:83], v161 offset:96
	v_mfma_f32_16x16x32_bf16 v[36:39], v[108:111], v[22:25], v[36:39]
	v_mfma_f32_16x16x32_bf16 v[44:47], v[108:111], v[18:21], v[44:47]
	v_mfma_f32_16x16x32_bf16 v[108:111], v[60:63], v[22:25], v[116:119]
	v_mfma_f32_16x16x32_bf16 v[116:119], v[56:59], v[18:21], v[140:143]
	v_mfma_f32_16x16x32_bf16 v[120:123], v[88:91], v[22:25], v[120:123]
	v_mfma_f32_16x16x32_bf16 v[92:95], v[84:87], v[22:25], v[92:95]
	v_mfma_f32_16x16x32_bf16 v[64:67], v[104:107], v[22:25], v[64:67]
	v_mfma_f32_16x16x32_bf16 v[48:51], v[96:99], v[22:25], v[48:51]
	v_mfma_f32_16x16x32_bf16 v[40:43], v[104:107], v[18:21], v[40:43]
	v_mfma_f32_16x16x32_bf16 v[36:39], v[96:99], v[18:21], v[36:39]
	v_mfma_f32_16x16x32_bf16 v[52:55], v[104:107], v[14:17], v[52:55]
	v_mfma_f32_16x16x32_bf16 v[44:47], v[96:99], v[14:17], v[44:47]
	s_waitcnt lgkmcnt(1)
	v_mfma_f32_16x16x32_bf16 v[96:99], v[76:79], v[22:25], v[100:103]
	v_mfma_f32_16x16x32_bf16 v[104:107], v[76:79], v[14:17], v[112:115]
	s_waitcnt lgkmcnt(0)
	v_mfma_f32_16x16x32_bf16 v[22:25], v[80:83], v[22:25], v[26:29]
	v_mfma_f32_16x16x32_bf16 v[26:29], v[80:83], v[18:21], v[30:33]
	v_mfma_f32_16x16x32_bf16 v[30:33], v[80:83], v[14:17], v[116:119]
	s_nop 2
	ds_read_b128 v[116:119], v161 offset:192
	ds_read_b128 v[112:115], v161 offset:160
	v_mfma_f32_16x16x32_bf16 v[100:103], v[76:79], v[18:21], v[108:111]
	v_mfma_f32_16x16x32_bf16 v[108:111], v[76:79], v[10:13], v[124:127]
	v_mfma_f32_16x16x32_bf16 v[124:127], v[80:83], v[10:13], v[128:131]
	v_mfma_f32_16x16x32_bf16 v[120:123], v[72:75], v[18:21], v[120:123]
	v_mfma_f32_16x16x32_bf16 v[92:95], v[68:71], v[18:21], v[92:95]
	v_mfma_f32_16x16x32_bf16 v[64:67], v[88:91], v[18:21], v[64:67]
	v_mfma_f32_16x16x32_bf16 v[48:51], v[84:87], v[18:21], v[48:51]
	v_mfma_f32_16x16x32_bf16 v[40:43], v[88:91], v[14:17], v[40:43]
	v_mfma_f32_16x16x32_bf16 v[36:39], v[84:87], v[14:17], v[36:39]
	v_mfma_f32_16x16x32_bf16 v[52:55], v[88:91], v[10:13], v[52:55]
	v_mfma_f32_16x16x32_bf16 v[44:47], v[84:87], v[10:13], v[44:47]
	s_waitcnt lgkmcnt(1)
; #define LAS __attribute__((address_space(3)))
; template <int L>
; __device__ __forceinline__ void hyena_unit(CArgs& a, int l, int c, LAS unsigned char* lds) {
;     ...
; #pragma unroll
;         for (int j = 2; j < 16; ++j) A[j] = *(const LAS bf16x8*)(ap - 32 * j);
; #pragma unroll 1
;         for (int ib = 0; ib < 8; ++ib) {
;             const bf16* zq = zp + 256 * (ib < 7 ? ib + 1 : 7);
; #pragma unroll
;             for (int ii = 0; ii < 8; ++ii) zn[ii] = *(const bf16x8*)(zq + 32 * ii);
; #pragma unroll
;             for (int ii = 0; ii < 8; ++ii) {
;                 A[(16 - 2 * ii) & 15] = *(const LAS bf16x8*)(ap + 64 * ii);
;                 A[(17 - 2 * ii) & 15] = *(const LAS bf16x8*)(ap + 64 * ii - 32);
; #pragma unroll
;                 for (int jj = 0; jj < 16; ++jj) { const int j = (jj + 2) & 15; acc[j] = __builtin_amdgcn_mfma_f32_16x16x32_bf16(A[(j + 16 - 2 * ii) & 15], zc[ii], acc[j], 0, 0, 0); }
;             }
;             ap += 512;
; #pragma unroll
;             for (int ii = 0; ii < 8; ++ii) zc[ii] = zn[ii];
;         }
	v_mfma_f32_16x16x32_bf16 v[84:87], v[116:119], v[18:21], v[96:99]
	v_mfma_f32_16x16x32_bf16 v[88:91], v[116:119], v[14:17], v[100:103]
	s_waitcnt lgkmcnt(0)
	v_mfma_f32_16x16x32_bf16 v[18:21], v[112:115], v[18:21], v[22:25]
	v_mfma_f32_16x16x32_bf16 v[22:25], v[112:115], v[14:17], v[26:29]
	v_mfma_f32_16x16x32_bf16 v[26:29], v[112:115], v[10:13], v[30:33]
	v_mfma_f32_16x16x32_bf16 v[30:33], v[116:119], v[6:9], v[108:111]
	ds_read_b128 v[100:103], v161 offset:256
	s_nop 1
	ds_read_b128 v[108:111], v161 offset:224
	v_mfma_f32_16x16x32_bf16 v[96:99], v[116:119], v[10:13], v[104:107]
	v_mfma_f32_16x16x32_bf16 v[104:107], v[112:115], v[6:9], v[124:127]
	v_mfma_f32_16x16x32_bf16 v[48:51], v[68:71], v[14:17], v[48:51]
	v_mfma_f32_16x16x32_bf16 v[36:39], v[68:71], v[10:13], v[36:39]
	v_mfma_f32_16x16x32_bf16 v[44:47], v[68:71], v[6:9], v[44:47]
	s_waitcnt lgkmcnt(1)
	v_mfma_f32_16x16x32_bf16 v[68:71], v[100:103], v[14:17], v[84:87]
	v_mfma_f32_16x16x32_bf16 v[84:87], v[100:103], v[6:9], v[96:99]
	s_waitcnt vmcnt(0) lgkmcnt(0)
	v_mfma_f32_16x16x32_bf16 v[124:127], v[108:111], v[2:5], v[104:107]
	s_nop 2
	ds_read_b128 v[104:107], v161 offset:320
	ds_read_b128 v[96:99], v161 offset:288
	v_mfma_f32_16x16x32_bf16 v[120:123], v[132:135], v[14:17], v[120:123]
	v_mfma_f32_16x16x32_bf16 v[92:95], v[136:139], v[14:17], v[92:95]
	v_mfma_f32_16x16x32_bf16 v[64:67], v[72:75], v[14:17], v[64:67]
	v_mfma_f32_16x16x32_bf16 v[14:17], v[108:111], v[14:17], v[18:21]
	v_mfma_f32_16x16x32_bf16 v[18:21], v[108:111], v[10:13], v[22:25]
	v_mfma_f32_16x16x32_bf16 v[22:25], v[108:111], v[6:9], v[26:29]
	s_waitcnt lgkmcnt(1)
	v_mfma_f32_16x16x32_bf16 v[26:29], v[104:107], v[10:13], v[68:71]
	s_nop 2
	v_lshl_add_u64 v[68:69], s[78:79], 1, v[158:159]
	v_mfma_f32_16x16x32_bf16 v[120:123], v[60:63], v[10:13], v[120:123]
	v_mfma_f32_16x16x32_bf16 v[92:95], v[56:59], v[10:13], v[92:95]
	v_mfma_f32_16x16x32_bf16 v[64:67], v[132:135], v[10:13], v[64:67]
	v_mfma_f32_16x16x32_bf16 v[48:51], v[136:139], v[10:13], v[48:51]
	v_mfma_f32_16x16x32_bf16 v[40:43], v[72:75], v[10:13], v[40:43]
	v_mfma_f32_16x16x32_bf16 v[52:55], v[72:75], v[6:9], v[52:55]
	v_mfma_f32_16x16x32_bf16 v[72:75], v[100:103], v[10:13], v[88:91]
	s_waitcnt lgkmcnt(0)
	v_mfma_f32_16x16x32_bf16 v[10:13], v[96:99], v[10:13], v[14:17]
	s_nop 2
	global_load_dwordx4 v[14:17], v[68:69], off
	v_mfma_f32_16x16x32_bf16 v[36:39], v[136:139], v[6:9], v[36:39]
	global_load_dwordx4 v[170:173], v[68:69], off offset:64
	global_load_dwordx4 v[174:177], v[68:69], off offset:128
	global_load_dwordx4 v[178:181], v[68:69], off offset:192
	v_mfma_f32_16x16x32_bf16 v[44:47], v[136:139], v[2:5], v[44:47]
	v_mfma_f32_16x16x32_bf16 v[136:139], v[104:107], v[2:5], v[84:87]
	ds_read_b128 v[88:91], v161 offset:384
	s_nop 1
	ds_read_b128 v[84:87], v161 offset:352
	global_load_dwordx4 v[182:185], v[68:69], off offset:256
	global_load_dwordx4 v[186:189], v[68:69], off offset:320
	global_load_dwordx4 v[202:205], v[68:69], off offset:384
	global_load_dwordx4 v[206:209], v[68:69], off offset:448
	v_mfma_f32_16x16x32_bf16 v[128:131], v[100:103], v[2:5], v[30:33]
	ds_read_b128 v[68:71], v161 offset:416
	v_mfma_f32_16x16x32_bf16 v[30:33], v[104:107], v[6:9], v[72:75]
	s_nop 2
	ds_read_b128 v[72:75], v161 offset:448
	v_mfma_f32_16x16x32_bf16 v[120:123], v[76:79], v[6:9], v[120:123]
	v_add_u32_e32 v161, 0x200, v161
	v_mfma_f32_16x16x32_bf16 v[92:95], v[80:83], v[6:9], v[92:95]
	v_mfma_f32_16x16x32_bf16 v[64:67], v[60:63], v[6:9], v[64:67]
	v_mfma_f32_16x16x32_bf16 v[48:51], v[56:59], v[6:9], v[48:51]
	v_mfma_f32_16x16x32_bf16 v[40:43], v[132:135], v[6:9], v[40:43]
	v_mfma_f32_16x16x32_bf16 v[52:55], v[132:135], v[2:5], v[52:55]
	v_mfma_f32_16x16x32_bf16 v[18:21], v[96:99], v[6:9], v[18:21]
	v_mfma_f32_16x16x32_bf16 v[132:135], v[96:99], v[2:5], v[22:25]
	s_waitcnt lgkmcnt(3)
	v_mfma_f32_16x16x32_bf16 v[22:25], v[88:91], v[6:9], v[26:29]
	s_waitcnt lgkmcnt(2)
	v_mfma_f32_16x16x32_bf16 v[6:9], v[84:87], v[6:9], v[10:13]
	s_waitcnt vmcnt(6)
	v_mov_b64_e32 v[26:27], v[170:171]
	v_mfma_f32_16x16x32_bf16 v[120:123], v[116:119], v[2:5], v[120:123]
	v_mov_b64_e32 v[28:29], v[172:173]
	s_waitcnt vmcnt(2)
	v_mov_b64_e32 v[10:11], v[186:187]
	v_mfma_f32_16x16x32_bf16 v[92:95], v[112:115], v[2:5], v[92:95]
	v_mov_b64_e32 v[12:13], v[188:189]
	v_mfma_f32_16x16x32_bf16 v[64:67], v[76:79], v[2:5], v[64:67]
	v_mfma_f32_16x16x32_bf16 v[48:51], v[80:83], v[2:5], v[48:51]
	v_mfma_f32_16x16x32_bf16 v[40:43], v[60:63], v[2:5], v[40:43]
	v_mfma_f32_16x16x32_bf16 v[36:39], v[56:59], v[2:5], v[36:39]
	v_mfma_f32_16x16x32_bf16 v[144:147], v[88:91], v[2:5], v[30:33]
	v_mfma_f32_16x16x32_bf16 v[140:143], v[84:87], v[2:5], v[18:21]
	s_nop 1
	v_mov_b64_e32 v[32:33], v[16:17]
	v_mov_b64_e32 v[30:31], v[14:15]
	v_mov_b64_e32 v[14:15], v[182:183]
	s_waitcnt lgkmcnt(0)
	v_mfma_f32_16x16x32_bf16 v[148:151], v[72:75], v[2:5], v[22:25]
	v_mov_b64_e32 v[18:19], v[178:179]
	v_mov_b64_e32 v[20:21], v[180:181]
	v_mov_b64_e32 v[16:17], v[184:185]
	v_mfma_f32_16x16x32_bf16 v[152:155], v[68:71], v[2:5], v[6:9]
	v_mov_b64_e32 v[22:23], v[174:175]
	s_waitcnt vmcnt(0)
	v_mov_b64_e32 v[2:3], v[206:207]
	v_mov_b64_e32 v[24:25], v[176:177]
	v_mov_b64_e32 v[6:7], v[202:203]
	v_mov_b64_e32 v[8:9], v[204:205]
	v_mov_b64_e32 v[4:5], v[208:209]
	s_cbranch_scc1 .LBB0_2257
; __device__ __forceinline__ unsigned pk2(float lo, float hi) { return f2bf(lo) | (f2bf(hi) << 16); }
; template <int L>
; __device__ __forceinline__ void hyena_unit(CArgs& a, int l, int c, LAS unsigned char* lds) {
;     ...
; #pragma unroll
;     for (int j = 0; j < NTW; ++j) *(u32x2*)(YT + 16 * (w * NTW + j) + 4 * kg) = (u32x2){pk2(acc[j][0], acc[j][1]), pk2(acc[j][2], acc[j][3])};
	v_lshlrev_b32_e32 v2, 8, v1
	v_cvt_pk_bf16_f32 v6, v148, v149
	v_lshl_add_u64 v[4:5], v[156:157], 0, v[34:35]
	v_cvt_pk_bf16_f32 v7, v150, v151
	v_ashrrev_i32_e32 v3, 31, v2
	v_lshl_add_u64 v[2:3], v[2:3], 1, v[4:5]
	s_mov_b64 s[14:15], 0x50400200
	v_lshl_add_u64 v[4:5], v[2:3], 0, s[14:15]
	s_mov_b32 s14, 0x50400000
	v_add_co_u32_e32 v2, vcc, s14, v2
	s_nop 0
	s_nop 0
	v_addc_co_u32_e32 v3, vcc, 0, v3, vcc
	global_store_dwordx2 v[2:3], v[6:7], off offset:512
	v_cvt_pk_bf16_f32 v2, v152, v153
	v_cvt_pk_bf16_f32 v3, v154, v155
	global_store_dwordx2 v[4:5], v[2:3], off offset:32
	v_cvt_pk_bf16_f32 v2, v144, v145
	v_cvt_pk_bf16_f32 v3, v146, v147
	global_store_dwordx2 v[4:5], v[2:3], off offset:64
	v_cvt_pk_bf16_f32 v2, v140, v141
	v_cvt_pk_bf16_f32 v3, v142, v143
	global_store_dwordx2 v[4:5], v[2:3], off offset:96
	v_cvt_pk_bf16_f32 v2, v136, v137
	v_cvt_pk_bf16_f32 v3, v138, v139
	global_store_dwordx2 v[4:5], v[2:3], off offset:128
	v_cvt_pk_bf16_f32 v2, v132, v133
	v_cvt_pk_bf16_f32 v3, v134, v135
	global_store_dwordx2 v[4:5], v[2:3], off offset:160
	v_cvt_pk_bf16_f32 v2, v128, v129
	v_cvt_pk_bf16_f32 v3, v130, v131
	global_store_dwordx2 v[4:5], v[2:3], off offset:192
	v_cvt_pk_bf16_f32 v2, v124, v125
	v_cvt_pk_bf16_f32 v3, v126, v127
	global_store_dwordx2 v[4:5], v[2:3], off offset:224
	v_cvt_pk_bf16_f32 v2, v120, v121
	v_cvt_pk_bf16_f32 v3, v122, v123
	global_store_dwordx2 v[4:5], v[2:3], off offset:256
	v_cvt_pk_bf16_f32 v2, v92, v93
	v_cvt_pk_bf16_f32 v3, v94, v95
	global_store_dwordx2 v[4:5], v[2:3], off offset:288
	v_cvt_pk_bf16_f32 v2, v64, v65
	v_cvt_pk_bf16_f32 v3, v66, v67
	global_store_dwordx2 v[4:5], v[2:3], off offset:320
	v_cvt_pk_bf16_f32 v2, v48, v49
	v_cvt_pk_bf16_f32 v3, v50, v51
	global_store_dwordx2 v[4:5], v[2:3], off offset:352
	v_cvt_pk_bf16_f32 v2, v40, v41
	v_cvt_pk_bf16_f32 v3, v42, v43
	global_store_dwordx2 v[4:5], v[2:3], off offset:384
	v_cvt_pk_bf16_f32 v2, v36, v37
	v_cvt_pk_bf16_f32 v3, v38, v39
	global_store_dwordx2 v[4:5], v[2:3], off offset:416
	v_cvt_pk_bf16_f32 v2, v52, v53
	v_cvt_pk_bf16_f32 v3, v54, v55
	global_store_dwordx2 v[4:5], v[2:3], off offset:448
	v_cvt_pk_bf16_f32 v2, v44, v45
	v_cvt_pk_bf16_f32 v1, v46, v46
	v_lshrrev_b32_e32 v1, 16, v1
	v_cvt_pk_bf16_f32 v3, v47, v47
	v_and_or_b32 v3, v3, s80, v1
	global_store_dwordx2 v[4:5], v[2:3], off offset:480
	s_barrier
	s_branch .LBB0_2061

; #define LAS __attribute__((address_space(3)))
; __device__ __forceinline__ unsigned f2bf(float f) { unsigned u = __float_as_uint(f); return (u + 0x7fffu + ((u >> 16) & 1u)) >> 16; }
; template <int L>
; __device__ __forceinline__ void hyena_unit(CArgs& a, int l, int c, LAS unsigned char* lds) {
;     ...
;     s = wave_sum(s);
;     if (lane == 0) red[w] = s;
;     __syncthreads();
;     float l1 = 0.f;
; #pragma unroll
;     for (int i = 0; i < 8; ++i) l1 += red[i];
;     const float inv = 1.f / l1;
; #pragma unroll
;     for (int q = 0; q < NI; ++q) {
;         const int idx = tid + 512 * q;
;         const bf16 gb = (bf16)f2bf(gv[q] * inv);
;         if (idx < 2 * L + 16) {
; #pragma unroll
;             for (int r = 0; r < 8; ++r) if (idx - r >= 0) *(LAS bf16*)(lds + r * CST + (idx - r) * 2) = gb;
;         }
.LBB0_2264:
	s_or_b64 exec, exec, s[6:7]
	s_add_i32 s6, 0, 0x10200
	v_mov_b32_e32 v41, s6
	s_waitcnt lgkmcnt(0)
	s_barrier
	ds_read_b128 v[56:59], v41
	v_readlane_b32 s6, v250, 7
	s_waitcnt lgkmcnt(0)
	v_add_f32_e32 v41, 0, v56
	v_add_f32_e32 v41, v41, v57
	v_add_f32_e32 v41, v41, v58
	v_mov_b32_e32 v55, s6
	v_add_f32_e32 v41, v41, v59
	ds_read_b128 v[56:59], v55
	s_waitcnt lgkmcnt(0)
	v_add_f32_e32 v41, v41, v56
	v_add_f32_e32 v41, v41, v57
	v_add_f32_e32 v41, v41, v58
	v_add_f32_e32 v41, v41, v59
	v_div_scale_f32 v55, s[6:7], v41, v41, 1.0
	v_rcp_f32_e32 v56, v55
	s_movk_i32 s6, 0x1010
	v_fma_f32 v57, -v55, v56, 1.0
	v_fmac_f32_e32 v56, v57, v56
	v_div_scale_f32 v57, vcc, 1.0, v41, 1.0
	v_mul_f32_e32 v58, v57, v56
	v_fma_f32 v59, -v55, v58, v57
	v_fmac_f32_e32 v58, v59, v56
	v_fma_f32 v55, -v55, v58, v57
	v_div_fmas_f32 v55, v55, v56, v58
	v_div_fixup_f32 v41, v55, v41, 1.0
	v_cmp_gt_i32_e32 vcc, s6, v37
	s_and_saveexec_b64 s[6:7], vcc
	s_cbranch_execz .LBB0_2282
	v_mul_f32_e32 v34, v34, v41
	v_cvt_pk_bf16_f32 v34, v34, v34
	v_lshrrev_b32_e32 v34, 16, v34
	v_cmp_lt_i32_e32 vcc, -1, v37
	s_and_saveexec_b64 s[14:15], vcc
	s_cbranch_execz .LBB0_2274
	v_lshl_add_u32 v55, v37, 1, 0
	ds_write_b16 v55, v34
	s_or_b64 exec, exec, s[14:15]
	v_cmp_lt_i32_e32 vcc, 0, v37
	s_and_saveexec_b64 s[14:15], vcc
	s_cbranch_execnz .LBB0_2275

; #define LAS __attribute__((address_space(3)))
; __device__ __forceinline__ unsigned f2bf(float f) { unsigned u = __float_as_uint(f); return (u + 0x7fffu + ((u >> 16) & 1u)) >> 16; }
; template <int L>
; __device__ __forceinline__ void hyena_unit(CArgs& a, int l, int c, LAS unsigned char* lds) {
;     ...
; #pragma unroll
;     for (int q = 0; q < NI; ++q) {
;         const int idx = tid + 512 * q;
;         const bf16 gb = (bf16)f2bf(gv[q] * inv);
;         if (idx < 2 * L + 16) {
; #pragma unroll
;             for (int r = 0; r < 8; ++r) if (idx - r >= 0) *(LAS bf16*)(lds + r * CST + (idx - r) * 2) = gb;
;         }
.LBB0_2282:
	s_or_b64 exec, exec, s[6:7]
	v_bfe_u32 v34, v37, 4, 2
	s_movk_i32 s6, 0xe10
	v_lshlrev_b32_e32 v34, 3, v34
	v_cmp_gt_i32_e32 vcc, s6, v37
	s_and_saveexec_b64 s[6:7], vcc
	s_cbranch_execz .LBB0_2297
	v_mul_f32_e32 v54, v54, v41
	v_cvt_pk_bf16_f32 v54, v54, v54
	s_movk_i32 s9, 0xfdff
	v_lshrrev_b32_e32 v54, 16, v54
	v_cmp_lt_i32_e32 vcc, s9, v37
	s_and_saveexec_b64 s[14:15], vcc
	s_cbranch_execz .LBB0_2430
	v_lshl_add_u32 v52, v52, 1, 0
	ds_write_b16 v52, v54
	s_or_b64 exec, exec, s[14:15]
	v_cmp_lt_i32_e32 vcc, s30, v37
	s_and_saveexec_b64 s[14:15], vcc
	s_cbranch_execnz .LBB0_2431

; #define LAS __attribute__((address_space(3)))
; __device__ __forceinline__ unsigned f2bf(float f) { unsigned u = __float_as_uint(f); return (u + 0x7fffu + ((u >> 16) & 1u)) >> 16; }
; template <int L>
; __device__ __forceinline__ void hyena_unit(CArgs& a, int l, int c, LAS unsigned char* lds) {
;     ...
; #pragma unroll
;     for (int q = 0; q < NI; ++q) {
;         const int idx = tid + 512 * q;
;         const bf16 gb = (bf16)f2bf(gv[q] * inv);
;         if (idx < 2 * L + 16) {
; #pragma unroll
;             for (int r = 0; r < 8; ++r) if (idx - r >= 0) *(LAS bf16*)(lds + r * CST + (idx - r) * 2) = gb;
;         }
.LBB0_2297:
	s_or_b64 exec, exec, s[6:7]
	s_movk_i32 s6, 0xc10
	v_cmp_gt_i32_e32 vcc, s6, v37
	s_and_saveexec_b64 s[6:7], vcc
	s_cbranch_execz .LBB0_2314
	v_mul_f32_e32 v52, v53, v41
	v_cvt_pk_bf16_f32 v52, v52, v52
	s_movk_i32 s9, 0xfbff
	v_lshrrev_b32_e32 v52, 16, v52
	v_cmp_lt_i32_e32 vcc, s9, v37
	s_and_saveexec_b64 s[14:15], vcc
	v_lshl_add_u32 v50, v50, 1, 0
	ds_write_b16 v50, v52
	s_or_b64 exec, exec, s[14:15]
	s_movk_i32 s9, 0xfc00
	v_cmp_lt_i32_e32 vcc, s9, v37
	s_and_saveexec_b64 s[14:15], vcc
	v_lshl_add_u32 v50, v37, 1, 0
	ds_write_b16 v50, v52 offset:10302
	s_or_b64 exec, exec, s[14:15]
	s_movk_i32 s9, 0xfc01
	v_cmp_lt_i32_e32 vcc, s9, v37
	s_and_saveexec_b64 s[14:15], vcc
	v_lshl_add_u32 v50, v37, 1, 0
	ds_write_b16 v50, v52 offset:18556
	s_or_b64 exec, exec, s[14:15]
	s_movk_i32 s9, 0xfc02
	v_cmp_lt_i32_e32 vcc, s9, v37
	s_and_saveexec_b64 s[14:15], vcc
	v_lshl_add_u32 v50, v37, 1, 0
	ds_write_b16 v50, v52 offset:26810
	s_or_b64 exec, exec, s[14:15]
	s_movk_i32 s9, 0xfc03
	v_cmp_lt_i32_e32 vcc, s9, v37
	s_and_saveexec_b64 s[14:15], vcc
	v_lshl_add_u32 v50, v37, 1, 0
	ds_write_b16 v50, v52 offset:35064
	s_or_b64 exec, exec, s[14:15]
	s_movk_i32 s9, 0xfc04
	v_cmp_lt_i32_e32 vcc, s9, v37
	s_and_saveexec_b64 s[14:15], vcc
	v_lshl_add_u32 v50, v37, 1, 0
	ds_write_b16 v50, v52 offset:43318
	s_or_b64 exec, exec, s[14:15]
	s_movk_i32 s9, 0xfc05
	v_cmp_lt_i32_e32 vcc, s9, v37
	s_and_saveexec_b64 s[14:15], vcc
	v_lshl_add_u32 v50, v37, 1, 0
	ds_write_b16 v50, v52 offset:51572
	s_or_b64 exec, exec, s[14:15]
	s_movk_i32 s9, 0xfc06
	v_cmp_lt_i32_e32 vcc, s9, v37
	s_and_b64 exec, exec, vcc
	v_lshl_add_u32 v50, v37, 1, 0
	ds_write_b16 v50, v52 offset:59826
.LBB0_2314:
	s_or_b64 exec, exec, s[6:7]
	s_movk_i32 s6, 0xa10
	v_cmp_gt_i32_e32 vcc, s6, v37
	s_and_saveexec_b64 s[6:7], vcc
	s_cbranch_execz .LBB0_2331
	v_mul_f32_e32 v50, v51, v41
	v_cvt_pk_bf16_f32 v50, v50, v50
	s_movk_i32 s9, 0xf9ff
	v_lshrrev_b32_e32 v50, 16, v50
	v_cmp_lt_i32_e32 vcc, s9, v37
	s_and_saveexec_b64 s[14:15], vcc
	v_lshl_add_u32 v48, v48, 1, 0
	ds_write_b16 v48, v50
	s_or_b64 exec, exec, s[14:15]
	s_movk_i32 s9, 0xfa00
	v_cmp_lt_i32_e32 vcc, s9, v37
	s_and_saveexec_b64 s[14:15], vcc
	v_lshl_add_u32 v48, v37, 1, 0
	ds_write_b16 v48, v50 offset:11326
	s_or_b64 exec, exec, s[14:15]
	s_movk_i32 s9, 0xfa01
	v_cmp_lt_i32_e32 vcc, s9, v37
	s_and_saveexec_b64 s[14:15], vcc
	v_lshl_add_u32 v48, v37, 1, 0
	ds_write_b16 v48, v50 offset:19580
	s_or_b64 exec, exec, s[14:15]
	s_movk_i32 s9, 0xfa02
	v_cmp_lt_i32_e32 vcc, s9, v37
	s_and_saveexec_b64 s[14:15], vcc
	v_lshl_add_u32 v48, v37, 1, 0
	ds_write_b16 v48, v50 offset:27834
	s_or_b64 exec, exec, s[14:15]
	s_movk_i32 s9, 0xfa03
	v_cmp_lt_i32_e32 vcc, s9, v37
	s_and_saveexec_b64 s[14:15], vcc
	v_lshl_add_u32 v48, v37, 1, 0
	ds_write_b16 v48, v50 offset:36088
	s_or_b64 exec, exec, s[14:15]
	s_movk_i32 s9, 0xfa04
	v_cmp_lt_i32_e32 vcc, s9, v37
	s_and_saveexec_b64 s[14:15], vcc
	v_lshl_add_u32 v48, v37, 1, 0
	ds_write_b16 v48, v50 offset:44342
	s_or_b64 exec, exec, s[14:15]
	s_movk_i32 s9, 0xfa05
	v_cmp_lt_i32_e32 vcc, s9, v37
	s_and_saveexec_b64 s[14:15], vcc
	v_lshl_add_u32 v48, v37, 1, 0
	ds_write_b16 v48, v50 offset:52596
	s_or_b64 exec, exec, s[14:15]
	s_movk_i32 s9, 0xfa06
	v_cmp_lt_i32_e32 vcc, s9, v37
	s_and_b64 exec, exec, vcc
	v_lshl_add_u32 v48, v37, 1, 0
	ds_write_b16 v48, v50 offset:60850
.LBB0_2331:
	s_or_b64 exec, exec, s[6:7]
	s_movk_i32 s6, 0x810
	v_cmp_gt_i32_e32 vcc, s6, v37
	s_and_saveexec_b64 s[6:7], vcc
	s_cbranch_execz .LBB0_2348
	v_mul_f32_e32 v48, v49, v41
	v_cvt_pk_bf16_f32 v48, v48, v48
	s_movk_i32 s9, 0xf7ff
	v_lshrrev_b32_e32 v48, 16, v48
	v_cmp_lt_i32_e32 vcc, s9, v37
	s_and_saveexec_b64 s[14:15], vcc
	v_lshl_add_u32 v46, v46, 1, 0
	ds_write_b16 v46, v48
	s_or_b64 exec, exec, s[14:15]
	s_movk_i32 s9, 0xf800
	v_cmp_lt_i32_e32 vcc, s9, v37
	s_and_saveexec_b64 s[14:15], vcc
	v_lshl_add_u32 v46, v37, 1, 0
	ds_write_b16 v46, v48 offset:12350
	s_or_b64 exec, exec, s[14:15]
	s_movk_i32 s9, 0xf801
	v_cmp_lt_i32_e32 vcc, s9, v37
	s_and_saveexec_b64 s[14:15], vcc
	v_lshl_add_u32 v46, v37, 1, 0
	ds_write_b16 v46, v48 offset:20604
	s_or_b64 exec, exec, s[14:15]
	s_movk_i32 s9, 0xf802
	v_cmp_lt_i32_e32 vcc, s9, v37
	s_and_saveexec_b64 s[14:15], vcc
	v_lshl_add_u32 v46, v37, 1, 0
	ds_write_b16 v46, v48 offset:28858
	s_or_b64 exec, exec, s[14:15]
	s_movk_i32 s9, 0xf803
	v_cmp_lt_i32_e32 vcc, s9, v37
	s_and_saveexec_b64 s[14:15], vcc
	v_lshl_add_u32 v46, v37, 1, 0
	ds_write_b16 v46, v48 offset:37112
	s_or_b64 exec, exec, s[14:15]
	s_movk_i32 s9, 0xf804
	v_cmp_lt_i32_e32 vcc, s9, v37
	s_and_saveexec_b64 s[14:15], vcc
	v_lshl_add_u32 v46, v37, 1, 0
	ds_write_b16 v46, v48 offset:45366
	s_or_b64 exec, exec, s[14:15]
	s_movk_i32 s9, 0xf805
	v_cmp_lt_i32_e32 vcc, s9, v37
	s_and_saveexec_b64 s[14:15], vcc
	v_lshl_add_u32 v46, v37, 1, 0
	ds_write_b16 v46, v48 offset:53620
	s_or_b64 exec, exec, s[14:15]
	s_movk_i32 s9, 0xf806
	v_cmp_lt_i32_e32 vcc, s9, v37
	s_and_b64 exec, exec, vcc
	v_lshl_add_u32 v46, v37, 1, 0
	ds_write_b16 v46, v48 offset:61874
; #define LAS __attribute__((address_space(3)))
; __device__ __forceinline__ unsigned f2bf(float f) { unsigned u = __float_as_uint(f); return (u + 0x7fffu + ((u >> 16) & 1u)) >> 16; }
; template <int L>
; __device__ __forceinline__ void hyena_unit(CArgs& a, int l, int c, LAS unsigned char* lds) {
;     ...
; #pragma unroll
;     for (int q = 0; q < NI; ++q) {
;         const int idx = tid + 512 * q;
;         const bf16 gb = (bf16)f2bf(gv[q] * inv);
;         if (idx < 2 * L + 16) {
; #pragma unroll
;             for (int r = 0; r < 8; ++r) if (idx - r >= 0) *(LAS bf16*)(lds + r * CST + (idx - r) * 2) = gb;
;         }
.LBB0_2348:
	s_or_b64 exec, exec, s[6:7]
	s_movk_i32 s6, 0x610
	v_cmp_gt_i32_e32 vcc, s6, v37
	s_and_saveexec_b64 s[6:7], vcc
	s_cbranch_execz .LBB0_2365
	v_mul_f32_e32 v46, v47, v41
	v_cvt_pk_bf16_f32 v46, v46, v46
	s_movk_i32 s9, 0xf5ff
	v_lshrrev_b32_e32 v46, 16, v46
	v_cmp_lt_i32_e32 vcc, s9, v37
	s_and_saveexec_b64 s[14:15], vcc
	v_lshl_add_u32 v44, v44, 1, 0
	ds_write_b16 v44, v46
	s_or_b64 exec, exec, s[14:15]
	s_movk_i32 s9, 0xf600
	v_cmp_lt_i32_e32 vcc, s9, v37
	s_and_saveexec_b64 s[14:15], vcc
	v_lshl_add_u32 v44, v37, 1, 0
	ds_write_b16 v44, v46 offset:13374
	s_or_b64 exec, exec, s[14:15]
	s_movk_i32 s9, 0xf601
	v_cmp_lt_i32_e32 vcc, s9, v37
	s_and_saveexec_b64 s[14:15], vcc
	v_lshl_add_u32 v44, v37, 1, 0
	ds_write_b16 v44, v46 offset:21628
	s_or_b64 exec, exec, s[14:15]
	s_movk_i32 s9, 0xf602
	v_cmp_lt_i32_e32 vcc, s9, v37
	s_and_saveexec_b64 s[14:15], vcc
	v_lshl_add_u32 v44, v37, 1, 0
	ds_write_b16 v44, v46 offset:29882
	s_or_b64 exec, exec, s[14:15]
	s_movk_i32 s9, 0xf603
	v_cmp_lt_i32_e32 vcc, s9, v37
	s_and_saveexec_b64 s[14:15], vcc
	v_lshl_add_u32 v44, v37, 1, 0
	ds_write_b16 v44, v46 offset:38136
	s_or_b64 exec, exec, s[14:15]
	s_movk_i32 s9, 0xf604
	v_cmp_lt_i32_e32 vcc, s9, v37
	s_and_saveexec_b64 s[14:15], vcc
	v_lshl_add_u32 v44, v37, 1, 0
	ds_write_b16 v44, v46 offset:46390
	s_or_b64 exec, exec, s[14:15]
	s_movk_i32 s9, 0xf605
	v_cmp_lt_i32_e32 vcc, s9, v37
	s_and_saveexec_b64 s[14:15], vcc
	v_lshl_add_u32 v44, v37, 1, 0
	ds_write_b16 v44, v46 offset:54644
	s_or_b64 exec, exec, s[14:15]
	s_movk_i32 s9, 0xf606
	v_cmp_lt_i32_e32 vcc, s9, v37
	s_and_b64 exec, exec, vcc
	v_lshl_add_u32 v44, v37, 1, 0
	ds_write_b16 v44, v46 offset:62898
.LBB0_2365:
	s_or_b64 exec, exec, s[6:7]
	s_movk_i32 s6, 0x410
	v_cmp_gt_i32_e32 vcc, s6, v37
	s_and_saveexec_b64 s[6:7], vcc
	s_cbranch_execz .LBB0_2382
	v_mul_f32_e32 v44, v45, v41
	v_cvt_pk_bf16_f32 v44, v44, v44
	s_movk_i32 s9, 0xf3ff
	v_lshrrev_b32_e32 v44, 16, v44
	v_cmp_lt_i32_e32 vcc, s9, v37
	s_and_saveexec_b64 s[14:15], vcc
	v_lshl_add_u32 v42, v42, 1, 0
	ds_write_b16 v42, v44
	s_or_b64 exec, exec, s[14:15]
	s_movk_i32 s9, 0xf400
	v_cmp_lt_i32_e32 vcc, s9, v37
	s_and_saveexec_b64 s[14:15], vcc
	v_lshl_add_u32 v42, v37, 1, 0
	ds_write_b16 v42, v44 offset:14398
	s_or_b64 exec, exec, s[14:15]
	s_movk_i32 s9, 0xf401
	v_cmp_lt_i32_e32 vcc, s9, v37
	s_and_saveexec_b64 s[14:15], vcc
	v_lshl_add_u32 v42, v37, 1, 0
	ds_write_b16 v42, v44 offset:22652
	s_or_b64 exec, exec, s[14:15]
	s_movk_i32 s9, 0xf402
	v_cmp_lt_i32_e32 vcc, s9, v37
	s_and_saveexec_b64 s[14:15], vcc
	v_lshl_add_u32 v42, v37, 1, 0
	ds_write_b16 v42, v44 offset:30906
	s_or_b64 exec, exec, s[14:15]
	s_movk_i32 s9, 0xf403
	v_cmp_lt_i32_e32 vcc, s9, v37
	s_and_saveexec_b64 s[14:15], vcc
	v_lshl_add_u32 v42, v37, 1, 0
	ds_write_b16 v42, v44 offset:39160
	s_or_b64 exec, exec, s[14:15]
	s_movk_i32 s9, 0xf404
	v_cmp_lt_i32_e32 vcc, s9, v37
	s_and_saveexec_b64 s[14:15], vcc
	v_lshl_add_u32 v42, v37, 1, 0
	ds_write_b16 v42, v44 offset:47414
	s_or_b64 exec, exec, s[14:15]
	s_movk_i32 s9, 0xf405
	v_cmp_lt_i32_e32 vcc, s9, v37
	s_and_saveexec_b64 s[14:15], vcc
	v_lshl_add_u32 v42, v37, 1, 0
	ds_write_b16 v42, v44 offset:55668
	s_or_b64 exec, exec, s[14:15]
	s_movk_i32 s9, 0xf406
	v_cmp_lt_i32_e32 vcc, s9, v37
	s_and_b64 exec, exec, vcc
	v_lshl_add_u32 v42, v37, 1, 0
	ds_write_b16 v42, v44 offset:63922
.LBB0_2382:
	s_or_b64 exec, exec, s[6:7]
	v_cmp_gt_i32_e32 vcc, s23, v37
	s_and_saveexec_b64 s[6:7], vcc
	s_cbranch_execz .LBB0_2399
	v_mul_f32_e32 v42, v43, v41
	v_cvt_pk_bf16_f32 v42, v42, v42
	s_movk_i32 s9, 0xf1ff
	v_lshrrev_b32_e32 v42, 16, v42
	v_cmp_lt_i32_e32 vcc, s9, v37
	s_and_saveexec_b64 s[14:15], vcc
	v_lshl_add_u32 v40, v40, 1, 0
	ds_write_b16 v40, v42
	s_or_b64 exec, exec, s[14:15]
	s_movk_i32 s9, 0xf200
	v_cmp_lt_i32_e32 vcc, s9, v37
	s_and_saveexec_b64 s[14:15], vcc
	v_lshl_add_u32 v40, v37, 1, 0
	ds_write_b16 v40, v42 offset:15422
	s_or_b64 exec, exec, s[14:15]
	s_movk_i32 s9, 0xf201
	v_cmp_lt_i32_e32 vcc, s9, v37
	s_and_saveexec_b64 s[14:15], vcc
	v_lshl_add_u32 v40, v37, 1, 0
	ds_write_b16 v40, v42 offset:23676
	s_or_b64 exec, exec, s[14:15]
	s_movk_i32 s9, 0xf202
	v_cmp_lt_i32_e32 vcc, s9, v37
	s_and_saveexec_b64 s[14:15], vcc
	v_lshl_add_u32 v40, v37, 1, 0
	ds_write_b16 v40, v42 offset:31930
	s_or_b64 exec, exec, s[14:15]
	s_movk_i32 s9, 0xf203
	v_cmp_lt_i32_e32 vcc, s9, v37
	s_and_saveexec_b64 s[14:15], vcc
	v_lshl_add_u32 v40, v37, 1, 0
	ds_write_b16 v40, v42 offset:40184
	s_or_b64 exec, exec, s[14:15]
	s_movk_i32 s9, 0xf204
	v_cmp_lt_i32_e32 vcc, s9, v37
	s_and_saveexec_b64 s[14:15], vcc
	v_lshl_add_u32 v40, v37, 1, 0
	ds_write_b16 v40, v42 offset:48438
	s_or_b64 exec, exec, s[14:15]
	s_movk_i32 s9, 0xf205
	v_cmp_lt_i32_e32 vcc, s9, v37
	s_and_saveexec_b64 s[14:15], vcc
	v_lshl_add_u32 v40, v37, 1, 0
	ds_write_b16 v40, v42 offset:56692
	s_or_b64 exec, exec, s[14:15]
	s_movk_i32 s9, 0xf206
	v_cmp_lt_i32_e32 vcc, s9, v37
	s_and_b64 exec, exec, vcc
	v_lshl_add_u32 v40, v37, 1, 0
	ds_write_b16 v40, v42 offset:64946
.LBB0_2399:
	s_or_b64 exec, exec, s[6:7]
	v_cmp_gt_i32_e32 vcc, 16, v37
	s_and_saveexec_b64 s[6:7], vcc
	s_cbranch_execz .LBB0_2416
	v_mul_f32_e32 v39, v39, v41
	v_cvt_pk_bf16_f32 v39, v39, v39
	s_movk_i32 s9, 0xefff
	v_lshrrev_b32_e32 v39, 16, v39
	v_cmp_lt_i32_e32 vcc, s9, v37
	s_and_saveexec_b64 s[14:15], vcc
	v_lshl_add_u32 v38, v38, 1, 0
	ds_write_b16 v38, v39
	s_or_b64 exec, exec, s[14:15]
	v_cmp_lt_i32_e32 vcc, s31, v37
	v_lshl_add_u32 v38, v37, 1, 0
	s_and_saveexec_b64 s[14:15], vcc
	ds_write_b16 v38, v39 offset:16446
	s_or_b64 exec, exec, s[14:15]
	s_movk_i32 s9, 0xf001
	v_cmp_lt_i32_e32 vcc, s9, v37
	s_and_saveexec_b64 s[14:15], vcc
	ds_write_b16 v38, v39 offset:24700
	s_or_b64 exec, exec, s[14:15]
	s_movk_i32 s9, 0xf002
	v_cmp_lt_i32_e32 vcc, s9, v37
	s_and_saveexec_b64 s[14:15], vcc
	ds_write_b16 v38, v39 offset:32954
	s_or_b64 exec, exec, s[14:15]
	s_movk_i32 s9, 0xf003
	v_cmp_lt_i32_e32 vcc, s9, v37
	s_and_saveexec_b64 s[14:15], vcc
	ds_write_b16 v38, v39 offset:41208
	s_or_b64 exec, exec, s[14:15]
	s_movk_i32 s9, 0xf004
	v_cmp_lt_i32_e32 vcc, s9, v37
	s_and_saveexec_b64 s[14:15], vcc
	ds_write_b16 v38, v39 offset:49462
	s_or_b64 exec, exec, s[14:15]
	s_movk_i32 s9, 0xf005
	v_cmp_lt_i32_e32 vcc, s9, v37
	s_and_saveexec_b64 s[14:15], vcc
	ds_write_b16 v38, v39 offset:57716
	s_or_b64 exec, exec, s[14:15]
	s_movk_i32 s9, 0xf006
	v_cmp_lt_i32_e32 vcc, s9, v37
	s_and_b64 exec, exec, vcc
	v_add_u32_e32 v38, 0x101b2, v38
	ds_write_b16 v38, v39

; #define LAS __attribute__((address_space(3)))
; template <int L>
; __device__ __forceinline__ void hyena_unit(CArgs& a, int l, int c, LAS unsigned char* lds) {
;     ...
;         for (int ib = 0; ib < 8; ++ib) {
;             const bf16* zq = zp + 256 * (ib < 7 ? ib + 1 : 7);
; #pragma unroll
;             for (int ii = 0; ii < 8; ++ii) zn[ii] = *(const bf16x8*)(zq + 32 * ii);
; #pragma unroll
;             for (int ii = 0; ii < 8; ++ii) {
;                 A[(16 - 2 * ii) & 15] = *(const LAS bf16x8*)(ap + 64 * ii);
;                 A[(17 - 2 * ii) & 15] = *(const LAS bf16x8*)(ap + 64 * ii - 32);
; #pragma unroll
;                 for (int jj = 0; jj < 16; ++jj) { const int j = (jj + 2) & 15; acc[j] = __builtin_amdgcn_mfma_f32_16x16x32_bf16(A[(j + 16 - 2 * ii) & 15], zc[ii], acc[j], 0, 0, 0); }
;             }
;             ap += 512;
; #pragma unroll
;             for (int ii = 0; ii < 8; ++ii) zc[ii] = zn[ii];
;         }
.LBB0_2417:
	s_waitcnt vmcnt(1) lgkmcnt(1)
	s_nop 0
	v_mfma_f32_16x16x32_bf16 v[44:47], v[56:59], v[30:33], v[44:47]
	s_cmpk_lg_i32 s6, 0x800
	s_cselect_b32 s78, s6, 0x700
	s_addk_i32 s6, 0x100
	v_mfma_f32_16x16x32_bf16 v[36:39], v[80:83], v[30:33], v[36:39]
	s_cmpk_lg_i32 s6, 0x900
	v_mfma_f32_16x16x32_bf16 v[44:47], v[80:83], v[26:29], v[44:47]
	v_mfma_f32_16x16x32_bf16 v[136:139], v[88:91], v[30:33], v[136:139]
	v_mfma_f32_16x16x32_bf16 v[132:135], v[84:87], v[30:33], v[132:135]
	v_mfma_f32_16x16x32_bf16 v[128:131], v[104:107], v[30:33], v[128:131]
	v_mfma_f32_16x16x32_bf16 v[124:127], v[96:99], v[30:33], v[124:127]
	v_mfma_f32_16x16x32_bf16 v[48:51], v[112:115], v[30:33], v[48:51]
	v_mfma_f32_16x16x32_bf16 v[36:39], v[112:115], v[26:29], v[36:39]
	v_mfma_f32_16x16x32_bf16 v[44:47], v[112:115], v[22:25], v[44:47]
	v_subrev_u32_e32 v112, 32, v161
	s_waitcnt lgkmcnt(0)
	v_mfma_f32_16x16x32_bf16 v[52:55], v[60:63], v[30:33], v[52:55]
	v_mfma_f32_16x16x32_bf16 v[56:59], v[72:75], v[26:29], v[136:139]
	v_mfma_f32_16x16x32_bf16 v[60:63], v[68:71], v[26:29], v[132:135]
	s_nop 1
	ds_read_b128 v[136:139], v112
	ds_read_b128 v[132:135], v161
	v_mfma_f32_16x16x32_bf16 v[128:131], v[88:91], v[26:29], v[128:131]
	v_mfma_f32_16x16x32_bf16 v[124:127], v[84:87], v[26:29], v[124:127]
	v_mfma_f32_16x16x32_bf16 v[140:143], v[68:71], v[30:33], v[140:143]
	v_mfma_f32_16x16x32_bf16 v[40:43], v[76:79], v[30:33], v[40:43]
	v_mfma_f32_16x16x32_bf16 v[52:55], v[76:79], v[26:29], v[52:55]
	v_mfma_f32_16x16x32_bf16 v[76:79], v[72:75], v[22:25], v[128:131]
	v_mfma_f32_16x16x32_bf16 v[80:83], v[68:71], v[22:25], v[124:127]
	v_mfma_f32_16x16x32_bf16 v[144:147], v[72:75], v[30:33], v[144:147]
	s_waitcnt lgkmcnt(0)
	v_mfma_f32_16x16x32_bf16 v[124:127], v[132:135], v[22:25], v[56:59]
	v_mfma_f32_16x16x32_bf16 v[128:131], v[136:139], v[26:29], v[140:143]
	v_mfma_f32_16x16x32_bf16 v[140:143], v[136:139], v[22:25], v[60:63]
	s_nop 2
	ds_read_b128 v[60:63], v161 offset:64
	ds_read_b128 v[56:59], v161 offset:32
	v_mfma_f32_16x16x32_bf16 v[120:123], v[100:103], v[30:33], v[120:123]
	v_mfma_f32_16x16x32_bf16 v[92:95], v[108:111], v[30:33], v[92:95]
	v_mfma_f32_16x16x32_bf16 v[64:67], v[116:119], v[30:33], v[64:67]
	v_mfma_f32_16x16x32_bf16 v[40:43], v[116:119], v[26:29], v[40:43]
	v_mfma_f32_16x16x32_bf16 v[52:55], v[116:119], v[22:25], v[52:55]
	v_mfma_f32_16x16x32_bf16 v[112:115], v[132:135], v[30:33], v[148:151]
	v_mfma_f32_16x16x32_bf16 v[30:33], v[136:139], v[30:33], v[152:155]
	v_mfma_f32_16x16x32_bf16 v[76:79], v[132:135], v[18:21], v[76:79]
	v_mfma_f32_16x16x32_bf16 v[80:83], v[136:139], v[18:21], v[80:83]
	v_mfma_f32_16x16x32_bf16 v[116:119], v[132:135], v[26:29], v[144:147]
	v_mfma_f32_16x16x32_bf16 v[120:123], v[104:107], v[26:29], v[120:123]
	v_mfma_f32_16x16x32_bf16 v[92:95], v[96:99], v[26:29], v[92:95]
	v_mfma_f32_16x16x32_bf16 v[64:67], v[100:103], v[26:29], v[64:67]
	v_mfma_f32_16x16x32_bf16 v[48:51], v[108:111], v[26:29], v[48:51]
	v_mfma_f32_16x16x32_bf16 v[40:43], v[100:103], v[22:25], v[40:43]
	v_mfma_f32_16x16x32_bf16 v[52:55], v[100:103], v[18:21], v[52:55]
	s_waitcnt lgkmcnt(1)
	v_mfma_f32_16x16x32_bf16 v[100:103], v[60:63], v[26:29], v[112:115]
	v_mfma_f32_16x16x32_bf16 v[112:115], v[60:63], v[18:21], v[124:127]
	s_waitcnt lgkmcnt(0)
	v_mfma_f32_16x16x32_bf16 v[26:29], v[56:59], v[26:29], v[30:33]
	v_mfma_f32_16x16x32_bf16 v[30:33], v[56:59], v[22:25], v[128:131]
	v_mfma_f32_16x16x32_bf16 v[124:127], v[60:63], v[14:17], v[76:79]
	v_mfma_f32_16x16x32_bf16 v[128:131], v[56:59], v[14:17], v[80:83]
	s_nop 1
	ds_read_b128 v[76:79], v161 offset:128
	ds_read_b128 v[80:83], v161 offset:96
	v_mfma_f32_16x16x32_bf16 v[36:39], v[108:111], v[22:25], v[36:39]
	v_mfma_f32_16x16x32_bf16 v[44:47], v[108:111], v[18:21], v[44:47]
	v_mfma_f32_16x16x32_bf16 v[108:111], v[60:63], v[22:25], v[116:119]
	v_mfma_f32_16x16x32_bf16 v[116:119], v[56:59], v[18:21], v[140:143]
	v_mfma_f32_16x16x32_bf16 v[120:123], v[88:91], v[22:25], v[120:123]
	v_mfma_f32_16x16x32_bf16 v[92:95], v[84:87], v[22:25], v[92:95]
	v_mfma_f32_16x16x32_bf16 v[64:67], v[104:107], v[22:25], v[64:67]
	v_mfma_f32_16x16x32_bf16 v[48:51], v[96:99], v[22:25], v[48:51]
	v_mfma_f32_16x16x32_bf16 v[40:43], v[104:107], v[18:21], v[40:43]
	v_mfma_f32_16x16x32_bf16 v[36:39], v[96:99], v[18:21], v[36:39]
	v_mfma_f32_16x16x32_bf16 v[52:55], v[104:107], v[14:17], v[52:55]
	v_mfma_f32_16x16x32_bf16 v[44:47], v[96:99], v[14:17], v[44:47]
	s_waitcnt lgkmcnt(1)
	v_mfma_f32_16x16x32_bf16 v[96:99], v[76:79], v[22:25], v[100:103]
	v_mfma_f32_16x16x32_bf16 v[104:107], v[76:79], v[14:17], v[112:115]
	s_waitcnt lgkmcnt(0)
	v_mfma_f32_16x16x32_bf16 v[22:25], v[80:83], v[22:25], v[26:29]
	v_mfma_f32_16x16x32_bf16 v[26:29], v[80:83], v[18:21], v[30:33]
	v_mfma_f32_16x16x32_bf16 v[30:33], v[80:83], v[14:17], v[116:119]
	s_nop 2
	ds_read_b128 v[116:119], v161 offset:192
	ds_read_b128 v[112:115], v161 offset:160
	v_mfma_f32_16x16x32_bf16 v[100:103], v[76:79], v[18:21], v[108:111]
	v_mfma_f32_16x16x32_bf16 v[108:111], v[76:79], v[10:13], v[124:127]
	v_mfma_f32_16x16x32_bf16 v[124:127], v[80:83], v[10:13], v[128:131]
	v_mfma_f32_16x16x32_bf16 v[120:123], v[72:75], v[18:21], v[120:123]
	v_mfma_f32_16x16x32_bf16 v[92:95], v[68:71], v[18:21], v[92:95]
	v_mfma_f32_16x16x32_bf16 v[64:67], v[88:91], v[18:21], v[64:67]
	v_mfma_f32_16x16x32_bf16 v[48:51], v[84:87], v[18:21], v[48:51]
	v_mfma_f32_16x16x32_bf16 v[40:43], v[88:91], v[14:17], v[40:43]
	v_mfma_f32_16x16x32_bf16 v[36:39], v[84:87], v[14:17], v[36:39]
	v_mfma_f32_16x16x32_bf16 v[52:55], v[88:91], v[10:13], v[52:55]
	v_mfma_f32_16x16x32_bf16 v[44:47], v[84:87], v[10:13], v[44:47]
	s_waitcnt lgkmcnt(1)
; #define LAS __attribute__((address_space(3)))
; template <int L>
; __device__ __forceinline__ void hyena_unit(CArgs& a, int l, int c, LAS unsigned char* lds) {
;     ...
;         for (int ib = 0; ib < 8; ++ib) {
;             const bf16* zq = zp + 256 * (ib < 7 ? ib + 1 : 7);
; #pragma unroll
;             for (int ii = 0; ii < 8; ++ii) zn[ii] = *(const bf16x8*)(zq + 32 * ii);
; #pragma unroll
;             for (int ii = 0; ii < 8; ++ii) {
;                 A[(16 - 2 * ii) & 15] = *(const LAS bf16x8*)(ap + 64 * ii);
;                 A[(17 - 2 * ii) & 15] = *(const LAS bf16x8*)(ap + 64 * ii - 32);
; #pragma unroll
;                 for (int jj = 0; jj < 16; ++jj) { const int j = (jj + 2) & 15; acc[j] = __builtin_amdgcn_mfma_f32_16x16x32_bf16(A[(j + 16 - 2 * ii) & 15], zc[ii], acc[j], 0, 0, 0); }
;             }
;             ap += 512;
; #pragma unroll
;             for (int ii = 0; ii < 8; ++ii) zc[ii] = zn[ii];
;         }
	v_mfma_f32_16x16x32_bf16 v[84:87], v[116:119], v[18:21], v[96:99]
	v_mfma_f32_16x16x32_bf16 v[88:91], v[116:119], v[14:17], v[100:103]
	s_waitcnt lgkmcnt(0)
	v_mfma_f32_16x16x32_bf16 v[18:21], v[112:115], v[18:21], v[22:25]
	v_mfma_f32_16x16x32_bf16 v[22:25], v[112:115], v[14:17], v[26:29]
	v_mfma_f32_16x16x32_bf16 v[26:29], v[112:115], v[10:13], v[30:33]
	v_mfma_f32_16x16x32_bf16 v[30:33], v[116:119], v[6:9], v[108:111]
	ds_read_b128 v[100:103], v161 offset:256
	s_nop 1
	ds_read_b128 v[108:111], v161 offset:224
	v_mfma_f32_16x16x32_bf16 v[96:99], v[116:119], v[10:13], v[104:107]
	v_mfma_f32_16x16x32_bf16 v[104:107], v[112:115], v[6:9], v[124:127]
	v_mfma_f32_16x16x32_bf16 v[48:51], v[68:71], v[14:17], v[48:51]
	v_mfma_f32_16x16x32_bf16 v[36:39], v[68:71], v[10:13], v[36:39]
	v_mfma_f32_16x16x32_bf16 v[44:47], v[68:71], v[6:9], v[44:47]
	s_waitcnt lgkmcnt(1)
	v_mfma_f32_16x16x32_bf16 v[68:71], v[100:103], v[14:17], v[84:87]
	v_mfma_f32_16x16x32_bf16 v[84:87], v[100:103], v[6:9], v[96:99]
	s_waitcnt vmcnt(0) lgkmcnt(0)
	v_mfma_f32_16x16x32_bf16 v[124:127], v[108:111], v[2:5], v[104:107]
	s_nop 2
	ds_read_b128 v[104:107], v161 offset:320
	ds_read_b128 v[96:99], v161 offset:288
	v_mfma_f32_16x16x32_bf16 v[120:123], v[132:135], v[14:17], v[120:123]
	v_mfma_f32_16x16x32_bf16 v[92:95], v[136:139], v[14:17], v[92:95]
	v_mfma_f32_16x16x32_bf16 v[64:67], v[72:75], v[14:17], v[64:67]
	v_mfma_f32_16x16x32_bf16 v[14:17], v[108:111], v[14:17], v[18:21]
	v_mfma_f32_16x16x32_bf16 v[18:21], v[108:111], v[10:13], v[22:25]
	v_mfma_f32_16x16x32_bf16 v[22:25], v[108:111], v[6:9], v[26:29]
	s_waitcnt lgkmcnt(1)
	v_mfma_f32_16x16x32_bf16 v[26:29], v[104:107], v[10:13], v[68:71]
	s_nop 2
	v_lshl_add_u64 v[68:69], s[78:79], 1, v[158:159]
	v_mfma_f32_16x16x32_bf16 v[120:123], v[60:63], v[10:13], v[120:123]
	v_mfma_f32_16x16x32_bf16 v[92:95], v[56:59], v[10:13], v[92:95]
	v_mfma_f32_16x16x32_bf16 v[64:67], v[132:135], v[10:13], v[64:67]
	v_mfma_f32_16x16x32_bf16 v[48:51], v[136:139], v[10:13], v[48:51]
	v_mfma_f32_16x16x32_bf16 v[40:43], v[72:75], v[10:13], v[40:43]
	v_mfma_f32_16x16x32_bf16 v[52:55], v[72:75], v[6:9], v[52:55]
	v_mfma_f32_16x16x32_bf16 v[72:75], v[100:103], v[10:13], v[88:91]
	s_waitcnt lgkmcnt(0)
	v_mfma_f32_16x16x32_bf16 v[10:13], v[96:99], v[10:13], v[14:17]
	s_nop 2
	global_load_dwordx4 v[14:17], v[68:69], off
	v_mfma_f32_16x16x32_bf16 v[36:39], v[136:139], v[6:9], v[36:39]
	global_load_dwordx4 v[170:173], v[68:69], off offset:64
	global_load_dwordx4 v[174:177], v[68:69], off offset:128
	global_load_dwordx4 v[178:181], v[68:69], off offset:192
	v_mfma_f32_16x16x32_bf16 v[44:47], v[136:139], v[2:5], v[44:47]
	v_mfma_f32_16x16x32_bf16 v[136:139], v[104:107], v[2:5], v[84:87]
	ds_read_b128 v[88:91], v161 offset:384
	s_nop 1
	ds_read_b128 v[84:87], v161 offset:352
	global_load_dwordx4 v[182:185], v[68:69], off offset:256
	global_load_dwordx4 v[186:189], v[68:69], off offset:320
	global_load_dwordx4 v[202:205], v[68:69], off offset:384
	global_load_dwordx4 v[206:209], v[68:69], off offset:448
	v_mfma_f32_16x16x32_bf16 v[128:131], v[100:103], v[2:5], v[30:33]
	ds_read_b128 v[68:71], v161 offset:416
	v_mfma_f32_16x16x32_bf16 v[30:33], v[104:107], v[6:9], v[72:75]
	s_nop 2
	ds_read_b128 v[72:75], v161 offset:448
	v_mfma_f32_16x16x32_bf16 v[120:123], v[76:79], v[6:9], v[120:123]
	v_add_u32_e32 v161, 0x200, v161
	v_mfma_f32_16x16x32_bf16 v[92:95], v[80:83], v[6:9], v[92:95]
	v_mfma_f32_16x16x32_bf16 v[64:67], v[60:63], v[6:9], v[64:67]
	v_mfma_f32_16x16x32_bf16 v[48:51], v[56:59], v[6:9], v[48:51]
	v_mfma_f32_16x16x32_bf16 v[40:43], v[132:135], v[6:9], v[40:43]
	v_mfma_f32_16x16x32_bf16 v[52:55], v[132:135], v[2:5], v[52:55]
	v_mfma_f32_16x16x32_bf16 v[18:21], v[96:99], v[6:9], v[18:21]
	v_mfma_f32_16x16x32_bf16 v[132:135], v[96:99], v[2:5], v[22:25]
	s_waitcnt lgkmcnt(3)
	v_mfma_f32_16x16x32_bf16 v[22:25], v[88:91], v[6:9], v[26:29]
	s_waitcnt lgkmcnt(2)
	v_mfma_f32_16x16x32_bf16 v[6:9], v[84:87], v[6:9], v[10:13]
	s_waitcnt vmcnt(6)
	v_mov_b64_e32 v[26:27], v[170:171]
	v_mfma_f32_16x16x32_bf16 v[120:123], v[116:119], v[2:5], v[120:123]
	v_mov_b64_e32 v[28:29], v[172:173]
	s_waitcnt vmcnt(2)
	v_mov_b64_e32 v[10:11], v[186:187]
	v_mfma_f32_16x16x32_bf16 v[92:95], v[112:115], v[2:5], v[92:95]
	v_mov_b64_e32 v[12:13], v[188:189]
	v_mfma_f32_16x16x32_bf16 v[64:67], v[76:79], v[2:5], v[64:67]
	v_mfma_f32_16x16x32_bf16 v[48:51], v[80:83], v[2:5], v[48:51]
	v_mfma_f32_16x16x32_bf16 v[40:43], v[60:63], v[2:5], v[40:43]
	v_mfma_f32_16x16x32_bf16 v[36:39], v[56:59], v[2:5], v[36:39]
	v_mfma_f32_16x16x32_bf16 v[144:147], v[88:91], v[2:5], v[30:33]
	v_mfma_f32_16x16x32_bf16 v[140:143], v[84:87], v[2:5], v[18:21]
	s_nop 1
	v_mov_b64_e32 v[32:33], v[16:17]
	v_mov_b64_e32 v[30:31], v[14:15]
	v_mov_b64_e32 v[14:15], v[182:183]
	s_waitcnt lgkmcnt(0)
	v_mfma_f32_16x16x32_bf16 v[148:151], v[72:75], v[2:5], v[22:25]
	v_mov_b64_e32 v[18:19], v[178:179]
	v_mov_b64_e32 v[20:21], v[180:181]
	v_mov_b64_e32 v[16:17], v[184:185]
	v_mfma_f32_16x16x32_bf16 v[152:155], v[68:71], v[2:5], v[6:9]
	v_mov_b64_e32 v[22:23], v[174:175]
	s_waitcnt vmcnt(0)
	v_mov_b64_e32 v[2:3], v[206:207]
	v_mov_b64_e32 v[24:25], v[176:177]
	v_mov_b64_e32 v[6:7], v[202:203]
	v_mov_b64_e32 v[8:9], v[204:205]
	v_mov_b64_e32 v[4:5], v[208:209]
	s_cbranch_scc1 .LBB0_2417
; #define LAS __attribute__((address_space(3)))
; __device__ __forceinline__ unsigned f2bf(float f) { unsigned u = __float_as_uint(f); return (u + 0x7fffu + ((u >> 16) & 1u)) >> 16; }
; __device__ __forceinline__ unsigned pk2(float lo, float hi) { return f2bf(lo) | (f2bf(hi) << 16); }
; template <int L>
; __device__ __forceinline__ void hyena_unit(CArgs& a, int l, int c, LAS unsigned char* lds) {
;     ...
;     const bf16* Z = (const bf16*)(a.ws + WS_MIX + MX_ZT) + ((size_t)(c * 16 + fr)) * 2304 + SOFF;
;     const bf16* zp = Z + 8 * kg;
;     bf16x8 zc[8];
; #pragma unroll
;     for (int ii = 0; ii < 8; ++ii) zc[ii] = *(const bf16x8*)(zp + 32 * ii);
;     constexpr int NI = (2 * L + 16 + 511) / 512;
;     float gv[NI];
;     float s = 0.f;
; #pragma unroll
;     for (int q = 0; q < NI; ++q) {
;         const int idx = tid + 512 * q, ic = min(max(idx, 1), 2 * L - 1);
;         const float v = *(ic <= L ? kf + (L - ic) : kb + (ic - L));
;         gv[q] = (idx >= 1 && idx < 2 * L) ? v : 0.f;
;         s += fabsf(gv[q]);
;     }
;     s = wave_sum(s);
;     if (lane == 0) red[w] = s;
;     __syncthreads();
;     float l1 = 0.f;
; #pragma unroll
;     for (int i = 0; i < 8; ++i) l1 += red[i];
;     const float inv = 1.f / l1;
; #pragma unroll
;     for (int q = 0; q < NI; ++q) {
;         const int idx = tid + 512 * q;
;         const bf16 gb = (bf16)f2bf(gv[q] * inv);
;         if (idx < 2 * L + 16) {
; #pragma unroll
;             for (int r = 0; r < 8; ++r) if (idx - r >= 0) *(LAS bf16*)(lds + r * CST + (idx - r) * 2) = gb;
;         }
;     ...
;     for (int j = 0; j < NTW; ++j) *(u32x2*)(YT + 16 * (w * NTW + j) + 4 * kg) = (u32x2){pk2(acc[j][0], acc[j][1]), pk2(acc[j][2], acc[j][3])};
;     __syncthreads();
	v_lshlrev_b32_e32 v2, 8, v1
	v_cvt_pk_bf16_f32 v6, v148, v149
	v_lshl_add_u64 v[4:5], v[156:157], 0, v[34:35]
	v_cvt_pk_bf16_f32 v7, v150, v151
	v_ashrrev_i32_e32 v3, 31, v2
	v_lshl_add_u64 v[2:3], v[2:3], 1, v[4:5]
	s_mov_b64 s[6:7], 0x50400200
	v_lshl_add_u64 v[4:5], v[2:3], 0, s[6:7]
	s_mov_b32 s6, 0x50400000
	v_add_co_u32_e32 v2, vcc, s6, v2
	s_nop 0
	s_nop 0
	v_addc_co_u32_e32 v3, vcc, 0, v3, vcc
	global_store_dwordx2 v[2:3], v[6:7], off offset:512
	v_cvt_pk_bf16_f32 v2, v152, v153
	v_cvt_pk_bf16_f32 v3, v154, v155
	global_store_dwordx2 v[4:5], v[2:3], off offset:32
	v_cvt_pk_bf16_f32 v2, v144, v145
	v_cvt_pk_bf16_f32 v3, v146, v147
	global_store_dwordx2 v[4:5], v[2:3], off offset:64
	v_cvt_pk_bf16_f32 v2, v140, v141
	v_cvt_pk_bf16_f32 v3, v142, v143
	global_store_dwordx2 v[4:5], v[2:3], off offset:96
	v_cvt_pk_bf16_f32 v2, v136, v137
	v_cvt_pk_bf16_f32 v3, v138, v139
	global_store_dwordx2 v[4:5], v[2:3], off offset:128
	v_cvt_pk_bf16_f32 v2, v132, v133
	v_cvt_pk_bf16_f32 v3, v134, v135
	global_store_dwordx2 v[4:5], v[2:3], off offset:160
	v_cvt_pk_bf16_f32 v2, v128, v129
	v_cvt_pk_bf16_f32 v3, v130, v131
	global_store_dwordx2 v[4:5], v[2:3], off offset:192
	v_cvt_pk_bf16_f32 v2, v124, v125
	v_cvt_pk_bf16_f32 v3, v126, v127
	global_store_dwordx2 v[4:5], v[2:3], off offset:224
	v_cvt_pk_bf16_f32 v2, v120, v121
	v_cvt_pk_bf16_f32 v3, v122, v123
	global_store_dwordx2 v[4:5], v[2:3], off offset:256
	v_cvt_pk_bf16_f32 v2, v92, v93
	v_cvt_pk_bf16_f32 v3, v94, v95
	global_store_dwordx2 v[4:5], v[2:3], off offset:288
	v_cvt_pk_bf16_f32 v2, v64, v65
	v_cvt_pk_bf16_f32 v3, v66, v67
	global_store_dwordx2 v[4:5], v[2:3], off offset:320
	v_cvt_pk_bf16_f32 v2, v48, v49
	v_cvt_pk_bf16_f32 v3, v50, v51
	global_store_dwordx2 v[4:5], v[2:3], off offset:352
	v_cvt_pk_bf16_f32 v2, v40, v41
	v_cvt_pk_bf16_f32 v3, v42, v43
	global_store_dwordx2 v[4:5], v[2:3], off offset:384
	v_cvt_pk_bf16_f32 v2, v36, v37
	v_cvt_pk_bf16_f32 v3, v38, v39
	global_store_dwordx2 v[4:5], v[2:3], off offset:416
	v_cvt_pk_bf16_f32 v2, v52, v53
	v_cvt_pk_bf16_f32 v3, v54, v55
	global_store_dwordx2 v[4:5], v[2:3], off offset:448
	v_cvt_pk_bf16_f32 v2, v44, v45
	v_cvt_pk_bf16_f32 v1, v46, v46
	v_readlane_b32 s10, v250, 58
	v_lshrrev_b32_e32 v1, 16, v1
	v_cvt_pk_bf16_f32 v3, v47, v47
	v_readlane_b32 s11, v250, 59
	v_and_or_b32 v3, v3, s80, v1
	s_mov_b64 s[6:7], 0
	s_andn2_b64 vcc, exec, s[10:11]
	s_mov_b64 s[14:15], 0
	global_store_dwordx2 v[4:5], v[2:3], off offset:480
	s_barrier
	s_cbranch_vccnz .LBB0_2494
	v_readlane_b32 s9, v252, 21
	s_add_i32 s10, s8, s9
	v_mov_b32_e32 v38, v0
	s_ashr_i32 s11, s10, 31
	s_lshl_b64 s[10:11], s[10:11], 13
	v_and_b32_e32 v39, 15, v38
	v_readlane_b32 s9, v252, 22
	s_add_u32 s26, s2, 0x4f000000
	s_addc_u32 s27, s3, 0
	v_or_b32_e32 v1, s9, v39
	s_movk_i32 s9, 0x900
	v_mad_u64_u32 v[36:37], s[14:15], v1, s9, 0
	v_lshl_add_u64 v[2:3], v[36:37], 1, s[26:27]
	v_and_b32_e32 v34, 48, v38
	s_add_u32 s10, s0, s10
	v_med3_i32 v1, v38, 1, v197
	v_lshl_add_u64 v[2:3], v[2:3], 0, v[34:35]
	s_addc_u32 s11, s1, s11
	v_sub_u32_e32 v34, 0x100, v1
	v_lshl_add_u64 v[4:5], v[34:35], 2, s[10:11]
	v_lshlrev_b32_e32 v34, 2, v1
	v_lshl_add_u64 v[6:7], s[10:11], 0, v[34:35]
	s_mov_b64 s[14:15], 0x1ffc00
	s_movk_i32 s9, 0x101
	v_lshl_add_u64 v[6:7], v[6:7], 0, s[14:15]
	v_cmp_gt_i32_e32 vcc, s9, v38
	v_add_u32_e32 v40, 0x200, v38
	v_med3_i32 v1, v40, 1, v197
	v_cndmask_b32_e32 v5, v7, v5, vcc
	v_cndmask_b32_e32 v4, v6, v4, vcc
	global_load_dword v41, v[4:5], off
	v_sub_u32_e32 v34, 0x100, v1
	v_lshl_add_u64 v[4:5], v[34:35], 2, s[10:11]
	v_lshlrev_b32_e32 v34, 2, v1
	v_lshl_add_u64 v[6:7], s[10:11], 0, v[34:35]
	s_movk_i32 s9, 0xff01
	v_lshl_add_u64 v[6:7], v[6:7], 0, s[14:15]
	v_cmp_gt_i32_e32 vcc, s9, v38
	v_add_u32_e32 v34, -1, v38
	s_movk_i32 s9, 0x1ff
	v_cndmask_b32_e32 v5, v7, v5, vcc
	v_cndmask_b32_e32 v4, v6, v4, vcc
	global_load_dword v42, v[4:5], off
	global_load_dwordx4 v[30:33], v[2:3], off
	global_load_dwordx4 v[26:29], v[2:3], off offset:64
	global_load_dwordx4 v[22:25], v[2:3], off offset:128
	global_load_dwordx4 v[18:21], v[2:3], off offset:192
	global_load_dwordx4 v[14:17], v[2:3], off offset:256
	global_load_dwordx4 v[10:13], v[2:3], off offset:320
	global_load_dwordx4 v[6:9], v[2:3], off offset:384
	s_nop 0
	global_load_dwordx4 v[2:5], v[2:3], off offset:448
	v_cmp_gt_u32_e32 vcc, s9, v34
	v_and_b32_e32 v43, 63, v38
	v_ashrrev_i32_e32 v1, 6, v38
	s_waitcnt vmcnt(9)
	v_cndmask_b32_e32 v34, 0, v41, vcc
	v_cmp_lt_u32_e32 vcc, s30, v38
	s_waitcnt vmcnt(8)
	s_nop 0
	v_cndmask_b32_e32 v41, 0, v42, vcc
	v_add_f32_e64 v42, |v34|, |v41|
	v_cmp_eq_u32_e32 vcc, 0, v43
	s_nop 0
	v_add_f32_dpp v42, v42, v42 quad_perm:[1,0,3,2] row_mask:0xf bank_mask:0xf bound_ctrl:1
	s_nop 1
	v_add_f32_dpp v42, v42, v42 quad_perm:[2,3,0,1] row_mask:0xf bank_mask:0xf bound_ctrl:1
	s_nop 1
	v_add_f32_dpp v42, v42, v42 row_half_mirror row_mask:0xf bank_mask:0xf bound_ctrl:1
	s_nop 1
	v_add_f32_dpp v42, v42, v42 row_mirror row_mask:0xf bank_mask:0xf bound_ctrl:1
	s_nop 0
	v_readlane_b32 s28, v42, 0
	v_readlane_b32 s9, v42, 16
	v_readlane_b32 s29, v42, 32
	v_readlane_b32 s10, v42, 48
	s_and_saveexec_b64 s[14:15], vcc
	s_cbranch_execz .LBB0_2421
	v_mov_b32_e32 v42, s9
	v_mov_b32_e32 v43, s10
	v_pk_add_f32 v[42:43], s[28:29], v[42:43]
	v_lshl_add_u32 v44, v1, 2, 0
	v_add_f32_e32 v42, v42, v43
	ds_write_b32 v44, v42 offset:8704
.LBB0_2421:
	s_or_b64 exec, exec, s[14:15]
	s_waitcnt lgkmcnt(0)
	s_barrier
	ds_read_b128 v[42:45], v35 offset:8704
	ds_read_b128 v[46:49], v35 offset:8720
	s_waitcnt lgkmcnt(1)
	v_add_f32_e32 v42, 0, v42
	v_add_f32_e32 v42, v42, v43
	v_add_f32_e32 v42, v42, v44
	v_add_f32_e32 v42, v42, v45
	s_waitcnt lgkmcnt(0)
	v_add_f32_e32 v42, v42, v46
	v_add_f32_e32 v42, v42, v47
	v_add_f32_e32 v42, v42, v48
	v_add_f32_e32 v42, v42, v49
	v_div_scale_f32 v43, s[10:11], v42, v42, 1.0
	v_rcp_f32_e32 v44, v43
	v_div_scale_f32 v45, vcc, 1.0, v42, 1.0
	v_fma_f32 v46, -v43, v44, 1.0
	v_fmac_f32_e32 v44, v46, v44
	v_mul_f32_e32 v46, v45, v44
	v_fma_f32 v47, -v43, v46, v45
	v_fmac_f32_e32 v46, v47, v44
	v_fma_f32 v43, -v43, v46, v45
	v_div_fmas_f32 v43, v43, v44, v46
	v_div_fixup_f32 v42, v43, v42, 1.0
	v_cmp_gt_i32_e32 vcc, s23, v38
	s_and_saveexec_b64 s[14:15], vcc
	s_cbranch_execz .LBB0_2440
	v_mul_f32_e32 v34, v34, v42
	v_cvt_pk_bf16_f32 v34, v34, v34
	v_lshrrev_b32_e32 v34, 16, v34
	v_cmp_lt_i32_e32 vcc, -1, v38
	s_and_saveexec_b64 s[28:29], vcc
	s_cbranch_execz .LBB0_2432
	v_lshl_add_u32 v43, v38, 1, 0
	ds_write_b16 v43, v34
	s_or_b64 exec, exec, s[28:29]
	v_cmp_lt_i32_e32 vcc, 0, v38
	s_and_saveexec_b64 s[28:29], vcc
	s_cbranch_execnz .LBB0_2433

; #define LAS __attribute__((address_space(3)))
; __device__ __forceinline__ unsigned f2bf(float f) { unsigned u = __float_as_uint(f); return (u + 0x7fffu + ((u >> 16) & 1u)) >> 16; }
; template <int L>
; __device__ __forceinline__ void hyena_unit(CArgs& a, int l, int c, LAS unsigned char* lds) {
;     ...
; #pragma unroll
;     for (int q = 0; q < NI; ++q) {
;         const int idx = tid + 512 * q;
;         const bf16 gb = (bf16)f2bf(gv[q] * inv);
;         if (idx < 2 * L + 16) {
; #pragma unroll
;             for (int r = 0; r < 8; ++r) if (idx - r >= 0) *(LAS bf16*)(lds + r * CST + (idx - r) * 2) = gb;
;         }
.LBB0_2440:
	s_or_b64 exec, exec, s[14:15]
	v_bfe_u32 v34, v38, 4, 2
	v_lshlrev_b32_e32 v34, 3, v34
	v_cmp_gt_i32_e32 vcc, 16, v38
	s_and_saveexec_b64 s[14:15], vcc
	s_cbranch_execz .LBB0_2457
	v_mul_f32_e32 v41, v41, v42
	v_cvt_pk_bf16_f32 v41, v41, v41
	s_movk_i32 s9, 0xfdff
	v_lshrrev_b32_e32 v41, 16, v41
	v_cmp_lt_i32_e32 vcc, s9, v38
	s_and_saveexec_b64 s[28:29], vcc
	v_lshl_add_u32 v40, v40, 1, 0
	ds_write_b16 v40, v41
	s_or_b64 exec, exec, s[28:29]
	v_cmp_lt_i32_e32 vcc, s30, v38
	v_lshl_add_u32 v40, v38, 1, 0
	s_and_saveexec_b64 s[28:29], vcc
	ds_write_b16 v40, v41 offset:2110
	s_or_b64 exec, exec, s[28:29]
	v_cmp_lt_i32_e32 vcc, s36, v38
	s_and_saveexec_b64 s[28:29], vcc
	ds_write_b16 v40, v41 offset:3196
	s_or_b64 exec, exec, s[28:29]
	s_movk_i32 s9, 0xfe02
	v_cmp_lt_i32_e32 vcc, s9, v38
	s_and_saveexec_b64 s[28:29], vcc
	ds_write_b16 v40, v41 offset:4282
	s_or_b64 exec, exec, s[28:29]
	s_movk_i32 s9, 0xfe03
	v_cmp_lt_i32_e32 vcc, s9, v38
	s_and_saveexec_b64 s[28:29], vcc
	ds_write_b16 v40, v41 offset:5368
	s_or_b64 exec, exec, s[28:29]
	s_movk_i32 s9, 0xfe04
	v_cmp_lt_i32_e32 vcc, s9, v38
	s_and_saveexec_b64 s[28:29], vcc
	ds_write_b16 v40, v41 offset:6454
	s_or_b64 exec, exec, s[28:29]
	s_movk_i32 s9, 0xfe05
	v_cmp_lt_i32_e32 vcc, s9, v38
	s_and_saveexec_b64 s[28:29], vcc
	ds_write_b16 v40, v41 offset:7540
	s_or_b64 exec, exec, s[28:29]
	s_movk_i32 s9, 0xfe06
	v_cmp_lt_i32_e32 vcc, s9, v38
	s_and_b64 exec, exec, vcc
	ds_write_b16 v40, v41 offset:8626

; #define LAS __attribute__((address_space(3)))
; __device__ __forceinline__ unsigned f2bf(float f) { unsigned u = __float_as_uint(f); return (u + 0x7fffu + ((u >> 16) & 1u)) >> 16; }
; template <int L>
; __device__ __forceinline__ void hyena_unit(CArgs& a, int l, int c, LAS unsigned char* lds) {
;     ...
;     s = wave_sum(s);
;     if (lane == 0) red[w] = s;
;     __syncthreads();
;     float l1 = 0.f;
; #pragma unroll
;     for (int i = 0; i < 8; ++i) l1 += red[i];
;     const float inv = 1.f / l1;
; #pragma unroll
;     for (int q = 0; q < NI; ++q) {
;         const int idx = tid + 512 * q;
;         const bf16 gb = (bf16)f2bf(gv[q] * inv);
;         if (idx < 2 * L + 16) {
; #pragma unroll
;             for (int r = 0; r < 8; ++r) if (idx - r >= 0) *(LAS bf16*)(lds + r * CST + (idx - r) * 2) = gb;
;         }
.LBB0_2459:
	s_or_b64 exec, exec, s[28:29]
	s_waitcnt lgkmcnt(0)
	s_barrier
	ds_read_b128 v[44:47], v35 offset:8704
	ds_read_b128 v[48:51], v35 offset:8720
	s_waitcnt lgkmcnt(1)
	v_add_f32_e32 v34, 0, v44
	v_add_f32_e32 v34, v34, v45
	v_add_f32_e32 v34, v34, v46
	v_add_f32_e32 v34, v34, v47
	s_waitcnt lgkmcnt(0)
	v_add_f32_e32 v34, v34, v48
	v_add_f32_e32 v34, v34, v49
	v_add_f32_e32 v34, v34, v50
	v_add_f32_e32 v34, v34, v51
	v_div_scale_f32 v43, s[0:1], v34, v34, 1.0
	v_rcp_f32_e32 v44, v43
	v_div_scale_f32 v45, vcc, 1.0, v34, 1.0
	v_fma_f32 v46, -v43, v44, 1.0
	v_fmac_f32_e32 v44, v46, v44
	v_mul_f32_e32 v46, v45, v44
	v_fma_f32 v47, -v43, v46, v45
	v_fmac_f32_e32 v46, v47, v44
	v_fma_f32 v43, -v43, v46, v45
	v_div_fmas_f32 v43, v43, v44, v46
	v_div_fixup_f32 v43, v43, v34, 1.0
	v_cmp_gt_i32_e32 vcc, s23, v1
	s_and_saveexec_b64 s[26:27], vcc
	s_cbranch_execz .LBB0_2476
	v_mul_f32_e32 v34, v42, v43
	v_cvt_pk_bf16_f32 v34, v34, v34
	v_lshrrev_b32_e32 v34, 16, v34
	v_cmp_lt_i32_e32 vcc, -1, v1
	s_and_saveexec_b64 s[28:29], vcc
	s_cbranch_execz .LBB0_2468
	v_lshl_add_u32 v42, v1, 1, 0
	ds_write_b16 v42, v34
	s_or_b64 exec, exec, s[28:29]
	v_cmp_lt_i32_e32 vcc, 0, v1
	s_and_saveexec_b64 s[28:29], vcc
	s_cbranch_execnz .LBB0_2469

; #define LAS __attribute__((address_space(3)))
; __device__ __forceinline__ unsigned f2bf(float f) { unsigned u = __float_as_uint(f); return (u + 0x7fffu + ((u >> 16) & 1u)) >> 16; }
; __device__ __forceinline__ unsigned pk2(float lo, float hi) { return f2bf(lo) | (f2bf(hi) << 16); }
; template <int L>
; __device__ __forceinline__ void hyena_unit(CArgs& a, int l, int c, LAS unsigned char* lds) {
;     ...
; #pragma unroll
;     for (int q = 0; q < NI; ++q) {
;         const int idx = tid + 512 * q;
;         const bf16 gb = (bf16)f2bf(gv[q] * inv);
;         if (idx < 2 * L + 16) {
; #pragma unroll
;             for (int r = 0; r < 8; ++r) if (idx - r >= 0) *(LAS bf16*)(lds + r * CST + (idx - r) * 2) = gb;
;         }
;     ...
;         static_assert(L == 256, "hyena_unit");
; #pragma unroll
;         for (int i = 0; i < 8; ++i)
; #pragma unroll
;             for (int j = 0; j < NTW; ++j) acc[j] = __builtin_amdgcn_mfma_f32_16x16x32_bf16(*(const LAS bf16x8*)(ap + (4 * i - 2 * j) * 16), zc[i], acc[j], 0, 0, 0);
;     }
; #pragma unroll
;     for (int j = 0; j < NTW; ++j) *(u32x2*)(YT + 16 * (w * NTW + j) + 4 * kg) = (u32x2){pk2(acc[j][0], acc[j][1]), pk2(acc[j][2], acc[j][3])};
;     __syncthreads();
.LBB0_2476:
	s_or_b64 exec, exec, s[26:27]
	v_bfe_u32 v34, v1, 4, 2
	v_lshlrev_b32_e32 v34, 3, v34
	v_cmp_gt_i32_e32 vcc, 16, v1
	s_and_saveexec_b64 s[26:27], vcc
	s_cbranch_execz .LBB0_2493
	v_mul_f32_e32 v41, v41, v43
	v_cvt_pk_bf16_f32 v41, v41, v41
	s_movk_i32 s0, 0xfdff
	v_lshrrev_b32_e32 v41, 16, v41
	v_cmp_lt_i32_e32 vcc, s0, v1
	s_and_saveexec_b64 s[28:29], vcc
	v_lshl_add_u32 v40, v40, 1, 0
	ds_write_b16 v40, v41
	s_or_b64 exec, exec, s[28:29]
	v_cmp_lt_i32_e32 vcc, s30, v1
	v_lshl_add_u32 v40, v1, 1, 0
	s_and_saveexec_b64 s[28:29], vcc
	ds_write_b16 v40, v41 offset:2110
	s_or_b64 exec, exec, s[28:29]
	v_cmp_lt_i32_e32 vcc, s36, v1
	s_and_saveexec_b64 s[28:29], vcc
	ds_write_b16 v40, v41 offset:3196
	s_or_b64 exec, exec, s[28:29]
	s_movk_i32 s0, 0xfe02
	v_cmp_lt_i32_e32 vcc, s0, v1
	s_and_saveexec_b64 s[28:29], vcc
	ds_write_b16 v40, v41 offset:4282
	s_or_b64 exec, exec, s[28:29]
	s_movk_i32 s0, 0xfe03
	v_cmp_lt_i32_e32 vcc, s0, v1
	s_and_saveexec_b64 s[28:29], vcc
	ds_write_b16 v40, v41 offset:5368
	s_or_b64 exec, exec, s[28:29]
	s_movk_i32 s0, 0xfe04
	v_cmp_lt_i32_e32 vcc, s0, v1
	s_and_saveexec_b64 s[28:29], vcc
	ds_write_b16 v40, v41 offset:6454
	s_or_b64 exec, exec, s[28:29]
	s_movk_i32 s0, 0xfe05
	v_cmp_lt_i32_e32 vcc, s0, v1
	s_and_saveexec_b64 s[28:29], vcc
	ds_write_b16 v40, v41 offset:7540
	s_or_b64 exec, exec, s[28:29]
	s_movk_i32 s0, 0xfe06
	v_cmp_lt_i32_e32 vcc, s0, v1
	s_and_b64 exec, exec, vcc
	ds_write_b16 v40, v41 offset:8626
.LBB0_2493:
	s_or_b64 exec, exec, s[26:27]
	v_sub_u32_e32 v38, v34, v38
	v_sub_u32_e32 v40, 0, v1
	v_lshlrev_b32_e32 v38, 1, v38
	v_and_b32_e32 v40, 7, v40
	v_and_b32_e32 v1, 0xffffffc0, v1
	v_and_b32_e32 v38, -16, v38
	v_mul_u32_u24_e32 v40, 0x440, v40
	v_sub_u32_e32 v1, v38, v1
	v_add3_u32 v1, 0, v40, v1
	s_waitcnt lgkmcnt(0)
	s_barrier
	ds_read_b128 v[40:43], v1 offset:480
	ds_read_b128 v[44:47], v1 offset:512
	s_waitcnt lgkmcnt(0)
	v_mfma_f32_16x16x32_bf16 v[44:47], v[44:47], v[30:33], 0
	v_mfma_f32_16x16x32_bf16 v[30:33], v[40:43], v[30:33], 0
	ds_read_b128 v[40:43], v1 offset:576
	s_waitcnt lgkmcnt(0)
	v_mfma_f32_16x16x32_bf16 v[40:43], v[40:43], v[26:29], v[44:47]
	s_nop 3
	ds_read_b128 v[44:47], v1 offset:544
	s_waitcnt lgkmcnt(0)
	v_mfma_f32_16x16x32_bf16 v[26:29], v[44:47], v[26:29], v[30:33]
	s_nop 2
	ds_read_b128 v[30:33], v1 offset:640
	s_waitcnt lgkmcnt(0)
	v_mfma_f32_16x16x32_bf16 v[30:33], v[30:33], v[22:25], v[40:43]
	s_nop 2
	ds_read_b128 v[40:43], v1 offset:608
	s_waitcnt lgkmcnt(0)
	v_mfma_f32_16x16x32_bf16 v[22:25], v[40:43], v[22:25], v[26:29]
	s_nop 2
	ds_read_b128 v[26:29], v1 offset:704
	s_waitcnt lgkmcnt(0)
	v_mfma_f32_16x16x32_bf16 v[26:29], v[26:29], v[18:21], v[30:33]
	s_nop 2
	ds_read_b128 v[30:33], v1 offset:672
	s_waitcnt lgkmcnt(0)
	v_mfma_f32_16x16x32_bf16 v[18:21], v[30:33], v[18:21], v[22:25]
	s_nop 2
	ds_read_b128 v[22:25], v1 offset:768
	s_waitcnt lgkmcnt(0)
	v_mfma_f32_16x16x32_bf16 v[22:25], v[22:25], v[14:17], v[26:29]
	s_nop 2
	ds_read_b128 v[26:29], v1 offset:736
	s_waitcnt lgkmcnt(0)
	v_mfma_f32_16x16x32_bf16 v[14:17], v[26:29], v[14:17], v[18:21]
	s_nop 2
	ds_read_b128 v[18:21], v1 offset:832
	s_waitcnt lgkmcnt(0)
	v_mfma_f32_16x16x32_bf16 v[18:21], v[18:21], v[10:13], v[22:25]
	s_nop 2
	ds_read_b128 v[22:25], v1 offset:800
	s_waitcnt lgkmcnt(0)
	v_mfma_f32_16x16x32_bf16 v[10:13], v[22:25], v[10:13], v[14:17]
	s_nop 2
	ds_read_b128 v[14:17], v1 offset:896
	s_waitcnt lgkmcnt(0)
	v_mfma_f32_16x16x32_bf16 v[14:17], v[14:17], v[6:9], v[18:21]
	s_nop 2
	ds_read_b128 v[18:21], v1 offset:864
	s_waitcnt lgkmcnt(0)
	v_mfma_f32_16x16x32_bf16 v[6:9], v[18:21], v[6:9], v[10:13]
	s_nop 2
	ds_read_b128 v[10:13], v1 offset:960
	s_waitcnt lgkmcnt(0)
	v_mfma_f32_16x16x32_bf16 v[10:13], v[10:13], v[2:5], v[14:17]
	s_nop 2
	ds_read_b128 v[14:17], v1 offset:928
	s_nop 3
	s_waitcnt lgkmcnt(0)
	v_mfma_f32_16x16x32_bf16 v[2:5], v[14:17], v[2:5], v[6:9]
	s_nop 1
	v_cvt_pk_bf16_f32 v10, v10, v11
	v_cvt_pk_bf16_f32 v11, v12, v13
	s_nop 3
	v_cvt_pk_bf16_f32 v2, v2, v3
	v_lshl_add_u64 v[6:7], v[36:37], 1, s[14:15]
	v_lshlrev_b32_e32 v8, 5, v39
	v_cvt_pk_bf16_f32 v1, v4, v4
	v_lshl_add_u64 v[6:7], v[6:7], 0, v[34:35]
	v_ashrrev_i32_e32 v9, 31, v8
	v_lshrrev_b32_e32 v1, 16, v1
	v_cvt_pk_bf16_f32 v3, v5, v5
	v_lshl_add_u64 v[6:7], v[8:9], 1, v[6:7]
	v_and_or_b32 v3, v3, s80, v1
	global_store_dwordx2 v[6:7], v[10:11], off
	global_store_dwordx2 v[6:7], v[2:3], off offset:32
	s_barrier
	s_mov_b64 s[14:15], -1

; #define LAS __attribute__((address_space(3)))
; __device__ __forceinline__ unsigned f2bf(float f) { unsigned u = __float_as_uint(f); return (u + 0x7fffu + ((u >> 16) & 1u)) >> 16; }
; template <int L>
; __device__ __forceinline__ void hyena_unit(CArgs& a, int l, int c, LAS unsigned char* lds) {
;     ...
;     s = wave_sum(s);
;     if (lane == 0) red[w] = s;
;     __syncthreads();
;     float l1 = 0.f;
; #pragma unroll
;     for (int i = 0; i < 8; ++i) l1 += red[i];
;     const float inv = 1.f / l1;
; #pragma unroll
;     for (int q = 0; q < NI; ++q) {
;         const int idx = tid + 512 * q;
;         const bf16 gb = (bf16)f2bf(gv[q] * inv);
;         if (idx < 2 * L + 16) {
; #pragma unroll
;             for (int r = 0; r < 8; ++r) if (idx - r >= 0) *(LAS bf16*)(lds + r * CST + (idx - r) * 2) = gb;
;         }
.LBB0_2497:
	s_or_b64 exec, exec, s[2:3]
	s_add_i32 s0, 0, 0x10200
	v_mov_b32_e32 v41, s0
	s_waitcnt lgkmcnt(0)
	s_barrier
	ds_read_b128 v[56:59], v41
	v_readlane_b32 s0, v250, 7
	s_waitcnt lgkmcnt(0)
	v_add_f32_e32 v41, 0, v56
	v_add_f32_e32 v41, v41, v57
	v_add_f32_e32 v41, v41, v58
	v_mov_b32_e32 v55, s0
	v_add_f32_e32 v41, v41, v59
	ds_read_b128 v[56:59], v55
	s_waitcnt lgkmcnt(0)
	v_add_f32_e32 v41, v41, v56
	v_add_f32_e32 v41, v41, v57
	v_add_f32_e32 v41, v41, v58
	v_add_f32_e32 v41, v41, v59
	v_div_scale_f32 v55, s[0:1], v41, v41, 1.0
	v_rcp_f32_e32 v56, v55
	s_movk_i32 s0, 0x1010
	v_fma_f32 v57, -v55, v56, 1.0
	v_fmac_f32_e32 v56, v57, v56
	v_div_scale_f32 v57, vcc, 1.0, v41, 1.0
	v_mul_f32_e32 v58, v57, v56
	v_fma_f32 v59, -v55, v58, v57
	v_fmac_f32_e32 v58, v59, v56
	v_fma_f32 v55, -v55, v58, v57
	v_div_fmas_f32 v55, v55, v56, v58
	v_div_fixup_f32 v41, v55, v41, 1.0
	v_cmp_gt_i32_e32 vcc, s0, v37
	s_and_saveexec_b64 s[2:3], vcc
	s_cbranch_execz .LBB0_2514
	v_mul_f32_e32 v34, v34, v41
	v_cvt_pk_bf16_f32 v34, v34, v34
	v_lshrrev_b32_e32 v34, 16, v34
	v_cmp_lt_i32_e32 vcc, -1, v37
	s_and_saveexec_b64 s[4:5], vcc
	s_cbranch_execz .LBB0_2506
	v_lshl_add_u32 v55, v37, 1, 0
	ds_write_b16 v55, v34
	s_or_b64 exec, exec, s[4:5]
	v_cmp_lt_i32_e32 vcc, 0, v37
	s_and_saveexec_b64 s[4:5], vcc
	s_cbranch_execnz .LBB0_2507

; #define LAS __attribute__((address_space(3)))
; __device__ __forceinline__ unsigned f2bf(float f) { unsigned u = __float_as_uint(f); return (u + 0x7fffu + ((u >> 16) & 1u)) >> 16; }
; template <int L>
; __device__ __forceinline__ void hyena_unit(CArgs& a, int l, int c, LAS unsigned char* lds) {
;     ...
; #pragma unroll
;     for (int q = 0; q < NI; ++q) {
;         const int idx = tid + 512 * q;
;         const bf16 gb = (bf16)f2bf(gv[q] * inv);
;         if (idx < 2 * L + 16) {
; #pragma unroll
;             for (int r = 0; r < 8; ++r) if (idx - r >= 0) *(LAS bf16*)(lds + r * CST + (idx - r) * 2) = gb;
;         }
.LBB0_2514:
	s_or_b64 exec, exec, s[2:3]
	v_bfe_u32 v34, v37, 4, 2
	s_movk_i32 s0, 0xe10
	v_lshlrev_b32_e32 v34, 3, v34
	v_cmp_gt_i32_e32 vcc, s0, v37
	s_and_saveexec_b64 s[2:3], vcc
	s_cbranch_execz .LBB0_2529
	v_mul_f32_e32 v54, v54, v41
	v_cvt_pk_bf16_f32 v54, v54, v54
	s_movk_i32 s0, 0xfdff
	v_lshrrev_b32_e32 v54, 16, v54
	v_cmp_lt_i32_e32 vcc, s0, v37
	s_and_saveexec_b64 s[4:5], vcc
	s_cbranch_execz .LBB0_2709
	v_lshl_add_u32 v52, v52, 1, 0
	ds_write_b16 v52, v54
	s_or_b64 exec, exec, s[4:5]
	v_cmp_lt_i32_e32 vcc, s30, v37
	s_and_saveexec_b64 s[4:5], vcc
	s_cbranch_execnz .LBB0_2710

; #define LAS __attribute__((address_space(3)))
; __device__ __forceinline__ unsigned f2bf(float f) { unsigned u = __float_as_uint(f); return (u + 0x7fffu + ((u >> 16) & 1u)) >> 16; }
; template <int L>
; __device__ __forceinline__ void hyena_unit(CArgs& a, int l, int c, LAS unsigned char* lds) {
;     ...
; #pragma unroll
;     for (int q = 0; q < NI; ++q) {
;         const int idx = tid + 512 * q;
;         const bf16 gb = (bf16)f2bf(gv[q] * inv);
;         if (idx < 2 * L + 16) {
; #pragma unroll
;             for (int r = 0; r < 8; ++r) if (idx - r >= 0) *(LAS bf16*)(lds + r * CST + (idx - r) * 2) = gb;
;         }
.LBB0_2529:
	s_or_b64 exec, exec, s[2:3]
	s_movk_i32 s0, 0xc10
	v_cmp_gt_i32_e32 vcc, s0, v37
	s_and_saveexec_b64 s[2:3], vcc
	s_cbranch_execz .LBB0_2546
	v_mul_f32_e32 v52, v53, v41
	v_cvt_pk_bf16_f32 v52, v52, v52
	s_movk_i32 s0, 0xfbff
	v_lshrrev_b32_e32 v52, 16, v52
	v_cmp_lt_i32_e32 vcc, s0, v37
	s_and_saveexec_b64 s[4:5], vcc
	v_lshl_add_u32 v50, v50, 1, 0
	ds_write_b16 v50, v52
	s_or_b64 exec, exec, s[4:5]
	s_movk_i32 s0, 0xfc00
	v_cmp_lt_i32_e32 vcc, s0, v37
	s_and_saveexec_b64 s[4:5], vcc
	v_lshl_add_u32 v50, v37, 1, 0
	ds_write_b16 v50, v52 offset:10302
	s_or_b64 exec, exec, s[4:5]
	s_movk_i32 s0, 0xfc01
	v_cmp_lt_i32_e32 vcc, s0, v37
	s_and_saveexec_b64 s[4:5], vcc
	v_lshl_add_u32 v50, v37, 1, 0
	ds_write_b16 v50, v52 offset:18556
	s_or_b64 exec, exec, s[4:5]
	s_movk_i32 s0, 0xfc02
	v_cmp_lt_i32_e32 vcc, s0, v37
	s_and_saveexec_b64 s[4:5], vcc
	v_lshl_add_u32 v50, v37, 1, 0
	ds_write_b16 v50, v52 offset:26810
	s_or_b64 exec, exec, s[4:5]
	s_movk_i32 s0, 0xfc03
	v_cmp_lt_i32_e32 vcc, s0, v37
	s_and_saveexec_b64 s[4:5], vcc
	v_lshl_add_u32 v50, v37, 1, 0
	ds_write_b16 v50, v52 offset:35064
	s_or_b64 exec, exec, s[4:5]
	s_movk_i32 s0, 0xfc04
	v_cmp_lt_i32_e32 vcc, s0, v37
	s_and_saveexec_b64 s[4:5], vcc
	v_lshl_add_u32 v50, v37, 1, 0
	ds_write_b16 v50, v52 offset:43318
	s_or_b64 exec, exec, s[4:5]
	s_movk_i32 s0, 0xfc05
	v_cmp_lt_i32_e32 vcc, s0, v37
	s_and_saveexec_b64 s[4:5], vcc
	v_lshl_add_u32 v50, v37, 1, 0
	ds_write_b16 v50, v52 offset:51572
	s_or_b64 exec, exec, s[4:5]
	s_movk_i32 s0, 0xfc06
	v_cmp_lt_i32_e32 vcc, s0, v37
	s_and_b64 exec, exec, vcc
	v_lshl_add_u32 v50, v37, 1, 0
	ds_write_b16 v50, v52 offset:59826
.LBB0_2546:
	s_or_b64 exec, exec, s[2:3]
	s_movk_i32 s0, 0xa10
	v_cmp_gt_i32_e32 vcc, s0, v37
	s_and_saveexec_b64 s[2:3], vcc
	s_cbranch_execz .LBB0_2563
	v_mul_f32_e32 v50, v51, v41
	v_cvt_pk_bf16_f32 v50, v50, v50
	s_movk_i32 s0, 0xf9ff
	v_lshrrev_b32_e32 v50, 16, v50
	v_cmp_lt_i32_e32 vcc, s0, v37
	s_and_saveexec_b64 s[4:5], vcc
	v_lshl_add_u32 v48, v48, 1, 0
	ds_write_b16 v48, v50
	s_or_b64 exec, exec, s[4:5]
	s_movk_i32 s0, 0xfa00
	v_cmp_lt_i32_e32 vcc, s0, v37
	s_and_saveexec_b64 s[4:5], vcc
	v_lshl_add_u32 v48, v37, 1, 0
	ds_write_b16 v48, v50 offset:11326
	s_or_b64 exec, exec, s[4:5]
	s_movk_i32 s0, 0xfa01
	v_cmp_lt_i32_e32 vcc, s0, v37
	s_and_saveexec_b64 s[4:5], vcc
	v_lshl_add_u32 v48, v37, 1, 0
	ds_write_b16 v48, v50 offset:19580
	s_or_b64 exec, exec, s[4:5]
	s_movk_i32 s0, 0xfa02
	v_cmp_lt_i32_e32 vcc, s0, v37
	s_and_saveexec_b64 s[4:5], vcc
	v_lshl_add_u32 v48, v37, 1, 0
	ds_write_b16 v48, v50 offset:27834
	s_or_b64 exec, exec, s[4:5]
	s_movk_i32 s0, 0xfa03
	v_cmp_lt_i32_e32 vcc, s0, v37
	s_and_saveexec_b64 s[4:5], vcc
	v_lshl_add_u32 v48, v37, 1, 0
	ds_write_b16 v48, v50 offset:36088
	s_or_b64 exec, exec, s[4:5]
	s_movk_i32 s0, 0xfa04
	v_cmp_lt_i32_e32 vcc, s0, v37
	s_and_saveexec_b64 s[4:5], vcc
	v_lshl_add_u32 v48, v37, 1, 0
	ds_write_b16 v48, v50 offset:44342
	s_or_b64 exec, exec, s[4:5]
	s_movk_i32 s0, 0xfa05
	v_cmp_lt_i32_e32 vcc, s0, v37
	s_and_saveexec_b64 s[4:5], vcc
	v_lshl_add_u32 v48, v37, 1, 0
	ds_write_b16 v48, v50 offset:52596
	s_or_b64 exec, exec, s[4:5]
	s_movk_i32 s0, 0xfa06
	v_cmp_lt_i32_e32 vcc, s0, v37
	s_and_b64 exec, exec, vcc
	v_lshl_add_u32 v48, v37, 1, 0
	ds_write_b16 v48, v50 offset:60850
.LBB0_2563:
	s_or_b64 exec, exec, s[2:3]
	s_movk_i32 s0, 0x810
	v_cmp_gt_i32_e32 vcc, s0, v37
	s_and_saveexec_b64 s[2:3], vcc
	s_cbranch_execz .LBB0_2580
	v_mul_f32_e32 v48, v49, v41
	v_cvt_pk_bf16_f32 v48, v48, v48
	s_movk_i32 s0, 0xf7ff
	v_lshrrev_b32_e32 v48, 16, v48
	v_cmp_lt_i32_e32 vcc, s0, v37
	s_and_saveexec_b64 s[4:5], vcc
	v_lshl_add_u32 v46, v46, 1, 0
	ds_write_b16 v46, v48
	s_or_b64 exec, exec, s[4:5]
	s_movk_i32 s0, 0xf800
	v_cmp_lt_i32_e32 vcc, s0, v37
	s_and_saveexec_b64 s[4:5], vcc
	v_lshl_add_u32 v46, v37, 1, 0
	ds_write_b16 v46, v48 offset:12350
	s_or_b64 exec, exec, s[4:5]
	s_movk_i32 s0, 0xf801
	v_cmp_lt_i32_e32 vcc, s0, v37
	s_and_saveexec_b64 s[4:5], vcc
	v_lshl_add_u32 v46, v37, 1, 0
	ds_write_b16 v46, v48 offset:20604
	s_or_b64 exec, exec, s[4:5]
	s_movk_i32 s0, 0xf802
	v_cmp_lt_i32_e32 vcc, s0, v37
	s_and_saveexec_b64 s[4:5], vcc
	v_lshl_add_u32 v46, v37, 1, 0
	ds_write_b16 v46, v48 offset:28858
	s_or_b64 exec, exec, s[4:5]
	s_movk_i32 s0, 0xf803
	v_cmp_lt_i32_e32 vcc, s0, v37
	s_and_saveexec_b64 s[4:5], vcc
	v_lshl_add_u32 v46, v37, 1, 0
	ds_write_b16 v46, v48 offset:37112
	s_or_b64 exec, exec, s[4:5]
	s_movk_i32 s0, 0xf804
	v_cmp_lt_i32_e32 vcc, s0, v37
	s_and_saveexec_b64 s[4:5], vcc
	v_lshl_add_u32 v46, v37, 1, 0
	ds_write_b16 v46, v48 offset:45366
	s_or_b64 exec, exec, s[4:5]
	s_movk_i32 s0, 0xf805
	v_cmp_lt_i32_e32 vcc, s0, v37
	s_and_saveexec_b64 s[4:5], vcc
	v_lshl_add_u32 v46, v37, 1, 0
	ds_write_b16 v46, v48 offset:53620
	s_or_b64 exec, exec, s[4:5]
	s_movk_i32 s0, 0xf806
	v_cmp_lt_i32_e32 vcc, s0, v37
	s_and_b64 exec, exec, vcc
	v_lshl_add_u32 v46, v37, 1, 0
	ds_write_b16 v46, v48 offset:61874
; #define LAS __attribute__((address_space(3)))
; __device__ __forceinline__ unsigned f2bf(float f) { unsigned u = __float_as_uint(f); return (u + 0x7fffu + ((u >> 16) & 1u)) >> 16; }
; template <int L>
; __device__ __forceinline__ void hyena_unit(CArgs& a, int l, int c, LAS unsigned char* lds) {
;     ...
; #pragma unroll
;     for (int q = 0; q < NI; ++q) {
;         const int idx = tid + 512 * q;
;         const bf16 gb = (bf16)f2bf(gv[q] * inv);
;         if (idx < 2 * L + 16) {
; #pragma unroll
;             for (int r = 0; r < 8; ++r) if (idx - r >= 0) *(LAS bf16*)(lds + r * CST + (idx - r) * 2) = gb;
;         }
.LBB0_2580:
	s_or_b64 exec, exec, s[2:3]
	s_movk_i32 s0, 0x610
	v_cmp_gt_i32_e32 vcc, s0, v37
	s_and_saveexec_b64 s[2:3], vcc
	s_cbranch_execz .LBB0_2597
	v_mul_f32_e32 v46, v47, v41
	v_cvt_pk_bf16_f32 v46, v46, v46
	s_movk_i32 s0, 0xf5ff
	v_lshrrev_b32_e32 v46, 16, v46
	v_cmp_lt_i32_e32 vcc, s0, v37
	s_and_saveexec_b64 s[4:5], vcc
	v_lshl_add_u32 v44, v44, 1, 0
	ds_write_b16 v44, v46
	s_or_b64 exec, exec, s[4:5]
	s_movk_i32 s0, 0xf600
	v_cmp_lt_i32_e32 vcc, s0, v37
	s_and_saveexec_b64 s[4:5], vcc
	v_lshl_add_u32 v44, v37, 1, 0
	ds_write_b16 v44, v46 offset:13374
	s_or_b64 exec, exec, s[4:5]
	s_movk_i32 s0, 0xf601
	v_cmp_lt_i32_e32 vcc, s0, v37
	s_and_saveexec_b64 s[4:5], vcc
	v_lshl_add_u32 v44, v37, 1, 0
	ds_write_b16 v44, v46 offset:21628
	s_or_b64 exec, exec, s[4:5]
	s_movk_i32 s0, 0xf602
	v_cmp_lt_i32_e32 vcc, s0, v37
	s_and_saveexec_b64 s[4:5], vcc
	v_lshl_add_u32 v44, v37, 1, 0
	ds_write_b16 v44, v46 offset:29882
	s_or_b64 exec, exec, s[4:5]
	s_movk_i32 s0, 0xf603
	v_cmp_lt_i32_e32 vcc, s0, v37
	s_and_saveexec_b64 s[4:5], vcc
	v_lshl_add_u32 v44, v37, 1, 0
	ds_write_b16 v44, v46 offset:38136
	s_or_b64 exec, exec, s[4:5]
	s_movk_i32 s0, 0xf604
	v_cmp_lt_i32_e32 vcc, s0, v37
	s_and_saveexec_b64 s[4:5], vcc
	v_lshl_add_u32 v44, v37, 1, 0
	ds_write_b16 v44, v46 offset:46390
	s_or_b64 exec, exec, s[4:5]
	s_movk_i32 s0, 0xf605
	v_cmp_lt_i32_e32 vcc, s0, v37
	s_and_saveexec_b64 s[4:5], vcc
	v_lshl_add_u32 v44, v37, 1, 0
	ds_write_b16 v44, v46 offset:54644
	s_or_b64 exec, exec, s[4:5]
	s_movk_i32 s0, 0xf606
	v_cmp_lt_i32_e32 vcc, s0, v37
	s_and_b64 exec, exec, vcc
	v_lshl_add_u32 v44, v37, 1, 0
	ds_write_b16 v44, v46 offset:62898
.LBB0_2597:
	s_or_b64 exec, exec, s[2:3]
	s_movk_i32 s0, 0x410
	v_cmp_gt_i32_e32 vcc, s0, v37
	s_and_saveexec_b64 s[2:3], vcc
	s_cbranch_execz .LBB0_2614
	v_mul_f32_e32 v44, v45, v41
	v_cvt_pk_bf16_f32 v44, v44, v44
	s_movk_i32 s0, 0xf3ff
	v_lshrrev_b32_e32 v44, 16, v44
	v_cmp_lt_i32_e32 vcc, s0, v37
	s_and_saveexec_b64 s[4:5], vcc
	v_lshl_add_u32 v42, v42, 1, 0
	ds_write_b16 v42, v44
	s_or_b64 exec, exec, s[4:5]
	s_movk_i32 s0, 0xf400
	v_cmp_lt_i32_e32 vcc, s0, v37
	s_and_saveexec_b64 s[4:5], vcc
	v_lshl_add_u32 v42, v37, 1, 0
	ds_write_b16 v42, v44 offset:14398
	s_or_b64 exec, exec, s[4:5]
	s_movk_i32 s0, 0xf401
	v_cmp_lt_i32_e32 vcc, s0, v37
	s_and_saveexec_b64 s[4:5], vcc
	v_lshl_add_u32 v42, v37, 1, 0
	ds_write_b16 v42, v44 offset:22652
	s_or_b64 exec, exec, s[4:5]
	s_movk_i32 s0, 0xf402
	v_cmp_lt_i32_e32 vcc, s0, v37
	s_and_saveexec_b64 s[4:5], vcc
	v_lshl_add_u32 v42, v37, 1, 0
	ds_write_b16 v42, v44 offset:30906
	s_or_b64 exec, exec, s[4:5]
	s_movk_i32 s0, 0xf403
	v_cmp_lt_i32_e32 vcc, s0, v37
	s_and_saveexec_b64 s[4:5], vcc
	v_lshl_add_u32 v42, v37, 1, 0
	ds_write_b16 v42, v44 offset:39160
	s_or_b64 exec, exec, s[4:5]
	s_movk_i32 s0, 0xf404
	v_cmp_lt_i32_e32 vcc, s0, v37
	s_and_saveexec_b64 s[4:5], vcc
	v_lshl_add_u32 v42, v37, 1, 0
	ds_write_b16 v42, v44 offset:47414
	s_or_b64 exec, exec, s[4:5]
	s_movk_i32 s0, 0xf405
	v_cmp_lt_i32_e32 vcc, s0, v37
	s_and_saveexec_b64 s[4:5], vcc
	v_lshl_add_u32 v42, v37, 1, 0
	ds_write_b16 v42, v44 offset:55668
	s_or_b64 exec, exec, s[4:5]
	s_movk_i32 s0, 0xf406
	v_cmp_lt_i32_e32 vcc, s0, v37
	s_and_b64 exec, exec, vcc
	v_lshl_add_u32 v42, v37, 1, 0
	ds_write_b16 v42, v44 offset:63922
.LBB0_2614:
	s_or_b64 exec, exec, s[2:3]
	v_cmp_gt_i32_e32 vcc, s23, v37
	s_and_saveexec_b64 s[2:3], vcc
	s_cbranch_execz .LBB0_2631
	v_mul_f32_e32 v42, v43, v41
	v_cvt_pk_bf16_f32 v42, v42, v42
	s_movk_i32 s0, 0xf1ff
	v_lshrrev_b32_e32 v42, 16, v42
	v_cmp_lt_i32_e32 vcc, s0, v37
	s_and_saveexec_b64 s[4:5], vcc
	v_lshl_add_u32 v40, v40, 1, 0
	ds_write_b16 v40, v42
	s_or_b64 exec, exec, s[4:5]
	s_movk_i32 s0, 0xf200
	v_cmp_lt_i32_e32 vcc, s0, v37
	s_and_saveexec_b64 s[4:5], vcc
	v_lshl_add_u32 v40, v37, 1, 0
	ds_write_b16 v40, v42 offset:15422
	s_or_b64 exec, exec, s[4:5]
	s_movk_i32 s0, 0xf201
	v_cmp_lt_i32_e32 vcc, s0, v37
	s_and_saveexec_b64 s[4:5], vcc
	v_lshl_add_u32 v40, v37, 1, 0
	ds_write_b16 v40, v42 offset:23676
	s_or_b64 exec, exec, s[4:5]
	s_movk_i32 s0, 0xf202
	v_cmp_lt_i32_e32 vcc, s0, v37
	s_and_saveexec_b64 s[4:5], vcc
	v_lshl_add_u32 v40, v37, 1, 0
	ds_write_b16 v40, v42 offset:31930
	s_or_b64 exec, exec, s[4:5]
	s_movk_i32 s0, 0xf203
	v_cmp_lt_i32_e32 vcc, s0, v37
	s_and_saveexec_b64 s[4:5], vcc
	v_lshl_add_u32 v40, v37, 1, 0
	ds_write_b16 v40, v42 offset:40184
	s_or_b64 exec, exec, s[4:5]
	s_movk_i32 s0, 0xf204
	v_cmp_lt_i32_e32 vcc, s0, v37
	s_and_saveexec_b64 s[4:5], vcc
	v_lshl_add_u32 v40, v37, 1, 0
	ds_write_b16 v40, v42 offset:48438
	s_or_b64 exec, exec, s[4:5]
	s_movk_i32 s0, 0xf205
	v_cmp_lt_i32_e32 vcc, s0, v37
	s_and_saveexec_b64 s[4:5], vcc
	v_lshl_add_u32 v40, v37, 1, 0
	ds_write_b16 v40, v42 offset:56692
	s_or_b64 exec, exec, s[4:5]
	s_movk_i32 s0, 0xf206
	v_cmp_lt_i32_e32 vcc, s0, v37
	s_and_b64 exec, exec, vcc
	v_lshl_add_u32 v40, v37, 1, 0
	ds_write_b16 v40, v42 offset:64946
.LBB0_2631:
	s_or_b64 exec, exec, s[2:3]
	v_cmp_gt_i32_e32 vcc, 16, v37
	s_and_saveexec_b64 s[2:3], vcc
	s_cbranch_execz .LBB0_2648
	v_mul_f32_e32 v39, v39, v41
	v_cvt_pk_bf16_f32 v39, v39, v39
	s_movk_i32 s0, 0xefff
	v_lshrrev_b32_e32 v39, 16, v39
	v_cmp_lt_i32_e32 vcc, s0, v37
	s_and_saveexec_b64 s[4:5], vcc
	v_lshl_add_u32 v38, v38, 1, 0
	ds_write_b16 v38, v39
	s_or_b64 exec, exec, s[4:5]
	v_cmp_lt_i32_e32 vcc, s31, v37
	v_lshl_add_u32 v38, v37, 1, 0
	s_and_saveexec_b64 s[4:5], vcc
	ds_write_b16 v38, v39 offset:16446
	s_or_b64 exec, exec, s[4:5]
	s_movk_i32 s0, 0xf001
	v_cmp_lt_i32_e32 vcc, s0, v37
	s_and_saveexec_b64 s[4:5], vcc
	ds_write_b16 v38, v39 offset:24700
	s_or_b64 exec, exec, s[4:5]
	s_movk_i32 s0, 0xf002
	v_cmp_lt_i32_e32 vcc, s0, v37
	s_and_saveexec_b64 s[4:5], vcc
	ds_write_b16 v38, v39 offset:32954
	s_or_b64 exec, exec, s[4:5]
	s_movk_i32 s0, 0xf003
	v_cmp_lt_i32_e32 vcc, s0, v37
	s_and_saveexec_b64 s[4:5], vcc
	ds_write_b16 v38, v39 offset:41208
	s_or_b64 exec, exec, s[4:5]
	s_movk_i32 s0, 0xf004
	v_cmp_lt_i32_e32 vcc, s0, v37
	s_and_saveexec_b64 s[4:5], vcc
	ds_write_b16 v38, v39 offset:49462
	s_or_b64 exec, exec, s[4:5]
	s_movk_i32 s0, 0xf005
	v_cmp_lt_i32_e32 vcc, s0, v37
	s_and_saveexec_b64 s[4:5], vcc
	ds_write_b16 v38, v39 offset:57716
	s_or_b64 exec, exec, s[4:5]
	s_movk_i32 s0, 0xf006
	v_cmp_lt_i32_e32 vcc, s0, v37
	s_and_b64 exec, exec, vcc
	v_add_u32_e32 v38, 0x101b2, v38
	ds_write_b16 v38, v39

; #define LAS __attribute__((address_space(3)))
; template <int L>
; __device__ __forceinline__ void hyena_unit(CArgs& a, int l, int c, LAS unsigned char* lds) {
;     ...
;         for (int ib = 0; ib < 8; ++ib) {
;             const bf16* zq = zp + 256 * (ib < 7 ? ib + 1 : 7);
; #pragma unroll
;             for (int ii = 0; ii < 8; ++ii) zn[ii] = *(const bf16x8*)(zq + 32 * ii);
; #pragma unroll
;             for (int ii = 0; ii < 8; ++ii) {
;                 A[(16 - 2 * ii) & 15] = *(const LAS bf16x8*)(ap + 64 * ii);
;                 A[(17 - 2 * ii) & 15] = *(const LAS bf16x8*)(ap + 64 * ii - 32);
; #pragma unroll
;                 for (int jj = 0; jj < 16; ++jj) { const int j = (jj + 2) & 15; acc[j] = __builtin_amdgcn_mfma_f32_16x16x32_bf16(A[(j + 16 - 2 * ii) & 15], zc[ii], acc[j], 0, 0, 0); }
;             }
;             ap += 512;
; #pragma unroll
;             for (int ii = 0; ii < 8; ++ii) zc[ii] = zn[ii];
;         }
.LBB0_2649:
	s_waitcnt vmcnt(1) lgkmcnt(1)
	s_nop 0
	v_mfma_f32_16x16x32_bf16 v[44:47], v[56:59], v[30:33], v[44:47]
	s_cmpk_lg_i32 s0, 0x800
	s_cselect_b32 s78, s0, 0x700
	s_addk_i32 s0, 0x100
	v_mfma_f32_16x16x32_bf16 v[36:39], v[80:83], v[30:33], v[36:39]
	s_cmpk_lg_i32 s0, 0x900
	v_mfma_f32_16x16x32_bf16 v[44:47], v[80:83], v[26:29], v[44:47]
	v_mfma_f32_16x16x32_bf16 v[136:139], v[88:91], v[30:33], v[136:139]
	v_mfma_f32_16x16x32_bf16 v[132:135], v[84:87], v[30:33], v[132:135]
	v_mfma_f32_16x16x32_bf16 v[128:131], v[104:107], v[30:33], v[128:131]
	v_mfma_f32_16x16x32_bf16 v[124:127], v[96:99], v[30:33], v[124:127]
	v_mfma_f32_16x16x32_bf16 v[48:51], v[112:115], v[30:33], v[48:51]
	v_mfma_f32_16x16x32_bf16 v[36:39], v[112:115], v[26:29], v[36:39]
	v_mfma_f32_16x16x32_bf16 v[44:47], v[112:115], v[22:25], v[44:47]
	v_subrev_u32_e32 v112, 32, v161
	s_waitcnt lgkmcnt(0)
	v_mfma_f32_16x16x32_bf16 v[52:55], v[60:63], v[30:33], v[52:55]
	v_mfma_f32_16x16x32_bf16 v[56:59], v[72:75], v[26:29], v[136:139]
	v_mfma_f32_16x16x32_bf16 v[60:63], v[68:71], v[26:29], v[132:135]
	s_nop 1
	ds_read_b128 v[136:139], v112
	ds_read_b128 v[132:135], v161
	v_mfma_f32_16x16x32_bf16 v[128:131], v[88:91], v[26:29], v[128:131]
	v_mfma_f32_16x16x32_bf16 v[124:127], v[84:87], v[26:29], v[124:127]
	v_mfma_f32_16x16x32_bf16 v[140:143], v[68:71], v[30:33], v[140:143]
	v_mfma_f32_16x16x32_bf16 v[40:43], v[76:79], v[30:33], v[40:43]
	v_mfma_f32_16x16x32_bf16 v[52:55], v[76:79], v[26:29], v[52:55]
	v_mfma_f32_16x16x32_bf16 v[76:79], v[72:75], v[22:25], v[128:131]
	v_mfma_f32_16x16x32_bf16 v[80:83], v[68:71], v[22:25], v[124:127]
	v_mfma_f32_16x16x32_bf16 v[144:147], v[72:75], v[30:33], v[144:147]
	s_waitcnt lgkmcnt(0)
	v_mfma_f32_16x16x32_bf16 v[124:127], v[132:135], v[22:25], v[56:59]
	v_mfma_f32_16x16x32_bf16 v[128:131], v[136:139], v[26:29], v[140:143]
	v_mfma_f32_16x16x32_bf16 v[140:143], v[136:139], v[22:25], v[60:63]
	s_nop 2
	ds_read_b128 v[60:63], v161 offset:64
	ds_read_b128 v[56:59], v161 offset:32
	v_mfma_f32_16x16x32_bf16 v[120:123], v[100:103], v[30:33], v[120:123]
	v_mfma_f32_16x16x32_bf16 v[92:95], v[108:111], v[30:33], v[92:95]
	v_mfma_f32_16x16x32_bf16 v[64:67], v[116:119], v[30:33], v[64:67]
	v_mfma_f32_16x16x32_bf16 v[40:43], v[116:119], v[26:29], v[40:43]
	v_mfma_f32_16x16x32_bf16 v[52:55], v[116:119], v[22:25], v[52:55]
	v_mfma_f32_16x16x32_bf16 v[112:115], v[132:135], v[30:33], v[148:151]
	v_mfma_f32_16x16x32_bf16 v[30:33], v[136:139], v[30:33], v[152:155]
	v_mfma_f32_16x16x32_bf16 v[76:79], v[132:135], v[18:21], v[76:79]
	v_mfma_f32_16x16x32_bf16 v[80:83], v[136:139], v[18:21], v[80:83]
	v_mfma_f32_16x16x32_bf16 v[116:119], v[132:135], v[26:29], v[144:147]
	v_mfma_f32_16x16x32_bf16 v[120:123], v[104:107], v[26:29], v[120:123]
	v_mfma_f32_16x16x32_bf16 v[92:95], v[96:99], v[26:29], v[92:95]
	v_mfma_f32_16x16x32_bf16 v[64:67], v[100:103], v[26:29], v[64:67]
	v_mfma_f32_16x16x32_bf16 v[48:51], v[108:111], v[26:29], v[48:51]
	v_mfma_f32_16x16x32_bf16 v[40:43], v[100:103], v[22:25], v[40:43]
	v_mfma_f32_16x16x32_bf16 v[52:55], v[100:103], v[18:21], v[52:55]
	s_waitcnt lgkmcnt(1)
	v_mfma_f32_16x16x32_bf16 v[100:103], v[60:63], v[26:29], v[112:115]
	v_mfma_f32_16x16x32_bf16 v[112:115], v[60:63], v[18:21], v[124:127]
	s_waitcnt lgkmcnt(0)
	v_mfma_f32_16x16x32_bf16 v[26:29], v[56:59], v[26:29], v[30:33]
	v_mfma_f32_16x16x32_bf16 v[30:33], v[56:59], v[22:25], v[128:131]
	v_mfma_f32_16x16x32_bf16 v[124:127], v[60:63], v[14:17], v[76:79]
	v_mfma_f32_16x16x32_bf16 v[128:131], v[56:59], v[14:17], v[80:83]
	s_nop 1
	ds_read_b128 v[76:79], v161 offset:128
	ds_read_b128 v[80:83], v161 offset:96
	v_mfma_f32_16x16x32_bf16 v[36:39], v[108:111], v[22:25], v[36:39]
	v_mfma_f32_16x16x32_bf16 v[44:47], v[108:111], v[18:21], v[44:47]
	v_mfma_f32_16x16x32_bf16 v[108:111], v[60:63], v[22:25], v[116:119]
	v_mfma_f32_16x16x32_bf16 v[116:119], v[56:59], v[18:21], v[140:143]
	v_mfma_f32_16x16x32_bf16 v[120:123], v[88:91], v[22:25], v[120:123]
	v_mfma_f32_16x16x32_bf16 v[92:95], v[84:87], v[22:25], v[92:95]
	v_mfma_f32_16x16x32_bf16 v[64:67], v[104:107], v[22:25], v[64:67]
	v_mfma_f32_16x16x32_bf16 v[48:51], v[96:99], v[22:25], v[48:51]
	v_mfma_f32_16x16x32_bf16 v[40:43], v[104:107], v[18:21], v[40:43]
	v_mfma_f32_16x16x32_bf16 v[36:39], v[96:99], v[18:21], v[36:39]
	v_mfma_f32_16x16x32_bf16 v[52:55], v[104:107], v[14:17], v[52:55]
	v_mfma_f32_16x16x32_bf16 v[44:47], v[96:99], v[14:17], v[44:47]
	s_waitcnt lgkmcnt(1)
	v_mfma_f32_16x16x32_bf16 v[96:99], v[76:79], v[22:25], v[100:103]
	v_mfma_f32_16x16x32_bf16 v[104:107], v[76:79], v[14:17], v[112:115]
	s_waitcnt lgkmcnt(0)
	v_mfma_f32_16x16x32_bf16 v[22:25], v[80:83], v[22:25], v[26:29]
	v_mfma_f32_16x16x32_bf16 v[26:29], v[80:83], v[18:21], v[30:33]
	v_mfma_f32_16x16x32_bf16 v[30:33], v[80:83], v[14:17], v[116:119]
	s_nop 2
	ds_read_b128 v[116:119], v161 offset:192
	ds_read_b128 v[112:115], v161 offset:160
	v_mfma_f32_16x16x32_bf16 v[100:103], v[76:79], v[18:21], v[108:111]
	v_mfma_f32_16x16x32_bf16 v[108:111], v[76:79], v[10:13], v[124:127]
	v_mfma_f32_16x16x32_bf16 v[124:127], v[80:83], v[10:13], v[128:131]
	v_mfma_f32_16x16x32_bf16 v[120:123], v[72:75], v[18:21], v[120:123]
	v_mfma_f32_16x16x32_bf16 v[92:95], v[68:71], v[18:21], v[92:95]
	v_mfma_f32_16x16x32_bf16 v[64:67], v[88:91], v[18:21], v[64:67]
	v_mfma_f32_16x16x32_bf16 v[48:51], v[84:87], v[18:21], v[48:51]
	v_mfma_f32_16x16x32_bf16 v[40:43], v[88:91], v[14:17], v[40:43]
	v_mfma_f32_16x16x32_bf16 v[36:39], v[84:87], v[14:17], v[36:39]
	v_mfma_f32_16x16x32_bf16 v[52:55], v[88:91], v[10:13], v[52:55]
	v_mfma_f32_16x16x32_bf16 v[44:47], v[84:87], v[10:13], v[44:47]
	s_waitcnt lgkmcnt(1)
; #define LAS __attribute__((address_space(3)))
; template <int L>
; __device__ __forceinline__ void hyena_unit(CArgs& a, int l, int c, LAS unsigned char* lds) {
;     ...
;         for (int ib = 0; ib < 8; ++ib) {
;             const bf16* zq = zp + 256 * (ib < 7 ? ib + 1 : 7);
; #pragma unroll
;             for (int ii = 0; ii < 8; ++ii) zn[ii] = *(const bf16x8*)(zq + 32 * ii);
; #pragma unroll
;             for (int ii = 0; ii < 8; ++ii) {
;                 A[(16 - 2 * ii) & 15] = *(const LAS bf16x8*)(ap + 64 * ii);
;                 A[(17 - 2 * ii) & 15] = *(const LAS bf16x8*)(ap + 64 * ii - 32);
; #pragma unroll
;                 for (int jj = 0; jj < 16; ++jj) { const int j = (jj + 2) & 15; acc[j] = __builtin_amdgcn_mfma_f32_16x16x32_bf16(A[(j + 16 - 2 * ii) & 15], zc[ii], acc[j], 0, 0, 0); }
;             }
;             ap += 512;
; #pragma unroll
;             for (int ii = 0; ii < 8; ++ii) zc[ii] = zn[ii];
;         }
	v_mfma_f32_16x16x32_bf16 v[84:87], v[116:119], v[18:21], v[96:99]
	v_mfma_f32_16x16x32_bf16 v[88:91], v[116:119], v[14:17], v[100:103]
	s_waitcnt lgkmcnt(0)
	v_mfma_f32_16x16x32_bf16 v[18:21], v[112:115], v[18:21], v[22:25]
	v_mfma_f32_16x16x32_bf16 v[22:25], v[112:115], v[14:17], v[26:29]
	v_mfma_f32_16x16x32_bf16 v[26:29], v[112:115], v[10:13], v[30:33]
	v_mfma_f32_16x16x32_bf16 v[30:33], v[116:119], v[6:9], v[108:111]
	ds_read_b128 v[100:103], v161 offset:256
	s_nop 1
	ds_read_b128 v[108:111], v161 offset:224
	v_mfma_f32_16x16x32_bf16 v[96:99], v[116:119], v[10:13], v[104:107]
	v_mfma_f32_16x16x32_bf16 v[104:107], v[112:115], v[6:9], v[124:127]
	v_mfma_f32_16x16x32_bf16 v[48:51], v[68:71], v[14:17], v[48:51]
	v_mfma_f32_16x16x32_bf16 v[36:39], v[68:71], v[10:13], v[36:39]
	v_mfma_f32_16x16x32_bf16 v[44:47], v[68:71], v[6:9], v[44:47]
	s_waitcnt lgkmcnt(1)
	v_mfma_f32_16x16x32_bf16 v[68:71], v[100:103], v[14:17], v[84:87]
	v_mfma_f32_16x16x32_bf16 v[84:87], v[100:103], v[6:9], v[96:99]
	s_waitcnt vmcnt(0) lgkmcnt(0)
	v_mfma_f32_16x16x32_bf16 v[124:127], v[108:111], v[2:5], v[104:107]
	s_nop 2
	ds_read_b128 v[104:107], v161 offset:320
	ds_read_b128 v[96:99], v161 offset:288
	v_mfma_f32_16x16x32_bf16 v[120:123], v[132:135], v[14:17], v[120:123]
	v_mfma_f32_16x16x32_bf16 v[92:95], v[136:139], v[14:17], v[92:95]
	v_mfma_f32_16x16x32_bf16 v[64:67], v[72:75], v[14:17], v[64:67]
	v_mfma_f32_16x16x32_bf16 v[14:17], v[108:111], v[14:17], v[18:21]
	v_mfma_f32_16x16x32_bf16 v[18:21], v[108:111], v[10:13], v[22:25]
	v_mfma_f32_16x16x32_bf16 v[22:25], v[108:111], v[6:9], v[26:29]
	s_waitcnt lgkmcnt(1)
	v_mfma_f32_16x16x32_bf16 v[26:29], v[104:107], v[10:13], v[68:71]
	s_nop 2
	v_lshl_add_u64 v[68:69], s[78:79], 1, v[158:159]
	v_mfma_f32_16x16x32_bf16 v[120:123], v[60:63], v[10:13], v[120:123]
	v_mfma_f32_16x16x32_bf16 v[92:95], v[56:59], v[10:13], v[92:95]
	v_mfma_f32_16x16x32_bf16 v[64:67], v[132:135], v[10:13], v[64:67]
	v_mfma_f32_16x16x32_bf16 v[48:51], v[136:139], v[10:13], v[48:51]
	v_mfma_f32_16x16x32_bf16 v[40:43], v[72:75], v[10:13], v[40:43]
	v_mfma_f32_16x16x32_bf16 v[52:55], v[72:75], v[6:9], v[52:55]
	v_mfma_f32_16x16x32_bf16 v[72:75], v[100:103], v[10:13], v[88:91]
	s_waitcnt lgkmcnt(0)
	v_mfma_f32_16x16x32_bf16 v[10:13], v[96:99], v[10:13], v[14:17]
	s_nop 2
	global_load_dwordx4 v[14:17], v[68:69], off
	v_mfma_f32_16x16x32_bf16 v[36:39], v[136:139], v[6:9], v[36:39]
	global_load_dwordx4 v[170:173], v[68:69], off offset:64
	global_load_dwordx4 v[174:177], v[68:69], off offset:128
	global_load_dwordx4 v[178:181], v[68:69], off offset:192
	v_mfma_f32_16x16x32_bf16 v[44:47], v[136:139], v[2:5], v[44:47]
	v_mfma_f32_16x16x32_bf16 v[136:139], v[104:107], v[2:5], v[84:87]
	ds_read_b128 v[88:91], v161 offset:384
	s_nop 1
	ds_read_b128 v[84:87], v161 offset:352
	global_load_dwordx4 v[182:185], v[68:69], off offset:256
	global_load_dwordx4 v[186:189], v[68:69], off offset:320
	global_load_dwordx4 v[202:205], v[68:69], off offset:384
	global_load_dwordx4 v[206:209], v[68:69], off offset:448
	v_mfma_f32_16x16x32_bf16 v[128:131], v[100:103], v[2:5], v[30:33]
	ds_read_b128 v[68:71], v161 offset:416
	v_mfma_f32_16x16x32_bf16 v[30:33], v[104:107], v[6:9], v[72:75]
	s_nop 2
	ds_read_b128 v[72:75], v161 offset:448
	v_mfma_f32_16x16x32_bf16 v[120:123], v[76:79], v[6:9], v[120:123]
	v_add_u32_e32 v161, 0x200, v161
	v_mfma_f32_16x16x32_bf16 v[92:95], v[80:83], v[6:9], v[92:95]
	v_mfma_f32_16x16x32_bf16 v[64:67], v[60:63], v[6:9], v[64:67]
	v_mfma_f32_16x16x32_bf16 v[48:51], v[56:59], v[6:9], v[48:51]
	v_mfma_f32_16x16x32_bf16 v[40:43], v[132:135], v[6:9], v[40:43]
	v_mfma_f32_16x16x32_bf16 v[52:55], v[132:135], v[2:5], v[52:55]
	v_mfma_f32_16x16x32_bf16 v[18:21], v[96:99], v[6:9], v[18:21]
	v_mfma_f32_16x16x32_bf16 v[132:135], v[96:99], v[2:5], v[22:25]
	s_waitcnt lgkmcnt(3)
	v_mfma_f32_16x16x32_bf16 v[22:25], v[88:91], v[6:9], v[26:29]
	s_waitcnt lgkmcnt(2)
	v_mfma_f32_16x16x32_bf16 v[6:9], v[84:87], v[6:9], v[10:13]
	s_waitcnt vmcnt(6)
	v_mov_b64_e32 v[26:27], v[170:171]
	v_mfma_f32_16x16x32_bf16 v[120:123], v[116:119], v[2:5], v[120:123]
	v_mov_b64_e32 v[28:29], v[172:173]
	s_waitcnt vmcnt(2)
	v_mov_b64_e32 v[10:11], v[186:187]
	v_mfma_f32_16x16x32_bf16 v[92:95], v[112:115], v[2:5], v[92:95]
	v_mov_b64_e32 v[12:13], v[188:189]
	v_mfma_f32_16x16x32_bf16 v[64:67], v[76:79], v[2:5], v[64:67]
	v_mfma_f32_16x16x32_bf16 v[48:51], v[80:83], v[2:5], v[48:51]
	v_mfma_f32_16x16x32_bf16 v[40:43], v[60:63], v[2:5], v[40:43]
	v_mfma_f32_16x16x32_bf16 v[36:39], v[56:59], v[2:5], v[36:39]
	v_mfma_f32_16x16x32_bf16 v[144:147], v[88:91], v[2:5], v[30:33]
	v_mfma_f32_16x16x32_bf16 v[140:143], v[84:87], v[2:5], v[18:21]
	s_nop 1
	v_mov_b64_e32 v[32:33], v[16:17]
	v_mov_b64_e32 v[30:31], v[14:15]
	v_mov_b64_e32 v[14:15], v[182:183]
	s_waitcnt lgkmcnt(0)
	v_mfma_f32_16x16x32_bf16 v[148:151], v[72:75], v[2:5], v[22:25]
	v_mov_b64_e32 v[18:19], v[178:179]
	v_mov_b64_e32 v[20:21], v[180:181]
	v_mov_b64_e32 v[16:17], v[184:185]
	v_mfma_f32_16x16x32_bf16 v[152:155], v[68:71], v[2:5], v[6:9]
	v_mov_b64_e32 v[22:23], v[174:175]
	s_waitcnt vmcnt(0)
	v_mov_b64_e32 v[2:3], v[206:207]
	v_mov_b64_e32 v[24:25], v[176:177]
	v_mov_b64_e32 v[6:7], v[202:203]
	v_mov_b64_e32 v[8:9], v[204:205]
	v_mov_b64_e32 v[4:5], v[208:209]
	s_cbranch_scc1 .LBB0_2649
; __device__ __forceinline__ unsigned pk2(float lo, float hi) { return f2bf(lo) | (f2bf(hi) << 16); }
; template <int L>
; __device__ __forceinline__ void hyena_unit(CArgs& a, int l, int c, LAS unsigned char* lds) {
;     ...
;     for (int j = 0; j < NTW; ++j) *(u32x2*)(YT + 16 * (w * NTW + j) + 4 * kg) = (u32x2){pk2(acc[j][0], acc[j][1]), pk2(acc[j][2], acc[j][3])};
;     __syncthreads();
	v_lshlrev_b32_e32 v2, 8, v1
	v_cvt_pk_bf16_f32 v6, v148, v149
	v_lshl_add_u64 v[4:5], v[156:157], 0, v[34:35]
	v_cvt_pk_bf16_f32 v7, v150, v151
	v_ashrrev_i32_e32 v3, 31, v2
	v_lshl_add_u64 v[2:3], v[2:3], 1, v[4:5]
	s_mov_b64 s[0:1], 0x50400200
	v_lshl_add_u64 v[4:5], v[2:3], 0, s[0:1]
	s_mov_b32 s0, 0x50400000
	v_add_co_u32_e32 v2, vcc, s0, v2
	s_nop 0
	s_nop 0
	v_addc_co_u32_e32 v3, vcc, 0, v3, vcc
	global_store_dwordx2 v[2:3], v[6:7], off offset:512
	v_cvt_pk_bf16_f32 v2, v152, v153
	v_cvt_pk_bf16_f32 v3, v154, v155
	global_store_dwordx2 v[4:5], v[2:3], off offset:32
	v_cvt_pk_bf16_f32 v2, v144, v145
	v_cvt_pk_bf16_f32 v3, v146, v147
	global_store_dwordx2 v[4:5], v[2:3], off offset:64
	v_cvt_pk_bf16_f32 v2, v140, v141
	v_cvt_pk_bf16_f32 v3, v142, v143
	global_store_dwordx2 v[4:5], v[2:3], off offset:96
	v_cvt_pk_bf16_f32 v2, v136, v137
	v_cvt_pk_bf16_f32 v3, v138, v139
	global_store_dwordx2 v[4:5], v[2:3], off offset:128
	v_cvt_pk_bf16_f32 v2, v132, v133
	v_cvt_pk_bf16_f32 v3, v134, v135
	global_store_dwordx2 v[4:5], v[2:3], off offset:160
	v_cvt_pk_bf16_f32 v2, v128, v129
	v_cvt_pk_bf16_f32 v3, v130, v131
	global_store_dwordx2 v[4:5], v[2:3], off offset:192
	v_cvt_pk_bf16_f32 v2, v124, v125
	v_cvt_pk_bf16_f32 v3, v126, v127
	global_store_dwordx2 v[4:5], v[2:3], off offset:224
	v_cvt_pk_bf16_f32 v2, v120, v121
	v_cvt_pk_bf16_f32 v3, v122, v123
	global_store_dwordx2 v[4:5], v[2:3], off offset:256
	v_cvt_pk_bf16_f32 v2, v92, v93
	v_cvt_pk_bf16_f32 v3, v94, v95
	global_store_dwordx2 v[4:5], v[2:3], off offset:288
	v_cvt_pk_bf16_f32 v2, v64, v65
	v_cvt_pk_bf16_f32 v3, v66, v67
	global_store_dwordx2 v[4:5], v[2:3], off offset:320
	v_cvt_pk_bf16_f32 v2, v48, v49
	v_cvt_pk_bf16_f32 v3, v50, v51
	global_store_dwordx2 v[4:5], v[2:3], off offset:352
	v_cvt_pk_bf16_f32 v2, v40, v41
	v_cvt_pk_bf16_f32 v3, v42, v43
	global_store_dwordx2 v[4:5], v[2:3], off offset:384
	v_cvt_pk_bf16_f32 v2, v36, v37
	v_cvt_pk_bf16_f32 v3, v38, v39
	global_store_dwordx2 v[4:5], v[2:3], off offset:416
	v_cvt_pk_bf16_f32 v2, v52, v53
	v_cvt_pk_bf16_f32 v3, v54, v55
	global_store_dwordx2 v[4:5], v[2:3], off offset:448
	v_cvt_pk_bf16_f32 v2, v44, v45
	v_cvt_pk_bf16_f32 v1, v46, v46
	v_lshrrev_b32_e32 v1, 16, v1
	v_cvt_pk_bf16_f32 v3, v47, v47
	v_and_or_b32 v3, v3, s80, v1
	s_mov_b64 s[14:15], -1
	global_store_dwordx2 v[4:5], v[2:3], off offset:480
	s_barrier

; #define LAS __attribute__((address_space(3)))
; __device__ __forceinline__ float lo_bf(unsigned w) { return __uint_as_float(w << 16); }
; __device__ __forceinline__ float hi_bf(unsigned w) { return __uint_as_float(w & 0xffff0000u); }
; __device__ __forceinline__ f32x4 bf4(u32x2 v) { return (f32x4){lo_bf(v.x), hi_bf(v.x), lo_bf(v.y), hi_bf(v.y)}; }
; __device__ __forceinline__ void ph_post_hyena(CArgs& a, int l, LAS unsigned char* lds, int bid, int nblk) {
;     ...
;     for (int it = bid + (l == DEPTH - 1 ? 64 : 0); it < 576; it += nblk) {
;         const Chunk c = chunk_of(it);
;         const int soff = c.L == CTXL ? 0 : CTXL;
;         { const int ch = tid & 255, half = tid >> 8;
;           const bf16* srcp = YT + ((size_t)(ch * 16 + c.b)) * 2304 + soff + c.t0 + half * 32;
;           u32x4 v8[4];
; #pragma unroll
;           for (int j = 0; j < 4; ++j) v8[j] = *(const u32x4*)(srcp + 8 * j);
; #pragma unroll
;           for (int j = 0; j < 4; ++j) { LAS float* d = yt + (half * 32 + 8 * j) * 260 + ch;
;               d[0] = lo_bf(v8[j].x); d[260] = hi_bf(v8[j].x); d[2 * 260] = lo_bf(v8[j].y); d[3 * 260] = hi_bf(v8[j].y); d[4 * 260] = lo_bf(v8[j].z); d[5 * 260] = hi_bf(v8[j].z); d[6 * 260] = lo_bf(v8[j].w); d[7 * 260] = hi_bf(v8[j].w); } }
;         __syncthreads();
;         const int tb = c.t0 + tg * 8;
;         const bf16* pb = P + (size_t)(c.row0 + tg * 8) * D_INP;
;         f32x4 x0[10], x1[10], vv[10];
; #pragma unroll
;         for (int r = 0; r < 10; ++r) { const int t = tb + r - 1, tc = min(max(t, c.lo), c.hi - 1); const float ok = (t == tc) ? 1.f : 0.f; const bf16* p = pb + (ptrdiff_t)(tc - tb) * D_INP;
;             x0[r] = ok * bf4(*(const u32x2*)(p + HY0 + c4));
;             x1[r] = ok * bf4(*(const u32x2*)(p + HY0 + 256 + c4)); vv[r] = ok * bf4(*(const u32x2*)(p + HY0 + 512 + c4)); }
.LBB0_2754:
	v_add_u32_e32 v62, s7, v1
	v_mov_b64_e32 v[60:61], s[4:5]
	s_movk_i32 s7, 0x1200
	v_mad_i64_i32 v[60:61], s[16:17], v62, s7, v[60:61]
	s_lshl_b32 s78, s14, 1
	v_lshl_add_u64 v[60:61], v[60:61], 0, s[78:79]
	s_mov_b32 s7, s79
	v_lshl_add_u64 v[60:61], s[6:7], 1, v[60:61]
	v_lshl_add_u64 v[60:61], v[56:57], 1, v[60:61]
	global_load_dwordx4 v[66:69], v[60:61], off
	global_load_dwordx4 v[70:73], v[60:61], off offset:16
	global_load_dwordx4 v[74:77], v[60:61], off offset:32
	global_load_dwordx4 v[78:81], v[60:61], off offset:48
	v_add_u32_e32 v64, s6, v188
	v_add_u32_e32 v65, -1, v64
	v_max_i32_e32 v61, s9, v65
	v_add_u32_e32 v60, s10, v188
	v_mov_b64_e32 v[62:63], s[2:3]
	v_mad_i64_i32 v[62:63], s[6:7], v60, s65, v[62:63]
	v_or_b32_e32 v111, 2, v64
	v_or_b32_e32 v112, 3, v64
	v_or_b32_e32 v115, 5, v64
	v_or_b32_e32 v206, 6, v64
	v_or_b32_e32 v208, 7, v64
	v_add_u32_e32 v210, 8, v64
	s_add_i32 s0, s0, s68
	s_waitcnt vmcnt(3)
	v_lshlrev_b32_e32 v82, 16, v66
	s_waitcnt vmcnt(2)
	v_lshlrev_b32_e32 v89, 16, v73
	v_and_b32_e32 v66, 0xffff0000, v66
	v_lshlrev_b32_e32 v83, 16, v67
	v_and_b32_e32 v67, 0xffff0000, v67
	v_lshlrev_b32_e32 v84, 16, v68
	v_and_b32_e32 v68, 0xffff0000, v68
	v_lshlrev_b32_e32 v85, 16, v69
	v_and_b32_e32 v69, 0xffff0000, v69
	v_lshlrev_b32_e32 v86, 16, v70
	v_and_b32_e32 v70, 0xffff0000, v70
	v_lshlrev_b32_e32 v87, 16, v71
	v_and_b32_e32 v71, 0xffff0000, v71
	v_lshlrev_b32_e32 v88, 16, v72
	v_and_b32_e32 v72, 0xffff0000, v72
	v_and_b32_e32 v73, 0xffff0000, v73
	s_waitcnt vmcnt(1)
	v_lshlrev_b32_e32 v90, 16, v74
	v_and_b32_e32 v74, 0xffff0000, v74
	v_lshlrev_b32_e32 v91, 16, v75
	v_and_b32_e32 v75, 0xffff0000, v75
	v_lshlrev_b32_e32 v92, 16, v76
	v_and_b32_e32 v76, 0xffff0000, v76
	v_lshlrev_b32_e32 v93, 16, v77
	v_and_b32_e32 v77, 0xffff0000, v77
	s_waitcnt vmcnt(0)
	v_lshlrev_b32_e32 v94, 16, v78
	v_and_b32_e32 v78, 0xffff0000, v78
	v_lshlrev_b32_e32 v95, 16, v79
	v_and_b32_e32 v79, 0xffff0000, v79
	v_lshlrev_b32_e32 v96, 16, v80
	v_and_b32_e32 v80, 0xffff0000, v80
	v_lshlrev_b32_e32 v97, 16, v81
	v_and_b32_e32 v81, 0xffff0000, v81
	ds_write_b32 v189, v82
	ds_write_b32 v189, v66 offset:1040
	ds_write_b32 v189, v83 offset:2080
	ds_write_b32 v189, v67 offset:3120
	ds_write_b32 v189, v84 offset:4160
	ds_write_b32 v189, v68 offset:5200
	ds_write_b32 v189, v85 offset:6240
	ds_write_b32 v189, v69 offset:7280
	ds_write_b32 v189, v86 offset:8320
	ds_write_b32 v189, v70 offset:9360
	ds_write_b32 v189, v87 offset:10400
	ds_write_b32 v189, v71 offset:11440
	ds_write_b32 v189, v88 offset:12480
	ds_write_b32 v189, v72 offset:13520
	ds_write_b32 v189, v89 offset:14560
	ds_write_b32 v189, v73 offset:15600
	ds_write_b32 v189, v90 offset:16640
	ds_write_b32 v189, v74 offset:17680
	ds_write_b32 v189, v91 offset:18720
	ds_write_b32 v189, v75 offset:19760
	ds_write_b32 v189, v92 offset:20800
	ds_write_b32 v189, v76 offset:21840
	ds_write_b32 v189, v93 offset:22880
	ds_write_b32 v189, v77 offset:23920
	ds_write_b32 v189, v94 offset:24960
	ds_write_b32 v189, v78 offset:26000
	ds_write_b32 v189, v95 offset:27040
	ds_write_b32 v189, v79 offset:28080
	ds_write_b32 v189, v96 offset:29120
	ds_write_b32 v189, v80 offset:30160
	ds_write_b32 v189, v97 offset:31200
	ds_write_b32 v189, v81 offset:32240
	v_min_u32_e32 v89, s8, v61
	v_sub_u32_e32 v61, v89, v64
	v_mad_i64_i32 v[66:67], s[6:7], v61, s65, v[62:63]
	v_lshl_add_u64 v[66:67], v[66:67], 0, v[34:35]
	s_waitcnt lgkmcnt(0)
	s_barrier
	global_load_dwordx2 v[68:69], v[66:67], off
	global_load_dwordx2 v[70:71], v[66:67], off offset:512
	s_nop 0
	global_load_dwordx2 v[66:67], v[66:67], off offset:1024
	v_max_i32_e32 v61, s9, v64
	v_min_u32_e32 v88, s8, v61
	v_sub_u32_e32 v61, v88, v64
	v_mad_i64_i32 v[72:73], s[6:7], v61, s65, v[62:63]
	v_lshl_add_u64 v[72:73], v[72:73], 0, v[34:35]
	global_load_dwordx2 v[74:75], v[72:73], off
	global_load_dwordx2 v[76:77], v[72:73], off offset:512
	s_nop 0
	global_load_dwordx2 v[72:73], v[72:73], off offset:1024
	v_or_b32_e32 v91, 1, v64
	v_max_i32_e32 v61, s9, v91
	v_min_u32_e32 v110, s8, v61
	v_sub_u32_e32 v61, v110, v64
	v_mad_i64_i32 v[78:79], s[6:7], v61, s65, v[62:63]
	v_lshl_add_u64 v[78:79], v[78:79], 0, v[34:35]
	v_max_i32_e32 v84, s9, v111
	global_load_dwordx2 v[80:81], v[78:79], off
	global_load_dwordx2 v[82:83], v[78:79], off offset:512
	v_min_u32_e32 v113, s8, v84
	v_sub_u32_e32 v84, v113, v64
	v_mad_i64_i32 v[84:85], s[6:7], v84, s65, v[62:63]
	global_load_dwordx2 v[78:79], v[78:79], off offset:1024
	v_lshl_add_u64 v[84:85], v[84:85], 0, v[34:35]
	global_load_dwordx2 v[86:87], v[84:85], off
	global_load_dwordx2 v[92:93], v[84:85], off offset:512
	v_max_i32_e32 v90, s9, v112
	v_cmp_eq_u32_e32 vcc, v88, v64
	v_min_u32_e32 v114, s8, v90
	v_ashrrev_i32_e32 v61, 31, v60
	v_cndmask_b32_e64 v88, 0, 1.0, vcc
	v_cmp_eq_u32_e32 vcc, v65, v89
	v_sub_u32_e32 v65, v114, v64
	v_mad_i64_i32 v[94:95], s[6:7], v65, s65, v[62:63]
	v_lshl_add_u64 v[94:95], v[94:95], 0, v[34:35]
	global_load_dwordx2 v[84:85], v[84:85], off offset:1024
	s_nop 0
	global_load_dwordx2 v[96:97], v[94:95], off
	v_cndmask_b32_e64 v90, 0, 1.0, vcc
	v_cmp_eq_u32_e32 vcc, v91, v110
	v_or_b32_e32 v65, 4, v64
	v_lshlrev_b64 v[60:61], 11, v[60:61]
	v_lshl_add_u64 v[60:61], v[58:59], 0, v[60:61]
	s_waitcnt vmcnt(12)
	v_lshlrev_b32_e32 v98, 16, v68
	v_and_b32_e32 v99, 0xffff0000, v68
	v_lshlrev_b32_e32 v68, 16, v69
	v_and_b32_e32 v69, 0xffff0000, v69
	v_pk_mul_f32 v[184:185], v[90:91], v[68:69] op_sel_hi:[0,1]
	global_load_dwordx2 v[68:69], v[94:95], off offset:512
	s_waitcnt vmcnt(11)
	v_lshlrev_b32_e32 v102, 16, v66
	v_and_b32_e32 v103, 0xffff0000, v66
	v_lshlrev_b32_e32 v66, 16, v67
	v_and_b32_e32 v67, 0xffff0000, v67
	s_waitcnt vmcnt(8)
; __device__ __forceinline__ f32x4 bf4(u32x2 v) { return (f32x4){lo_bf(v.x), hi_bf(v.x), lo_bf(v.y), hi_bf(v.y)}; }
; __device__ __forceinline__ void ph_post_hyena(CArgs& a, int l, LAS unsigned char* lds, int bid, int nblk) {
;     ...
;         f32x4 x0[10], x1[10], vv[10];
; #pragma unroll
;         for (int r = 0; r < 10; ++r) { const int t = tb + r - 1, tc = min(max(t, c.lo), c.hi - 1); const float ok = (t == tc) ? 1.f : 0.f; const bf16* p = pb + (ptrdiff_t)(tc - tb) * D_INP;
;             x0[r] = ok * bf4(*(const u32x2*)(p + HY0 + c4));
;             x1[r] = ok * bf4(*(const u32x2*)(p + HY0 + 256 + c4)); vv[r] = ok * bf4(*(const u32x2*)(p + HY0 + 512 + c4)); }
	v_lshlrev_b32_e32 v108, 16, v72
	v_pk_mul_f32 v[176:177], v[90:91], v[66:67] op_sel_hi:[0,1]
	v_and_b32_e32 v109, 0xffff0000, v72
	v_lshlrev_b32_e32 v66, 16, v73
	v_and_b32_e32 v67, 0xffff0000, v73
	global_load_dwordx2 v[72:73], v[94:95], off offset:1024
	v_lshlrev_b32_e32 v100, 16, v70
	v_and_b32_e32 v101, 0xffff0000, v70
	v_lshlrev_b32_e32 v70, 16, v71
	v_and_b32_e32 v71, 0xffff0000, v71
	v_lshlrev_b32_e32 v104, 16, v74
	v_and_b32_e32 v105, 0xffff0000, v74
	v_lshlrev_b32_e32 v74, 16, v75
	v_and_b32_e32 v75, 0xffff0000, v75
	v_pk_mul_f32 v[180:181], v[90:91], v[70:71] op_sel_hi:[0,1]
	v_pk_mul_f32 v[152:153], v[88:89], v[74:75] op_sel_hi:[0,1]
	v_pk_mul_f32 v[156:157], v[88:89], v[66:67] op_sel_hi:[0,1]
	v_cndmask_b32_e64 v66, 0, 1.0, vcc
	s_waitcnt vmcnt(8)
	v_lshlrev_b32_e32 v70, 16, v80
	v_and_b32_e32 v71, 0xffff0000, v80
	v_lshlrev_b32_e32 v74, 16, v81
	v_and_b32_e32 v75, 0xffff0000, v81
	v_pk_mul_f32 v[138:139], v[66:67], v[70:71] op_sel_hi:[0,1]
	v_pk_mul_f32 v[140:141], v[66:67], v[74:75] op_sel_hi:[0,1]
	s_waitcnt vmcnt(7)
	v_lshlrev_b32_e32 v70, 16, v82
	v_and_b32_e32 v71, 0xffff0000, v82
	v_lshlrev_b32_e32 v74, 16, v83
	v_and_b32_e32 v75, 0xffff0000, v83
	v_pk_mul_f32 v[134:135], v[66:67], v[70:71] op_sel_hi:[0,1]
	v_pk_mul_f32 v[136:137], v[66:67], v[74:75] op_sel_hi:[0,1]
	v_max_i32_e32 v67, s9, v65
	v_lshlrev_b32_e32 v106, 16, v76
	v_and_b32_e32 v107, 0xffff0000, v76
	v_lshlrev_b32_e32 v76, 16, v77
	v_and_b32_e32 v77, 0xffff0000, v77
	v_pk_mul_f32 v[178:179], v[90:91], v[102:103] op_sel_hi:[0,1]
	v_min_u32_e32 v102, s8, v67
	v_pk_mul_f32 v[144:145], v[88:89], v[76:77] op_sel_hi:[0,1]
	v_sub_u32_e32 v67, v102, v64
	s_waitcnt vmcnt(6)
	v_lshlrev_b32_e32 v76, 16, v78
	v_and_b32_e32 v77, 0xffff0000, v78
	v_lshlrev_b32_e32 v78, 16, v79
	v_and_b32_e32 v79, 0xffff0000, v79
	v_cmp_eq_u32_e32 vcc, v111, v113
	v_pk_mul_f32 v[158:159], v[66:67], v[76:77] op_sel_hi:[0,1]
	v_pk_mul_f32 v[160:161], v[66:67], v[78:79] op_sel_hi:[0,1]
	v_cndmask_b32_e64 v66, 0, 1.0, vcc
	s_waitcnt vmcnt(5)
	v_lshlrev_b32_e32 v78, 16, v87
	v_and_b32_e32 v79, 0xffff0000, v87
	v_lshlrev_b32_e32 v76, 16, v86
	v_and_b32_e32 v77, 0xffff0000, v86
	v_pk_mul_f32 v[82:83], v[66:67], v[78:79] op_sel_hi:[0,1]
	s_waitcnt vmcnt(4)
	v_lshlrev_b32_e32 v78, 16, v92
	v_and_b32_e32 v79, 0xffff0000, v92
	v_lshlrev_b32_e32 v86, 16, v93
	v_and_b32_e32 v87, 0xffff0000, v93
	v_pk_mul_f32 v[186:187], v[90:91], v[98:99] op_sel_hi:[0,1]
	v_pk_mul_f32 v[182:183], v[90:91], v[100:101] op_sel_hi:[0,1]
	v_mad_i64_i32 v[70:71], s[6:7], v67, s65, v[62:63]
	v_pk_mul_f32 v[80:81], v[66:67], v[76:77] op_sel_hi:[0,1]
	v_pk_mul_f32 v[90:91], v[66:67], v[78:79] op_sel_hi:[0,1]
	v_pk_mul_f32 v[92:93], v[66:67], v[86:87] op_sel_hi:[0,1]
	v_max_i32_e32 v67, s9, v115
	v_min_u32_e32 v116, s8, v67
	s_waitcnt vmcnt(3)
	v_lshlrev_b32_e32 v78, 16, v84
	v_sub_u32_e32 v67, v116, v64
	v_and_b32_e32 v79, 0xffff0000, v84
	v_pk_mul_f32 v[142:143], v[88:89], v[106:107] op_sel_hi:[0,1]
	v_pk_mul_f32 v[106:107], v[66:67], v[78:79] op_sel_hi:[0,1]
	v_max_i32_e32 v79, s9, v206
	v_mad_i64_i32 v[86:87], s[6:7], v67, s65, v[62:63]
	v_lshlrev_b32_e32 v84, 16, v85
	v_and_b32_e32 v85, 0xffff0000, v85
	v_cmp_eq_u32_e32 vcc, v112, v114
	v_min_u32_e32 v207, s8, v79
	v_pk_mul_f32 v[154:155], v[88:89], v[108:109] op_sel_hi:[0,1]
	v_lshl_add_u64 v[70:71], v[70:71], 0, v[34:35]
	v_lshl_add_u64 v[86:87], v[86:87], 0, v[34:35]
	v_pk_mul_f32 v[108:109], v[66:67], v[84:85] op_sel_hi:[0,1]
	v_cndmask_b32_e64 v78, 0, 1.0, vcc
	s_waitcnt vmcnt(2)
	v_lshlrev_b32_e32 v84, 16, v96
	v_and_b32_e32 v85, 0xffff0000, v96
	v_sub_u32_e32 v79, v207, v64
	v_pk_mul_f32 v[150:151], v[88:89], v[104:105] op_sel_hi:[0,1]
	global_load_dwordx2 v[76:77], v[70:71], off offset:512
	global_load_dwordx2 v[88:89], v[86:87], off
	v_pk_mul_f32 v[110:111], v[78:79], v[84:85] op_sel_hi:[0,1]
	s_waitcnt vmcnt(3)
	v_lshlrev_b32_e32 v84, 16, v68
	v_and_b32_e32 v85, 0xffff0000, v68
	v_lshlrev_b32_e32 v68, 16, v69
	v_and_b32_e32 v69, 0xffff0000, v69
	v_pk_mul_f32 v[132:133], v[78:79], v[68:69] op_sel_hi:[0,1]
	v_max_i32_e32 v69, s9, v208
	v_cmp_eq_u32_e32 vcc, v65, v102
	v_max_i32_e32 v65, s9, v210
	v_min_u32_e32 v209, s8, v69
	v_min_u32_e32 v211, s8, v65
	v_sub_u32_e32 v69, v209, v64
	v_sub_u32_e32 v64, v211, v64
	v_lshlrev_b32_e32 v94, 16, v97
	v_mad_i64_i32 v[98:99], s[6:7], v79, s65, v[62:63]
	v_and_b32_e32 v95, 0xffff0000, v97
	v_mad_i64_i32 v[96:97], s[6:7], v69, s65, v[62:63]
	v_mad_i64_i32 v[62:63], s[6:7], v64, s65, v[62:63]
	v_lshl_add_u64 v[62:63], v[62:63], 0, v[34:35]
	global_load_dwordx2 v[74:75], v[70:71], off
	global_load_dwordx2 v[102:103], v[62:63], off
	global_load_dwordx2 v[104:105], v[62:63], off offset:512
	global_load_dwordx2 v[204:205], v[62:63], off offset:1024
	global_load_dwordx2 v[66:67], v[86:87], off offset:512
	v_lshl_add_u64 v[98:99], v[98:99], 0, v[34:35]
	global_load_dwordx2 v[70:71], v[70:71], off offset:1024
	v_lshl_add_u64 v[96:97], v[96:97], 0, v[34:35]
	global_load_dwordx2 v[100:101], v[98:99], off
	v_pk_mul_f32 v[112:113], v[78:79], v[94:95] op_sel_hi:[0,1]
	global_load_dwordx2 v[94:95], v[98:99], off offset:512
	v_pk_mul_f32 v[130:131], v[78:79], v[84:85] op_sel_hi:[0,1]
	global_load_dwordx2 v[84:85], v[98:99], off offset:1024
	s_waitcnt vmcnt(11)
	v_lshlrev_b32_e32 v68, 16, v72
	global_load_dwordx2 v[98:99], v[96:97], off
	v_and_b32_e32 v69, 0xffff0000, v72
	global_load_dwordx2 v[86:87], v[86:87], off offset:1024
	v_lshlrev_b32_e32 v72, 16, v73
	v_and_b32_e32 v73, 0xffff0000, v73
	v_pk_mul_f32 v[172:173], v[78:79], v[68:69] op_sel_hi:[0,1]
	v_pk_mul_f32 v[174:175], v[78:79], v[72:73] op_sel_hi:[0,1]
	global_load_dwordx2 v[78:79], v[96:97], off offset:512
	v_cndmask_b32_e64 v68, 0, 1.0, vcc
	global_load_dwordx2 v[96:97], v[96:97], off offset:1024
	v_cmp_eq_u32_e32 vcc, v115, v116
	s_movk_i32 s6, 0x1000
	s_waitcnt vmcnt(14)
; #define LAS __attribute__((address_space(3)))
; __device__ __forceinline__ unsigned pk2(float lo, float hi) { return f2bf(lo) | (f2bf(hi) << 16); }
; __device__ __forceinline__ f32x4 bf4(u32x2 v) { return (f32x4){lo_bf(v.x), hi_bf(v.x), lo_bf(v.y), hi_bf(v.y)}; }
; __device__ __forceinline__ void ph_post_hyena(CArgs& a, int l, LAS unsigned char* lds, int bid, int nblk) {
;     ...
;         f32x4 x0[10], x1[10], vv[10];
; #pragma unroll
;         for (int r = 0; r < 10; ++r) { const int t = tb + r - 1, tc = min(max(t, c.lo), c.hi - 1); const float ok = (t == tc) ? 1.f : 0.f; const bf16* p = pb + (ptrdiff_t)(tc - tb) * D_INP;
;             x0[r] = ok * bf4(*(const u32x2*)(p + HY0 + c4));
;             x1[r] = ok * bf4(*(const u32x2*)(p + HY0 + 256 + c4)); vv[r] = ok * bf4(*(const u32x2*)(p + HY0 + 512 + c4)); }
; #pragma unroll
;         for (int tt = 0; tt < 8; ++tt) {
;             const f32x4 u0 = w0[0] * x0[tt] + w0[1] * x0[tt + 1] + w0[2] * x0[tt + 2] + b0;
;             const f32x4 xx = wx[0] * x1[tt] + wx[1] * x1[tt + 1] + wx[2] * x1[tt + 2] + bx, v2 = wv[0] * vv[tt] + wv[1] * vv[tt + 1] + wv[2] * vv[tt + 2] + bv, z = xx * v2;
;             const f32x4 y = *(const LAS f32x4*)(yt + (tg * 8 + tt) * 260 + c4);
;             const f32x4 o = (y + z * hd) * u0;
;             u32x2 oo; oo.x = pk2(o[0], o[1]); oo.y = pk2(o[2], o[3]); *(u32x2*)(YMIX + (size_t)(c.row0 + tg * 8 + tt) * D + c4) = oo;
	v_lshlrev_b32_e32 v64, 16, v76
	v_and_b32_e32 v65, 0xffff0000, v76
	v_pk_mul_f32 v[146:147], v[68:69], v[64:65] op_sel_hi:[0,1]
	s_waitcnt vmcnt(12)
	v_lshlrev_b32_e32 v72, 16, v74
	v_and_b32_e32 v73, 0xffff0000, v74
	v_lshlrev_b32_e32 v74, 16, v75
	v_and_b32_e32 v75, 0xffff0000, v75
	v_pk_mul_f32 v[126:127], v[68:69], v[72:73] op_sel_hi:[0,1]
	v_lshlrev_b32_e32 v72, 16, v77
	s_waitcnt vmcnt(7)
	v_lshlrev_b32_e32 v64, 16, v70
	v_and_b32_e32 v65, 0xffff0000, v70
	v_lshlrev_b32_e32 v62, 16, v71
	v_and_b32_e32 v63, 0xffff0000, v71
	v_pk_mul_f32 v[162:163], v[68:69], v[64:65] op_sel_hi:[0,1]
	v_pk_mul_f32 v[170:171], v[68:69], v[62:63] op_sel_hi:[0,1]
	v_cndmask_b32_e64 v62, 0, 1.0, vcc
	v_lshlrev_b32_e32 v64, 16, v88
	v_and_b32_e32 v65, 0xffff0000, v88
	v_and_b32_e32 v73, 0xffff0000, v77
	v_pk_mul_f32 v[122:123], v[62:63], v[64:65] op_sel_hi:[0,1]
	v_lshlrev_b32_e32 v64, 16, v66
	v_and_b32_e32 v65, 0xffff0000, v66
	v_lshlrev_b32_e32 v66, 16, v67
	v_and_b32_e32 v67, 0xffff0000, v67
	v_pk_mul_f32 v[128:129], v[68:69], v[74:75] op_sel_hi:[0,1]
	v_pk_mul_f32 v[148:149], v[68:69], v[72:73] op_sel_hi:[0,1]
	v_lshlrev_b32_e32 v68, 16, v89
	v_and_b32_e32 v69, 0xffff0000, v89
	v_pk_mul_f32 v[118:119], v[62:63], v[64:65] op_sel_hi:[0,1]
	v_pk_mul_f32 v[120:121], v[62:63], v[66:67] op_sel_hi:[0,1]
	s_waitcnt vmcnt(2)
	v_lshlrev_b32_e32 v64, 16, v86
	v_and_b32_e32 v65, 0xffff0000, v86
	v_lshlrev_b32_e32 v66, 16, v87
	v_and_b32_e32 v67, 0xffff0000, v87
	v_cmp_eq_u32_e32 vcc, v206, v207
	v_pk_mul_f32 v[124:125], v[62:63], v[68:69] op_sel_hi:[0,1]
	v_pk_mul_f32 v[114:115], v[62:63], v[64:65] op_sel_hi:[0,1]
	v_pk_mul_f32 v[116:117], v[62:63], v[66:67] op_sel_hi:[0,1]
	v_cndmask_b32_e64 v64, 0, 1.0, vcc
	v_lshlrev_b32_e32 v62, 16, v100
	v_and_b32_e32 v63, 0xffff0000, v100
	v_lshlrev_b32_e32 v66, 16, v101
	v_and_b32_e32 v67, 0xffff0000, v101
	v_pk_mul_f32 v[70:71], v[64:65], v[62:63] op_sel_hi:[0,1]
	v_lshlrev_b32_e32 v62, 16, v94
	v_and_b32_e32 v63, 0xffff0000, v94
	v_pk_mul_f32 v[72:73], v[64:65], v[66:67] op_sel_hi:[0,1]
	v_lshlrev_b32_e32 v68, 16, v95
	v_and_b32_e32 v69, 0xffff0000, v95
	v_pk_mul_f32 v[66:67], v[64:65], v[62:63] op_sel_hi:[0,1]
	v_lshlrev_b32_e32 v62, 16, v84
	v_and_b32_e32 v63, 0xffff0000, v84
	v_lshlrev_b32_e32 v74, 16, v85
	v_and_b32_e32 v75, 0xffff0000, v85
	v_cmp_eq_u32_e32 vcc, v208, v209
	v_pk_mul_f32 v[68:69], v[64:65], v[68:69] op_sel_hi:[0,1]
	v_pk_mul_f32 v[62:63], v[64:65], v[62:63] op_sel_hi:[0,1]
	v_pk_mul_f32 v[64:65], v[64:65], v[74:75] op_sel_hi:[0,1]
	v_cndmask_b32_e64 v94, 0, 1.0, vcc
	v_lshlrev_b32_e32 v74, 16, v98
	v_and_b32_e32 v75, 0xffff0000, v98
	v_lshlrev_b32_e32 v76, 16, v99
	v_and_b32_e32 v77, 0xffff0000, v99
	v_pk_mul_f32 v[84:85], v[94:95], v[74:75] op_sel_hi:[0,1]
	s_waitcnt vmcnt(1)
	v_lshlrev_b32_e32 v74, 16, v78
	v_and_b32_e32 v75, 0xffff0000, v78
	v_lshlrev_b32_e32 v78, 16, v79
	v_and_b32_e32 v79, 0xffff0000, v79
	v_cmp_eq_u32_e32 vcc, v210, v211
	v_pk_mul_f32 v[88:89], v[94:95], v[76:77] op_sel_hi:[0,1]
	v_pk_mul_f32 v[76:77], v[94:95], v[74:75] op_sel_hi:[0,1]
	v_pk_mul_f32 v[86:87], v[94:95], v[78:79] op_sel_hi:[0,1]
	s_waitcnt vmcnt(0)
	v_lshlrev_b32_e32 v74, 16, v96
	v_and_b32_e32 v75, 0xffff0000, v96
	v_lshlrev_b32_e32 v78, 16, v97
	v_and_b32_e32 v79, 0xffff0000, v97
	v_cndmask_b32_e64 v206, 0, 1.0, vcc
	v_lshlrev_b32_e32 v96, 16, v103
	v_and_b32_e32 v97, 0xffff0000, v103
	v_pk_mul_f32 v[74:75], v[94:95], v[74:75] op_sel_hi:[0,1]
	v_pk_mul_f32 v[78:79], v[94:95], v[78:79] op_sel_hi:[0,1]
	v_lshlrev_b32_e32 v94, 16, v102
	v_and_b32_e32 v95, 0xffff0000, v102
	v_pk_mul_f32 v[102:103], v[206:207], v[96:97] op_sel_hi:[0,1]
	v_lshlrev_b32_e32 v96, 16, v105
	v_and_b32_e32 v97, 0xffff0000, v105
	v_pk_mul_f32 v[98:99], v[206:207], v[94:95] op_sel_hi:[0,1]
	v_lshlrev_b32_e32 v94, 16, v104
	v_and_b32_e32 v95, 0xffff0000, v104
	v_pk_mul_f32 v[100:101], v[206:207], v[96:97] op_sel_hi:[0,1]
	v_lshlrev_b32_e32 v96, 16, v204
	v_and_b32_e32 v97, 0xffff0000, v204
	v_lshlrev_b32_e32 v104, 16, v205
	v_and_b32_e32 v105, 0xffff0000, v205
	v_pk_mul_f32 v[94:95], v[206:207], v[94:95] op_sel_hi:[0,1]
	v_pk_mul_f32 v[96:97], v[206:207], v[96:97] op_sel_hi:[0,1]
	v_pk_mul_f32 v[104:105], v[206:207], v[104:105] op_sel_hi:[0,1]
	v_pk_mul_f32 v[204:205], v[16:17], v[152:153]
	v_pk_mul_f32 v[206:207], v[14:15], v[150:151]
	v_pk_fma_f32 v[184:185], v[4:5], v[184:185], v[204:205]
	v_pk_fma_f32 v[186:187], v[2:3], v[186:187], v[206:207]
	v_pk_mul_f32 v[204:205], v[20:21], v[144:145]
	v_pk_mul_f32 v[206:207], v[18:19], v[142:143]
	v_pk_fma_f32 v[180:181], v[8:9], v[180:181], v[204:205]
	v_pk_fma_f32 v[182:183], v[6:7], v[182:183], v[206:207]
	v_pk_mul_f32 v[204:205], v[24:25], v[156:157]
	v_pk_mul_f32 v[206:207], v[22:23], v[154:155]
	v_pk_fma_f32 v[176:177], v[12:13], v[176:177], v[204:205]
	v_pk_fma_f32 v[178:179], v[10:11], v[178:179], v[206:207]
	v_pk_fma_f32 v[204:205], v[38:39], v[160:161], v[176:177]
	v_pk_fma_f32 v[176:177], v[36:37], v[158:159], v[178:179]
	v_pk_fma_f32 v[182:183], v[30:31], v[134:135], v[182:183]
	v_pk_add_f32 v[206:207], v[48:49], v[176:177]
	ds_read_b128 v[176:179], v202
	v_pk_fma_f32 v[180:181], v[32:33], v[136:137], v[180:181]
	v_pk_add_f32 v[182:183], v[44:45], v[182:183]
	v_pk_fma_f32 v[186:187], v[26:27], v[138:139], v[186:187]
	v_pk_add_f32 v[180:181], v[46:47], v[180:181]
	v_pk_add_f32 v[204:205], v[50:51], v[204:205]
	v_pk_mul_f32 v[206:207], v[182:183], v[206:207]
	v_pk_fma_f32 v[184:185], v[28:29], v[140:141], v[184:185]
	v_pk_add_f32 v[186:187], v[40:41], v[186:187]
	v_pk_mul_f32 v[204:205], v[180:181], v[204:205]
	ds_read_b128 v[180:183], v202 offset:1040
	s_waitcnt lgkmcnt(1)
; #define LAS __attribute__((address_space(3)))
; __device__ __forceinline__ unsigned pk2(float lo, float hi) { return f2bf(lo) | (f2bf(hi) << 16); }
; __device__ __forceinline__ void ph_post_hyena(CArgs& a, int l, LAS unsigned char* lds, int bid, int nblk) {
;     ...
;         for (int tt = 0; tt < 8; ++tt) {
;             const f32x4 u0 = w0[0] * x0[tt] + w0[1] * x0[tt + 1] + w0[2] * x0[tt + 2] + b0;
;             const f32x4 xx = wx[0] * x1[tt] + wx[1] * x1[tt + 1] + wx[2] * x1[tt + 2] + bx, v2 = wv[0] * vv[tt] + wv[1] * vv[tt + 1] + wv[2] * vv[tt + 2] + bv, z = xx * v2;
;             const f32x4 y = *(const LAS f32x4*)(yt + (tg * 8 + tt) * 260 + c4);
;             const f32x4 o = (y + z * hd) * u0;
;             u32x2 oo; oo.x = pk2(o[0], o[1]); oo.y = pk2(o[2], o[3]); *(u32x2*)(YMIX + (size_t)(c.row0 + tg * 8 + tt) * D + c4) = oo;
	v_pk_fma_f32 v[176:177], v[52:53], v[206:207], v[176:177]
	v_pk_add_f32 v[184:185], v[42:43], v[184:185]
	v_pk_fma_f32 v[178:179], v[54:55], v[204:205], v[178:179]
	v_pk_mul_f32 v[176:177], v[186:187], v[176:177]
	v_pk_mul_f32 v[178:179], v[184:185], v[178:179]
	v_cvt_pk_bf16_f32 v176, v176, v176
	v_lshrrev_b32_e32 v176, 16, v176
	v_cvt_pk_bf16_f32 v177, v177, v177
	v_and_or_b32 v176, v177, s80, v176
	v_cvt_pk_bf16_f32 v177, v178, v179
	v_pk_mul_f32 v[178:179], v[14:15], v[138:139]
	global_store_dwordx2 v[60:61], v[176:177], off
	v_pk_fma_f32 v[150:151], v[2:3], v[150:151], v[178:179]
	v_pk_mul_f32 v[178:179], v[18:19], v[134:135]
	v_pk_mul_f32 v[176:177], v[16:17], v[140:141]
	v_pk_fma_f32 v[142:143], v[6:7], v[142:143], v[178:179]
	v_pk_mul_f32 v[178:179], v[22:23], v[158:159]
	v_pk_fma_f32 v[152:153], v[4:5], v[152:153], v[176:177]
	v_pk_fma_f32 v[154:155], v[10:11], v[154:155], v[178:179]
	v_pk_mul_f32 v[176:177], v[20:21], v[136:137]
	v_pk_fma_f32 v[142:143], v[30:31], v[90:91], v[142:143]
	v_pk_fma_f32 v[154:155], v[36:37], v[106:107], v[154:155]
	v_pk_fma_f32 v[144:145], v[8:9], v[144:145], v[176:177]
	v_pk_add_f32 v[142:143], v[44:45], v[142:143]
	v_pk_mul_f32 v[176:177], v[24:25], v[160:161]
	v_pk_add_f32 v[154:155], v[48:49], v[154:155]
	v_pk_fma_f32 v[150:151], v[26:27], v[80:81], v[150:151]
	v_pk_fma_f32 v[156:157], v[12:13], v[156:157], v[176:177]
	v_pk_mul_f32 v[142:143], v[142:143], v[154:155]
	v_pk_add_f32 v[150:151], v[40:41], v[150:151]
	v_pk_fma_f32 v[144:145], v[32:33], v[92:93], v[144:145]
	v_pk_fma_f32 v[156:157], v[38:39], v[108:109], v[156:157]
	s_waitcnt lgkmcnt(0)
	v_pk_fma_f32 v[142:143], v[52:53], v[142:143], v[180:181]
	v_pk_add_f32 v[144:145], v[46:47], v[144:145]
	v_pk_add_f32 v[156:157], v[50:51], v[156:157]
	v_pk_mul_f32 v[142:143], v[150:151], v[142:143]
	v_pk_fma_f32 v[152:153], v[28:29], v[82:83], v[152:153]
	v_pk_mul_f32 v[144:145], v[144:145], v[156:157]
	v_pk_add_f32 v[152:153], v[42:43], v[152:153]
	v_pk_fma_f32 v[144:145], v[54:55], v[144:145], v[182:183]
	v_pk_mul_f32 v[144:145], v[152:153], v[144:145]
	v_cvt_pk_bf16_f32 v142, v142, v143
	v_cvt_pk_bf16_f32 v143, v144, v145
	global_store_dwordx2 v[60:61], v[142:143], off offset:2048
	v_pk_mul_f32 v[142:143], v[16:17], v[82:83]
	v_pk_mul_f32 v[144:145], v[14:15], v[80:81]
	v_pk_fma_f32 v[140:141], v[4:5], v[140:141], v[142:143]
	v_pk_fma_f32 v[138:139], v[2:3], v[138:139], v[144:145]
	v_pk_fma_f32 v[140:141], v[28:29], v[112:113], v[140:141]
	v_pk_fma_f32 v[138:139], v[26:27], v[110:111], v[138:139]
	v_pk_add_f32 v[144:145], v[42:43], v[140:141]
	v_pk_add_f32 v[142:143], v[40:41], v[138:139]
	v_pk_mul_f32 v[138:139], v[20:21], v[92:93]
	v_pk_mul_f32 v[140:141], v[18:19], v[90:91]
	v_pk_fma_f32 v[136:137], v[8:9], v[136:137], v[138:139]
	v_pk_fma_f32 v[134:135], v[6:7], v[134:135], v[140:141]
	v_pk_fma_f32 v[136:137], v[32:33], v[132:133], v[136:137]
	v_pk_fma_f32 v[134:135], v[30:31], v[130:131], v[134:135]
	v_pk_add_f32 v[140:141], v[46:47], v[136:137]
	v_pk_add_f32 v[138:139], v[44:45], v[134:135]
	v_pk_mul_f32 v[134:135], v[24:25], v[108:109]
	v_pk_mul_f32 v[136:137], v[22:23], v[106:107]
	v_pk_fma_f32 v[134:135], v[12:13], v[160:161], v[134:135]
	v_pk_fma_f32 v[136:137], v[10:11], v[158:159], v[136:137]
	v_pk_fma_f32 v[150:151], v[38:39], v[174:175], v[134:135]
	v_pk_fma_f32 v[134:135], v[36:37], v[172:173], v[136:137]
	v_pk_add_f32 v[150:151], v[50:51], v[150:151]
	v_pk_add_f32 v[152:153], v[48:49], v[134:135]
	ds_read_b128 v[134:137], v202 offset:2080
	v_pk_mul_f32 v[152:153], v[138:139], v[152:153]
	v_pk_mul_f32 v[150:151], v[140:141], v[150:151]
	ds_read_b128 v[138:141], v202 offset:3120
	s_waitcnt lgkmcnt(1)
	v_pk_fma_f32 v[134:135], v[52:53], v[152:153], v[134:135]
	s_nop 0
	v_pk_mul_f32 v[134:135], v[142:143], v[134:135]
	v_pk_fma_f32 v[136:137], v[54:55], v[150:151], v[136:137]
	v_pk_mul_f32 v[136:137], v[144:145], v[136:137]
	v_cvt_pk_bf16_f32 v134, v134, v135
	v_cvt_pk_bf16_f32 v135, v136, v137
	v_add_co_u32_e32 v136, vcc, s6, v60
	s_movk_i32 s6, 0x2000
	s_nop 0
	v_addc_co_u32_e32 v137, vcc, 0, v61, vcc
	v_pk_mul_f32 v[144:145], v[14:15], v[110:111]
	v_add_co_u32_e32 v142, vcc, s6, v60
	v_pk_fma_f32 v[80:81], v[2:3], v[80:81], v[144:145]
	v_pk_mul_f32 v[144:145], v[18:19], v[130:131]
	v_addc_co_u32_e32 v143, vcc, 0, v61, vcc
	v_pk_fma_f32 v[90:91], v[6:7], v[90:91], v[144:145]
	v_pk_mul_f32 v[144:145], v[22:23], v[172:173]
	global_store_dwordx2 v[142:143], v[134:135], off offset:-4096
	v_pk_mul_f32 v[134:135], v[16:17], v[112:113]
	v_pk_fma_f32 v[106:107], v[10:11], v[106:107], v[144:145]
	v_pk_fma_f32 v[82:83], v[4:5], v[82:83], v[134:135]
	v_pk_mul_f32 v[134:135], v[20:21], v[132:133]
	v_pk_fma_f32 v[90:91], v[30:31], v[146:147], v[90:91]
	v_pk_fma_f32 v[106:107], v[36:37], v[162:163], v[106:107]
	v_pk_fma_f32 v[92:93], v[8:9], v[92:93], v[134:135]
	v_pk_add_f32 v[90:91], v[44:45], v[90:91]
	v_pk_mul_f32 v[134:135], v[24:25], v[174:175]
	v_pk_add_f32 v[106:107], v[48:49], v[106:107]
	v_pk_fma_f32 v[80:81], v[26:27], v[126:127], v[80:81]
	v_pk_fma_f32 v[108:109], v[12:13], v[108:109], v[134:135]
	v_pk_mul_f32 v[90:91], v[90:91], v[106:107]
	v_pk_add_f32 v[80:81], v[40:41], v[80:81]
	v_pk_fma_f32 v[92:93], v[32:33], v[148:149], v[92:93]
	v_pk_fma_f32 v[108:109], v[38:39], v[170:171], v[108:109]
	s_waitcnt lgkmcnt(0)
; #define LAS __attribute__((address_space(3)))
; __device__ __forceinline__ unsigned pk2(float lo, float hi) { return f2bf(lo) | (f2bf(hi) << 16); }
; __device__ __forceinline__ void ph_post_hyena(CArgs& a, int l, LAS unsigned char* lds, int bid, int nblk) {
;     ...
;         for (int tt = 0; tt < 8; ++tt) {
;             const f32x4 u0 = w0[0] * x0[tt] + w0[1] * x0[tt + 1] + w0[2] * x0[tt + 2] + b0;
;             const f32x4 xx = wx[0] * x1[tt] + wx[1] * x1[tt + 1] + wx[2] * x1[tt + 2] + bx, v2 = wv[0] * vv[tt] + wv[1] * vv[tt + 1] + wv[2] * vv[tt + 2] + bv, z = xx * v2;
;             const f32x4 y = *(const LAS f32x4*)(yt + (tg * 8 + tt) * 260 + c4);
;             const f32x4 o = (y + z * hd) * u0;
;             u32x2 oo; oo.x = pk2(o[0], o[1]); oo.y = pk2(o[2], o[3]); *(u32x2*)(YMIX + (size_t)(c.row0 + tg * 8 + tt) * D + c4) = oo;
	v_pk_fma_f32 v[90:91], v[52:53], v[90:91], v[138:139]
	v_pk_add_f32 v[92:93], v[46:47], v[92:93]
	v_pk_add_f32 v[108:109], v[50:51], v[108:109]
	v_pk_mul_f32 v[80:81], v[80:81], v[90:91]
	v_pk_fma_f32 v[82:83], v[28:29], v[128:129], v[82:83]
	v_pk_mul_f32 v[92:93], v[92:93], v[108:109]
	v_pk_add_f32 v[82:83], v[42:43], v[82:83]
	v_pk_fma_f32 v[92:93], v[54:55], v[92:93], v[140:141]
	v_pk_mul_f32 v[82:83], v[82:83], v[92:93]
	v_cvt_pk_bf16_f32 v80, v80, v81
	v_cvt_pk_bf16_f32 v81, v82, v83
	global_store_dwordx2 v[136:137], v[80:81], off offset:2048
	v_pk_mul_f32 v[80:81], v[16:17], v[128:129]
	v_pk_mul_f32 v[82:83], v[14:15], v[126:127]
	v_pk_fma_f32 v[80:81], v[4:5], v[112:113], v[80:81]
	v_pk_fma_f32 v[82:83], v[2:3], v[110:111], v[82:83]
	v_pk_fma_f32 v[80:81], v[28:29], v[124:125], v[80:81]
	v_pk_fma_f32 v[82:83], v[26:27], v[122:123], v[82:83]
	v_pk_add_f32 v[108:109], v[42:43], v[80:81]
	v_pk_add_f32 v[106:107], v[40:41], v[82:83]
	v_pk_mul_f32 v[80:81], v[20:21], v[148:149]
	v_pk_mul_f32 v[82:83], v[18:19], v[146:147]
	v_pk_fma_f32 v[80:81], v[8:9], v[132:133], v[80:81]
	v_pk_fma_f32 v[82:83], v[6:7], v[130:131], v[82:83]
	v_pk_fma_f32 v[80:81], v[32:33], v[120:121], v[80:81]
	v_pk_fma_f32 v[82:83], v[30:31], v[118:119], v[82:83]
	v_pk_add_f32 v[92:93], v[46:47], v[80:81]
	v_pk_add_f32 v[90:91], v[44:45], v[82:83]
	v_pk_mul_f32 v[80:81], v[24:25], v[170:171]
	v_pk_mul_f32 v[82:83], v[22:23], v[162:163]
	v_pk_fma_f32 v[80:81], v[12:13], v[174:175], v[80:81]
	v_pk_fma_f32 v[82:83], v[10:11], v[172:173], v[82:83]
	v_pk_fma_f32 v[110:111], v[38:39], v[116:117], v[80:81]
	v_pk_fma_f32 v[80:81], v[36:37], v[114:115], v[82:83]
	v_pk_add_f32 v[110:111], v[50:51], v[110:111]
	v_pk_add_f32 v[112:113], v[48:49], v[80:81]
	ds_read_b128 v[80:83], v202 offset:4160
	v_pk_mul_f32 v[112:113], v[90:91], v[112:113]
	v_pk_mul_f32 v[110:111], v[92:93], v[110:111]
	ds_read_b128 v[90:93], v202 offset:5200
	s_movk_i32 s6, 0x3000
	s_waitcnt lgkmcnt(1)
	v_pk_fma_f32 v[80:81], v[52:53], v[112:113], v[80:81]
	v_pk_fma_f32 v[82:83], v[54:55], v[110:111], v[82:83]
	v_pk_mul_f32 v[80:81], v[106:107], v[80:81]
	v_pk_mul_f32 v[82:83], v[108:109], v[82:83]
	v_cvt_pk_bf16_f32 v80, v80, v81
	v_pk_mul_f32 v[108:109], v[18:19], v[118:119]
	v_pk_mul_f32 v[112:113], v[22:23], v[114:115]
	v_pk_fma_f32 v[108:109], v[6:7], v[146:147], v[108:109]
	v_pk_fma_f32 v[112:113], v[10:11], v[162:163], v[112:113]
	v_cvt_pk_bf16_f32 v81, v82, v83
	v_pk_mul_f32 v[82:83], v[14:15], v[122:123]
	v_pk_fma_f32 v[108:109], v[30:31], v[66:67], v[108:109]
	v_pk_fma_f32 v[112:113], v[36:37], v[62:63], v[112:113]
	v_pk_fma_f32 v[82:83], v[2:3], v[126:127], v[82:83]
	v_pk_mul_f32 v[106:107], v[20:21], v[120:121]
	v_pk_add_f32 v[108:109], v[44:45], v[108:109]
	v_pk_mul_f32 v[110:111], v[24:25], v[116:117]
	v_pk_add_f32 v[112:113], v[48:49], v[112:113]
	v_pk_fma_f32 v[82:83], v[26:27], v[70:71], v[82:83]
	v_pk_fma_f32 v[106:107], v[8:9], v[148:149], v[106:107]
	v_pk_fma_f32 v[110:111], v[12:13], v[170:171], v[110:111]
	v_pk_mul_f32 v[108:109], v[108:109], v[112:113]
	global_store_dwordx2 v[142:143], v[80:81], off
	v_pk_mul_f32 v[80:81], v[16:17], v[124:125]
	v_pk_add_f32 v[82:83], v[40:41], v[82:83]
	v_pk_fma_f32 v[106:107], v[32:33], v[68:69], v[106:107]
	v_pk_fma_f32 v[110:111], v[38:39], v[64:65], v[110:111]
	s_waitcnt lgkmcnt(0)
; #define LAS __attribute__((address_space(3)))
; __device__ __forceinline__ unsigned pk2(float lo, float hi) { return f2bf(lo) | (f2bf(hi) << 16); }
; __device__ __forceinline__ void ph_post_hyena(CArgs& a, int l, LAS unsigned char* lds, int bid, int nblk) {
;     ...
;         for (int tt = 0; tt < 8; ++tt) {
;             const f32x4 u0 = w0[0] * x0[tt] + w0[1] * x0[tt + 1] + w0[2] * x0[tt + 2] + b0;
;             const f32x4 xx = wx[0] * x1[tt] + wx[1] * x1[tt + 1] + wx[2] * x1[tt + 2] + bx, v2 = wv[0] * vv[tt] + wv[1] * vv[tt + 1] + wv[2] * vv[tt + 2] + bv, z = xx * v2;
;             const f32x4 y = *(const LAS f32x4*)(yt + (tg * 8 + tt) * 260 + c4);
;             const f32x4 o = (y + z * hd) * u0;
;             u32x2 oo; oo.x = pk2(o[0], o[1]); oo.y = pk2(o[2], o[3]); *(u32x2*)(YMIX + (size_t)(c.row0 + tg * 8 + tt) * D + c4) = oo;
;         }
;         __syncthreads();
	v_pk_fma_f32 v[90:91], v[52:53], v[108:109], v[90:91]
	v_pk_fma_f32 v[80:81], v[4:5], v[128:129], v[80:81]
	v_pk_add_f32 v[106:107], v[46:47], v[106:107]
	v_pk_add_f32 v[110:111], v[50:51], v[110:111]
	v_pk_mul_f32 v[82:83], v[82:83], v[90:91]
	v_pk_fma_f32 v[80:81], v[28:29], v[72:73], v[80:81]
	v_pk_mul_f32 v[106:107], v[106:107], v[110:111]
	v_pk_add_f32 v[80:81], v[42:43], v[80:81]
	v_pk_fma_f32 v[92:93], v[54:55], v[106:107], v[92:93]
	v_pk_mul_f32 v[80:81], v[80:81], v[92:93]
	v_cvt_pk_bf16_f32 v82, v82, v83
	v_cvt_pk_bf16_f32 v83, v80, v81
	global_store_dwordx2 v[142:143], v[82:83], off offset:2048
	v_pk_mul_f32 v[80:81], v[16:17], v[72:73]
	v_pk_mul_f32 v[82:83], v[14:15], v[70:71]
	v_pk_fma_f32 v[80:81], v[4:5], v[124:125], v[80:81]
	v_pk_fma_f32 v[82:83], v[2:3], v[122:123], v[82:83]
	v_pk_fma_f32 v[80:81], v[28:29], v[88:89], v[80:81]
	v_pk_fma_f32 v[82:83], v[26:27], v[84:85], v[82:83]
	v_pk_add_f32 v[108:109], v[42:43], v[80:81]
	v_pk_add_f32 v[106:107], v[40:41], v[82:83]
	v_pk_mul_f32 v[80:81], v[20:21], v[68:69]
	v_pk_mul_f32 v[82:83], v[18:19], v[66:67]
	v_pk_fma_f32 v[80:81], v[8:9], v[120:121], v[80:81]
	v_pk_fma_f32 v[82:83], v[6:7], v[118:119], v[82:83]
	v_pk_fma_f32 v[80:81], v[32:33], v[86:87], v[80:81]
	v_pk_fma_f32 v[82:83], v[30:31], v[76:77], v[82:83]
	v_pk_add_f32 v[92:93], v[46:47], v[80:81]
	v_pk_add_f32 v[90:91], v[44:45], v[82:83]
	v_pk_mul_f32 v[80:81], v[24:25], v[64:65]
	v_pk_mul_f32 v[82:83], v[22:23], v[62:63]
	v_pk_fma_f32 v[80:81], v[12:13], v[116:117], v[80:81]
	v_pk_fma_f32 v[82:83], v[10:11], v[114:115], v[82:83]
	v_pk_fma_f32 v[110:111], v[38:39], v[78:79], v[80:81]
	v_pk_fma_f32 v[80:81], v[36:37], v[74:75], v[82:83]
	v_pk_add_f32 v[110:111], v[50:51], v[110:111]
	v_pk_add_f32 v[112:113], v[48:49], v[80:81]
	ds_read_b128 v[80:83], v202 offset:6240
	v_pk_mul_f32 v[112:113], v[90:91], v[112:113]
	v_pk_mul_f32 v[110:111], v[92:93], v[110:111]
	ds_read_b128 v[90:93], v203
	v_add_co_u32_e32 v60, vcc, s6, v60
	s_waitcnt lgkmcnt(1)
	v_pk_fma_f32 v[80:81], v[52:53], v[112:113], v[80:81]
	v_pk_fma_f32 v[82:83], v[54:55], v[110:111], v[82:83]
	v_pk_mul_f32 v[80:81], v[106:107], v[80:81]
	v_pk_mul_f32 v[82:83], v[108:109], v[82:83]
	v_cvt_pk_bf16_f32 v80, v80, v80
	v_lshrrev_b32_e32 v80, 16, v80
	v_cvt_pk_bf16_f32 v81, v81, v81
	v_and_or_b32 v80, v81, s80, v80
	v_pk_mul_f32 v[76:77], v[18:19], v[76:77]
	v_pk_mul_f32 v[74:75], v[22:23], v[74:75]
	v_cvt_pk_bf16_f32 v81, v82, v83
	v_addc_co_u32_e32 v61, vcc, 0, v61, vcc
	v_pk_fma_f32 v[66:67], v[6:7], v[66:67], v[76:77]
	v_pk_fma_f32 v[62:63], v[10:11], v[62:63], v[74:75]
	global_store_dwordx2 v[60:61], v[80:81], off
	v_pk_mul_f32 v[80:81], v[16:17], v[88:89]
	v_pk_mul_f32 v[82:83], v[14:15], v[84:85]
	v_pk_fma_f32 v[66:67], v[30:31], v[94:95], v[66:67]
	v_pk_fma_f32 v[62:63], v[36:37], v[96:97], v[62:63]
	v_pk_fma_f32 v[70:71], v[2:3], v[70:71], v[82:83]
	v_pk_fma_f32 v[72:73], v[4:5], v[72:73], v[80:81]
	v_pk_mul_f32 v[80:81], v[20:21], v[86:87]
	v_pk_add_f32 v[66:67], v[44:45], v[66:67]
	v_pk_mul_f32 v[76:77], v[24:25], v[78:79]
	v_pk_add_f32 v[62:63], v[48:49], v[62:63]
	v_pk_fma_f32 v[70:71], v[26:27], v[98:99], v[70:71]
	v_pk_fma_f32 v[68:69], v[8:9], v[68:69], v[80:81]
	v_pk_fma_f32 v[64:65], v[12:13], v[64:65], v[76:77]
	v_pk_mul_f32 v[62:63], v[66:67], v[62:63]
	v_pk_add_f32 v[70:71], v[40:41], v[70:71]
	v_pk_fma_f32 v[68:69], v[32:33], v[100:101], v[68:69]
	v_pk_fma_f32 v[64:65], v[38:39], v[104:105], v[64:65]
	s_waitcnt lgkmcnt(0)
	v_pk_fma_f32 v[62:63], v[52:53], v[62:63], v[90:91]
	v_pk_add_f32 v[68:69], v[46:47], v[68:69]
	v_pk_add_f32 v[64:65], v[50:51], v[64:65]
	v_pk_mul_f32 v[62:63], v[70:71], v[62:63]
	v_pk_fma_f32 v[72:73], v[28:29], v[102:103], v[72:73]
	v_pk_mul_f32 v[64:65], v[68:69], v[64:65]
	v_pk_add_f32 v[72:73], v[42:43], v[72:73]
	v_pk_fma_f32 v[64:65], v[54:55], v[64:65], v[92:93]
	v_cvt_pk_bf16_f32 v62, v62, v62
	v_pk_mul_f32 v[64:65], v[72:73], v[64:65]
	v_lshrrev_b32_e32 v62, 16, v62
	v_cvt_pk_bf16_f32 v63, v63, v63
	v_and_or_b32 v62, v63, s80, v62
	v_cvt_pk_bf16_f32 v63, v64, v64
	v_bfe_u32 v64, v65, 16, 1
	v_readlane_b32 s6, v252, 57
	v_lshrrev_b32_e32 v63, 16, v63
	v_add3_u32 v64, v65, v64, s81
	s_add_i32 s1, s1, s6
	v_and_or_b32 v63, v64, s80, v63
	s_cmpk_lt_i32 s0, 0x240
	global_store_dwordx2 v[60:61], v[62:63], off offset:2048
	s_barrier
	s_cbranch_scc0 .LBB0_2759

; #define LAS __attribute__((address_space(3)))
; __device__ __forceinline__ unsigned pk2(float lo, float hi) { return f2bf(lo) | (f2bf(hi) << 16); }
; __device__ __forceinline__ float lo_bf(unsigned w) { return __uint_as_float(w << 16); }
; __device__ __forceinline__ float hi_bf(unsigned w) { return __uint_as_float(w & 0xffff0000u); }
; __device__ __forceinline__ void ph_ln1_route(CArgs& a, int l, LAS unsigned char* lds, int bid, int nblk) {
;     ...
;             f32x4 acc[2] = {(f32x4){0.f, 0.f, 0.f, 0.f}, (f32x4){0.f, 0.f, 0.f, 0.f}};
; #pragma unroll
;             for (int ss = 0; ss < 4; ++ss) { const int k0 = 128 * w + 32 * ss + 8 * kg;
;                 const f32x4 h0 = *(const LAS f32x4*)(hrow + fr * 1028 + k0), h1 = *(const LAS f32x4*)(hrow + fr * 1028 + k0 + 4);
;                 u32x4 ah, al;
;                 ah.x = pk2(h0[0], h0[1]); ah.y = pk2(h0[2], h0[3]); ah.z = pk2(h1[0], h1[1]); ah.w = pk2(h1[2], h1[3]);
;                 al.x = pk2(h0[0] - lo_bf(ah.x), h0[1] - hi_bf(ah.x)); al.y = pk2(h0[2] - lo_bf(ah.y), h0[3] - hi_bf(ah.y)); al.z = pk2(h1[0] - lo_bf(ah.z), h1[1] - hi_bf(ah.z)); al.w = pk2(h1[2] - lo_bf(ah.w), h1[3] - hi_bf(ah.w));
;                 const bf16x8 Ah = __builtin_bit_cast(bf16x8, ah), Al = __builtin_bit_cast(bf16x8, al);
; #pragma unroll
;                 for (int t = 0; t < 2; ++t) {
;                     acc[t] = __builtin_amdgcn_mfma_f32_16x16x32_bf16(Ah, Bh[ss][t], acc[t], 0, 0, 0);
;                     acc[t] = __builtin_amdgcn_mfma_f32_16x16x32_bf16(Ah, Bl[ss][t], acc[t], 0, 0, 0);
;                     acc[t] = __builtin_amdgcn_mfma_f32_16x16x32_bf16(Al, Bh[ss][t], acc[t], 0, 0, 0); } }
.LBB0_2948:
	ds_read_b128 v[138:141], v178
	ds_read_b128 v[142:145], v178 offset:16
	s_and_b64 vcc, exec, s[54:55]
	s_waitcnt lgkmcnt(1)
	v_and_b32_sdwa v181, v138, v169 dst_sel:DWORD dst_unused:UNUSED_PAD src0_sel:WORD_1 src1_sel:DWORD
	v_mov_b32_e32 v146, v138
	v_and_b32_sdwa v34, v140, v169 dst_sel:DWORD dst_unused:UNUSED_PAD src0_sel:WORD_1 src1_sel:DWORD
	v_add3_u32 v181, v138, v181, s81
	v_and_b32_sdwa v138, v141, v169 dst_sel:DWORD dst_unused:UNUSED_PAD src0_sel:WORD_1 src1_sel:DWORD
	v_and_b32_sdwa v182, v139, v169 dst_sel:DWORD dst_unused:UNUSED_PAD src0_sel:WORD_1 src1_sel:DWORD
	v_mov_b32_e32 v147, v140
	v_add3_u32 v34, v140, v34, s81
	v_mov_b32_e32 v140, v139
	v_add3_u32 v138, v141, v138, s81
	v_add3_u32 v139, v139, v182, s81
	v_and_b32_e32 v183, 0xffff0000, v138
	v_and_b32_e32 v182, 0xffff0000, v139
	v_or_b32_sdwa v138, v182, v181 dst_sel:DWORD dst_unused:UNUSED_PAD src0_sel:DWORD src1_sel:WORD_1
	v_or_b32_sdwa v139, v183, v34 dst_sel:DWORD dst_unused:UNUSED_PAD src0_sel:DWORD src1_sel:WORD_1
	v_pk_add_f32 v[182:183], v[140:141], v[182:183] neg_lo:[0,1] neg_hi:[0,1]
	s_waitcnt lgkmcnt(0)
	v_and_b32_sdwa v140, v142, v169 dst_sel:DWORD dst_unused:UNUSED_PAD src0_sel:WORD_1 src1_sel:DWORD
	v_and_b32_e32 v184, 0xffff0000, v181
	v_add3_u32 v181, v142, v140, s81
	v_and_b32_sdwa v140, v145, v169 dst_sel:DWORD dst_unused:UNUSED_PAD src0_sel:WORD_1 src1_sel:DWORD
	v_and_b32_sdwa v141, v143, v169 dst_sel:DWORD dst_unused:UNUSED_PAD src0_sel:WORD_1 src1_sel:DWORD
	v_and_b32_e32 v185, 0xffff0000, v34
	v_and_b32_sdwa v34, v144, v169 dst_sel:DWORD dst_unused:UNUSED_PAD src0_sel:WORD_1 src1_sel:DWORD
	v_add3_u32 v140, v145, v140, s81
	v_add3_u32 v141, v143, v141, s81
	v_pk_add_f32 v[146:147], v[146:147], v[184:185] neg_lo:[0,1] neg_hi:[0,1]
	v_mov_b32_e32 v184, v142
	v_mov_b32_e32 v185, v144
	v_add3_u32 v34, v144, v34, s81
	v_mov_b32_e32 v144, v143
	v_and_b32_e32 v143, 0xffff0000, v140
	v_and_b32_e32 v142, 0xffff0000, v141
	v_or_b32_sdwa v140, v142, v181 dst_sel:DWORD dst_unused:UNUSED_PAD src0_sel:DWORD src1_sel:WORD_1
	v_or_b32_sdwa v141, v143, v34 dst_sel:DWORD dst_unused:UNUSED_PAD src0_sel:DWORD src1_sel:WORD_1
	v_and_b32_e32 v187, 0xffff0000, v34
	v_and_b32_e32 v186, 0xffff0000, v181
	v_pk_add_f32 v[142:143], v[144:145], v[142:143] neg_lo:[0,1] neg_hi:[0,1]
	v_pk_add_f32 v[184:185], v[184:185], v[186:187] neg_lo:[0,1] neg_hi:[0,1]
	v_bfe_u32 v144, v142, 16, 1
	v_bfe_u32 v145, v183, 16, 1
	v_bfe_u32 v181, v182, 16, 1
	v_add3_u32 v181, v182, v181, s81
	v_add3_u32 v182, v183, v145, s81
	v_add3_u32 v183, v142, v144, s81
	v_cvt_pk_bf16_f32 v34, v143, v143
	v_bfe_u32 v142, v146, 16, 1
	v_bfe_u32 v143, v147, 16, 1
	v_bfe_u32 v144, v184, 16, 1
	v_bfe_u32 v145, v185, 16, 1
	v_add3_u32 v145, v185, v145, s81
	v_add3_u32 v144, v184, v144, s81
	v_add3_u32 v143, v147, v143, s81
	v_add3_u32 v142, v146, v142, s81
	v_lshrrev_b32_e32 v146, 16, v142
	v_lshrrev_b32_e32 v147, 16, v143
	v_lshrrev_b32_e32 v184, 16, v144
	v_lshrrev_b32_e32 v185, 16, v145
	s_waitcnt vmcnt(30)
	v_mfma_f32_16x16x32_bf16 v[142:145], v[138:141], v[26:29], 0
	v_and_or_b32 v185, v34, s80, v185
	v_and_or_b32 v184, v183, s80, v184
	v_and_or_b32 v183, v182, s80, v147
	v_mfma_f32_16x16x32_bf16 v[186:189], v[138:141], v[22:25], 0
	v_and_or_b32 v182, v181, s80, v146
	v_mfma_f32_16x16x32_bf16 v[142:145], v[138:141], v[18:21], v[142:145]
	s_waitcnt vmcnt(20)
	v_mfma_f32_16x16x32_bf16 v[138:141], v[138:141], v[76:79], v[186:189]
	s_nop 3
	ds_read_b128 v[186:189], v178 offset:128
	v_mfma_f32_16x16x32_bf16 v[142:145], v[182:185], v[26:29], v[142:145]
	v_mfma_f32_16x16x32_bf16 v[138:141], v[182:185], v[22:25], v[138:141]
	ds_read_b128 v[182:185], v178 offset:144
	s_waitcnt lgkmcnt(1)
	v_and_b32_sdwa v34, v188, v169 dst_sel:DWORD dst_unused:UNUSED_PAD src0_sel:WORD_1 src1_sel:DWORD
	v_and_b32_sdwa v181, v186, v169 dst_sel:DWORD dst_unused:UNUSED_PAD src0_sel:WORD_1 src1_sel:DWORD
	v_and_b32_sdwa v202, v187, v169 dst_sel:DWORD dst_unused:UNUSED_PAD src0_sel:WORD_1 src1_sel:DWORD
	v_mov_b32_e32 v146, v186
	v_mov_b32_e32 v147, v188
	v_add3_u32 v34, v188, v34, s81
	v_add3_u32 v181, v186, v181, s81
	v_mov_b32_e32 v188, v187
	v_and_b32_sdwa v186, v189, v169 dst_sel:DWORD dst_unused:UNUSED_PAD src0_sel:WORD_1 src1_sel:DWORD
	v_add3_u32 v187, v187, v202, s81
	v_add3_u32 v186, v189, v186, s81
	v_and_b32_e32 v202, 0xffff0000, v187
	v_and_b32_e32 v203, 0xffff0000, v186
	v_or_b32_sdwa v186, v202, v181 dst_sel:DWORD dst_unused:UNUSED_PAD src0_sel:DWORD src1_sel:WORD_1
	v_and_b32_e32 v205, 0xffff0000, v34
	v_and_b32_e32 v204, 0xffff0000, v181
	s_waitcnt lgkmcnt(0)
; #define LAS __attribute__((address_space(3)))
; __device__ __forceinline__ unsigned pk2(float lo, float hi) { return f2bf(lo) | (f2bf(hi) << 16); }
; __device__ __forceinline__ float lo_bf(unsigned w) { return __uint_as_float(w << 16); }
; __device__ __forceinline__ float hi_bf(unsigned w) { return __uint_as_float(w & 0xffff0000u); }
; __device__ __forceinline__ void ph_ln1_route(CArgs& a, int l, LAS unsigned char* lds, int bid, int nblk) {
;     ...
;             f32x4 acc[2] = {(f32x4){0.f, 0.f, 0.f, 0.f}, (f32x4){0.f, 0.f, 0.f, 0.f}};
; #pragma unroll
;             for (int ss = 0; ss < 4; ++ss) { const int k0 = 128 * w + 32 * ss + 8 * kg;
;                 const f32x4 h0 = *(const LAS f32x4*)(hrow + fr * 1028 + k0), h1 = *(const LAS f32x4*)(hrow + fr * 1028 + k0 + 4);
;                 u32x4 ah, al;
;                 ah.x = pk2(h0[0], h0[1]); ah.y = pk2(h0[2], h0[3]); ah.z = pk2(h1[0], h1[1]); ah.w = pk2(h1[2], h1[3]);
;                 al.x = pk2(h0[0] - lo_bf(ah.x), h0[1] - hi_bf(ah.x)); al.y = pk2(h0[2] - lo_bf(ah.y), h0[3] - hi_bf(ah.y)); al.z = pk2(h1[0] - lo_bf(ah.z), h1[1] - hi_bf(ah.z)); al.w = pk2(h1[2] - lo_bf(ah.w), h1[3] - hi_bf(ah.w));
;                 const bf16x8 Ah = __builtin_bit_cast(bf16x8, ah), Al = __builtin_bit_cast(bf16x8, al);
; #pragma unroll
;                 for (int t = 0; t < 2; ++t) {
;                     acc[t] = __builtin_amdgcn_mfma_f32_16x16x32_bf16(Ah, Bh[ss][t], acc[t], 0, 0, 0);
;                     acc[t] = __builtin_amdgcn_mfma_f32_16x16x32_bf16(Ah, Bl[ss][t], acc[t], 0, 0, 0);
;                     acc[t] = __builtin_amdgcn_mfma_f32_16x16x32_bf16(Al, Bh[ss][t], acc[t], 0, 0, 0); } }
	v_and_b32_sdwa v181, v182, v169 dst_sel:DWORD dst_unused:UNUSED_PAD src0_sel:WORD_1 src1_sel:DWORD
	v_or_b32_sdwa v187, v203, v34 dst_sel:DWORD dst_unused:UNUSED_PAD src0_sel:DWORD src1_sel:WORD_1
	v_pk_add_f32 v[146:147], v[146:147], v[204:205] neg_lo:[0,1] neg_hi:[0,1]
	v_pk_add_f32 v[202:203], v[188:189], v[202:203] neg_lo:[0,1] neg_hi:[0,1]
	v_mov_b32_e32 v204, v182
	v_add3_u32 v181, v182, v181, s81
	v_and_b32_sdwa v182, v185, v169 dst_sel:DWORD dst_unused:UNUSED_PAD src0_sel:WORD_1 src1_sel:DWORD
	v_and_b32_sdwa v188, v183, v169 dst_sel:DWORD dst_unused:UNUSED_PAD src0_sel:WORD_1 src1_sel:DWORD
	v_and_b32_sdwa v34, v184, v169 dst_sel:DWORD dst_unused:UNUSED_PAD src0_sel:WORD_1 src1_sel:DWORD
	v_add3_u32 v182, v185, v182, s81
	v_add3_u32 v188, v183, v188, s81
	v_mov_b32_e32 v205, v184
	v_add3_u32 v34, v184, v34, s81
	v_mov_b32_e32 v184, v183
	v_and_b32_e32 v183, 0xffff0000, v182
	v_and_b32_e32 v182, 0xffff0000, v188
	v_or_b32_sdwa v188, v182, v181 dst_sel:DWORD dst_unused:UNUSED_PAD src0_sel:DWORD src1_sel:WORD_1
	v_or_b32_sdwa v189, v183, v34 dst_sel:DWORD dst_unused:UNUSED_PAD src0_sel:DWORD src1_sel:WORD_1
	v_and_b32_e32 v207, 0xffff0000, v34
	v_and_b32_e32 v206, 0xffff0000, v181
	v_pk_add_f32 v[182:183], v[184:185], v[182:183] neg_lo:[0,1] neg_hi:[0,1]
	v_pk_add_f32 v[204:205], v[204:205], v[206:207] neg_lo:[0,1] neg_hi:[0,1]
	v_bfe_u32 v181, v182, 16, 1
	v_bfe_u32 v184, v203, 16, 1
	v_bfe_u32 v185, v202, 16, 1
	v_add3_u32 v202, v202, v185, s81
	v_add3_u32 v203, v203, v184, s81
	v_add3_u32 v181, v182, v181, s81
	v_cvt_pk_bf16_f32 v34, v183, v183
	v_bfe_u32 v183, v147, 16, 1
	v_bfe_u32 v184, v204, 16, 1
	v_bfe_u32 v185, v205, 16, 1
	v_mfma_f32_16x16x32_bf16 v[142:145], v[186:189], v[36:39], v[142:145]
	v_add3_u32 v185, v205, v185, s81
	v_add3_u32 v184, v204, v184, s81
	v_add3_u32 v147, v147, v183, s81
	v_mfma_f32_16x16x32_bf16 v[138:141], v[186:189], v[48:51], v[138:141]
	v_cvt_pk_bf16_f32 v146, v146, v146
	v_lshrrev_b32_e32 v146, 16, v146
	v_lshrrev_b32_e32 v147, 16, v147
	v_lshrrev_b32_e32 v182, 16, v184
	v_lshrrev_b32_e32 v183, 16, v185
	v_and_or_b32 v185, v34, s80, v183
	v_and_or_b32 v184, v181, s80, v182
	v_and_or_b32 v183, v203, s80, v147
	v_and_or_b32 v182, v202, s80, v146
	v_mfma_f32_16x16x32_bf16 v[142:145], v[186:189], v[40:43], v[142:145]
	v_mfma_f32_16x16x32_bf16 v[138:141], v[186:189], v[44:47], v[138:141]
	ds_read_b128 v[186:189], v178 offset:256
	v_mfma_f32_16x16x32_bf16 v[142:145], v[182:185], v[36:39], v[142:145]
	v_mfma_f32_16x16x32_bf16 v[138:141], v[182:185], v[48:51], v[138:141]
	ds_read_b128 v[182:185], v178 offset:272
	s_waitcnt lgkmcnt(1)
	v_and_b32_sdwa v34, v188, v169 dst_sel:DWORD dst_unused:UNUSED_PAD src0_sel:WORD_1 src1_sel:DWORD
	v_and_b32_sdwa v181, v186, v169 dst_sel:DWORD dst_unused:UNUSED_PAD src0_sel:WORD_1 src1_sel:DWORD
	v_and_b32_sdwa v202, v187, v169 dst_sel:DWORD dst_unused:UNUSED_PAD src0_sel:WORD_1 src1_sel:DWORD
	v_mov_b32_e32 v146, v186
	v_mov_b32_e32 v147, v188
	v_add3_u32 v34, v188, v34, s81
	v_add3_u32 v181, v186, v181, s81
	v_mov_b32_e32 v188, v187
	v_and_b32_sdwa v186, v189, v169 dst_sel:DWORD dst_unused:UNUSED_PAD src0_sel:WORD_1 src1_sel:DWORD
	v_add3_u32 v187, v187, v202, s81
	v_add3_u32 v186, v189, v186, s81
	v_and_b32_e32 v202, 0xffff0000, v187
	v_and_b32_e32 v203, 0xffff0000, v186
	v_or_b32_sdwa v186, v202, v181 dst_sel:DWORD dst_unused:UNUSED_PAD src0_sel:DWORD src1_sel:WORD_1
	v_and_b32_e32 v205, 0xffff0000, v34
	v_and_b32_e32 v204, 0xffff0000, v181
	s_waitcnt lgkmcnt(0)
	v_and_b32_sdwa v181, v182, v169 dst_sel:DWORD dst_unused:UNUSED_PAD src0_sel:WORD_1 src1_sel:DWORD
	v_or_b32_sdwa v187, v203, v34 dst_sel:DWORD dst_unused:UNUSED_PAD src0_sel:DWORD src1_sel:WORD_1
	v_pk_add_f32 v[146:147], v[146:147], v[204:205] neg_lo:[0,1] neg_hi:[0,1]
	v_pk_add_f32 v[202:203], v[188:189], v[202:203] neg_lo:[0,1] neg_hi:[0,1]
	v_mov_b32_e32 v204, v182
	v_add3_u32 v181, v182, v181, s81
	v_and_b32_sdwa v182, v185, v169 dst_sel:DWORD dst_unused:UNUSED_PAD src0_sel:WORD_1 src1_sel:DWORD
	v_and_b32_sdwa v188, v183, v169 dst_sel:DWORD dst_unused:UNUSED_PAD src0_sel:WORD_1 src1_sel:DWORD
	v_and_b32_sdwa v34, v184, v169 dst_sel:DWORD dst_unused:UNUSED_PAD src0_sel:WORD_1 src1_sel:DWORD
	v_add3_u32 v182, v185, v182, s81
	v_add3_u32 v188, v183, v188, s81
	v_mov_b32_e32 v205, v184
	v_add3_u32 v34, v184, v34, s81
	v_mov_b32_e32 v184, v183
	v_and_b32_e32 v183, 0xffff0000, v182
	v_and_b32_e32 v182, 0xffff0000, v188
	v_or_b32_sdwa v188, v182, v181 dst_sel:DWORD dst_unused:UNUSED_PAD src0_sel:DWORD src1_sel:WORD_1
	v_or_b32_sdwa v189, v183, v34 dst_sel:DWORD dst_unused:UNUSED_PAD src0_sel:DWORD src1_sel:WORD_1
	v_and_b32_e32 v207, 0xffff0000, v34
	v_and_b32_e32 v206, 0xffff0000, v181
	v_pk_add_f32 v[182:183], v[184:185], v[182:183] neg_lo:[0,1] neg_hi:[0,1]
	v_pk_add_f32 v[204:205], v[204:205], v[206:207] neg_lo:[0,1] neg_hi:[0,1]
	v_bfe_u32 v181, v182, 16, 1
	v_bfe_u32 v184, v203, 16, 1
	v_bfe_u32 v185, v202, 16, 1
	v_add3_u32 v202, v202, v185, s81
	v_add3_u32 v203, v203, v184, s81
	v_add3_u32 v181, v182, v181, s81
	v_cvt_pk_bf16_f32 v34, v183, v183
	v_bfe_u32 v183, v147, 16, 1
	v_bfe_u32 v184, v204, 16, 1
	v_bfe_u32 v185, v205, 16, 1
	v_mfma_f32_16x16x32_bf16 v[142:145], v[186:189], v[68:71], v[142:145]
	v_add3_u32 v185, v205, v185, s81
	v_add3_u32 v184, v204, v184, s81
	v_add3_u32 v147, v147, v183, s81
	v_mfma_f32_16x16x32_bf16 v[138:141], v[186:189], v[52:55], v[138:141]
	v_cvt_pk_bf16_f32 v146, v146, v146
	v_lshrrev_b32_e32 v146, 16, v146
	v_lshrrev_b32_e32 v147, 16, v147
	v_lshrrev_b32_e32 v182, 16, v184
	v_lshrrev_b32_e32 v183, 16, v185
	v_and_or_b32 v185, v34, s80, v183
	v_and_or_b32 v184, v181, s80, v182
	v_and_or_b32 v183, v203, s80, v147
	v_and_or_b32 v182, v202, s80, v146
	v_mfma_f32_16x16x32_bf16 v[142:145], v[186:189], v[56:59], v[142:145]
	v_mfma_f32_16x16x32_bf16 v[138:141], v[186:189], v[60:63], v[138:141]
	ds_read_b128 v[186:189], v178 offset:384
	v_mfma_f32_16x16x32_bf16 v[142:145], v[182:185], v[68:71], v[142:145]
	v_mfma_f32_16x16x32_bf16 v[138:141], v[182:185], v[52:55], v[138:141]
	ds_read_b128 v[182:185], v178 offset:400
	s_waitcnt lgkmcnt(1)
; #define LAS __attribute__((address_space(3)))
; __device__ __forceinline__ unsigned pk2(float lo, float hi) { return f2bf(lo) | (f2bf(hi) << 16); }
; __device__ __forceinline__ float lo_bf(unsigned w) { return __uint_as_float(w << 16); }
; __device__ __forceinline__ float hi_bf(unsigned w) { return __uint_as_float(w & 0xffff0000u); }
; __device__ __forceinline__ void ph_ln1_route(CArgs& a, int l, LAS unsigned char* lds, int bid, int nblk) {
;     ...
;             f32x4 acc[2] = {(f32x4){0.f, 0.f, 0.f, 0.f}, (f32x4){0.f, 0.f, 0.f, 0.f}};
; #pragma unroll
;             for (int ss = 0; ss < 4; ++ss) { const int k0 = 128 * w + 32 * ss + 8 * kg;
;                 const f32x4 h0 = *(const LAS f32x4*)(hrow + fr * 1028 + k0), h1 = *(const LAS f32x4*)(hrow + fr * 1028 + k0 + 4);
;                 u32x4 ah, al;
;                 ah.x = pk2(h0[0], h0[1]); ah.y = pk2(h0[2], h0[3]); ah.z = pk2(h1[0], h1[1]); ah.w = pk2(h1[2], h1[3]);
;                 al.x = pk2(h0[0] - lo_bf(ah.x), h0[1] - hi_bf(ah.x)); al.y = pk2(h0[2] - lo_bf(ah.y), h0[3] - hi_bf(ah.y)); al.z = pk2(h1[0] - lo_bf(ah.z), h1[1] - hi_bf(ah.z)); al.w = pk2(h1[2] - lo_bf(ah.w), h1[3] - hi_bf(ah.w));
;                 const bf16x8 Ah = __builtin_bit_cast(bf16x8, ah), Al = __builtin_bit_cast(bf16x8, al);
; #pragma unroll
;                 for (int t = 0; t < 2; ++t) {
;                     acc[t] = __builtin_amdgcn_mfma_f32_16x16x32_bf16(Ah, Bh[ss][t], acc[t], 0, 0, 0);
;                     acc[t] = __builtin_amdgcn_mfma_f32_16x16x32_bf16(Ah, Bl[ss][t], acc[t], 0, 0, 0);
;                     acc[t] = __builtin_amdgcn_mfma_f32_16x16x32_bf16(Al, Bh[ss][t], acc[t], 0, 0, 0); } }
; #pragma unroll
;             for (int t = 0; t < 2; ++t)
; #pragma unroll
;                 for (int j = 0; j < 4; ++j) part[((w * 2 + t) * 16 + 4 * kg + j) * 16 + fr] = acc[t][j];
;         }
;         if (more) { *(LAS f32x4*)(mods + 4 * tid) = mnext[0]; if (tid < 256) *(LAS f32x4*)(mods + 2048 + 4 * tid) = mnext[1]; }
	v_and_b32_sdwa v34, v188, v169 dst_sel:DWORD dst_unused:UNUSED_PAD src0_sel:WORD_1 src1_sel:DWORD
	v_and_b32_sdwa v181, v186, v169 dst_sel:DWORD dst_unused:UNUSED_PAD src0_sel:WORD_1 src1_sel:DWORD
	v_and_b32_sdwa v202, v187, v169 dst_sel:DWORD dst_unused:UNUSED_PAD src0_sel:WORD_1 src1_sel:DWORD
	v_mov_b32_e32 v146, v186
	v_mov_b32_e32 v147, v188
	v_add3_u32 v34, v188, v34, s81
	v_add3_u32 v181, v186, v181, s81
	v_mov_b32_e32 v188, v187
	v_and_b32_sdwa v186, v189, v169 dst_sel:DWORD dst_unused:UNUSED_PAD src0_sel:WORD_1 src1_sel:DWORD
	v_add3_u32 v187, v187, v202, s81
	v_add3_u32 v186, v189, v186, s81
	v_and_b32_e32 v202, 0xffff0000, v187
	v_and_b32_e32 v203, 0xffff0000, v186
	v_or_b32_sdwa v186, v202, v181 dst_sel:DWORD dst_unused:UNUSED_PAD src0_sel:DWORD src1_sel:WORD_1
	v_and_b32_e32 v205, 0xffff0000, v34
	v_and_b32_e32 v204, 0xffff0000, v181
	s_waitcnt lgkmcnt(0)
	v_and_b32_sdwa v181, v182, v169 dst_sel:DWORD dst_unused:UNUSED_PAD src0_sel:WORD_1 src1_sel:DWORD
	v_or_b32_sdwa v187, v203, v34 dst_sel:DWORD dst_unused:UNUSED_PAD src0_sel:DWORD src1_sel:WORD_1
	v_pk_add_f32 v[146:147], v[146:147], v[204:205] neg_lo:[0,1] neg_hi:[0,1]
	v_pk_add_f32 v[202:203], v[188:189], v[202:203] neg_lo:[0,1] neg_hi:[0,1]
	v_mov_b32_e32 v204, v182
	v_add3_u32 v181, v182, v181, s81
	v_and_b32_sdwa v182, v185, v169 dst_sel:DWORD dst_unused:UNUSED_PAD src0_sel:WORD_1 src1_sel:DWORD
	v_and_b32_sdwa v188, v183, v169 dst_sel:DWORD dst_unused:UNUSED_PAD src0_sel:WORD_1 src1_sel:DWORD
	v_and_b32_sdwa v34, v184, v169 dst_sel:DWORD dst_unused:UNUSED_PAD src0_sel:WORD_1 src1_sel:DWORD
	v_add3_u32 v182, v185, v182, s81
	v_add3_u32 v188, v183, v188, s81
	v_mov_b32_e32 v205, v184
	v_add3_u32 v34, v184, v34, s81
	v_mov_b32_e32 v184, v183
	v_and_b32_e32 v183, 0xffff0000, v182
	v_and_b32_e32 v182, 0xffff0000, v188
	v_or_b32_sdwa v188, v182, v181 dst_sel:DWORD dst_unused:UNUSED_PAD src0_sel:DWORD src1_sel:WORD_1
	v_or_b32_sdwa v189, v183, v34 dst_sel:DWORD dst_unused:UNUSED_PAD src0_sel:DWORD src1_sel:WORD_1
	v_and_b32_e32 v207, 0xffff0000, v34
	v_and_b32_e32 v206, 0xffff0000, v181
	v_pk_add_f32 v[182:183], v[184:185], v[182:183] neg_lo:[0,1] neg_hi:[0,1]
	v_pk_add_f32 v[204:205], v[204:205], v[206:207] neg_lo:[0,1] neg_hi:[0,1]
	v_bfe_u32 v181, v182, 16, 1
	v_bfe_u32 v184, v203, 16, 1
	v_bfe_u32 v185, v202, 16, 1
	v_add3_u32 v202, v202, v185, s81
	v_add3_u32 v203, v203, v184, s81
	v_add3_u32 v181, v182, v181, s81
	v_cvt_pk_bf16_f32 v34, v183, v183
	v_bfe_u32 v183, v147, 16, 1
	v_bfe_u32 v184, v204, 16, 1
	v_bfe_u32 v185, v205, 16, 1
	v_mfma_f32_16x16x32_bf16 v[142:145], v[186:189], v[72:75], v[142:145]
	v_add3_u32 v185, v205, v185, s81
	v_add3_u32 v184, v204, v184, s81
	v_add3_u32 v147, v147, v183, s81
	v_mfma_f32_16x16x32_bf16 v[138:141], v[186:189], v[80:83], v[138:141]
	v_cvt_pk_bf16_f32 v146, v146, v146
	v_lshrrev_b32_e32 v146, 16, v146
	v_lshrrev_b32_e32 v147, 16, v147
	v_lshrrev_b32_e32 v182, 16, v184
	v_lshrrev_b32_e32 v183, 16, v185
	v_and_or_b32 v185, v34, s80, v183
	v_and_or_b32 v184, v181, s80, v182
	v_and_or_b32 v183, v203, s80, v147
	v_and_or_b32 v182, v202, s80, v146
	v_mfma_f32_16x16x32_bf16 v[142:145], v[186:189], v[84:87], v[142:145]
	v_add_u32_e32 v34, 0x400, v179
	v_mfma_f32_16x16x32_bf16 v[138:141], v[186:189], v[88:91], v[138:141]
	v_mfma_f32_16x16x32_bf16 v[142:145], v[182:185], v[72:75], v[142:145]
	s_nop 7
	ds_write2_b32 v179, v142, v143 offset1:16
	ds_write2_b32 v179, v144, v145 offset0:32 offset1:48
	v_mfma_f32_16x16x32_bf16 v[138:141], v[182:185], v[80:83], v[138:141]
	s_nop 7
	ds_write2_b32 v34, v138, v139 offset1:16
	ds_write2_b32 v34, v140, v141 offset0:32 offset1:48
	s_cbranch_vccnz .LBB0_2952
	s_waitcnt vmcnt(16)
	ds_write_b128 v150, v[100:103]
	s_and_saveexec_b64 s[54:55], s[40:41]
	ds_write_b128 v151, v[104:107]
	s_or_b64 exec, exec, s[54:55]

; __device__ __forceinline__ unsigned pk2(float lo, float hi) { return f2bf(lo) | (f2bf(hi) << 16); }
; __device__ __forceinline__ void ph_ln2(CArgs& a, int l, LAS unsigned char* lds, int gw, int ngw) {
;     ...
;             for (int j = 0; j < 4; ++j) { const int c0 = j * 256 + 4 * lane;
;                 const f32x4 xn = v[j] * rstd * lgv[j] + lbv[j];
;                 if (lastl) *(f32x4*)(a.out + (size_t)(row - NTOK_C) * D + c0) = xn;
;                 else { *(u32x2*)(X + (size_t)row * D + c0) = (u32x2){pk2(xn[0], xn[1]), pk2(xn[2], xn[3])}; const f32x4 hh = xn * (1.f + scv[j]) + shv[j];
;                     u32x2 o; o.x = pk2(hh[0], hh[1]); o.y = pk2(hh[2], hh[3]); *(u32x2*)(HB + (size_t)row * D + c0) = o; } }
.LBB0_3309:
	s_andn2_b64 vcc, exec, s[28:29]
	s_cbranch_vccnz .LBB0_3311
	v_cvt_pk_bf16_f32 v140, v88, v89
	v_pk_fma_f32 v[88:89], v[114:115], v[88:89], v[64:65]
	v_cvt_pk_bf16_f32 v141, v90, v91
	v_pk_fma_f32 v[90:91], v[116:117], v[90:91], v[66:67]
	v_cvt_pk_bf16_f32 v88, v88, v89
	s_mov_b32 s18, 0xf6fff200
	v_cvt_pk_bf16_f32 v34, v90, v90
	s_mov_b32 s19, -1
	v_lshrrev_b32_e32 v34, 16, v34
	v_cvt_pk_bf16_f32 v89, v91, v91
	v_lshl_add_u64 v[138:139], v[100:101], 0, s[18:19]
	v_and_or_b32 v89, v89, s80, v34
	global_store_dwordx2 v[138:139], v[140:141], off
	global_store_dwordx2 v[100:101], v[88:89], off offset:-3584

; __device__ __forceinline__ unsigned pk2(float lo, float hi) { return f2bf(lo) | (f2bf(hi) << 16); }
; __device__ __forceinline__ void ph_ln2(CArgs& a, int l, LAS unsigned char* lds, int gw, int ngw) {
;     ...
;             for (int j = 0; j < 4; ++j) { const int c0 = j * 256 + 4 * lane;
;                 const f32x4 xn = v[j] * rstd * lgv[j] + lbv[j];
;                 if (lastl) *(f32x4*)(a.out + (size_t)(row - NTOK_C) * D + c0) = xn;
;                 else { *(u32x2*)(X + (size_t)row * D + c0) = (u32x2){pk2(xn[0], xn[1]), pk2(xn[2], xn[3])}; const f32x4 hh = xn * (1.f + scv[j]) + shv[j];
;                     u32x2 o; o.x = pk2(hh[0], hh[1]); o.y = pk2(hh[2], hh[3]); *(u32x2*)(HB + (size_t)row * D + c0) = o; } }
.LBB0_3313:
	s_andn2_b64 vcc, exec, s[28:29]
	s_cbranch_vccnz .LBB0_3315
	v_cvt_pk_bf16_f32 v136, v88, v89
	v_pk_fma_f32 v[88:89], v[106:107], v[88:89], v[52:53]
	v_cvt_pk_bf16_f32 v137, v90, v91
	v_pk_fma_f32 v[90:91], v[112:113], v[90:91], v[54:55]
	v_cvt_pk_bf16_f32 v88, v88, v89
	s_mov_b32 s18, 0xf6fff400
	v_cvt_pk_bf16_f32 v34, v90, v90
	s_mov_b32 s19, -1
	v_lshrrev_b32_e32 v34, 16, v34
	v_cvt_pk_bf16_f32 v89, v91, v91
	v_lshl_add_u64 v[132:133], v[100:101], 0, s[18:19]
	v_and_or_b32 v89, v89, s80, v34
	global_store_dwordx2 v[132:133], v[136:137], off
	global_store_dwordx2 v[100:101], v[88:89], off offset:-3072

; __device__ __forceinline__ unsigned pk2(float lo, float hi) { return f2bf(lo) | (f2bf(hi) << 16); }
; __device__ __forceinline__ void ph_ln2(CArgs& a, int l, LAS unsigned char* lds, int gw, int ngw) {
;     ...
;             for (int j = 0; j < 4; ++j) { const int c0 = j * 256 + 4 * lane;
;                 const f32x4 xn = v[j] * rstd * lgv[j] + lbv[j];
;                 if (lastl) *(f32x4*)(a.out + (size_t)(row - NTOK_C) * D + c0) = xn;
;                 else { *(u32x2*)(X + (size_t)row * D + c0) = (u32x2){pk2(xn[0], xn[1]), pk2(xn[2], xn[3])}; const f32x4 hh = xn * (1.f + scv[j]) + shv[j];
;                     u32x2 o; o.x = pk2(hh[0], hh[1]); o.y = pk2(hh[2], hh[3]); *(u32x2*)(HB + (size_t)row * D + c0) = o; } }
.LBB0_3317:
	s_andn2_b64 vcc, exec, s[28:29]
	s_cbranch_vccnz .LBB0_3319
	v_cvt_pk_bf16_f32 v132, v88, v89
	v_pk_fma_f32 v[88:89], v[108:109], v[88:89], v[60:61]
	v_cvt_pk_bf16_f32 v133, v90, v91
	v_pk_fma_f32 v[90:91], v[110:111], v[90:91], v[62:63]
	v_cvt_pk_bf16_f32 v88, v88, v89
	s_mov_b32 s18, 0xf6fff600
	v_cvt_pk_bf16_f32 v34, v90, v90
	s_mov_b32 s19, -1
	v_lshrrev_b32_e32 v34, 16, v34
	v_cvt_pk_bf16_f32 v89, v91, v91
	v_lshl_add_u64 v[130:131], v[100:101], 0, s[18:19]
	v_and_or_b32 v89, v89, s80, v34
	global_store_dwordx2 v[130:131], v[132:133], off
	global_store_dwordx2 v[100:101], v[88:89], off offset:-2560

; __device__ __forceinline__ unsigned pk2(float lo, float hi) { return f2bf(lo) | (f2bf(hi) << 16); }
; __device__ __forceinline__ void ph_ln2(CArgs& a, int l, LAS unsigned char* lds, int gw, int ngw) {
;     ...
;             for (int j = 0; j < 4; ++j) { const int c0 = j * 256 + 4 * lane;
;                 const f32x4 xn = v[j] * rstd * lgv[j] + lbv[j];
;                 if (lastl) *(f32x4*)(a.out + (size_t)(row - NTOK_C) * D + c0) = xn;
;                 else { *(u32x2*)(X + (size_t)row * D + c0) = (u32x2){pk2(xn[0], xn[1]), pk2(xn[2], xn[3])}; const f32x4 hh = xn * (1.f + scv[j]) + shv[j];
;                     u32x2 o; o.x = pk2(hh[0], hh[1]); o.y = pk2(hh[2], hh[3]); *(u32x2*)(HB + (size_t)row * D + c0) = o; } }
.LBB0_3325:
	s_andn2_b64 vcc, exec, s[26:27]
	s_cbranch_vccnz .LBB0_3327
	v_cvt_pk_bf16_f32 v88, v68, v69
	v_pk_fma_f32 v[64:65], v[114:115], v[68:69], v[64:65]
	v_cvt_pk_bf16_f32 v89, v70, v71
	v_pk_fma_f32 v[66:67], v[116:117], v[70:71], v[66:67]
	v_cvt_pk_bf16_f32 v64, v64, v65
	s_mov_b32 s18, 0xf6fffa00
	v_cvt_pk_bf16_f32 v34, v66, v66
	s_mov_b32 s19, -1
	v_lshrrev_b32_e32 v34, 16, v34
	v_cvt_pk_bf16_f32 v65, v67, v67
	v_lshl_add_u64 v[86:87], v[100:101], 0, s[18:19]
	v_and_or_b32 v65, v65, s80, v34
	global_store_dwordx2 v[86:87], v[88:89], off
	global_store_dwordx2 v[100:101], v[64:65], off offset:-1536

; __device__ __forceinline__ unsigned pk2(float lo, float hi) { return f2bf(lo) | (f2bf(hi) << 16); }
; __device__ __forceinline__ void ph_ln2(CArgs& a, int l, LAS unsigned char* lds, int gw, int ngw) {
;     ...
;             for (int j = 0; j < 4; ++j) { const int c0 = j * 256 + 4 * lane;
;                 const f32x4 xn = v[j] * rstd * lgv[j] + lbv[j];
;                 if (lastl) *(f32x4*)(a.out + (size_t)(row - NTOK_C) * D + c0) = xn;
;                 else { *(u32x2*)(X + (size_t)row * D + c0) = (u32x2){pk2(xn[0], xn[1]), pk2(xn[2], xn[3])}; const f32x4 hh = xn * (1.f + scv[j]) + shv[j];
;                     u32x2 o; o.x = pk2(hh[0], hh[1]); o.y = pk2(hh[2], hh[3]); *(u32x2*)(HB + (size_t)row * D + c0) = o; } }
.LBB0_3329:
	s_andn2_b64 vcc, exec, s[26:27]
	s_cbranch_vccnz .LBB0_3331
	v_cvt_pk_bf16_f32 v70, v64, v65
	v_pk_fma_f32 v[52:53], v[106:107], v[64:65], v[52:53]
	v_cvt_pk_bf16_f32 v71, v66, v67
	v_pk_fma_f32 v[54:55], v[112:113], v[66:67], v[54:55]
	v_cvt_pk_bf16_f32 v52, v52, v53
	s_mov_b32 s18, 0xf6fffc00
	v_cvt_pk_bf16_f32 v34, v54, v54
	s_mov_b32 s19, -1
	v_lshrrev_b32_e32 v34, 16, v34
	v_cvt_pk_bf16_f32 v53, v55, v55
	v_lshl_add_u64 v[68:69], v[100:101], 0, s[18:19]
	v_and_or_b32 v53, v53, s80, v34
	global_store_dwordx2 v[68:69], v[70:71], off
	global_store_dwordx2 v[100:101], v[52:53], off offset:-1024

; __device__ __forceinline__ unsigned pk2(float lo, float hi) { return f2bf(lo) | (f2bf(hi) << 16); }
; __device__ __forceinline__ void ph_ln2(CArgs& a, int l, LAS unsigned char* lds, int gw, int ngw) {
;     ...
;             for (int j = 0; j < 4; ++j) { const int c0 = j * 256 + 4 * lane;
;                 const f32x4 xn = v[j] * rstd * lgv[j] + lbv[j];
;                 if (lastl) *(f32x4*)(a.out + (size_t)(row - NTOK_C) * D + c0) = xn;
;                 else { *(u32x2*)(X + (size_t)row * D + c0) = (u32x2){pk2(xn[0], xn[1]), pk2(xn[2], xn[3])}; const f32x4 hh = xn * (1.f + scv[j]) + shv[j];
;                     u32x2 o; o.x = pk2(hh[0], hh[1]); o.y = pk2(hh[2], hh[3]); *(u32x2*)(HB + (size_t)row * D + c0) = o; } }
.LBB0_3333:
	s_andn2_b64 vcc, exec, s[26:27]
	s_cbranch_vccnz .LBB0_3335
	v_cvt_pk_bf16_f32 v66, v52, v53
	v_pk_fma_f32 v[52:53], v[108:109], v[52:53], v[60:61]
	v_cvt_pk_bf16_f32 v67, v54, v55
	v_pk_fma_f32 v[54:55], v[110:111], v[54:55], v[62:63]
	v_cvt_pk_bf16_f32 v52, v52, v53
	s_mov_b32 s18, 0xf6fffe00
	v_cvt_pk_bf16_f32 v34, v54, v54
	s_mov_b32 s19, -1
	v_lshrrev_b32_e32 v34, 16, v34
	v_cvt_pk_bf16_f32 v53, v55, v55
	v_lshl_add_u64 v[64:65], v[100:101], 0, s[18:19]
	v_and_or_b32 v53, v53, s80, v34
	global_store_dwordx2 v[64:65], v[66:67], off
	global_store_dwordx2 v[100:101], v[52:53], off offset:-512

; __device__ __forceinline__ unsigned pk2(float lo, float hi) { return f2bf(lo) | (f2bf(hi) << 16); }
; __device__ __forceinline__ void ph_ln2(CArgs& a, int l, LAS unsigned char* lds, int gw, int ngw) {
;     ...
;             for (int j = 0; j < 4; ++j) { const int c0 = j * 256 + 4 * lane;
;                 const f32x4 xn = v[j] * rstd * lgv[j] + lbv[j];
;                 if (lastl) *(f32x4*)(a.out + (size_t)(row - NTOK_C) * D + c0) = xn;
;                 else { *(u32x2*)(X + (size_t)row * D + c0) = (u32x2){pk2(xn[0], xn[1]), pk2(xn[2], xn[3])}; const f32x4 hh = xn * (1.f + scv[j]) + shv[j];
;                     u32x2 o; o.x = pk2(hh[0], hh[1]); o.y = pk2(hh[2], hh[3]); *(u32x2*)(HB + (size_t)row * D + c0) = o; } }
.LBB0_3337:
	s_andn2_b64 vcc, exec, s[26:27]
	s_cbranch_vccnz .LBB0_3298
	v_cvt_pk_bf16_f32 v62, v52, v53
	v_pk_fma_f32 v[48:49], v[102:103], v[52:53], v[48:49]
	v_cvt_pk_bf16_f32 v63, v54, v55
	v_pk_fma_f32 v[50:51], v[104:105], v[54:55], v[50:51]
	v_cvt_pk_bf16_f32 v48, v48, v49
	s_mov_b32 s14, 0xf7000000
	v_cvt_pk_bf16_f32 v34, v50, v50
	s_mov_b32 s15, -1
	v_lshrrev_b32_e32 v34, 16, v34
	v_cvt_pk_bf16_f32 v49, v51, v51
	v_lshl_add_u64 v[60:61], v[100:101], 0, s[14:15]
	v_and_or_b32 v49, v49, s80, v34
	global_store_dwordx2 v[60:61], v[62:63], off
	global_store_dwordx2 v[100:101], v[48:49], off
	s_branch .LBB0_3298
